# v55 + P3/P7 routed-combine loops fully unrolled and double-buffered (next round's 20 row loads issued before this round's arithmetic, counted waits)
# baseline (speedup 1.0000x reference)
.LBB0_462:
	s_add_i32 s10, s18, s19
	s_add_i32 s12, s10, 2
	s_add_i32 s16, s5, s20
	s_ashr_i32 s13, s12, 31
	s_add_i32 s42, s16, -15
	s_lshl_b64 s[12:13], s[12:13], 11
	s_ashr_i32 s43, s42, 31
	v_lshl_add_u64 v[2:3], v[82:83], 0, s[12:13]
	s_lshl_b64 s[42:43], s[42:43], 10
	global_load_dwordx4 v[42:45], v[2:3], off offset:16
	global_load_dwordx4 v[62:65], v[2:3], off
	v_lshl_add_u64 v[2:3], v[84:85], 0, s[42:43]
	s_add_i32 s42, s16, -14
	s_ashr_i32 s43, s42, 31
	s_lshl_b64 s[42:43], s[42:43], 10
	global_load_dwordx4 v[46:49], v[2:3], off
	v_lshl_add_u64 v[2:3], v[84:85], 0, s[42:43]
	s_add_i32 s42, s16, -13
	s_ashr_i32 s43, s42, 31
	s_lshl_b64 s[42:43], s[42:43], 10
	global_load_dwordx4 v[50:53], v[2:3], off
	v_lshl_add_u64 v[2:3], v[84:85], 0, s[42:43]
	s_add_i32 s42, s16, -12
	s_ashr_i32 s43, s42, 31
	s_lshl_b64 s[42:43], s[42:43], 10
	global_load_dwordx4 v[54:57], v[2:3], off
	v_lshl_add_u64 v[2:3], v[84:85], 0, s[42:43]
	s_add_i32 s42, s16, -11
	s_ashr_i32 s43, s42, 31
	s_lshl_b64 s[42:43], s[42:43], 10
	global_load_dwordx4 v[58:61], v[2:3], off
	v_lshl_add_u64 v[2:3], v[84:85], 0, s[42:43]
	s_add_i32 s42, s16, -10
	s_ashr_i32 s43, s42, 31
	s_lshl_b64 s[42:43], s[42:43], 10
	global_load_dwordx4 v[66:69], v[2:3], off
	v_lshl_add_u64 v[2:3], v[84:85], 0, s[42:43]
	s_add_i32 s42, s16, -9
	s_ashr_i32 s43, s42, 31
	s_lshl_b64 s[42:43], s[42:43], 10
	global_load_dwordx4 v[70:73], v[2:3], off
	v_lshl_add_u64 v[2:3], v[84:85], 0, s[42:43]
	s_add_i32 s42, s16, -8
	s_ashr_i32 s43, s42, 31
	s_lshl_b64 s[42:43], s[42:43], 10
	global_load_dwordx4 v[74:77], v[2:3], off
	v_lshl_add_u64 v[2:3], v[84:85], 0, s[42:43]
	global_load_dwordx4 v[78:81], v[2:3], off
	s_add_i32 s10, s10, 3
	s_ashr_i32 s11, s10, 31
	s_add_i32 s42, s16, -7
	s_lshl_b64 s[10:11], s[10:11], 11
	s_ashr_i32 s43, s42, 31
	v_lshl_add_u64 v[6:7], v[82:83], 0, s[10:11]
	s_lshl_b64 s[42:43], s[42:43], 10
	global_load_dwordx4 v[2:5], v[6:7], off offset:16
	global_load_dwordx4 v[26:29], v[6:7], off
	v_lshl_add_u64 v[6:7], v[84:85], 0, s[42:43]
	s_add_i32 s42, s16, -6
	s_ashr_i32 s43, s42, 31
	s_lshl_b64 s[42:43], s[42:43], 10
	v_lshl_add_u64 v[10:11], v[84:85], 0, s[42:43]
	s_add_i32 s42, s16, -5
	s_ashr_i32 s43, s42, 31
	s_lshl_b64 s[42:43], s[42:43], 10
	v_lshl_add_u64 v[14:15], v[84:85], 0, s[42:43]
	s_add_i32 s42, s16, -4
	s_ashr_i32 s43, s42, 31
	s_lshl_b64 s[42:43], s[42:43], 10
	v_lshl_add_u64 v[18:19], v[84:85], 0, s[42:43]
	s_add_i32 s42, s16, -3
	s_ashr_i32 s43, s42, 31
	s_lshl_b64 s[42:43], s[42:43], 10
	v_lshl_add_u64 v[22:23], v[84:85], 0, s[42:43]
	s_add_i32 s42, s16, -2
	global_load_dwordx4 v[6:9], v[6:7], off
	s_ashr_i32 s43, s42, 31
	global_load_dwordx4 v[10:13], v[10:11], off
	s_lshl_b64 s[42:43], s[42:43], 10
	global_load_dwordx4 v[14:17], v[14:15], off
	v_lshl_add_u64 v[30:31], v[84:85], 0, s[42:43]
	s_add_i32 s42, s16, -1
	global_load_dwordx4 v[18:21], v[18:19], off
	s_ashr_i32 s43, s42, 31
	global_load_dwordx4 v[22:25], v[22:23], off
	s_lshl_b64 s[42:43], s[42:43], 10
	s_ashr_i32 s17, s16, 31
	global_load_dwordx4 v[30:33], v[30:31], off
	v_lshl_add_u64 v[34:35], v[84:85], 0, s[42:43]
	s_lshl_b64 s[16:17], s[16:17], 10
	global_load_dwordx4 v[34:37], v[34:35], off
	v_lshl_add_u64 v[38:39], v[84:85], 0, s[16:17]
	global_load_dwordx4 v[38:41], v[38:39], off
	s_add_i32 s19, s19, 2
	s_add_i32 s20, s20, 16
	s_add_i32 s98, s18, s19
	s_add_i32 s100, s98, 2
	s_add_i32 s16, s5, s20
	s_ashr_i32 s101, s100, 31
	s_add_i32 s42, s16, -15
	s_lshl_b64 s[100:101], s[100:101], 11
	s_ashr_i32 s43, s42, 31
	v_lshl_add_u64 v[122:123], v[82:83], 0, s[100:101]
	s_lshl_b64 s[42:43], s[42:43], 10
	global_load_dwordx4 v[162:165], v[122:123], off offset:16
	global_load_dwordx4 v[182:185], v[122:123], off
	v_lshl_add_u64 v[122:123], v[84:85], 0, s[42:43]
	s_add_i32 s42, s16, -14
	s_ashr_i32 s43, s42, 31
	s_lshl_b64 s[42:43], s[42:43], 10
	global_load_dwordx4 v[166:169], v[122:123], off
	v_lshl_add_u64 v[122:123], v[84:85], 0, s[42:43]
	s_add_i32 s42, s16, -13
	s_ashr_i32 s43, s42, 31
	s_lshl_b64 s[42:43], s[42:43], 10
	global_load_dwordx4 v[170:173], v[122:123], off
	v_lshl_add_u64 v[122:123], v[84:85], 0, s[42:43]
	s_add_i32 s42, s16, -12
	s_ashr_i32 s43, s42, 31
	s_lshl_b64 s[42:43], s[42:43], 10
	global_load_dwordx4 v[174:177], v[122:123], off
	v_lshl_add_u64 v[122:123], v[84:85], 0, s[42:43]
	s_add_i32 s42, s16, -11
	s_ashr_i32 s43, s42, 31
	s_lshl_b64 s[42:43], s[42:43], 10
	global_load_dwordx4 v[178:181], v[122:123], off
	v_lshl_add_u64 v[122:123], v[84:85], 0, s[42:43]
	s_add_i32 s42, s16, -10
	s_ashr_i32 s43, s42, 31
	s_lshl_b64 s[42:43], s[42:43], 10
	global_load_dwordx4 v[186:189], v[122:123], off
	v_lshl_add_u64 v[122:123], v[84:85], 0, s[42:43]
	s_add_i32 s42, s16, -9
	s_ashr_i32 s43, s42, 31
	s_lshl_b64 s[42:43], s[42:43], 10
	global_load_dwordx4 v[190:193], v[122:123], off
	v_lshl_add_u64 v[122:123], v[84:85], 0, s[42:43]
	s_add_i32 s42, s16, -8
	s_ashr_i32 s43, s42, 31
	s_lshl_b64 s[42:43], s[42:43], 10
	global_load_dwordx4 v[194:197], v[122:123], off
	v_lshl_add_u64 v[122:123], v[84:85], 0, s[42:43]
	global_load_dwordx4 v[198:201], v[122:123], off
	s_add_i32 s98, s98, 3
	s_ashr_i32 s99, s98, 31
	s_add_i32 s42, s16, -7
	s_lshl_b64 s[98:99], s[98:99], 11
	s_ashr_i32 s43, s42, 31
	v_lshl_add_u64 v[126:127], v[82:83], 0, s[98:99]
	s_lshl_b64 s[42:43], s[42:43], 10
	global_load_dwordx4 v[122:125], v[126:127], off offset:16
	global_load_dwordx4 v[146:149], v[126:127], off
	v_lshl_add_u64 v[126:127], v[84:85], 0, s[42:43]
	s_add_i32 s42, s16, -6
	s_ashr_i32 s43, s42, 31
	s_lshl_b64 s[42:43], s[42:43], 10
	v_lshl_add_u64 v[130:131], v[84:85], 0, s[42:43]
	s_add_i32 s42, s16, -5
	s_ashr_i32 s43, s42, 31
	s_lshl_b64 s[42:43], s[42:43], 10
	v_lshl_add_u64 v[134:135], v[84:85], 0, s[42:43]
	s_add_i32 s42, s16, -4
	s_ashr_i32 s43, s42, 31
	s_lshl_b64 s[42:43], s[42:43], 10
	v_lshl_add_u64 v[138:139], v[84:85], 0, s[42:43]
	s_add_i32 s42, s16, -3
	s_ashr_i32 s43, s42, 31
	s_lshl_b64 s[42:43], s[42:43], 10
	v_lshl_add_u64 v[142:143], v[84:85], 0, s[42:43]
	s_add_i32 s42, s16, -2
	global_load_dwordx4 v[126:129], v[126:127], off
	s_ashr_i32 s43, s42, 31
	global_load_dwordx4 v[130:133], v[130:131], off
	s_lshl_b64 s[42:43], s[42:43], 10
	global_load_dwordx4 v[134:137], v[134:135], off
	v_lshl_add_u64 v[150:151], v[84:85], 0, s[42:43]
	s_add_i32 s42, s16, -1
	global_load_dwordx4 v[138:141], v[138:139], off
	s_ashr_i32 s43, s42, 31
	global_load_dwordx4 v[142:145], v[142:143], off
	s_lshl_b64 s[42:43], s[42:43], 10
	s_ashr_i32 s17, s16, 31
	global_load_dwordx4 v[150:153], v[150:151], off
	v_lshl_add_u64 v[154:155], v[84:85], 0, s[42:43]
	s_lshl_b64 s[16:17], s[16:17], 10
	global_load_dwordx4 v[154:157], v[154:155], off
	v_lshl_add_u64 v[158:159], v[84:85], 0, s[16:17]
	global_load_dwordx4 v[158:161], v[158:159], off
	s_add_i32 s19, s19, 2
	s_add_i32 s20, s20, 16
	s_waitcnt vmcnt(37)
	v_cvt_pk_f32_fp8_e32 v[88:89], v46
	v_cvt_pk_f32_fp8_sdwa v[90:91], v46 src0_sel:WORD_1
	v_pk_add_f32 v[88:89], v[88:89], 0 op_sel_hi:[1,0]
	s_waitcnt vmcnt(36)
	v_cvt_pk_f32_fp8_e32 v[92:93], v50
	v_cvt_pk_f32_fp8_sdwa v[94:95], v50 src0_sel:WORD_1
	v_pk_add_f32 v[88:89], v[88:89], v[92:93]
	s_waitcnt vmcnt(35)
	v_cvt_pk_f32_fp8_e32 v[96:97], v54
	v_lshlrev_b32_e32 v92, 16, v62
	v_and_b32_e32 v93, 0xffff0000, v62
	v_cvt_pk_f32_fp8_sdwa v[98:99], v54 src0_sel:WORD_1
	v_pk_add_f32 v[88:89], v[88:89], v[96:97]
	s_waitcnt vmcnt(34)
	v_cvt_pk_f32_fp8_e32 v[100:101], v58
	v_pk_mul_f32 v[92:93], v[92:93], s[78:79] op_sel_hi:[1,0]
	v_cvt_pk_f32_fp8_sdwa v[102:103], v58 src0_sel:WORD_1
	v_pk_add_f32 v[88:89], v[88:89], v[100:101]
	s_waitcnt vmcnt(33)
	v_cvt_pk_f32_fp8_e32 v[104:105], v66
	v_cvt_pk_f32_fp8_sdwa v[106:107], v66 src0_sel:WORD_1
	v_cvt_pk_f32_fp8_e32 v[96:97], v67
	v_cvt_pk_f32_fp8_sdwa v[66:67], v67 src0_sel:WORD_1
	v_pk_add_f32 v[88:89], v[88:89], v[104:105]
	s_waitcnt vmcnt(32)
	v_cvt_pk_f32_fp8_e32 v[108:109], v70
	v_cvt_pk_f32_fp8_sdwa v[110:111], v70 src0_sel:WORD_1
	v_pk_add_f32 v[88:89], v[88:89], v[108:109]
	s_waitcnt vmcnt(31)
	v_cvt_pk_f32_fp8_e32 v[112:113], v74
	v_cvt_pk_f32_fp8_sdwa v[114:115], v74 src0_sel:WORD_1
	s_waitcnt vmcnt(30)
	v_cvt_pk_f32_fp8_e32 v[116:117], v78
	v_cvt_pk_f32_fp8_sdwa v[118:119], v78 src0_sel:WORD_1
	v_pk_add_f32 v[88:89], v[88:89], v[112:113]
	v_cvt_pk_f32_fp8_e32 v[100:101], v75
	v_pk_add_f32 v[88:89], v[88:89], v[116:117]
	v_cvt_pk_f32_fp8_sdwa v[74:75], v75 src0_sel:WORD_1
	v_pk_fma_f32 v[88:89], v[88:89], s[80:81], v[92:93] op_sel_hi:[1,0,1]
	v_cvt_pk_f32_fp8_e32 v[92:93], v55
	v_cvt_pk_bf16_f32 v62, v88, v89
	v_pk_add_f32 v[88:89], v[90:91], 0 op_sel_hi:[1,0]
	v_lshlrev_b32_e32 v90, 16, v63
	v_pk_add_f32 v[88:89], v[88:89], v[94:95]
	v_and_b32_e32 v91, 0xffff0000, v63
	v_pk_add_f32 v[88:89], v[88:89], v[98:99]
	v_pk_mul_f32 v[90:91], v[90:91], s[78:79] op_sel_hi:[1,0]
	v_pk_add_f32 v[88:89], v[88:89], v[102:103]
	v_cvt_pk_f32_fp8_sdwa v[54:55], v55 src0_sel:WORD_1
	v_pk_add_f32 v[88:89], v[88:89], v[106:107]
	v_cvt_pk_f32_fp8_e32 v[94:95], v59
	v_pk_add_f32 v[88:89], v[88:89], v[110:111]
	v_cvt_pk_f32_fp8_sdwa v[58:59], v59 src0_sel:WORD_1
	v_pk_add_f32 v[88:89], v[88:89], v[114:115]
	v_cvt_pk_f32_fp8_e32 v[98:99], v71
	v_pk_add_f32 v[88:89], v[88:89], v[118:119]
	v_cvt_pk_f32_fp8_sdwa v[70:71], v71 src0_sel:WORD_1
	v_pk_fma_f32 v[88:89], v[88:89], s[80:81], v[90:91] op_sel_hi:[1,0,1]
	v_cvt_pk_f32_fp8_e32 v[90:91], v51
	v_cvt_pk_bf16_f32 v63, v88, v89
	v_cvt_pk_f32_fp8_e32 v[88:89], v47
	v_cvt_pk_f32_fp8_sdwa v[46:47], v47 src0_sel:WORD_1
	v_cvt_pk_f32_fp8_sdwa v[50:51], v51 src0_sel:WORD_1
	v_cvt_pk_f32_fp8_e32 v[102:103], v79
	v_pk_add_f32 v[88:89], v[88:89], 0 op_sel_hi:[1,0]
	v_pk_add_f32 v[46:47], v[46:47], 0 op_sel_hi:[1,0]
	v_pk_add_f32 v[88:89], v[88:89], v[90:91]
	v_pk_add_f32 v[46:47], v[46:47], v[50:51]
	v_pk_add_f32 v[88:89], v[88:89], v[92:93]
	v_pk_add_f32 v[46:47], v[46:47], v[54:55]
	v_cvt_pk_f32_fp8_sdwa v[78:79], v79 src0_sel:WORD_1
	v_pk_add_f32 v[88:89], v[88:89], v[94:95]
	v_pk_add_f32 v[46:47], v[46:47], v[58:59]
	v_pk_add_f32 v[88:89], v[88:89], v[96:97]
	v_pk_add_f32 v[46:47], v[46:47], v[66:67]
	v_pk_add_f32 v[88:89], v[88:89], v[98:99]
	v_pk_add_f32 v[46:47], v[46:47], v[70:71]
	v_pk_add_f32 v[88:89], v[88:89], v[100:101]
	v_lshlrev_b32_e32 v90, 16, v64
	v_and_b32_e32 v91, 0xffff0000, v64
	v_pk_add_f32 v[46:47], v[46:47], v[74:75]
	v_lshlrev_b32_e32 v50, 16, v65
	v_and_b32_e32 v51, 0xffff0000, v65
	v_pk_add_f32 v[88:89], v[88:89], v[102:103]
	v_pk_mul_f32 v[90:91], v[90:91], s[78:79] op_sel_hi:[1,0]
	v_pk_add_f32 v[46:47], v[46:47], v[78:79]
	v_pk_mul_f32 v[50:51], v[50:51], s[78:79] op_sel_hi:[1,0]
	v_pk_fma_f32 v[88:89], v[88:89], s[80:81], v[90:91] op_sel_hi:[1,0,1]
	v_pk_fma_f32 v[46:47], v[46:47], s[80:81], v[50:51] op_sel_hi:[1,0,1]
	v_cvt_pk_f32_fp8_e32 v[50:51], v48
	v_cvt_pk_bf16_f32 v64, v88, v89
	v_cvt_pk_bf16_f32 v65, v46, v47
	v_lshl_add_u64 v[46:47], v[86:87], 0, s[12:13]
	v_cvt_pk_f32_fp8_e32 v[58:59], v52
	global_store_dwordx4 v[46:47], v[62:65], off
	v_cvt_pk_f32_fp8_e32 v[70:71], v60
	v_cvt_pk_f32_fp8_e32 v[78:79], v68
	v_cvt_pk_f32_fp8_e32 v[64:65], v56
	v_pk_add_f32 v[50:51], v[50:51], 0 op_sel_hi:[1,0]
	v_cvt_pk_f32_fp8_e32 v[90:91], v72
	v_pk_add_f32 v[50:51], v[50:51], v[58:59]
	v_cvt_pk_f32_fp8_e32 v[94:95], v76
	v_pk_add_f32 v[50:51], v[50:51], v[64:65]
	v_cvt_pk_f32_fp8_e32 v[98:99], v80
	v_pk_add_f32 v[50:51], v[50:51], v[70:71]
	v_cvt_pk_f32_fp8_sdwa v[54:55], v48 src0_sel:WORD_1
	v_pk_add_f32 v[50:51], v[50:51], v[78:79]
	v_cvt_pk_f32_fp8_sdwa v[62:63], v52 src0_sel:WORD_1
	v_pk_add_f32 v[50:51], v[50:51], v[90:91]
	v_lshlrev_b32_e32 v58, 16, v42
	v_pk_add_f32 v[50:51], v[50:51], v[94:95]
	v_and_b32_e32 v59, 0xffff0000, v42
	v_cvt_pk_f32_fp8_sdwa v[66:67], v56 src0_sel:WORD_1
	v_pk_add_f32 v[50:51], v[50:51], v[98:99]
	v_pk_mul_f32 v[58:59], v[58:59], s[78:79] op_sel_hi:[1,0]
	v_cvt_pk_f32_fp8_sdwa v[74:75], v60 src0_sel:WORD_1
	v_pk_fma_f32 v[50:51], v[50:51], s[80:81], v[58:59] op_sel_hi:[1,0,1]
	v_cvt_pk_f32_fp8_sdwa v[88:89], v68 src0_sel:WORD_1
	v_cvt_pk_bf16_f32 v42, v50, v51
	v_pk_add_f32 v[50:51], v[54:55], 0 op_sel_hi:[1,0]
	v_cvt_pk_f32_fp8_sdwa v[92:93], v72 src0_sel:WORD_1
	v_pk_add_f32 v[50:51], v[50:51], v[62:63]
	v_cvt_pk_f32_fp8_sdwa v[96:97], v76 src0_sel:WORD_1
	v_pk_add_f32 v[50:51], v[50:51], v[66:67]
	v_cvt_pk_f32_fp8_sdwa v[100:101], v80 src0_sel:WORD_1
	v_pk_add_f32 v[50:51], v[50:51], v[74:75]
	v_lshlrev_b32_e32 v54, 16, v43
	v_pk_add_f32 v[50:51], v[50:51], v[88:89]
	v_and_b32_e32 v55, 0xffff0000, v43
	v_pk_add_f32 v[50:51], v[50:51], v[92:93]
	v_pk_mul_f32 v[54:55], v[54:55], s[78:79] op_sel_hi:[1,0]
	v_pk_add_f32 v[50:51], v[50:51], v[96:97]
	v_cvt_pk_f32_fp8_e32 v[58:59], v57
	v_pk_add_f32 v[50:51], v[50:51], v[100:101]
	v_cvt_pk_f32_fp8_e32 v[62:63], v61
	v_pk_fma_f32 v[50:51], v[50:51], s[80:81], v[54:55] op_sel_hi:[1,0,1]
	v_cvt_pk_f32_fp8_e32 v[54:55], v53
	v_cvt_pk_bf16_f32 v43, v50, v51
	v_cvt_pk_f32_fp8_e32 v[50:51], v49
	v_cvt_pk_f32_fp8_sdwa v[48:49], v49 src0_sel:WORD_1
	v_cvt_pk_f32_fp8_sdwa v[52:53], v53 src0_sel:WORD_1
	v_cvt_pk_f32_fp8_e32 v[64:65], v69
	v_pk_add_f32 v[50:51], v[50:51], 0 op_sel_hi:[1,0]
	v_cvt_pk_f32_fp8_sdwa v[56:57], v57 src0_sel:WORD_1
	v_cvt_pk_f32_fp8_sdwa v[66:67], v69 src0_sel:WORD_1
	v_cvt_pk_f32_fp8_e32 v[68:69], v73
	v_pk_add_f32 v[50:51], v[50:51], v[54:55]
	v_cvt_pk_f32_fp8_sdwa v[60:61], v61 src0_sel:WORD_1
	v_cvt_pk_f32_fp8_sdwa v[70:71], v73 src0_sel:WORD_1
	v_cvt_pk_f32_fp8_e32 v[72:73], v77
	v_pk_add_f32 v[50:51], v[50:51], v[58:59]
	v_cvt_pk_f32_fp8_sdwa v[74:75], v77 src0_sel:WORD_1
	v_cvt_pk_f32_fp8_e32 v[76:77], v81
	v_pk_add_f32 v[50:51], v[50:51], v[62:63]
	v_pk_add_f32 v[48:49], v[48:49], 0 op_sel_hi:[1,0]
	v_pk_add_f32 v[50:51], v[50:51], v[64:65]
	v_pk_add_f32 v[48:49], v[48:49], v[52:53]
	v_pk_add_f32 v[50:51], v[50:51], v[68:69]
	v_pk_add_f32 v[48:49], v[48:49], v[56:57]
	v_cvt_pk_f32_fp8_sdwa v[78:79], v81 src0_sel:WORD_1
	v_pk_add_f32 v[50:51], v[50:51], v[72:73]
	v_lshlrev_b32_e32 v54, 16, v44
	v_and_b32_e32 v55, 0xffff0000, v44
	v_pk_add_f32 v[48:49], v[48:49], v[60:61]
	v_pk_add_f32 v[50:51], v[50:51], v[76:77]
	v_pk_mul_f32 v[54:55], v[54:55], s[78:79] op_sel_hi:[1,0]
	v_pk_add_f32 v[48:49], v[48:49], v[66:67]
	v_pk_fma_f32 v[50:51], v[50:51], s[80:81], v[54:55] op_sel_hi:[1,0,1]
	v_pk_add_f32 v[48:49], v[48:49], v[70:71]
	v_cvt_pk_bf16_f32 v44, v50, v51
	v_pk_add_f32 v[48:49], v[48:49], v[74:75]
	v_lshlrev_b32_e32 v50, 16, v45
	v_and_b32_e32 v51, 0xffff0000, v45
	v_pk_add_f32 v[48:49], v[48:49], v[78:79]
	v_pk_mul_f32 v[50:51], v[50:51], s[78:79] op_sel_hi:[1,0]
	s_waitcnt vmcnt(23)
	v_cvt_pk_f32_fp8_sdwa v[52:53], v30 src0_sel:WORD_1
	v_pk_fma_f32 v[48:49], v[48:49], s[80:81], v[50:51] op_sel_hi:[1,0,1]
	v_cvt_pk_f32_fp8_sdwa v[50:51], v22 src0_sel:WORD_1
	v_cvt_pk_bf16_f32 v45, v48, v49
	global_store_dwordx4 v[46:47], v[42:45], off offset:16
	v_cvt_pk_f32_fp8_sdwa v[46:47], v14 src0_sel:WORD_1
	v_cvt_pk_f32_fp8_sdwa v[48:49], v18 src0_sel:WORD_1
	v_cvt_pk_f32_fp8_sdwa v[42:43], v6 src0_sel:WORD_1
	v_cvt_pk_f32_fp8_sdwa v[44:45], v10 src0_sel:WORD_1
	s_waitcnt vmcnt(23)
	v_cvt_pk_f32_fp8_sdwa v[54:55], v34 src0_sel:WORD_1
	s_waitcnt vmcnt(22)
	v_cvt_pk_f32_fp8_sdwa v[56:57], v38 src0_sel:WORD_1
	v_pk_add_f32 v[42:43], v[42:43], 0 op_sel_hi:[1,0]
	v_cvt_pk_f32_fp8_e32 v[58:59], v6
	v_pk_add_f32 v[42:43], v[42:43], v[44:45]
	v_lshlrev_b32_e32 v44, 16, v27
	v_pk_add_f32 v[42:43], v[42:43], v[46:47]
	v_and_b32_e32 v45, 0xffff0000, v27
	v_pk_add_f32 v[42:43], v[42:43], v[48:49]
	v_pk_mul_f32 v[44:45], v[44:45], s[78:79] op_sel_hi:[1,0]
	v_pk_add_f32 v[42:43], v[42:43], v[50:51]
	v_cvt_pk_f32_fp8_e32 v[60:61], v10
	v_pk_add_f32 v[42:43], v[42:43], v[52:53]
	v_cvt_pk_f32_fp8_e32 v[62:63], v14
	v_pk_add_f32 v[42:43], v[42:43], v[54:55]
	v_cvt_pk_f32_fp8_e32 v[46:47], v15
	v_pk_add_f32 v[42:43], v[42:43], v[56:57]
	v_cvt_pk_f32_fp8_sdwa v[14:15], v15 src0_sel:WORD_1
	v_pk_fma_f32 v[42:43], v[42:43], s[80:81], v[44:45] op_sel_hi:[1,0,1]
	v_cvt_pk_f32_fp8_e32 v[44:45], v11
	v_cvt_pk_bf16_f32 v27, v42, v43
	v_cvt_pk_f32_fp8_e32 v[42:43], v7
	v_cvt_pk_f32_fp8_sdwa v[6:7], v7 src0_sel:WORD_1
	v_cvt_pk_f32_fp8_sdwa v[10:11], v11 src0_sel:WORD_1
	v_cvt_pk_f32_fp8_e32 v[64:65], v18
	v_cvt_pk_f32_fp8_e32 v[48:49], v19
	v_cvt_pk_f32_fp8_sdwa v[18:19], v19 src0_sel:WORD_1
	v_cvt_pk_f32_fp8_e32 v[66:67], v22
	v_pk_add_f32 v[58:59], v[58:59], 0 op_sel_hi:[1,0]
	v_cvt_pk_f32_fp8_e32 v[50:51], v23
	v_cvt_pk_f32_fp8_sdwa v[22:23], v23 src0_sel:WORD_1
	v_pk_add_f32 v[42:43], v[42:43], 0 op_sel_hi:[1,0]
	v_pk_add_f32 v[6:7], v[6:7], 0 op_sel_hi:[1,0]
	v_cvt_pk_f32_fp8_e32 v[68:69], v30
	v_pk_add_f32 v[58:59], v[58:59], v[60:61]
	v_cvt_pk_f32_fp8_e32 v[52:53], v31
	v_cvt_pk_f32_fp8_sdwa v[30:31], v31 src0_sel:WORD_1
	v_pk_add_f32 v[42:43], v[42:43], v[44:45]
	v_pk_add_f32 v[6:7], v[6:7], v[10:11]
	v_cvt_pk_f32_fp8_e32 v[70:71], v34
	v_pk_add_f32 v[58:59], v[58:59], v[62:63]
	v_cvt_pk_f32_fp8_e32 v[54:55], v35
	v_cvt_pk_f32_fp8_sdwa v[34:35], v35 src0_sel:WORD_1
	v_pk_add_f32 v[42:43], v[42:43], v[46:47]
	v_pk_add_f32 v[6:7], v[6:7], v[14:15]
	v_cvt_pk_f32_fp8_e32 v[72:73], v38
	v_pk_add_f32 v[58:59], v[58:59], v[64:65]
	v_cvt_pk_f32_fp8_e32 v[56:57], v39
	v_cvt_pk_f32_fp8_sdwa v[38:39], v39 src0_sel:WORD_1
	v_pk_add_f32 v[42:43], v[42:43], v[48:49]
	v_pk_add_f32 v[6:7], v[6:7], v[18:19]
	v_pk_add_f32 v[58:59], v[58:59], v[66:67]
	v_pk_add_f32 v[42:43], v[42:43], v[50:51]
	v_pk_add_f32 v[6:7], v[6:7], v[22:23]
	v_pk_add_f32 v[58:59], v[58:59], v[68:69]
	v_pk_add_f32 v[42:43], v[42:43], v[52:53]
	v_pk_add_f32 v[6:7], v[6:7], v[30:31]
	v_pk_add_f32 v[58:59], v[58:59], v[70:71]
	v_lshlrev_b32_e32 v60, 16, v26
	v_and_b32_e32 v61, 0xffff0000, v26
	v_pk_add_f32 v[42:43], v[42:43], v[54:55]
	v_lshlrev_b32_e32 v44, 16, v28
	v_and_b32_e32 v45, 0xffff0000, v28
	v_pk_add_f32 v[6:7], v[6:7], v[34:35]
	v_lshlrev_b32_e32 v10, 16, v29
	v_and_b32_e32 v11, 0xffff0000, v29
	v_pk_add_f32 v[58:59], v[58:59], v[72:73]
	v_pk_mul_f32 v[60:61], v[60:61], s[78:79] op_sel_hi:[1,0]
	v_pk_add_f32 v[42:43], v[42:43], v[56:57]
	v_pk_mul_f32 v[44:45], v[44:45], s[78:79] op_sel_hi:[1,0]
	v_pk_add_f32 v[6:7], v[6:7], v[38:39]
	v_pk_mul_f32 v[10:11], v[10:11], s[78:79] op_sel_hi:[1,0]
	v_pk_fma_f32 v[58:59], v[58:59], s[80:81], v[60:61] op_sel_hi:[1,0,1]
	v_pk_fma_f32 v[42:43], v[42:43], s[80:81], v[44:45] op_sel_hi:[1,0,1]
	v_pk_fma_f32 v[6:7], v[6:7], s[80:81], v[10:11] op_sel_hi:[1,0,1]
	v_cvt_pk_f32_fp8_e32 v[10:11], v8
	v_cvt_pk_bf16_f32 v26, v58, v59
	v_cvt_pk_bf16_f32 v28, v42, v43
	v_cvt_pk_bf16_f32 v29, v6, v7
	v_lshl_add_u64 v[6:7], v[86:87], 0, s[10:11]
	v_cvt_pk_f32_fp8_e32 v[18:19], v12
	global_store_dwordx4 v[6:7], v[26:29], off
	v_cvt_pk_f32_fp8_e32 v[30:31], v20
	v_cvt_pk_f32_fp8_e32 v[38:39], v24
	v_cvt_pk_f32_fp8_e32 v[26:27], v16
	v_pk_add_f32 v[10:11], v[10:11], 0 op_sel_hi:[1,0]
	v_cvt_pk_f32_fp8_e32 v[44:45], v32
	v_pk_add_f32 v[10:11], v[10:11], v[18:19]
	v_cvt_pk_f32_fp8_e32 v[48:49], v36
	v_pk_add_f32 v[10:11], v[10:11], v[26:27]
	v_cvt_pk_f32_fp8_e32 v[52:53], v40
	v_pk_add_f32 v[10:11], v[10:11], v[30:31]
	v_cvt_pk_f32_fp8_sdwa v[14:15], v8 src0_sel:WORD_1
	v_pk_add_f32 v[10:11], v[10:11], v[38:39]
	v_cvt_pk_f32_fp8_sdwa v[22:23], v12 src0_sel:WORD_1
	v_pk_add_f32 v[10:11], v[10:11], v[44:45]
	v_lshlrev_b32_e32 v18, 16, v2
	v_pk_add_f32 v[10:11], v[10:11], v[48:49]
	v_and_b32_e32 v19, 0xffff0000, v2
	v_cvt_pk_f32_fp8_sdwa v[28:29], v16 src0_sel:WORD_1
	v_pk_add_f32 v[10:11], v[10:11], v[52:53]
	v_pk_mul_f32 v[18:19], v[18:19], s[78:79] op_sel_hi:[1,0]
	v_cvt_pk_f32_fp8_sdwa v[34:35], v20 src0_sel:WORD_1
	v_pk_fma_f32 v[10:11], v[10:11], s[80:81], v[18:19] op_sel_hi:[1,0,1]
	v_cvt_pk_f32_fp8_sdwa v[42:43], v24 src0_sel:WORD_1
	v_cvt_pk_bf16_f32 v2, v10, v11
	v_pk_add_f32 v[10:11], v[14:15], 0 op_sel_hi:[1,0]
	v_cvt_pk_f32_fp8_sdwa v[46:47], v32 src0_sel:WORD_1
	v_pk_add_f32 v[10:11], v[10:11], v[22:23]
	v_cvt_pk_f32_fp8_sdwa v[50:51], v36 src0_sel:WORD_1
	v_pk_add_f32 v[10:11], v[10:11], v[28:29]
	v_cvt_pk_f32_fp8_sdwa v[54:55], v40 src0_sel:WORD_1
	v_pk_add_f32 v[10:11], v[10:11], v[34:35]
	v_lshlrev_b32_e32 v14, 16, v3
	v_pk_add_f32 v[10:11], v[10:11], v[42:43]
	v_and_b32_e32 v15, 0xffff0000, v3
	v_pk_add_f32 v[10:11], v[10:11], v[46:47]
	v_pk_mul_f32 v[14:15], v[14:15], s[78:79] op_sel_hi:[1,0]
	v_pk_add_f32 v[10:11], v[10:11], v[50:51]
	v_cvt_pk_f32_fp8_e32 v[26:27], v9
	v_pk_add_f32 v[10:11], v[10:11], v[54:55]
	v_cvt_pk_f32_fp8_sdwa v[8:9], v9 src0_sel:WORD_1
	v_pk_fma_f32 v[10:11], v[10:11], s[80:81], v[14:15] op_sel_hi:[1,0,1]
	v_cvt_pk_f32_fp8_e32 v[28:29], v13
	v_cvt_pk_bf16_f32 v3, v10, v11
	v_cvt_pk_f32_fp8_sdwa v[10:11], v13 src0_sel:WORD_1
	v_cvt_pk_f32_fp8_e32 v[30:31], v17
	v_cvt_pk_f32_fp8_sdwa v[12:13], v17 src0_sel:WORD_1
	v_cvt_pk_f32_fp8_e32 v[34:35], v21
	v_cvt_pk_f32_fp8_sdwa v[14:15], v21 src0_sel:WORD_1
	v_cvt_pk_f32_fp8_e32 v[38:39], v25
	v_cvt_pk_f32_fp8_sdwa v[16:17], v25 src0_sel:WORD_1
	v_pk_add_f32 v[26:27], v[26:27], 0 op_sel_hi:[1,0]
	v_pk_add_f32 v[8:9], v[8:9], 0 op_sel_hi:[1,0]
	v_cvt_pk_f32_fp8_e32 v[24:25], v33
	v_cvt_pk_f32_fp8_sdwa v[18:19], v33 src0_sel:WORD_1
	v_pk_add_f32 v[26:27], v[26:27], v[28:29]
	v_pk_add_f32 v[8:9], v[8:9], v[10:11]
	v_cvt_pk_f32_fp8_e32 v[32:33], v37
	v_cvt_pk_f32_fp8_sdwa v[20:21], v37 src0_sel:WORD_1
	v_pk_add_f32 v[26:27], v[26:27], v[30:31]
	v_pk_add_f32 v[8:9], v[8:9], v[12:13]
	v_cvt_pk_f32_fp8_e32 v[36:37], v41
	v_cvt_pk_f32_fp8_sdwa v[22:23], v41 src0_sel:WORD_1
	v_pk_add_f32 v[26:27], v[26:27], v[34:35]
	v_pk_add_f32 v[8:9], v[8:9], v[14:15]
	v_pk_add_f32 v[26:27], v[26:27], v[38:39]
	v_pk_add_f32 v[8:9], v[8:9], v[16:17]
	v_pk_add_f32 v[24:25], v[26:27], v[24:25]
	v_pk_add_f32 v[8:9], v[8:9], v[18:19]
	v_pk_add_f32 v[24:25], v[24:25], v[32:33]
	v_lshlrev_b32_e32 v26, 16, v4
	v_and_b32_e32 v27, 0xffff0000, v4
	v_pk_add_f32 v[8:9], v[8:9], v[20:21]
	v_lshlrev_b32_e32 v10, 16, v5
	v_and_b32_e32 v11, 0xffff0000, v5
	v_pk_add_f32 v[24:25], v[24:25], v[36:37]
	v_pk_mul_f32 v[26:27], v[26:27], s[78:79] op_sel_hi:[1,0]
	v_pk_add_f32 v[8:9], v[8:9], v[22:23]
	v_pk_mul_f32 v[10:11], v[10:11], s[78:79] op_sel_hi:[1,0]
	v_pk_fma_f32 v[24:25], v[24:25], s[80:81], v[26:27] op_sel_hi:[1,0,1]
	v_pk_fma_f32 v[8:9], v[8:9], s[80:81], v[10:11] op_sel_hi:[1,0,1]
	v_cvt_pk_bf16_f32 v4, v24, v25
	v_cvt_pk_bf16_f32 v5, v8, v9
	global_store_dwordx4 v[6:7], v[2:5], off offset:16
	s_add_i32 s10, s18, s19
	s_add_i32 s12, s10, 2
	s_add_i32 s16, s5, s20
	s_ashr_i32 s13, s12, 31
	s_add_i32 s42, s16, -15
	s_lshl_b64 s[12:13], s[12:13], 11
	s_ashr_i32 s43, s42, 31
	v_lshl_add_u64 v[2:3], v[82:83], 0, s[12:13]
	s_lshl_b64 s[42:43], s[42:43], 10
	global_load_dwordx4 v[42:45], v[2:3], off offset:16
	global_load_dwordx4 v[62:65], v[2:3], off
	v_lshl_add_u64 v[2:3], v[84:85], 0, s[42:43]
	s_add_i32 s42, s16, -14
	s_ashr_i32 s43, s42, 31
	s_lshl_b64 s[42:43], s[42:43], 10
	global_load_dwordx4 v[46:49], v[2:3], off
	v_lshl_add_u64 v[2:3], v[84:85], 0, s[42:43]
	s_add_i32 s42, s16, -13
	s_ashr_i32 s43, s42, 31
	s_lshl_b64 s[42:43], s[42:43], 10
	global_load_dwordx4 v[50:53], v[2:3], off
	v_lshl_add_u64 v[2:3], v[84:85], 0, s[42:43]
	s_add_i32 s42, s16, -12
	s_ashr_i32 s43, s42, 31
	s_lshl_b64 s[42:43], s[42:43], 10
	global_load_dwordx4 v[54:57], v[2:3], off
	v_lshl_add_u64 v[2:3], v[84:85], 0, s[42:43]
	s_add_i32 s42, s16, -11
	s_ashr_i32 s43, s42, 31
	s_lshl_b64 s[42:43], s[42:43], 10
	global_load_dwordx4 v[58:61], v[2:3], off
	v_lshl_add_u64 v[2:3], v[84:85], 0, s[42:43]
	s_add_i32 s42, s16, -10
	s_ashr_i32 s43, s42, 31
	s_lshl_b64 s[42:43], s[42:43], 10
	global_load_dwordx4 v[66:69], v[2:3], off
	v_lshl_add_u64 v[2:3], v[84:85], 0, s[42:43]
	s_add_i32 s42, s16, -9
	s_ashr_i32 s43, s42, 31
	s_lshl_b64 s[42:43], s[42:43], 10
	global_load_dwordx4 v[70:73], v[2:3], off
	v_lshl_add_u64 v[2:3], v[84:85], 0, s[42:43]
	s_add_i32 s42, s16, -8
	s_ashr_i32 s43, s42, 31
	s_lshl_b64 s[42:43], s[42:43], 10
	global_load_dwordx4 v[74:77], v[2:3], off
	v_lshl_add_u64 v[2:3], v[84:85], 0, s[42:43]
	global_load_dwordx4 v[78:81], v[2:3], off
	s_add_i32 s10, s10, 3
	s_ashr_i32 s11, s10, 31
	s_add_i32 s42, s16, -7
	s_lshl_b64 s[10:11], s[10:11], 11
	s_ashr_i32 s43, s42, 31
	v_lshl_add_u64 v[6:7], v[82:83], 0, s[10:11]
	s_lshl_b64 s[42:43], s[42:43], 10
	global_load_dwordx4 v[2:5], v[6:7], off offset:16
	global_load_dwordx4 v[26:29], v[6:7], off
	v_lshl_add_u64 v[6:7], v[84:85], 0, s[42:43]
	s_add_i32 s42, s16, -6
	s_ashr_i32 s43, s42, 31
	s_lshl_b64 s[42:43], s[42:43], 10
	v_lshl_add_u64 v[10:11], v[84:85], 0, s[42:43]
	s_add_i32 s42, s16, -5
	s_ashr_i32 s43, s42, 31
	s_lshl_b64 s[42:43], s[42:43], 10
	v_lshl_add_u64 v[14:15], v[84:85], 0, s[42:43]
	s_add_i32 s42, s16, -4
	s_ashr_i32 s43, s42, 31
	s_lshl_b64 s[42:43], s[42:43], 10
	v_lshl_add_u64 v[18:19], v[84:85], 0, s[42:43]
	s_add_i32 s42, s16, -3
	s_ashr_i32 s43, s42, 31
	s_lshl_b64 s[42:43], s[42:43], 10
	v_lshl_add_u64 v[22:23], v[84:85], 0, s[42:43]
	s_add_i32 s42, s16, -2
	global_load_dwordx4 v[6:9], v[6:7], off
	s_ashr_i32 s43, s42, 31
	global_load_dwordx4 v[10:13], v[10:11], off
	s_lshl_b64 s[42:43], s[42:43], 10
	global_load_dwordx4 v[14:17], v[14:15], off
	v_lshl_add_u64 v[30:31], v[84:85], 0, s[42:43]
	s_add_i32 s42, s16, -1
	global_load_dwordx4 v[18:21], v[18:19], off
	s_ashr_i32 s43, s42, 31
	global_load_dwordx4 v[22:25], v[22:23], off
	s_lshl_b64 s[42:43], s[42:43], 10
	s_ashr_i32 s17, s16, 31
	global_load_dwordx4 v[30:33], v[30:31], off
	v_lshl_add_u64 v[34:35], v[84:85], 0, s[42:43]
	s_lshl_b64 s[16:17], s[16:17], 10
	global_load_dwordx4 v[34:37], v[34:35], off
	v_lshl_add_u64 v[38:39], v[84:85], 0, s[16:17]
	global_load_dwordx4 v[38:41], v[38:39], off
	s_add_i32 s19, s19, 2
	s_add_i32 s20, s20, 16
	s_waitcnt vmcnt(41)
	v_cvt_pk_f32_fp8_e32 v[88:89], v166
	v_cvt_pk_f32_fp8_sdwa v[90:91], v166 src0_sel:WORD_1
	v_pk_add_f32 v[88:89], v[88:89], 0 op_sel_hi:[1,0]
	s_waitcnt vmcnt(40)
	v_cvt_pk_f32_fp8_e32 v[92:93], v170
	v_cvt_pk_f32_fp8_sdwa v[94:95], v170 src0_sel:WORD_1
	v_pk_add_f32 v[88:89], v[88:89], v[92:93]
	s_waitcnt vmcnt(39)
	v_cvt_pk_f32_fp8_e32 v[96:97], v174
	v_lshlrev_b32_e32 v92, 16, v182
	v_and_b32_e32 v93, 0xffff0000, v182
	v_cvt_pk_f32_fp8_sdwa v[98:99], v174 src0_sel:WORD_1
	v_pk_add_f32 v[88:89], v[88:89], v[96:97]
	s_waitcnt vmcnt(38)
	v_cvt_pk_f32_fp8_e32 v[100:101], v178
	v_pk_mul_f32 v[92:93], v[92:93], s[78:79] op_sel_hi:[1,0]
	v_cvt_pk_f32_fp8_sdwa v[102:103], v178 src0_sel:WORD_1
	v_pk_add_f32 v[88:89], v[88:89], v[100:101]
	s_waitcnt vmcnt(37)
	v_cvt_pk_f32_fp8_e32 v[104:105], v186
	v_cvt_pk_f32_fp8_sdwa v[106:107], v186 src0_sel:WORD_1
	v_cvt_pk_f32_fp8_e32 v[96:97], v187
	v_cvt_pk_f32_fp8_sdwa v[186:187], v187 src0_sel:WORD_1
	v_pk_add_f32 v[88:89], v[88:89], v[104:105]
	s_waitcnt vmcnt(36)
	v_cvt_pk_f32_fp8_e32 v[108:109], v190
	v_cvt_pk_f32_fp8_sdwa v[110:111], v190 src0_sel:WORD_1
	v_pk_add_f32 v[88:89], v[88:89], v[108:109]
	s_waitcnt vmcnt(35)
	v_cvt_pk_f32_fp8_e32 v[112:113], v194
	v_cvt_pk_f32_fp8_sdwa v[114:115], v194 src0_sel:WORD_1
	s_waitcnt vmcnt(34)
	v_cvt_pk_f32_fp8_e32 v[116:117], v198
	v_cvt_pk_f32_fp8_sdwa v[118:119], v198 src0_sel:WORD_1
	v_pk_add_f32 v[88:89], v[88:89], v[112:113]
	v_cvt_pk_f32_fp8_e32 v[100:101], v195
	v_pk_add_f32 v[88:89], v[88:89], v[116:117]
	v_cvt_pk_f32_fp8_sdwa v[194:195], v195 src0_sel:WORD_1
	v_pk_fma_f32 v[88:89], v[88:89], s[80:81], v[92:93] op_sel_hi:[1,0,1]
	v_cvt_pk_f32_fp8_e32 v[92:93], v175
	v_cvt_pk_bf16_f32 v182, v88, v89
	v_pk_add_f32 v[88:89], v[90:91], 0 op_sel_hi:[1,0]
	v_lshlrev_b32_e32 v90, 16, v183
	v_pk_add_f32 v[88:89], v[88:89], v[94:95]
	v_and_b32_e32 v91, 0xffff0000, v183
	v_pk_add_f32 v[88:89], v[88:89], v[98:99]
	v_pk_mul_f32 v[90:91], v[90:91], s[78:79] op_sel_hi:[1,0]
	v_pk_add_f32 v[88:89], v[88:89], v[102:103]
	v_cvt_pk_f32_fp8_sdwa v[174:175], v175 src0_sel:WORD_1
	v_pk_add_f32 v[88:89], v[88:89], v[106:107]
	v_cvt_pk_f32_fp8_e32 v[94:95], v179
	v_pk_add_f32 v[88:89], v[88:89], v[110:111]
	v_cvt_pk_f32_fp8_sdwa v[178:179], v179 src0_sel:WORD_1
	v_pk_add_f32 v[88:89], v[88:89], v[114:115]
	v_cvt_pk_f32_fp8_e32 v[98:99], v191
	v_pk_add_f32 v[88:89], v[88:89], v[118:119]
	v_cvt_pk_f32_fp8_sdwa v[190:191], v191 src0_sel:WORD_1
	v_pk_fma_f32 v[88:89], v[88:89], s[80:81], v[90:91] op_sel_hi:[1,0,1]
	v_cvt_pk_f32_fp8_e32 v[90:91], v171
	v_cvt_pk_bf16_f32 v183, v88, v89
	v_cvt_pk_f32_fp8_e32 v[88:89], v167
	v_cvt_pk_f32_fp8_sdwa v[166:167], v167 src0_sel:WORD_1
	v_cvt_pk_f32_fp8_sdwa v[170:171], v171 src0_sel:WORD_1
	v_cvt_pk_f32_fp8_e32 v[102:103], v199
	v_pk_add_f32 v[88:89], v[88:89], 0 op_sel_hi:[1,0]
	v_pk_add_f32 v[166:167], v[166:167], 0 op_sel_hi:[1,0]
	v_pk_add_f32 v[88:89], v[88:89], v[90:91]
	v_pk_add_f32 v[166:167], v[166:167], v[170:171]
	v_pk_add_f32 v[88:89], v[88:89], v[92:93]
	v_pk_add_f32 v[166:167], v[166:167], v[174:175]
	v_cvt_pk_f32_fp8_sdwa v[198:199], v199 src0_sel:WORD_1
	v_pk_add_f32 v[88:89], v[88:89], v[94:95]
	v_pk_add_f32 v[166:167], v[166:167], v[178:179]
	v_pk_add_f32 v[88:89], v[88:89], v[96:97]
	v_pk_add_f32 v[166:167], v[166:167], v[186:187]
	v_pk_add_f32 v[88:89], v[88:89], v[98:99]
	v_pk_add_f32 v[166:167], v[166:167], v[190:191]
	v_pk_add_f32 v[88:89], v[88:89], v[100:101]
	v_lshlrev_b32_e32 v90, 16, v184
	v_and_b32_e32 v91, 0xffff0000, v184
	v_pk_add_f32 v[166:167], v[166:167], v[194:195]
	v_lshlrev_b32_e32 v170, 16, v185
	v_and_b32_e32 v171, 0xffff0000, v185
	v_pk_add_f32 v[88:89], v[88:89], v[102:103]
	v_pk_mul_f32 v[90:91], v[90:91], s[78:79] op_sel_hi:[1,0]
	v_pk_add_f32 v[166:167], v[166:167], v[198:199]
	v_pk_mul_f32 v[170:171], v[170:171], s[78:79] op_sel_hi:[1,0]
	v_pk_fma_f32 v[88:89], v[88:89], s[80:81], v[90:91] op_sel_hi:[1,0,1]
	v_pk_fma_f32 v[166:167], v[166:167], s[80:81], v[170:171] op_sel_hi:[1,0,1]
	v_cvt_pk_f32_fp8_e32 v[170:171], v168
	v_cvt_pk_bf16_f32 v184, v88, v89
	v_cvt_pk_bf16_f32 v185, v166, v167
	v_lshl_add_u64 v[166:167], v[86:87], 0, s[100:101]
	v_cvt_pk_f32_fp8_e32 v[178:179], v172
	global_store_dwordx4 v[166:167], v[182:185], off
	v_cvt_pk_f32_fp8_e32 v[190:191], v180
	v_cvt_pk_f32_fp8_e32 v[198:199], v188
	v_cvt_pk_f32_fp8_e32 v[184:185], v176
	v_pk_add_f32 v[170:171], v[170:171], 0 op_sel_hi:[1,0]
	v_cvt_pk_f32_fp8_e32 v[90:91], v192
	v_pk_add_f32 v[170:171], v[170:171], v[178:179]
	v_cvt_pk_f32_fp8_e32 v[94:95], v196
	v_pk_add_f32 v[170:171], v[170:171], v[184:185]
	v_cvt_pk_f32_fp8_e32 v[98:99], v200
	v_pk_add_f32 v[170:171], v[170:171], v[190:191]
	v_cvt_pk_f32_fp8_sdwa v[174:175], v168 src0_sel:WORD_1
	v_pk_add_f32 v[170:171], v[170:171], v[198:199]
	v_cvt_pk_f32_fp8_sdwa v[182:183], v172 src0_sel:WORD_1
	v_pk_add_f32 v[170:171], v[170:171], v[90:91]
	v_lshlrev_b32_e32 v178, 16, v162
	v_pk_add_f32 v[170:171], v[170:171], v[94:95]
	v_and_b32_e32 v179, 0xffff0000, v162
	v_cvt_pk_f32_fp8_sdwa v[186:187], v176 src0_sel:WORD_1
	v_pk_add_f32 v[170:171], v[170:171], v[98:99]
	v_pk_mul_f32 v[178:179], v[178:179], s[78:79] op_sel_hi:[1,0]
	v_cvt_pk_f32_fp8_sdwa v[194:195], v180 src0_sel:WORD_1
	v_pk_fma_f32 v[170:171], v[170:171], s[80:81], v[178:179] op_sel_hi:[1,0,1]
	v_cvt_pk_f32_fp8_sdwa v[88:89], v188 src0_sel:WORD_1
	v_cvt_pk_bf16_f32 v162, v170, v171
	v_pk_add_f32 v[170:171], v[174:175], 0 op_sel_hi:[1,0]
	v_cvt_pk_f32_fp8_sdwa v[92:93], v192 src0_sel:WORD_1
	v_pk_add_f32 v[170:171], v[170:171], v[182:183]
	v_cvt_pk_f32_fp8_sdwa v[96:97], v196 src0_sel:WORD_1
	v_pk_add_f32 v[170:171], v[170:171], v[186:187]
	v_cvt_pk_f32_fp8_sdwa v[100:101], v200 src0_sel:WORD_1
	v_pk_add_f32 v[170:171], v[170:171], v[194:195]
	v_lshlrev_b32_e32 v174, 16, v163
	v_pk_add_f32 v[170:171], v[170:171], v[88:89]
	v_and_b32_e32 v175, 0xffff0000, v163
	v_pk_add_f32 v[170:171], v[170:171], v[92:93]
	v_pk_mul_f32 v[174:175], v[174:175], s[78:79] op_sel_hi:[1,0]
	v_pk_add_f32 v[170:171], v[170:171], v[96:97]
	v_cvt_pk_f32_fp8_e32 v[178:179], v177
	v_pk_add_f32 v[170:171], v[170:171], v[100:101]
	v_cvt_pk_f32_fp8_e32 v[182:183], v181
	v_pk_fma_f32 v[170:171], v[170:171], s[80:81], v[174:175] op_sel_hi:[1,0,1]
	v_cvt_pk_f32_fp8_e32 v[174:175], v173
	v_cvt_pk_bf16_f32 v163, v170, v171
	v_cvt_pk_f32_fp8_e32 v[170:171], v169
	v_cvt_pk_f32_fp8_sdwa v[168:169], v169 src0_sel:WORD_1
	v_cvt_pk_f32_fp8_sdwa v[172:173], v173 src0_sel:WORD_1
	v_cvt_pk_f32_fp8_e32 v[184:185], v189
	v_pk_add_f32 v[170:171], v[170:171], 0 op_sel_hi:[1,0]
	v_cvt_pk_f32_fp8_sdwa v[176:177], v177 src0_sel:WORD_1
	v_cvt_pk_f32_fp8_sdwa v[186:187], v189 src0_sel:WORD_1
	v_cvt_pk_f32_fp8_e32 v[188:189], v193
	v_pk_add_f32 v[170:171], v[170:171], v[174:175]
	v_cvt_pk_f32_fp8_sdwa v[180:181], v181 src0_sel:WORD_1
	v_cvt_pk_f32_fp8_sdwa v[190:191], v193 src0_sel:WORD_1
	v_cvt_pk_f32_fp8_e32 v[192:193], v197
	v_pk_add_f32 v[170:171], v[170:171], v[178:179]
	v_cvt_pk_f32_fp8_sdwa v[194:195], v197 src0_sel:WORD_1
	v_cvt_pk_f32_fp8_e32 v[196:197], v201
	v_pk_add_f32 v[170:171], v[170:171], v[182:183]
	v_pk_add_f32 v[168:169], v[168:169], 0 op_sel_hi:[1,0]
	v_pk_add_f32 v[170:171], v[170:171], v[184:185]
	v_pk_add_f32 v[168:169], v[168:169], v[172:173]
	v_pk_add_f32 v[170:171], v[170:171], v[188:189]
	v_pk_add_f32 v[168:169], v[168:169], v[176:177]
	v_cvt_pk_f32_fp8_sdwa v[198:199], v201 src0_sel:WORD_1
	v_pk_add_f32 v[170:171], v[170:171], v[192:193]
	v_lshlrev_b32_e32 v174, 16, v164
	v_and_b32_e32 v175, 0xffff0000, v164
	v_pk_add_f32 v[168:169], v[168:169], v[180:181]
	v_pk_add_f32 v[170:171], v[170:171], v[196:197]
	v_pk_mul_f32 v[174:175], v[174:175], s[78:79] op_sel_hi:[1,0]
	v_pk_add_f32 v[168:169], v[168:169], v[186:187]
	v_pk_fma_f32 v[170:171], v[170:171], s[80:81], v[174:175] op_sel_hi:[1,0,1]
	v_pk_add_f32 v[168:169], v[168:169], v[190:191]
	v_cvt_pk_bf16_f32 v164, v170, v171
	v_pk_add_f32 v[168:169], v[168:169], v[194:195]
	v_lshlrev_b32_e32 v170, 16, v165
	v_and_b32_e32 v171, 0xffff0000, v165
	v_pk_add_f32 v[168:169], v[168:169], v[198:199]
	v_pk_mul_f32 v[170:171], v[170:171], s[78:79] op_sel_hi:[1,0]
	s_waitcnt vmcnt(27)
	v_cvt_pk_f32_fp8_sdwa v[172:173], v150 src0_sel:WORD_1
	v_pk_fma_f32 v[168:169], v[168:169], s[80:81], v[170:171] op_sel_hi:[1,0,1]
	v_cvt_pk_f32_fp8_sdwa v[170:171], v142 src0_sel:WORD_1
	v_cvt_pk_bf16_f32 v165, v168, v169
	global_store_dwordx4 v[166:167], v[162:165], off offset:16
	v_cvt_pk_f32_fp8_sdwa v[166:167], v134 src0_sel:WORD_1
	v_cvt_pk_f32_fp8_sdwa v[168:169], v138 src0_sel:WORD_1
	v_cvt_pk_f32_fp8_sdwa v[162:163], v126 src0_sel:WORD_1
	v_cvt_pk_f32_fp8_sdwa v[164:165], v130 src0_sel:WORD_1
	s_waitcnt vmcnt(27)
	v_cvt_pk_f32_fp8_sdwa v[174:175], v154 src0_sel:WORD_1
	s_waitcnt vmcnt(26)
	v_cvt_pk_f32_fp8_sdwa v[176:177], v158 src0_sel:WORD_1
	v_pk_add_f32 v[162:163], v[162:163], 0 op_sel_hi:[1,0]
	v_cvt_pk_f32_fp8_e32 v[178:179], v126
	v_pk_add_f32 v[162:163], v[162:163], v[164:165]
	v_lshlrev_b32_e32 v164, 16, v147
	v_pk_add_f32 v[162:163], v[162:163], v[166:167]
	v_and_b32_e32 v165, 0xffff0000, v147
	v_pk_add_f32 v[162:163], v[162:163], v[168:169]
	v_pk_mul_f32 v[164:165], v[164:165], s[78:79] op_sel_hi:[1,0]
	v_pk_add_f32 v[162:163], v[162:163], v[170:171]
	v_cvt_pk_f32_fp8_e32 v[180:181], v130
	v_pk_add_f32 v[162:163], v[162:163], v[172:173]
	v_cvt_pk_f32_fp8_e32 v[182:183], v134
	v_pk_add_f32 v[162:163], v[162:163], v[174:175]
	v_cvt_pk_f32_fp8_e32 v[166:167], v135
	v_pk_add_f32 v[162:163], v[162:163], v[176:177]
	v_cvt_pk_f32_fp8_sdwa v[134:135], v135 src0_sel:WORD_1
	v_pk_fma_f32 v[162:163], v[162:163], s[80:81], v[164:165] op_sel_hi:[1,0,1]
	v_cvt_pk_f32_fp8_e32 v[164:165], v131
	v_cvt_pk_bf16_f32 v147, v162, v163
	v_cvt_pk_f32_fp8_e32 v[162:163], v127
	v_cvt_pk_f32_fp8_sdwa v[126:127], v127 src0_sel:WORD_1
	v_cvt_pk_f32_fp8_sdwa v[130:131], v131 src0_sel:WORD_1
	v_cvt_pk_f32_fp8_e32 v[184:185], v138
	v_cvt_pk_f32_fp8_e32 v[168:169], v139
	v_cvt_pk_f32_fp8_sdwa v[138:139], v139 src0_sel:WORD_1
	v_cvt_pk_f32_fp8_e32 v[186:187], v142
	v_pk_add_f32 v[178:179], v[178:179], 0 op_sel_hi:[1,0]
	v_cvt_pk_f32_fp8_e32 v[170:171], v143
	v_cvt_pk_f32_fp8_sdwa v[142:143], v143 src0_sel:WORD_1
	v_pk_add_f32 v[162:163], v[162:163], 0 op_sel_hi:[1,0]
	v_pk_add_f32 v[126:127], v[126:127], 0 op_sel_hi:[1,0]
	v_cvt_pk_f32_fp8_e32 v[188:189], v150
	v_pk_add_f32 v[178:179], v[178:179], v[180:181]
	v_cvt_pk_f32_fp8_e32 v[172:173], v151
	v_cvt_pk_f32_fp8_sdwa v[150:151], v151 src0_sel:WORD_1
	v_pk_add_f32 v[162:163], v[162:163], v[164:165]
	v_pk_add_f32 v[126:127], v[126:127], v[130:131]
	v_cvt_pk_f32_fp8_e32 v[190:191], v154
	v_pk_add_f32 v[178:179], v[178:179], v[182:183]
	v_cvt_pk_f32_fp8_e32 v[174:175], v155
	v_cvt_pk_f32_fp8_sdwa v[154:155], v155 src0_sel:WORD_1
	v_pk_add_f32 v[162:163], v[162:163], v[166:167]
	v_pk_add_f32 v[126:127], v[126:127], v[134:135]
	v_cvt_pk_f32_fp8_e32 v[192:193], v158
	v_pk_add_f32 v[178:179], v[178:179], v[184:185]
	v_cvt_pk_f32_fp8_e32 v[176:177], v159
	v_cvt_pk_f32_fp8_sdwa v[158:159], v159 src0_sel:WORD_1
	v_pk_add_f32 v[162:163], v[162:163], v[168:169]
	v_pk_add_f32 v[126:127], v[126:127], v[138:139]
	v_pk_add_f32 v[178:179], v[178:179], v[186:187]
	v_pk_add_f32 v[162:163], v[162:163], v[170:171]
	v_pk_add_f32 v[126:127], v[126:127], v[142:143]
	v_pk_add_f32 v[178:179], v[178:179], v[188:189]
	v_pk_add_f32 v[162:163], v[162:163], v[172:173]
	v_pk_add_f32 v[126:127], v[126:127], v[150:151]
	v_pk_add_f32 v[178:179], v[178:179], v[190:191]
	v_lshlrev_b32_e32 v180, 16, v146
	v_and_b32_e32 v181, 0xffff0000, v146
	v_pk_add_f32 v[162:163], v[162:163], v[174:175]
	v_lshlrev_b32_e32 v164, 16, v148
	v_and_b32_e32 v165, 0xffff0000, v148
	v_pk_add_f32 v[126:127], v[126:127], v[154:155]
	v_lshlrev_b32_e32 v130, 16, v149
	v_and_b32_e32 v131, 0xffff0000, v149
	v_pk_add_f32 v[178:179], v[178:179], v[192:193]
	v_pk_mul_f32 v[180:181], v[180:181], s[78:79] op_sel_hi:[1,0]
	v_pk_add_f32 v[162:163], v[162:163], v[176:177]
	v_pk_mul_f32 v[164:165], v[164:165], s[78:79] op_sel_hi:[1,0]
	v_pk_add_f32 v[126:127], v[126:127], v[158:159]
	v_pk_mul_f32 v[130:131], v[130:131], s[78:79] op_sel_hi:[1,0]
	v_pk_fma_f32 v[178:179], v[178:179], s[80:81], v[180:181] op_sel_hi:[1,0,1]
	v_pk_fma_f32 v[162:163], v[162:163], s[80:81], v[164:165] op_sel_hi:[1,0,1]
	v_pk_fma_f32 v[126:127], v[126:127], s[80:81], v[130:131] op_sel_hi:[1,0,1]
	v_cvt_pk_f32_fp8_e32 v[130:131], v128
	v_cvt_pk_bf16_f32 v146, v178, v179
	v_cvt_pk_bf16_f32 v148, v162, v163
	v_cvt_pk_bf16_f32 v149, v126, v127
	v_lshl_add_u64 v[126:127], v[86:87], 0, s[98:99]
	v_cvt_pk_f32_fp8_e32 v[138:139], v132
	global_store_dwordx4 v[126:127], v[146:149], off
	v_cvt_pk_f32_fp8_e32 v[150:151], v140
	v_cvt_pk_f32_fp8_e32 v[158:159], v144
	v_cvt_pk_f32_fp8_e32 v[146:147], v136
	v_pk_add_f32 v[130:131], v[130:131], 0 op_sel_hi:[1,0]
	v_cvt_pk_f32_fp8_e32 v[164:165], v152
	v_pk_add_f32 v[130:131], v[130:131], v[138:139]
	v_cvt_pk_f32_fp8_e32 v[168:169], v156
	v_pk_add_f32 v[130:131], v[130:131], v[146:147]
	v_cvt_pk_f32_fp8_e32 v[172:173], v160
	v_pk_add_f32 v[130:131], v[130:131], v[150:151]
	v_cvt_pk_f32_fp8_sdwa v[134:135], v128 src0_sel:WORD_1
	v_pk_add_f32 v[130:131], v[130:131], v[158:159]
	v_cvt_pk_f32_fp8_sdwa v[142:143], v132 src0_sel:WORD_1
	v_pk_add_f32 v[130:131], v[130:131], v[164:165]
	v_lshlrev_b32_e32 v138, 16, v122
	v_pk_add_f32 v[130:131], v[130:131], v[168:169]
	v_and_b32_e32 v139, 0xffff0000, v122
	v_cvt_pk_f32_fp8_sdwa v[148:149], v136 src0_sel:WORD_1
	v_pk_add_f32 v[130:131], v[130:131], v[172:173]
	v_pk_mul_f32 v[138:139], v[138:139], s[78:79] op_sel_hi:[1,0]
	v_cvt_pk_f32_fp8_sdwa v[154:155], v140 src0_sel:WORD_1
	v_pk_fma_f32 v[130:131], v[130:131], s[80:81], v[138:139] op_sel_hi:[1,0,1]
	v_cvt_pk_f32_fp8_sdwa v[162:163], v144 src0_sel:WORD_1
	v_cvt_pk_bf16_f32 v122, v130, v131
	v_pk_add_f32 v[130:131], v[134:135], 0 op_sel_hi:[1,0]
	v_cvt_pk_f32_fp8_sdwa v[166:167], v152 src0_sel:WORD_1
	v_pk_add_f32 v[130:131], v[130:131], v[142:143]
	v_cvt_pk_f32_fp8_sdwa v[170:171], v156 src0_sel:WORD_1
	v_pk_add_f32 v[130:131], v[130:131], v[148:149]
	v_cvt_pk_f32_fp8_sdwa v[174:175], v160 src0_sel:WORD_1
	v_pk_add_f32 v[130:131], v[130:131], v[154:155]
	v_lshlrev_b32_e32 v134, 16, v123
	v_pk_add_f32 v[130:131], v[130:131], v[162:163]
	v_and_b32_e32 v135, 0xffff0000, v123
	v_pk_add_f32 v[130:131], v[130:131], v[166:167]
	v_pk_mul_f32 v[134:135], v[134:135], s[78:79] op_sel_hi:[1,0]
	v_pk_add_f32 v[130:131], v[130:131], v[170:171]
	v_cvt_pk_f32_fp8_e32 v[146:147], v129
	v_pk_add_f32 v[130:131], v[130:131], v[174:175]
	v_cvt_pk_f32_fp8_sdwa v[128:129], v129 src0_sel:WORD_1
	v_pk_fma_f32 v[130:131], v[130:131], s[80:81], v[134:135] op_sel_hi:[1,0,1]
	v_cvt_pk_f32_fp8_e32 v[148:149], v133
	v_cvt_pk_bf16_f32 v123, v130, v131
	v_cvt_pk_f32_fp8_sdwa v[130:131], v133 src0_sel:WORD_1
	v_cvt_pk_f32_fp8_e32 v[150:151], v137
	v_cvt_pk_f32_fp8_sdwa v[132:133], v137 src0_sel:WORD_1
	v_cvt_pk_f32_fp8_e32 v[154:155], v141
	v_cvt_pk_f32_fp8_sdwa v[134:135], v141 src0_sel:WORD_1
	v_cvt_pk_f32_fp8_e32 v[158:159], v145
	v_cvt_pk_f32_fp8_sdwa v[136:137], v145 src0_sel:WORD_1
	v_pk_add_f32 v[146:147], v[146:147], 0 op_sel_hi:[1,0]
	v_pk_add_f32 v[128:129], v[128:129], 0 op_sel_hi:[1,0]
	v_cvt_pk_f32_fp8_e32 v[144:145], v153
	v_cvt_pk_f32_fp8_sdwa v[138:139], v153 src0_sel:WORD_1
	v_pk_add_f32 v[146:147], v[146:147], v[148:149]
	v_pk_add_f32 v[128:129], v[128:129], v[130:131]
	v_cvt_pk_f32_fp8_e32 v[152:153], v157
	v_cvt_pk_f32_fp8_sdwa v[140:141], v157 src0_sel:WORD_1
	v_pk_add_f32 v[146:147], v[146:147], v[150:151]
	v_pk_add_f32 v[128:129], v[128:129], v[132:133]
	v_cvt_pk_f32_fp8_e32 v[156:157], v161
	v_cvt_pk_f32_fp8_sdwa v[142:143], v161 src0_sel:WORD_1
	v_pk_add_f32 v[146:147], v[146:147], v[154:155]
	v_pk_add_f32 v[128:129], v[128:129], v[134:135]
	v_pk_add_f32 v[146:147], v[146:147], v[158:159]
	v_pk_add_f32 v[128:129], v[128:129], v[136:137]
	v_pk_add_f32 v[144:145], v[146:147], v[144:145]
	v_pk_add_f32 v[128:129], v[128:129], v[138:139]
	v_pk_add_f32 v[144:145], v[144:145], v[152:153]
	v_lshlrev_b32_e32 v146, 16, v124
	v_and_b32_e32 v147, 0xffff0000, v124
	v_pk_add_f32 v[128:129], v[128:129], v[140:141]
	v_lshlrev_b32_e32 v130, 16, v125
	v_and_b32_e32 v131, 0xffff0000, v125
	v_pk_add_f32 v[144:145], v[144:145], v[156:157]
	v_pk_mul_f32 v[146:147], v[146:147], s[78:79] op_sel_hi:[1,0]
	v_pk_add_f32 v[128:129], v[128:129], v[142:143]
	v_pk_mul_f32 v[130:131], v[130:131], s[78:79] op_sel_hi:[1,0]
	v_pk_fma_f32 v[144:145], v[144:145], s[80:81], v[146:147] op_sel_hi:[1,0,1]
	v_pk_fma_f32 v[128:129], v[128:129], s[80:81], v[130:131] op_sel_hi:[1,0,1]
	v_cvt_pk_bf16_f32 v124, v144, v145
	v_cvt_pk_bf16_f32 v125, v128, v129
	global_store_dwordx4 v[126:127], v[122:125], off offset:16
	s_add_i32 s98, s18, s19
	s_add_i32 s100, s98, 2
	s_add_i32 s16, s5, s20
	s_ashr_i32 s101, s100, 31
	s_add_i32 s42, s16, -15
	s_lshl_b64 s[100:101], s[100:101], 11
	s_ashr_i32 s43, s42, 31
	v_lshl_add_u64 v[122:123], v[82:83], 0, s[100:101]
	s_lshl_b64 s[42:43], s[42:43], 10
	global_load_dwordx4 v[162:165], v[122:123], off offset:16
	global_load_dwordx4 v[182:185], v[122:123], off
	v_lshl_add_u64 v[122:123], v[84:85], 0, s[42:43]
	s_add_i32 s42, s16, -14
	s_ashr_i32 s43, s42, 31
	s_lshl_b64 s[42:43], s[42:43], 10
	global_load_dwordx4 v[166:169], v[122:123], off
	v_lshl_add_u64 v[122:123], v[84:85], 0, s[42:43]
	s_add_i32 s42, s16, -13
	s_ashr_i32 s43, s42, 31
	s_lshl_b64 s[42:43], s[42:43], 10
	global_load_dwordx4 v[170:173], v[122:123], off
	v_lshl_add_u64 v[122:123], v[84:85], 0, s[42:43]
	s_add_i32 s42, s16, -12
	s_ashr_i32 s43, s42, 31
	s_lshl_b64 s[42:43], s[42:43], 10
	global_load_dwordx4 v[174:177], v[122:123], off
	v_lshl_add_u64 v[122:123], v[84:85], 0, s[42:43]
	s_add_i32 s42, s16, -11
	s_ashr_i32 s43, s42, 31
	s_lshl_b64 s[42:43], s[42:43], 10
	global_load_dwordx4 v[178:181], v[122:123], off
	v_lshl_add_u64 v[122:123], v[84:85], 0, s[42:43]
	s_add_i32 s42, s16, -10
	s_ashr_i32 s43, s42, 31
	s_lshl_b64 s[42:43], s[42:43], 10
	global_load_dwordx4 v[186:189], v[122:123], off
	v_lshl_add_u64 v[122:123], v[84:85], 0, s[42:43]
	s_add_i32 s42, s16, -9
	s_ashr_i32 s43, s42, 31
	s_lshl_b64 s[42:43], s[42:43], 10
	global_load_dwordx4 v[190:193], v[122:123], off
	v_lshl_add_u64 v[122:123], v[84:85], 0, s[42:43]
	s_add_i32 s42, s16, -8
	s_ashr_i32 s43, s42, 31
	s_lshl_b64 s[42:43], s[42:43], 10
	global_load_dwordx4 v[194:197], v[122:123], off
	v_lshl_add_u64 v[122:123], v[84:85], 0, s[42:43]
	global_load_dwordx4 v[198:201], v[122:123], off
	s_add_i32 s98, s98, 3
	s_ashr_i32 s99, s98, 31
	s_add_i32 s42, s16, -7
	s_lshl_b64 s[98:99], s[98:99], 11
	s_ashr_i32 s43, s42, 31
	v_lshl_add_u64 v[126:127], v[82:83], 0, s[98:99]
	s_lshl_b64 s[42:43], s[42:43], 10
	global_load_dwordx4 v[122:125], v[126:127], off offset:16
	global_load_dwordx4 v[146:149], v[126:127], off
	v_lshl_add_u64 v[126:127], v[84:85], 0, s[42:43]
	s_add_i32 s42, s16, -6
	s_ashr_i32 s43, s42, 31
	s_lshl_b64 s[42:43], s[42:43], 10
	v_lshl_add_u64 v[130:131], v[84:85], 0, s[42:43]
	s_add_i32 s42, s16, -5
	s_ashr_i32 s43, s42, 31
	s_lshl_b64 s[42:43], s[42:43], 10
	v_lshl_add_u64 v[134:135], v[84:85], 0, s[42:43]
	s_add_i32 s42, s16, -4
	s_ashr_i32 s43, s42, 31
	s_lshl_b64 s[42:43], s[42:43], 10
	v_lshl_add_u64 v[138:139], v[84:85], 0, s[42:43]
	s_add_i32 s42, s16, -3
	s_ashr_i32 s43, s42, 31
	s_lshl_b64 s[42:43], s[42:43], 10
	v_lshl_add_u64 v[142:143], v[84:85], 0, s[42:43]
	s_add_i32 s42, s16, -2
	global_load_dwordx4 v[126:129], v[126:127], off
	s_ashr_i32 s43, s42, 31
	global_load_dwordx4 v[130:133], v[130:131], off
	s_lshl_b64 s[42:43], s[42:43], 10
	global_load_dwordx4 v[134:137], v[134:135], off
	v_lshl_add_u64 v[150:151], v[84:85], 0, s[42:43]
	s_add_i32 s42, s16, -1
	global_load_dwordx4 v[138:141], v[138:139], off
	s_ashr_i32 s43, s42, 31
	global_load_dwordx4 v[142:145], v[142:143], off
	s_lshl_b64 s[42:43], s[42:43], 10
	s_ashr_i32 s17, s16, 31
	global_load_dwordx4 v[150:153], v[150:151], off
	v_lshl_add_u64 v[154:155], v[84:85], 0, s[42:43]
	s_lshl_b64 s[16:17], s[16:17], 10
	global_load_dwordx4 v[154:157], v[154:155], off
	v_lshl_add_u64 v[158:159], v[84:85], 0, s[16:17]
	global_load_dwordx4 v[158:161], v[158:159], off
	s_add_i32 s19, s19, 2
	s_add_i32 s20, s20, 16
	s_waitcnt vmcnt(41)
	v_cvt_pk_f32_fp8_e32 v[88:89], v46
	v_cvt_pk_f32_fp8_sdwa v[90:91], v46 src0_sel:WORD_1
	v_pk_add_f32 v[88:89], v[88:89], 0 op_sel_hi:[1,0]
	s_waitcnt vmcnt(40)
	v_cvt_pk_f32_fp8_e32 v[92:93], v50
	v_cvt_pk_f32_fp8_sdwa v[94:95], v50 src0_sel:WORD_1
	v_pk_add_f32 v[88:89], v[88:89], v[92:93]
	s_waitcnt vmcnt(39)
	v_cvt_pk_f32_fp8_e32 v[96:97], v54
	v_lshlrev_b32_e32 v92, 16, v62
	v_and_b32_e32 v93, 0xffff0000, v62
	v_cvt_pk_f32_fp8_sdwa v[98:99], v54 src0_sel:WORD_1
	v_pk_add_f32 v[88:89], v[88:89], v[96:97]
	s_waitcnt vmcnt(38)
	v_cvt_pk_f32_fp8_e32 v[100:101], v58
	v_pk_mul_f32 v[92:93], v[92:93], s[78:79] op_sel_hi:[1,0]
	v_cvt_pk_f32_fp8_sdwa v[102:103], v58 src0_sel:WORD_1
	v_pk_add_f32 v[88:89], v[88:89], v[100:101]
	s_waitcnt vmcnt(37)
	v_cvt_pk_f32_fp8_e32 v[104:105], v66
	v_cvt_pk_f32_fp8_sdwa v[106:107], v66 src0_sel:WORD_1
	v_cvt_pk_f32_fp8_e32 v[96:97], v67
	v_cvt_pk_f32_fp8_sdwa v[66:67], v67 src0_sel:WORD_1
	v_pk_add_f32 v[88:89], v[88:89], v[104:105]
	s_waitcnt vmcnt(36)
	v_cvt_pk_f32_fp8_e32 v[108:109], v70
	v_cvt_pk_f32_fp8_sdwa v[110:111], v70 src0_sel:WORD_1
	v_pk_add_f32 v[88:89], v[88:89], v[108:109]
	s_waitcnt vmcnt(35)
	v_cvt_pk_f32_fp8_e32 v[112:113], v74
	v_cvt_pk_f32_fp8_sdwa v[114:115], v74 src0_sel:WORD_1
	s_waitcnt vmcnt(34)
	v_cvt_pk_f32_fp8_e32 v[116:117], v78
	v_cvt_pk_f32_fp8_sdwa v[118:119], v78 src0_sel:WORD_1
	v_pk_add_f32 v[88:89], v[88:89], v[112:113]
	v_cvt_pk_f32_fp8_e32 v[100:101], v75
	v_pk_add_f32 v[88:89], v[88:89], v[116:117]
	v_cvt_pk_f32_fp8_sdwa v[74:75], v75 src0_sel:WORD_1
	v_pk_fma_f32 v[88:89], v[88:89], s[80:81], v[92:93] op_sel_hi:[1,0,1]
	v_cvt_pk_f32_fp8_e32 v[92:93], v55
	v_cvt_pk_bf16_f32 v62, v88, v89
	v_pk_add_f32 v[88:89], v[90:91], 0 op_sel_hi:[1,0]
	v_lshlrev_b32_e32 v90, 16, v63
	v_pk_add_f32 v[88:89], v[88:89], v[94:95]
	v_and_b32_e32 v91, 0xffff0000, v63
	v_pk_add_f32 v[88:89], v[88:89], v[98:99]
	v_pk_mul_f32 v[90:91], v[90:91], s[78:79] op_sel_hi:[1,0]
	v_pk_add_f32 v[88:89], v[88:89], v[102:103]
	v_cvt_pk_f32_fp8_sdwa v[54:55], v55 src0_sel:WORD_1
	v_pk_add_f32 v[88:89], v[88:89], v[106:107]
	v_cvt_pk_f32_fp8_e32 v[94:95], v59
	v_pk_add_f32 v[88:89], v[88:89], v[110:111]
	v_cvt_pk_f32_fp8_sdwa v[58:59], v59 src0_sel:WORD_1
	v_pk_add_f32 v[88:89], v[88:89], v[114:115]
	v_cvt_pk_f32_fp8_e32 v[98:99], v71
	v_pk_add_f32 v[88:89], v[88:89], v[118:119]
	v_cvt_pk_f32_fp8_sdwa v[70:71], v71 src0_sel:WORD_1
	v_pk_fma_f32 v[88:89], v[88:89], s[80:81], v[90:91] op_sel_hi:[1,0,1]
	v_cvt_pk_f32_fp8_e32 v[90:91], v51
	v_cvt_pk_bf16_f32 v63, v88, v89
	v_cvt_pk_f32_fp8_e32 v[88:89], v47
	v_cvt_pk_f32_fp8_sdwa v[46:47], v47 src0_sel:WORD_1
	v_cvt_pk_f32_fp8_sdwa v[50:51], v51 src0_sel:WORD_1
	v_cvt_pk_f32_fp8_e32 v[102:103], v79
	v_pk_add_f32 v[88:89], v[88:89], 0 op_sel_hi:[1,0]
	v_pk_add_f32 v[46:47], v[46:47], 0 op_sel_hi:[1,0]
	v_pk_add_f32 v[88:89], v[88:89], v[90:91]
	v_pk_add_f32 v[46:47], v[46:47], v[50:51]
	v_pk_add_f32 v[88:89], v[88:89], v[92:93]
	v_pk_add_f32 v[46:47], v[46:47], v[54:55]
	v_cvt_pk_f32_fp8_sdwa v[78:79], v79 src0_sel:WORD_1
	v_pk_add_f32 v[88:89], v[88:89], v[94:95]
	v_pk_add_f32 v[46:47], v[46:47], v[58:59]
	v_pk_add_f32 v[88:89], v[88:89], v[96:97]
	v_pk_add_f32 v[46:47], v[46:47], v[66:67]
	v_pk_add_f32 v[88:89], v[88:89], v[98:99]
	v_pk_add_f32 v[46:47], v[46:47], v[70:71]
	v_pk_add_f32 v[88:89], v[88:89], v[100:101]
	v_lshlrev_b32_e32 v90, 16, v64
	v_and_b32_e32 v91, 0xffff0000, v64
	v_pk_add_f32 v[46:47], v[46:47], v[74:75]
	v_lshlrev_b32_e32 v50, 16, v65
	v_and_b32_e32 v51, 0xffff0000, v65
	v_pk_add_f32 v[88:89], v[88:89], v[102:103]
	v_pk_mul_f32 v[90:91], v[90:91], s[78:79] op_sel_hi:[1,0]
	v_pk_add_f32 v[46:47], v[46:47], v[78:79]
	v_pk_mul_f32 v[50:51], v[50:51], s[78:79] op_sel_hi:[1,0]
	v_pk_fma_f32 v[88:89], v[88:89], s[80:81], v[90:91] op_sel_hi:[1,0,1]
	v_pk_fma_f32 v[46:47], v[46:47], s[80:81], v[50:51] op_sel_hi:[1,0,1]
	v_cvt_pk_f32_fp8_e32 v[50:51], v48
	v_cvt_pk_bf16_f32 v64, v88, v89
	v_cvt_pk_bf16_f32 v65, v46, v47
	v_lshl_add_u64 v[46:47], v[86:87], 0, s[12:13]
	v_cvt_pk_f32_fp8_e32 v[58:59], v52
	global_store_dwordx4 v[46:47], v[62:65], off
	v_cvt_pk_f32_fp8_e32 v[70:71], v60
	v_cvt_pk_f32_fp8_e32 v[78:79], v68
	v_cvt_pk_f32_fp8_e32 v[64:65], v56
	v_pk_add_f32 v[50:51], v[50:51], 0 op_sel_hi:[1,0]
	v_cvt_pk_f32_fp8_e32 v[90:91], v72
	v_pk_add_f32 v[50:51], v[50:51], v[58:59]
	v_cvt_pk_f32_fp8_e32 v[94:95], v76
	v_pk_add_f32 v[50:51], v[50:51], v[64:65]
	v_cvt_pk_f32_fp8_e32 v[98:99], v80
	v_pk_add_f32 v[50:51], v[50:51], v[70:71]
	v_cvt_pk_f32_fp8_sdwa v[54:55], v48 src0_sel:WORD_1
	v_pk_add_f32 v[50:51], v[50:51], v[78:79]
	v_cvt_pk_f32_fp8_sdwa v[62:63], v52 src0_sel:WORD_1
	v_pk_add_f32 v[50:51], v[50:51], v[90:91]
	v_lshlrev_b32_e32 v58, 16, v42
	v_pk_add_f32 v[50:51], v[50:51], v[94:95]
	v_and_b32_e32 v59, 0xffff0000, v42
	v_cvt_pk_f32_fp8_sdwa v[66:67], v56 src0_sel:WORD_1
	v_pk_add_f32 v[50:51], v[50:51], v[98:99]
	v_pk_mul_f32 v[58:59], v[58:59], s[78:79] op_sel_hi:[1,0]
	v_cvt_pk_f32_fp8_sdwa v[74:75], v60 src0_sel:WORD_1
	v_pk_fma_f32 v[50:51], v[50:51], s[80:81], v[58:59] op_sel_hi:[1,0,1]
	v_cvt_pk_f32_fp8_sdwa v[88:89], v68 src0_sel:WORD_1
	v_cvt_pk_bf16_f32 v42, v50, v51
	v_pk_add_f32 v[50:51], v[54:55], 0 op_sel_hi:[1,0]
	v_cvt_pk_f32_fp8_sdwa v[92:93], v72 src0_sel:WORD_1
	v_pk_add_f32 v[50:51], v[50:51], v[62:63]
	v_cvt_pk_f32_fp8_sdwa v[96:97], v76 src0_sel:WORD_1
	v_pk_add_f32 v[50:51], v[50:51], v[66:67]
	v_cvt_pk_f32_fp8_sdwa v[100:101], v80 src0_sel:WORD_1
	v_pk_add_f32 v[50:51], v[50:51], v[74:75]
	v_lshlrev_b32_e32 v54, 16, v43
	v_pk_add_f32 v[50:51], v[50:51], v[88:89]
	v_and_b32_e32 v55, 0xffff0000, v43
	v_pk_add_f32 v[50:51], v[50:51], v[92:93]
	v_pk_mul_f32 v[54:55], v[54:55], s[78:79] op_sel_hi:[1,0]
	v_pk_add_f32 v[50:51], v[50:51], v[96:97]
	v_cvt_pk_f32_fp8_e32 v[58:59], v57
	v_pk_add_f32 v[50:51], v[50:51], v[100:101]
	v_cvt_pk_f32_fp8_e32 v[62:63], v61
	v_pk_fma_f32 v[50:51], v[50:51], s[80:81], v[54:55] op_sel_hi:[1,0,1]
	v_cvt_pk_f32_fp8_e32 v[54:55], v53
	v_cvt_pk_bf16_f32 v43, v50, v51
	v_cvt_pk_f32_fp8_e32 v[50:51], v49
	v_cvt_pk_f32_fp8_sdwa v[48:49], v49 src0_sel:WORD_1
	v_cvt_pk_f32_fp8_sdwa v[52:53], v53 src0_sel:WORD_1
	v_cvt_pk_f32_fp8_e32 v[64:65], v69
	v_pk_add_f32 v[50:51], v[50:51], 0 op_sel_hi:[1,0]
	v_cvt_pk_f32_fp8_sdwa v[56:57], v57 src0_sel:WORD_1
	v_cvt_pk_f32_fp8_sdwa v[66:67], v69 src0_sel:WORD_1
	v_cvt_pk_f32_fp8_e32 v[68:69], v73
	v_pk_add_f32 v[50:51], v[50:51], v[54:55]
	v_cvt_pk_f32_fp8_sdwa v[60:61], v61 src0_sel:WORD_1
	v_cvt_pk_f32_fp8_sdwa v[70:71], v73 src0_sel:WORD_1
	v_cvt_pk_f32_fp8_e32 v[72:73], v77
	v_pk_add_f32 v[50:51], v[50:51], v[58:59]
	v_cvt_pk_f32_fp8_sdwa v[74:75], v77 src0_sel:WORD_1
	v_cvt_pk_f32_fp8_e32 v[76:77], v81
	v_pk_add_f32 v[50:51], v[50:51], v[62:63]
	v_pk_add_f32 v[48:49], v[48:49], 0 op_sel_hi:[1,0]
	v_pk_add_f32 v[50:51], v[50:51], v[64:65]
	v_pk_add_f32 v[48:49], v[48:49], v[52:53]
	v_pk_add_f32 v[50:51], v[50:51], v[68:69]
	v_pk_add_f32 v[48:49], v[48:49], v[56:57]
	v_cvt_pk_f32_fp8_sdwa v[78:79], v81 src0_sel:WORD_1
	v_pk_add_f32 v[50:51], v[50:51], v[72:73]
	v_lshlrev_b32_e32 v54, 16, v44
	v_and_b32_e32 v55, 0xffff0000, v44
	v_pk_add_f32 v[48:49], v[48:49], v[60:61]
	v_pk_add_f32 v[50:51], v[50:51], v[76:77]
	v_pk_mul_f32 v[54:55], v[54:55], s[78:79] op_sel_hi:[1,0]
	v_pk_add_f32 v[48:49], v[48:49], v[66:67]
	v_pk_fma_f32 v[50:51], v[50:51], s[80:81], v[54:55] op_sel_hi:[1,0,1]
	v_pk_add_f32 v[48:49], v[48:49], v[70:71]
	v_cvt_pk_bf16_f32 v44, v50, v51
	v_pk_add_f32 v[48:49], v[48:49], v[74:75]
	v_lshlrev_b32_e32 v50, 16, v45
	v_and_b32_e32 v51, 0xffff0000, v45
	v_pk_add_f32 v[48:49], v[48:49], v[78:79]
	v_pk_mul_f32 v[50:51], v[50:51], s[78:79] op_sel_hi:[1,0]
	s_waitcnt vmcnt(27)
	v_cvt_pk_f32_fp8_sdwa v[52:53], v30 src0_sel:WORD_1
	v_pk_fma_f32 v[48:49], v[48:49], s[80:81], v[50:51] op_sel_hi:[1,0,1]
	v_cvt_pk_f32_fp8_sdwa v[50:51], v22 src0_sel:WORD_1
	v_cvt_pk_bf16_f32 v45, v48, v49
	global_store_dwordx4 v[46:47], v[42:45], off offset:16
	v_cvt_pk_f32_fp8_sdwa v[46:47], v14 src0_sel:WORD_1
	v_cvt_pk_f32_fp8_sdwa v[48:49], v18 src0_sel:WORD_1
	v_cvt_pk_f32_fp8_sdwa v[42:43], v6 src0_sel:WORD_1
	v_cvt_pk_f32_fp8_sdwa v[44:45], v10 src0_sel:WORD_1
	s_waitcnt vmcnt(27)
	v_cvt_pk_f32_fp8_sdwa v[54:55], v34 src0_sel:WORD_1
	s_waitcnt vmcnt(26)
	v_cvt_pk_f32_fp8_sdwa v[56:57], v38 src0_sel:WORD_1
	v_pk_add_f32 v[42:43], v[42:43], 0 op_sel_hi:[1,0]
	v_cvt_pk_f32_fp8_e32 v[58:59], v6
	v_pk_add_f32 v[42:43], v[42:43], v[44:45]
	v_lshlrev_b32_e32 v44, 16, v27
	v_pk_add_f32 v[42:43], v[42:43], v[46:47]
	v_and_b32_e32 v45, 0xffff0000, v27
	v_pk_add_f32 v[42:43], v[42:43], v[48:49]
	v_pk_mul_f32 v[44:45], v[44:45], s[78:79] op_sel_hi:[1,0]
	v_pk_add_f32 v[42:43], v[42:43], v[50:51]
	v_cvt_pk_f32_fp8_e32 v[60:61], v10
	v_pk_add_f32 v[42:43], v[42:43], v[52:53]
	v_cvt_pk_f32_fp8_e32 v[62:63], v14
	v_pk_add_f32 v[42:43], v[42:43], v[54:55]
	v_cvt_pk_f32_fp8_e32 v[46:47], v15
	v_pk_add_f32 v[42:43], v[42:43], v[56:57]
	v_cvt_pk_f32_fp8_sdwa v[14:15], v15 src0_sel:WORD_1
	v_pk_fma_f32 v[42:43], v[42:43], s[80:81], v[44:45] op_sel_hi:[1,0,1]
	v_cvt_pk_f32_fp8_e32 v[44:45], v11
	v_cvt_pk_bf16_f32 v27, v42, v43
	v_cvt_pk_f32_fp8_e32 v[42:43], v7
	v_cvt_pk_f32_fp8_sdwa v[6:7], v7 src0_sel:WORD_1
	v_cvt_pk_f32_fp8_sdwa v[10:11], v11 src0_sel:WORD_1
	v_cvt_pk_f32_fp8_e32 v[64:65], v18
	v_cvt_pk_f32_fp8_e32 v[48:49], v19
	v_cvt_pk_f32_fp8_sdwa v[18:19], v19 src0_sel:WORD_1
	v_cvt_pk_f32_fp8_e32 v[66:67], v22
	v_pk_add_f32 v[58:59], v[58:59], 0 op_sel_hi:[1,0]
	v_cvt_pk_f32_fp8_e32 v[50:51], v23
	v_cvt_pk_f32_fp8_sdwa v[22:23], v23 src0_sel:WORD_1
	v_pk_add_f32 v[42:43], v[42:43], 0 op_sel_hi:[1,0]
	v_pk_add_f32 v[6:7], v[6:7], 0 op_sel_hi:[1,0]
	v_cvt_pk_f32_fp8_e32 v[68:69], v30
	v_pk_add_f32 v[58:59], v[58:59], v[60:61]
	v_cvt_pk_f32_fp8_e32 v[52:53], v31
	v_cvt_pk_f32_fp8_sdwa v[30:31], v31 src0_sel:WORD_1
	v_pk_add_f32 v[42:43], v[42:43], v[44:45]
	v_pk_add_f32 v[6:7], v[6:7], v[10:11]
	v_cvt_pk_f32_fp8_e32 v[70:71], v34
	v_pk_add_f32 v[58:59], v[58:59], v[62:63]
	v_cvt_pk_f32_fp8_e32 v[54:55], v35
	v_cvt_pk_f32_fp8_sdwa v[34:35], v35 src0_sel:WORD_1
	v_pk_add_f32 v[42:43], v[42:43], v[46:47]
	v_pk_add_f32 v[6:7], v[6:7], v[14:15]
	v_cvt_pk_f32_fp8_e32 v[72:73], v38
	v_pk_add_f32 v[58:59], v[58:59], v[64:65]
	v_cvt_pk_f32_fp8_e32 v[56:57], v39
	v_cvt_pk_f32_fp8_sdwa v[38:39], v39 src0_sel:WORD_1
	v_pk_add_f32 v[42:43], v[42:43], v[48:49]
	v_pk_add_f32 v[6:7], v[6:7], v[18:19]
	v_pk_add_f32 v[58:59], v[58:59], v[66:67]
	v_pk_add_f32 v[42:43], v[42:43], v[50:51]
	v_pk_add_f32 v[6:7], v[6:7], v[22:23]
	v_pk_add_f32 v[58:59], v[58:59], v[68:69]
	v_pk_add_f32 v[42:43], v[42:43], v[52:53]
	v_pk_add_f32 v[6:7], v[6:7], v[30:31]
	v_pk_add_f32 v[58:59], v[58:59], v[70:71]
	v_lshlrev_b32_e32 v60, 16, v26
	v_and_b32_e32 v61, 0xffff0000, v26
	v_pk_add_f32 v[42:43], v[42:43], v[54:55]
	v_lshlrev_b32_e32 v44, 16, v28
	v_and_b32_e32 v45, 0xffff0000, v28
	v_pk_add_f32 v[6:7], v[6:7], v[34:35]
	v_lshlrev_b32_e32 v10, 16, v29
	v_and_b32_e32 v11, 0xffff0000, v29
	v_pk_add_f32 v[58:59], v[58:59], v[72:73]
	v_pk_mul_f32 v[60:61], v[60:61], s[78:79] op_sel_hi:[1,0]
	v_pk_add_f32 v[42:43], v[42:43], v[56:57]
	v_pk_mul_f32 v[44:45], v[44:45], s[78:79] op_sel_hi:[1,0]
	v_pk_add_f32 v[6:7], v[6:7], v[38:39]
	v_pk_mul_f32 v[10:11], v[10:11], s[78:79] op_sel_hi:[1,0]
	v_pk_fma_f32 v[58:59], v[58:59], s[80:81], v[60:61] op_sel_hi:[1,0,1]
	v_pk_fma_f32 v[42:43], v[42:43], s[80:81], v[44:45] op_sel_hi:[1,0,1]
	v_pk_fma_f32 v[6:7], v[6:7], s[80:81], v[10:11] op_sel_hi:[1,0,1]
	v_cvt_pk_f32_fp8_e32 v[10:11], v8
	v_cvt_pk_bf16_f32 v26, v58, v59
	v_cvt_pk_bf16_f32 v28, v42, v43
	v_cvt_pk_bf16_f32 v29, v6, v7
	v_lshl_add_u64 v[6:7], v[86:87], 0, s[10:11]
	v_cvt_pk_f32_fp8_e32 v[18:19], v12
	global_store_dwordx4 v[6:7], v[26:29], off
	v_cvt_pk_f32_fp8_e32 v[30:31], v20
	v_cvt_pk_f32_fp8_e32 v[38:39], v24
	v_cvt_pk_f32_fp8_e32 v[26:27], v16
	v_pk_add_f32 v[10:11], v[10:11], 0 op_sel_hi:[1,0]
	v_cvt_pk_f32_fp8_e32 v[44:45], v32
	v_pk_add_f32 v[10:11], v[10:11], v[18:19]
	v_cvt_pk_f32_fp8_e32 v[48:49], v36
	v_pk_add_f32 v[10:11], v[10:11], v[26:27]
	v_cvt_pk_f32_fp8_e32 v[52:53], v40
	v_pk_add_f32 v[10:11], v[10:11], v[30:31]
	v_cvt_pk_f32_fp8_sdwa v[14:15], v8 src0_sel:WORD_1
	v_pk_add_f32 v[10:11], v[10:11], v[38:39]
	v_cvt_pk_f32_fp8_sdwa v[22:23], v12 src0_sel:WORD_1
	v_pk_add_f32 v[10:11], v[10:11], v[44:45]
	v_lshlrev_b32_e32 v18, 16, v2
	v_pk_add_f32 v[10:11], v[10:11], v[48:49]
	v_and_b32_e32 v19, 0xffff0000, v2
	v_cvt_pk_f32_fp8_sdwa v[28:29], v16 src0_sel:WORD_1
	v_pk_add_f32 v[10:11], v[10:11], v[52:53]
	v_pk_mul_f32 v[18:19], v[18:19], s[78:79] op_sel_hi:[1,0]
	v_cvt_pk_f32_fp8_sdwa v[34:35], v20 src0_sel:WORD_1
	v_pk_fma_f32 v[10:11], v[10:11], s[80:81], v[18:19] op_sel_hi:[1,0,1]
	v_cvt_pk_f32_fp8_sdwa v[42:43], v24 src0_sel:WORD_1
	v_cvt_pk_bf16_f32 v2, v10, v11
	v_pk_add_f32 v[10:11], v[14:15], 0 op_sel_hi:[1,0]
	v_cvt_pk_f32_fp8_sdwa v[46:47], v32 src0_sel:WORD_1
	v_pk_add_f32 v[10:11], v[10:11], v[22:23]
	v_cvt_pk_f32_fp8_sdwa v[50:51], v36 src0_sel:WORD_1
	v_pk_add_f32 v[10:11], v[10:11], v[28:29]
	v_cvt_pk_f32_fp8_sdwa v[54:55], v40 src0_sel:WORD_1
	v_pk_add_f32 v[10:11], v[10:11], v[34:35]
	v_lshlrev_b32_e32 v14, 16, v3
	v_pk_add_f32 v[10:11], v[10:11], v[42:43]
	v_and_b32_e32 v15, 0xffff0000, v3
	v_pk_add_f32 v[10:11], v[10:11], v[46:47]
	v_pk_mul_f32 v[14:15], v[14:15], s[78:79] op_sel_hi:[1,0]
	v_pk_add_f32 v[10:11], v[10:11], v[50:51]
	v_cvt_pk_f32_fp8_e32 v[26:27], v9
	v_pk_add_f32 v[10:11], v[10:11], v[54:55]
	v_cvt_pk_f32_fp8_sdwa v[8:9], v9 src0_sel:WORD_1
	v_pk_fma_f32 v[10:11], v[10:11], s[80:81], v[14:15] op_sel_hi:[1,0,1]
	v_cvt_pk_f32_fp8_e32 v[28:29], v13
	v_cvt_pk_bf16_f32 v3, v10, v11
	v_cvt_pk_f32_fp8_sdwa v[10:11], v13 src0_sel:WORD_1
	v_cvt_pk_f32_fp8_e32 v[30:31], v17
	v_cvt_pk_f32_fp8_sdwa v[12:13], v17 src0_sel:WORD_1
	v_cvt_pk_f32_fp8_e32 v[34:35], v21
	v_cvt_pk_f32_fp8_sdwa v[14:15], v21 src0_sel:WORD_1
	v_cvt_pk_f32_fp8_e32 v[38:39], v25
	v_cvt_pk_f32_fp8_sdwa v[16:17], v25 src0_sel:WORD_1
	v_pk_add_f32 v[26:27], v[26:27], 0 op_sel_hi:[1,0]
	v_pk_add_f32 v[8:9], v[8:9], 0 op_sel_hi:[1,0]
	v_cvt_pk_f32_fp8_e32 v[24:25], v33
	v_cvt_pk_f32_fp8_sdwa v[18:19], v33 src0_sel:WORD_1
	v_pk_add_f32 v[26:27], v[26:27], v[28:29]
	v_pk_add_f32 v[8:9], v[8:9], v[10:11]
	v_cvt_pk_f32_fp8_e32 v[32:33], v37
	v_cvt_pk_f32_fp8_sdwa v[20:21], v37 src0_sel:WORD_1
	v_pk_add_f32 v[26:27], v[26:27], v[30:31]
	v_pk_add_f32 v[8:9], v[8:9], v[12:13]
	v_cvt_pk_f32_fp8_e32 v[36:37], v41
	v_cvt_pk_f32_fp8_sdwa v[22:23], v41 src0_sel:WORD_1
	v_pk_add_f32 v[26:27], v[26:27], v[34:35]
	v_pk_add_f32 v[8:9], v[8:9], v[14:15]
	v_pk_add_f32 v[26:27], v[26:27], v[38:39]
	v_pk_add_f32 v[8:9], v[8:9], v[16:17]
	v_pk_add_f32 v[24:25], v[26:27], v[24:25]
	v_pk_add_f32 v[8:9], v[8:9], v[18:19]
	v_pk_add_f32 v[24:25], v[24:25], v[32:33]
	v_lshlrev_b32_e32 v26, 16, v4
	v_and_b32_e32 v27, 0xffff0000, v4
	v_pk_add_f32 v[8:9], v[8:9], v[20:21]
	v_lshlrev_b32_e32 v10, 16, v5
	v_and_b32_e32 v11, 0xffff0000, v5
	v_pk_add_f32 v[24:25], v[24:25], v[36:37]
	v_pk_mul_f32 v[26:27], v[26:27], s[78:79] op_sel_hi:[1,0]
	v_pk_add_f32 v[8:9], v[8:9], v[22:23]
	v_pk_mul_f32 v[10:11], v[10:11], s[78:79] op_sel_hi:[1,0]
	v_pk_fma_f32 v[24:25], v[24:25], s[80:81], v[26:27] op_sel_hi:[1,0,1]
	v_pk_fma_f32 v[8:9], v[8:9], s[80:81], v[10:11] op_sel_hi:[1,0,1]
	v_cvt_pk_bf16_f32 v4, v24, v25
	v_cvt_pk_bf16_f32 v5, v8, v9
	global_store_dwordx4 v[6:7], v[2:5], off offset:16
	s_waitcnt vmcnt(21)
	v_cvt_pk_f32_fp8_e32 v[88:89], v166
	v_cvt_pk_f32_fp8_sdwa v[90:91], v166 src0_sel:WORD_1
	v_pk_add_f32 v[88:89], v[88:89], 0 op_sel_hi:[1,0]
	s_waitcnt vmcnt(20)
	v_cvt_pk_f32_fp8_e32 v[92:93], v170
	v_cvt_pk_f32_fp8_sdwa v[94:95], v170 src0_sel:WORD_1
	v_pk_add_f32 v[88:89], v[88:89], v[92:93]
	s_waitcnt vmcnt(19)
	v_cvt_pk_f32_fp8_e32 v[96:97], v174
	v_lshlrev_b32_e32 v92, 16, v182
	v_and_b32_e32 v93, 0xffff0000, v182
	v_cvt_pk_f32_fp8_sdwa v[98:99], v174 src0_sel:WORD_1
	v_pk_add_f32 v[88:89], v[88:89], v[96:97]
	s_waitcnt vmcnt(18)
	v_cvt_pk_f32_fp8_e32 v[100:101], v178
	v_pk_mul_f32 v[92:93], v[92:93], s[78:79] op_sel_hi:[1,0]
	v_cvt_pk_f32_fp8_sdwa v[102:103], v178 src0_sel:WORD_1
	v_pk_add_f32 v[88:89], v[88:89], v[100:101]
	s_waitcnt vmcnt(17)
	v_cvt_pk_f32_fp8_e32 v[104:105], v186
	v_cvt_pk_f32_fp8_sdwa v[106:107], v186 src0_sel:WORD_1
	v_cvt_pk_f32_fp8_e32 v[96:97], v187
	v_cvt_pk_f32_fp8_sdwa v[186:187], v187 src0_sel:WORD_1
	v_pk_add_f32 v[88:89], v[88:89], v[104:105]
	s_waitcnt vmcnt(16)
	v_cvt_pk_f32_fp8_e32 v[108:109], v190
	v_cvt_pk_f32_fp8_sdwa v[110:111], v190 src0_sel:WORD_1
	v_pk_add_f32 v[88:89], v[88:89], v[108:109]
	s_waitcnt vmcnt(15)
	v_cvt_pk_f32_fp8_e32 v[112:113], v194
	v_cvt_pk_f32_fp8_sdwa v[114:115], v194 src0_sel:WORD_1
	s_waitcnt vmcnt(14)
	v_cvt_pk_f32_fp8_e32 v[116:117], v198
	v_cvt_pk_f32_fp8_sdwa v[118:119], v198 src0_sel:WORD_1
	v_pk_add_f32 v[88:89], v[88:89], v[112:113]
	v_cvt_pk_f32_fp8_e32 v[100:101], v195
	v_pk_add_f32 v[88:89], v[88:89], v[116:117]
	v_cvt_pk_f32_fp8_sdwa v[194:195], v195 src0_sel:WORD_1
	v_pk_fma_f32 v[88:89], v[88:89], s[80:81], v[92:93] op_sel_hi:[1,0,1]
	v_cvt_pk_f32_fp8_e32 v[92:93], v175
	v_cvt_pk_bf16_f32 v182, v88, v89
	v_pk_add_f32 v[88:89], v[90:91], 0 op_sel_hi:[1,0]
	v_lshlrev_b32_e32 v90, 16, v183
	v_pk_add_f32 v[88:89], v[88:89], v[94:95]
	v_and_b32_e32 v91, 0xffff0000, v183
	v_pk_add_f32 v[88:89], v[88:89], v[98:99]
	v_pk_mul_f32 v[90:91], v[90:91], s[78:79] op_sel_hi:[1,0]
	v_pk_add_f32 v[88:89], v[88:89], v[102:103]
	v_cvt_pk_f32_fp8_sdwa v[174:175], v175 src0_sel:WORD_1
	v_pk_add_f32 v[88:89], v[88:89], v[106:107]
	v_cvt_pk_f32_fp8_e32 v[94:95], v179
	v_pk_add_f32 v[88:89], v[88:89], v[110:111]
	v_cvt_pk_f32_fp8_sdwa v[178:179], v179 src0_sel:WORD_1
	v_pk_add_f32 v[88:89], v[88:89], v[114:115]
	v_cvt_pk_f32_fp8_e32 v[98:99], v191
	v_pk_add_f32 v[88:89], v[88:89], v[118:119]
	v_cvt_pk_f32_fp8_sdwa v[190:191], v191 src0_sel:WORD_1
	v_pk_fma_f32 v[88:89], v[88:89], s[80:81], v[90:91] op_sel_hi:[1,0,1]
	v_cvt_pk_f32_fp8_e32 v[90:91], v171
	v_cvt_pk_bf16_f32 v183, v88, v89
	v_cvt_pk_f32_fp8_e32 v[88:89], v167
	v_cvt_pk_f32_fp8_sdwa v[166:167], v167 src0_sel:WORD_1
	v_cvt_pk_f32_fp8_sdwa v[170:171], v171 src0_sel:WORD_1
	v_cvt_pk_f32_fp8_e32 v[102:103], v199
	v_pk_add_f32 v[88:89], v[88:89], 0 op_sel_hi:[1,0]
	v_pk_add_f32 v[166:167], v[166:167], 0 op_sel_hi:[1,0]
	v_pk_add_f32 v[88:89], v[88:89], v[90:91]
	v_pk_add_f32 v[166:167], v[166:167], v[170:171]
	v_pk_add_f32 v[88:89], v[88:89], v[92:93]
	v_pk_add_f32 v[166:167], v[166:167], v[174:175]
	v_cvt_pk_f32_fp8_sdwa v[198:199], v199 src0_sel:WORD_1
	v_pk_add_f32 v[88:89], v[88:89], v[94:95]
	v_pk_add_f32 v[166:167], v[166:167], v[178:179]
	v_pk_add_f32 v[88:89], v[88:89], v[96:97]
	v_pk_add_f32 v[166:167], v[166:167], v[186:187]
	v_pk_add_f32 v[88:89], v[88:89], v[98:99]
	v_pk_add_f32 v[166:167], v[166:167], v[190:191]
	v_pk_add_f32 v[88:89], v[88:89], v[100:101]
	v_lshlrev_b32_e32 v90, 16, v184
	v_and_b32_e32 v91, 0xffff0000, v184
	v_pk_add_f32 v[166:167], v[166:167], v[194:195]
	v_lshlrev_b32_e32 v170, 16, v185
	v_and_b32_e32 v171, 0xffff0000, v185
	v_pk_add_f32 v[88:89], v[88:89], v[102:103]
	v_pk_mul_f32 v[90:91], v[90:91], s[78:79] op_sel_hi:[1,0]
	v_pk_add_f32 v[166:167], v[166:167], v[198:199]
	v_pk_mul_f32 v[170:171], v[170:171], s[78:79] op_sel_hi:[1,0]
	v_pk_fma_f32 v[88:89], v[88:89], s[80:81], v[90:91] op_sel_hi:[1,0,1]
	v_pk_fma_f32 v[166:167], v[166:167], s[80:81], v[170:171] op_sel_hi:[1,0,1]
	v_cvt_pk_f32_fp8_e32 v[170:171], v168
	v_cvt_pk_bf16_f32 v184, v88, v89
	v_cvt_pk_bf16_f32 v185, v166, v167
	v_lshl_add_u64 v[166:167], v[86:87], 0, s[100:101]
	v_cvt_pk_f32_fp8_e32 v[178:179], v172
	global_store_dwordx4 v[166:167], v[182:185], off
	v_cvt_pk_f32_fp8_e32 v[190:191], v180
	v_cvt_pk_f32_fp8_e32 v[198:199], v188
	v_cvt_pk_f32_fp8_e32 v[184:185], v176
	v_pk_add_f32 v[170:171], v[170:171], 0 op_sel_hi:[1,0]
	v_cvt_pk_f32_fp8_e32 v[90:91], v192
	v_pk_add_f32 v[170:171], v[170:171], v[178:179]
	v_cvt_pk_f32_fp8_e32 v[94:95], v196
	v_pk_add_f32 v[170:171], v[170:171], v[184:185]
	v_cvt_pk_f32_fp8_e32 v[98:99], v200
	v_pk_add_f32 v[170:171], v[170:171], v[190:191]
	v_cvt_pk_f32_fp8_sdwa v[174:175], v168 src0_sel:WORD_1
	v_pk_add_f32 v[170:171], v[170:171], v[198:199]
	v_cvt_pk_f32_fp8_sdwa v[182:183], v172 src0_sel:WORD_1
	v_pk_add_f32 v[170:171], v[170:171], v[90:91]
	v_lshlrev_b32_e32 v178, 16, v162
	v_pk_add_f32 v[170:171], v[170:171], v[94:95]
	v_and_b32_e32 v179, 0xffff0000, v162
	v_cvt_pk_f32_fp8_sdwa v[186:187], v176 src0_sel:WORD_1
	v_pk_add_f32 v[170:171], v[170:171], v[98:99]
	v_pk_mul_f32 v[178:179], v[178:179], s[78:79] op_sel_hi:[1,0]
	v_cvt_pk_f32_fp8_sdwa v[194:195], v180 src0_sel:WORD_1
	v_pk_fma_f32 v[170:171], v[170:171], s[80:81], v[178:179] op_sel_hi:[1,0,1]
	v_cvt_pk_f32_fp8_sdwa v[88:89], v188 src0_sel:WORD_1
	v_cvt_pk_bf16_f32 v162, v170, v171
	v_pk_add_f32 v[170:171], v[174:175], 0 op_sel_hi:[1,0]
	v_cvt_pk_f32_fp8_sdwa v[92:93], v192 src0_sel:WORD_1
	v_pk_add_f32 v[170:171], v[170:171], v[182:183]
	v_cvt_pk_f32_fp8_sdwa v[96:97], v196 src0_sel:WORD_1
	v_pk_add_f32 v[170:171], v[170:171], v[186:187]
	v_cvt_pk_f32_fp8_sdwa v[100:101], v200 src0_sel:WORD_1
	v_pk_add_f32 v[170:171], v[170:171], v[194:195]
	v_lshlrev_b32_e32 v174, 16, v163
	v_pk_add_f32 v[170:171], v[170:171], v[88:89]
	v_and_b32_e32 v175, 0xffff0000, v163
	v_pk_add_f32 v[170:171], v[170:171], v[92:93]
	v_pk_mul_f32 v[174:175], v[174:175], s[78:79] op_sel_hi:[1,0]
	v_pk_add_f32 v[170:171], v[170:171], v[96:97]
	v_cvt_pk_f32_fp8_e32 v[178:179], v177
	v_pk_add_f32 v[170:171], v[170:171], v[100:101]
	v_cvt_pk_f32_fp8_e32 v[182:183], v181
	v_pk_fma_f32 v[170:171], v[170:171], s[80:81], v[174:175] op_sel_hi:[1,0,1]
	v_cvt_pk_f32_fp8_e32 v[174:175], v173
	v_cvt_pk_bf16_f32 v163, v170, v171
	v_cvt_pk_f32_fp8_e32 v[170:171], v169
	v_cvt_pk_f32_fp8_sdwa v[168:169], v169 src0_sel:WORD_1
	v_cvt_pk_f32_fp8_sdwa v[172:173], v173 src0_sel:WORD_1
	v_cvt_pk_f32_fp8_e32 v[184:185], v189
	v_pk_add_f32 v[170:171], v[170:171], 0 op_sel_hi:[1,0]
	v_cvt_pk_f32_fp8_sdwa v[176:177], v177 src0_sel:WORD_1
	v_cvt_pk_f32_fp8_sdwa v[186:187], v189 src0_sel:WORD_1
	v_cvt_pk_f32_fp8_e32 v[188:189], v193
	v_pk_add_f32 v[170:171], v[170:171], v[174:175]
	v_cvt_pk_f32_fp8_sdwa v[180:181], v181 src0_sel:WORD_1
	v_cvt_pk_f32_fp8_sdwa v[190:191], v193 src0_sel:WORD_1
	v_cvt_pk_f32_fp8_e32 v[192:193], v197
	v_pk_add_f32 v[170:171], v[170:171], v[178:179]
	v_cvt_pk_f32_fp8_sdwa v[194:195], v197 src0_sel:WORD_1
	v_cvt_pk_f32_fp8_e32 v[196:197], v201
	v_pk_add_f32 v[170:171], v[170:171], v[182:183]
	v_pk_add_f32 v[168:169], v[168:169], 0 op_sel_hi:[1,0]
	v_pk_add_f32 v[170:171], v[170:171], v[184:185]
	v_pk_add_f32 v[168:169], v[168:169], v[172:173]
	v_pk_add_f32 v[170:171], v[170:171], v[188:189]
	v_pk_add_f32 v[168:169], v[168:169], v[176:177]
	v_cvt_pk_f32_fp8_sdwa v[198:199], v201 src0_sel:WORD_1
	v_pk_add_f32 v[170:171], v[170:171], v[192:193]
	v_lshlrev_b32_e32 v174, 16, v164
	v_and_b32_e32 v175, 0xffff0000, v164
	v_pk_add_f32 v[168:169], v[168:169], v[180:181]
	v_pk_add_f32 v[170:171], v[170:171], v[196:197]
	v_pk_mul_f32 v[174:175], v[174:175], s[78:79] op_sel_hi:[1,0]
	v_pk_add_f32 v[168:169], v[168:169], v[186:187]
	v_pk_fma_f32 v[170:171], v[170:171], s[80:81], v[174:175] op_sel_hi:[1,0,1]
	v_pk_add_f32 v[168:169], v[168:169], v[190:191]
	v_cvt_pk_bf16_f32 v164, v170, v171
	v_pk_add_f32 v[168:169], v[168:169], v[194:195]
	v_lshlrev_b32_e32 v170, 16, v165
	v_and_b32_e32 v171, 0xffff0000, v165
	v_pk_add_f32 v[168:169], v[168:169], v[198:199]
	v_pk_mul_f32 v[170:171], v[170:171], s[78:79] op_sel_hi:[1,0]
	s_waitcnt vmcnt(7)
	v_cvt_pk_f32_fp8_sdwa v[172:173], v150 src0_sel:WORD_1
	v_pk_fma_f32 v[168:169], v[168:169], s[80:81], v[170:171] op_sel_hi:[1,0,1]
	v_cvt_pk_f32_fp8_sdwa v[170:171], v142 src0_sel:WORD_1
	v_cvt_pk_bf16_f32 v165, v168, v169
	global_store_dwordx4 v[166:167], v[162:165], off offset:16
	v_cvt_pk_f32_fp8_sdwa v[166:167], v134 src0_sel:WORD_1
	v_cvt_pk_f32_fp8_sdwa v[168:169], v138 src0_sel:WORD_1
	v_cvt_pk_f32_fp8_sdwa v[162:163], v126 src0_sel:WORD_1
	v_cvt_pk_f32_fp8_sdwa v[164:165], v130 src0_sel:WORD_1
	s_waitcnt vmcnt(7)
	v_cvt_pk_f32_fp8_sdwa v[174:175], v154 src0_sel:WORD_1
	s_waitcnt vmcnt(6)
	v_cvt_pk_f32_fp8_sdwa v[176:177], v158 src0_sel:WORD_1
	v_pk_add_f32 v[162:163], v[162:163], 0 op_sel_hi:[1,0]
	v_cvt_pk_f32_fp8_e32 v[178:179], v126
	v_pk_add_f32 v[162:163], v[162:163], v[164:165]
	v_lshlrev_b32_e32 v164, 16, v147
	v_pk_add_f32 v[162:163], v[162:163], v[166:167]
	v_and_b32_e32 v165, 0xffff0000, v147
	v_pk_add_f32 v[162:163], v[162:163], v[168:169]
	v_pk_mul_f32 v[164:165], v[164:165], s[78:79] op_sel_hi:[1,0]
	v_pk_add_f32 v[162:163], v[162:163], v[170:171]
	v_cvt_pk_f32_fp8_e32 v[180:181], v130
	v_pk_add_f32 v[162:163], v[162:163], v[172:173]
	v_cvt_pk_f32_fp8_e32 v[182:183], v134
	v_pk_add_f32 v[162:163], v[162:163], v[174:175]
	v_cvt_pk_f32_fp8_e32 v[166:167], v135
	v_pk_add_f32 v[162:163], v[162:163], v[176:177]
	v_cvt_pk_f32_fp8_sdwa v[134:135], v135 src0_sel:WORD_1
	v_pk_fma_f32 v[162:163], v[162:163], s[80:81], v[164:165] op_sel_hi:[1,0,1]
	v_cvt_pk_f32_fp8_e32 v[164:165], v131
	v_cvt_pk_bf16_f32 v147, v162, v163
	v_cvt_pk_f32_fp8_e32 v[162:163], v127
	v_cvt_pk_f32_fp8_sdwa v[126:127], v127 src0_sel:WORD_1
	v_cvt_pk_f32_fp8_sdwa v[130:131], v131 src0_sel:WORD_1
	v_cvt_pk_f32_fp8_e32 v[184:185], v138
	v_cvt_pk_f32_fp8_e32 v[168:169], v139
	v_cvt_pk_f32_fp8_sdwa v[138:139], v139 src0_sel:WORD_1
	v_cvt_pk_f32_fp8_e32 v[186:187], v142
	v_pk_add_f32 v[178:179], v[178:179], 0 op_sel_hi:[1,0]
	v_cvt_pk_f32_fp8_e32 v[170:171], v143
	v_cvt_pk_f32_fp8_sdwa v[142:143], v143 src0_sel:WORD_1
	v_pk_add_f32 v[162:163], v[162:163], 0 op_sel_hi:[1,0]
	v_pk_add_f32 v[126:127], v[126:127], 0 op_sel_hi:[1,0]
	v_cvt_pk_f32_fp8_e32 v[188:189], v150
	v_pk_add_f32 v[178:179], v[178:179], v[180:181]
	v_cvt_pk_f32_fp8_e32 v[172:173], v151
	v_cvt_pk_f32_fp8_sdwa v[150:151], v151 src0_sel:WORD_1
	v_pk_add_f32 v[162:163], v[162:163], v[164:165]
	v_pk_add_f32 v[126:127], v[126:127], v[130:131]
	v_cvt_pk_f32_fp8_e32 v[190:191], v154
	v_pk_add_f32 v[178:179], v[178:179], v[182:183]
	v_cvt_pk_f32_fp8_e32 v[174:175], v155
	v_cvt_pk_f32_fp8_sdwa v[154:155], v155 src0_sel:WORD_1
	v_pk_add_f32 v[162:163], v[162:163], v[166:167]
	v_pk_add_f32 v[126:127], v[126:127], v[134:135]
	v_cvt_pk_f32_fp8_e32 v[192:193], v158
	v_pk_add_f32 v[178:179], v[178:179], v[184:185]
	v_cvt_pk_f32_fp8_e32 v[176:177], v159
	v_cvt_pk_f32_fp8_sdwa v[158:159], v159 src0_sel:WORD_1
	v_pk_add_f32 v[162:163], v[162:163], v[168:169]
	v_pk_add_f32 v[126:127], v[126:127], v[138:139]
	v_pk_add_f32 v[178:179], v[178:179], v[186:187]
	v_pk_add_f32 v[162:163], v[162:163], v[170:171]
	v_pk_add_f32 v[126:127], v[126:127], v[142:143]
	v_pk_add_f32 v[178:179], v[178:179], v[188:189]
	v_pk_add_f32 v[162:163], v[162:163], v[172:173]
	v_pk_add_f32 v[126:127], v[126:127], v[150:151]
	v_pk_add_f32 v[178:179], v[178:179], v[190:191]
	v_lshlrev_b32_e32 v180, 16, v146
	v_and_b32_e32 v181, 0xffff0000, v146
	v_pk_add_f32 v[162:163], v[162:163], v[174:175]
	v_lshlrev_b32_e32 v164, 16, v148
	v_and_b32_e32 v165, 0xffff0000, v148
	v_pk_add_f32 v[126:127], v[126:127], v[154:155]
	v_lshlrev_b32_e32 v130, 16, v149
	v_and_b32_e32 v131, 0xffff0000, v149
	v_pk_add_f32 v[178:179], v[178:179], v[192:193]
	v_pk_mul_f32 v[180:181], v[180:181], s[78:79] op_sel_hi:[1,0]
	v_pk_add_f32 v[162:163], v[162:163], v[176:177]
	v_pk_mul_f32 v[164:165], v[164:165], s[78:79] op_sel_hi:[1,0]
	v_pk_add_f32 v[126:127], v[126:127], v[158:159]
	v_pk_mul_f32 v[130:131], v[130:131], s[78:79] op_sel_hi:[1,0]
	v_pk_fma_f32 v[178:179], v[178:179], s[80:81], v[180:181] op_sel_hi:[1,0,1]
	v_pk_fma_f32 v[162:163], v[162:163], s[80:81], v[164:165] op_sel_hi:[1,0,1]
	v_pk_fma_f32 v[126:127], v[126:127], s[80:81], v[130:131] op_sel_hi:[1,0,1]
	v_cvt_pk_f32_fp8_e32 v[130:131], v128
	v_cvt_pk_bf16_f32 v146, v178, v179
	v_cvt_pk_bf16_f32 v148, v162, v163
	v_cvt_pk_bf16_f32 v149, v126, v127
	v_lshl_add_u64 v[126:127], v[86:87], 0, s[98:99]
	v_cvt_pk_f32_fp8_e32 v[138:139], v132
	global_store_dwordx4 v[126:127], v[146:149], off
	v_cvt_pk_f32_fp8_e32 v[150:151], v140
	v_cvt_pk_f32_fp8_e32 v[158:159], v144
	v_cvt_pk_f32_fp8_e32 v[146:147], v136
	v_pk_add_f32 v[130:131], v[130:131], 0 op_sel_hi:[1,0]
	v_cvt_pk_f32_fp8_e32 v[164:165], v152
	v_pk_add_f32 v[130:131], v[130:131], v[138:139]
	v_cvt_pk_f32_fp8_e32 v[168:169], v156
	v_pk_add_f32 v[130:131], v[130:131], v[146:147]
	v_cvt_pk_f32_fp8_e32 v[172:173], v160
	v_pk_add_f32 v[130:131], v[130:131], v[150:151]
	v_cvt_pk_f32_fp8_sdwa v[134:135], v128 src0_sel:WORD_1
	v_pk_add_f32 v[130:131], v[130:131], v[158:159]
	v_cvt_pk_f32_fp8_sdwa v[142:143], v132 src0_sel:WORD_1
	v_pk_add_f32 v[130:131], v[130:131], v[164:165]
	v_lshlrev_b32_e32 v138, 16, v122
	v_pk_add_f32 v[130:131], v[130:131], v[168:169]
	v_and_b32_e32 v139, 0xffff0000, v122
	v_cvt_pk_f32_fp8_sdwa v[148:149], v136 src0_sel:WORD_1
	v_pk_add_f32 v[130:131], v[130:131], v[172:173]
	v_pk_mul_f32 v[138:139], v[138:139], s[78:79] op_sel_hi:[1,0]
	v_cvt_pk_f32_fp8_sdwa v[154:155], v140 src0_sel:WORD_1
	v_pk_fma_f32 v[130:131], v[130:131], s[80:81], v[138:139] op_sel_hi:[1,0,1]
	v_cvt_pk_f32_fp8_sdwa v[162:163], v144 src0_sel:WORD_1
	v_cvt_pk_bf16_f32 v122, v130, v131
	v_pk_add_f32 v[130:131], v[134:135], 0 op_sel_hi:[1,0]
	v_cvt_pk_f32_fp8_sdwa v[166:167], v152 src0_sel:WORD_1
	v_pk_add_f32 v[130:131], v[130:131], v[142:143]
	v_cvt_pk_f32_fp8_sdwa v[170:171], v156 src0_sel:WORD_1
	v_pk_add_f32 v[130:131], v[130:131], v[148:149]
	v_cvt_pk_f32_fp8_sdwa v[174:175], v160 src0_sel:WORD_1
	v_pk_add_f32 v[130:131], v[130:131], v[154:155]
	v_lshlrev_b32_e32 v134, 16, v123
	v_pk_add_f32 v[130:131], v[130:131], v[162:163]
	v_and_b32_e32 v135, 0xffff0000, v123
	v_pk_add_f32 v[130:131], v[130:131], v[166:167]
	v_pk_mul_f32 v[134:135], v[134:135], s[78:79] op_sel_hi:[1,0]
	v_pk_add_f32 v[130:131], v[130:131], v[170:171]
	v_cvt_pk_f32_fp8_e32 v[146:147], v129
	v_pk_add_f32 v[130:131], v[130:131], v[174:175]
	v_cvt_pk_f32_fp8_sdwa v[128:129], v129 src0_sel:WORD_1
	v_pk_fma_f32 v[130:131], v[130:131], s[80:81], v[134:135] op_sel_hi:[1,0,1]
	v_cvt_pk_f32_fp8_e32 v[148:149], v133
	v_cvt_pk_bf16_f32 v123, v130, v131
	v_cvt_pk_f32_fp8_sdwa v[130:131], v133 src0_sel:WORD_1
	v_cvt_pk_f32_fp8_e32 v[150:151], v137
	v_cvt_pk_f32_fp8_sdwa v[132:133], v137 src0_sel:WORD_1
	v_cvt_pk_f32_fp8_e32 v[154:155], v141
	v_cvt_pk_f32_fp8_sdwa v[134:135], v141 src0_sel:WORD_1
	v_cvt_pk_f32_fp8_e32 v[158:159], v145
	v_cvt_pk_f32_fp8_sdwa v[136:137], v145 src0_sel:WORD_1
	v_pk_add_f32 v[146:147], v[146:147], 0 op_sel_hi:[1,0]
	v_pk_add_f32 v[128:129], v[128:129], 0 op_sel_hi:[1,0]
	v_cvt_pk_f32_fp8_e32 v[144:145], v153
	v_cvt_pk_f32_fp8_sdwa v[138:139], v153 src0_sel:WORD_1
	v_pk_add_f32 v[146:147], v[146:147], v[148:149]
	v_pk_add_f32 v[128:129], v[128:129], v[130:131]
	v_cvt_pk_f32_fp8_e32 v[152:153], v157
	v_cvt_pk_f32_fp8_sdwa v[140:141], v157 src0_sel:WORD_1
	v_pk_add_f32 v[146:147], v[146:147], v[150:151]
	v_pk_add_f32 v[128:129], v[128:129], v[132:133]
	v_cvt_pk_f32_fp8_e32 v[156:157], v161
	v_cvt_pk_f32_fp8_sdwa v[142:143], v161 src0_sel:WORD_1
	v_pk_add_f32 v[146:147], v[146:147], v[154:155]
	v_pk_add_f32 v[128:129], v[128:129], v[134:135]
	v_pk_add_f32 v[146:147], v[146:147], v[158:159]
	v_pk_add_f32 v[128:129], v[128:129], v[136:137]
	v_pk_add_f32 v[144:145], v[146:147], v[144:145]
	v_pk_add_f32 v[128:129], v[128:129], v[138:139]
	v_pk_add_f32 v[144:145], v[144:145], v[152:153]
	v_lshlrev_b32_e32 v146, 16, v124
	v_and_b32_e32 v147, 0xffff0000, v124
	v_pk_add_f32 v[128:129], v[128:129], v[140:141]
	v_lshlrev_b32_e32 v130, 16, v125
	v_and_b32_e32 v131, 0xffff0000, v125
	v_pk_add_f32 v[144:145], v[144:145], v[156:157]
	v_pk_mul_f32 v[146:147], v[146:147], s[78:79] op_sel_hi:[1,0]
	v_pk_add_f32 v[128:129], v[128:129], v[142:143]
	v_pk_mul_f32 v[130:131], v[130:131], s[78:79] op_sel_hi:[1,0]
	v_pk_fma_f32 v[144:145], v[144:145], s[80:81], v[146:147] op_sel_hi:[1,0,1]
	v_pk_fma_f32 v[128:129], v[128:129], s[80:81], v[130:131] op_sel_hi:[1,0,1]
	v_cvt_pk_bf16_f32 v124, v144, v145
	v_cvt_pk_bf16_f32 v125, v128, v129
	global_store_dwordx4 v[126:127], v[122:125], off offset:16
	s_mov_b64 s[30:31], 0

.LBB0_487:
	s_add_i32 s16, s37, s39
	s_add_i32 s18, s16, 2
	s_add_i32 s20, s23, s42
	s_ashr_i32 s19, s18, 31
	s_add_i32 s64, s20, -15
	s_lshl_b64 s[18:19], s[18:19], 11
	s_ashr_i32 s65, s64, 31
	v_lshl_add_u64 v[2:3], v[82:83], 0, s[18:19]
	s_lshl_b64 s[64:65], s[64:65], 10
	global_load_dwordx4 v[42:45], v[2:3], off offset:16
	global_load_dwordx4 v[62:65], v[2:3], off
	v_lshl_add_u64 v[2:3], v[84:85], 0, s[64:65]
	s_add_i32 s64, s20, -14
	s_ashr_i32 s65, s64, 31
	s_lshl_b64 s[64:65], s[64:65], 10
	global_load_dwordx4 v[46:49], v[2:3], off
	v_lshl_add_u64 v[2:3], v[84:85], 0, s[64:65]
	s_add_i32 s64, s20, -13
	s_ashr_i32 s65, s64, 31
	s_lshl_b64 s[64:65], s[64:65], 10
	global_load_dwordx4 v[50:53], v[2:3], off
	v_lshl_add_u64 v[2:3], v[84:85], 0, s[64:65]
	s_add_i32 s64, s20, -12
	s_ashr_i32 s65, s64, 31
	s_lshl_b64 s[64:65], s[64:65], 10
	global_load_dwordx4 v[54:57], v[2:3], off
	v_lshl_add_u64 v[2:3], v[84:85], 0, s[64:65]
	s_add_i32 s64, s20, -11
	s_ashr_i32 s65, s64, 31
	s_lshl_b64 s[64:65], s[64:65], 10
	global_load_dwordx4 v[58:61], v[2:3], off
	v_lshl_add_u64 v[2:3], v[84:85], 0, s[64:65]
	s_add_i32 s64, s20, -10
	s_ashr_i32 s65, s64, 31
	s_lshl_b64 s[64:65], s[64:65], 10
	global_load_dwordx4 v[66:69], v[2:3], off
	v_lshl_add_u64 v[2:3], v[84:85], 0, s[64:65]
	s_add_i32 s64, s20, -9
	s_ashr_i32 s65, s64, 31
	s_lshl_b64 s[64:65], s[64:65], 10
	global_load_dwordx4 v[70:73], v[2:3], off
	v_lshl_add_u64 v[2:3], v[84:85], 0, s[64:65]
	s_add_i32 s64, s20, -8
	s_ashr_i32 s65, s64, 31
	s_lshl_b64 s[64:65], s[64:65], 10
	global_load_dwordx4 v[74:77], v[2:3], off
	v_lshl_add_u64 v[2:3], v[84:85], 0, s[64:65]
	global_load_dwordx4 v[78:81], v[2:3], off
	s_add_i32 s16, s16, 3
	s_ashr_i32 s17, s16, 31
	s_add_i32 s64, s20, -7
	s_lshl_b64 s[16:17], s[16:17], 11
	s_ashr_i32 s65, s64, 31
	v_lshl_add_u64 v[6:7], v[82:83], 0, s[16:17]
	s_lshl_b64 s[64:65], s[64:65], 10
	global_load_dwordx4 v[2:5], v[6:7], off offset:16
	global_load_dwordx4 v[26:29], v[6:7], off
	v_lshl_add_u64 v[6:7], v[84:85], 0, s[64:65]
	s_add_i32 s64, s20, -6
	s_ashr_i32 s65, s64, 31
	s_lshl_b64 s[64:65], s[64:65], 10
	v_lshl_add_u64 v[10:11], v[84:85], 0, s[64:65]
	s_add_i32 s64, s20, -5
	s_ashr_i32 s65, s64, 31
	s_lshl_b64 s[64:65], s[64:65], 10
	v_lshl_add_u64 v[14:15], v[84:85], 0, s[64:65]
	s_add_i32 s64, s20, -4
	s_ashr_i32 s65, s64, 31
	s_lshl_b64 s[64:65], s[64:65], 10
	v_lshl_add_u64 v[18:19], v[84:85], 0, s[64:65]
	s_add_i32 s64, s20, -3
	s_ashr_i32 s65, s64, 31
	s_lshl_b64 s[64:65], s[64:65], 10
	v_lshl_add_u64 v[22:23], v[84:85], 0, s[64:65]
	s_add_i32 s64, s20, -2
	global_load_dwordx4 v[6:9], v[6:7], off
	s_ashr_i32 s65, s64, 31
	global_load_dwordx4 v[10:13], v[10:11], off
	s_lshl_b64 s[64:65], s[64:65], 10
	global_load_dwordx4 v[14:17], v[14:15], off
	v_lshl_add_u64 v[30:31], v[84:85], 0, s[64:65]
	s_add_i32 s64, s20, -1
	global_load_dwordx4 v[18:21], v[18:19], off
	s_ashr_i32 s65, s64, 31
	global_load_dwordx4 v[22:25], v[22:23], off
	s_lshl_b64 s[64:65], s[64:65], 10
	s_ashr_i32 s21, s20, 31
	global_load_dwordx4 v[30:33], v[30:31], off
	v_lshl_add_u64 v[34:35], v[84:85], 0, s[64:65]
	s_lshl_b64 s[20:21], s[20:21], 10
	global_load_dwordx4 v[34:37], v[34:35], off
	v_lshl_add_u64 v[38:39], v[84:85], 0, s[20:21]
	global_load_dwordx4 v[38:41], v[38:39], off
	s_add_i32 s39, s39, 2
	s_add_i32 s42, s42, 16
	s_add_i32 s98, s37, s39
	s_add_i32 s100, s98, 2
	s_add_i32 s20, s23, s42
	s_ashr_i32 s101, s100, 31
	s_add_i32 s64, s20, -15
	s_lshl_b64 s[100:101], s[100:101], 11
	s_ashr_i32 s65, s64, 31
	v_lshl_add_u64 v[122:123], v[82:83], 0, s[100:101]
	s_lshl_b64 s[64:65], s[64:65], 10
	global_load_dwordx4 v[162:165], v[122:123], off offset:16
	global_load_dwordx4 v[182:185], v[122:123], off
	v_lshl_add_u64 v[122:123], v[84:85], 0, s[64:65]
	s_add_i32 s64, s20, -14
	s_ashr_i32 s65, s64, 31
	s_lshl_b64 s[64:65], s[64:65], 10
	global_load_dwordx4 v[166:169], v[122:123], off
	v_lshl_add_u64 v[122:123], v[84:85], 0, s[64:65]
	s_add_i32 s64, s20, -13
	s_ashr_i32 s65, s64, 31
	s_lshl_b64 s[64:65], s[64:65], 10
	global_load_dwordx4 v[170:173], v[122:123], off
	v_lshl_add_u64 v[122:123], v[84:85], 0, s[64:65]
	s_add_i32 s64, s20, -12
	s_ashr_i32 s65, s64, 31
	s_lshl_b64 s[64:65], s[64:65], 10
	global_load_dwordx4 v[174:177], v[122:123], off
	v_lshl_add_u64 v[122:123], v[84:85], 0, s[64:65]
	s_add_i32 s64, s20, -11
	s_ashr_i32 s65, s64, 31
	s_lshl_b64 s[64:65], s[64:65], 10
	global_load_dwordx4 v[178:181], v[122:123], off
	v_lshl_add_u64 v[122:123], v[84:85], 0, s[64:65]
	s_add_i32 s64, s20, -10
	s_ashr_i32 s65, s64, 31
	s_lshl_b64 s[64:65], s[64:65], 10
	global_load_dwordx4 v[186:189], v[122:123], off
	v_lshl_add_u64 v[122:123], v[84:85], 0, s[64:65]
	s_add_i32 s64, s20, -9
	s_ashr_i32 s65, s64, 31
	s_lshl_b64 s[64:65], s[64:65], 10
	global_load_dwordx4 v[190:193], v[122:123], off
	v_lshl_add_u64 v[122:123], v[84:85], 0, s[64:65]
	s_add_i32 s64, s20, -8
	s_ashr_i32 s65, s64, 31
	s_lshl_b64 s[64:65], s[64:65], 10
	global_load_dwordx4 v[194:197], v[122:123], off
	v_lshl_add_u64 v[122:123], v[84:85], 0, s[64:65]
	global_load_dwordx4 v[198:201], v[122:123], off
	s_add_i32 s98, s98, 3
	s_ashr_i32 s99, s98, 31
	s_add_i32 s64, s20, -7
	s_lshl_b64 s[98:99], s[98:99], 11
	s_ashr_i32 s65, s64, 31
	v_lshl_add_u64 v[126:127], v[82:83], 0, s[98:99]
	s_lshl_b64 s[64:65], s[64:65], 10
	global_load_dwordx4 v[122:125], v[126:127], off offset:16
	global_load_dwordx4 v[146:149], v[126:127], off
	v_lshl_add_u64 v[126:127], v[84:85], 0, s[64:65]
	s_add_i32 s64, s20, -6
	s_ashr_i32 s65, s64, 31
	s_lshl_b64 s[64:65], s[64:65], 10
	v_lshl_add_u64 v[130:131], v[84:85], 0, s[64:65]
	s_add_i32 s64, s20, -5
	s_ashr_i32 s65, s64, 31
	s_lshl_b64 s[64:65], s[64:65], 10
	v_lshl_add_u64 v[134:135], v[84:85], 0, s[64:65]
	s_add_i32 s64, s20, -4
	s_ashr_i32 s65, s64, 31
	s_lshl_b64 s[64:65], s[64:65], 10
	v_lshl_add_u64 v[138:139], v[84:85], 0, s[64:65]
	s_add_i32 s64, s20, -3
	s_ashr_i32 s65, s64, 31
	s_lshl_b64 s[64:65], s[64:65], 10
	v_lshl_add_u64 v[142:143], v[84:85], 0, s[64:65]
	s_add_i32 s64, s20, -2
	global_load_dwordx4 v[126:129], v[126:127], off
	s_ashr_i32 s65, s64, 31
	global_load_dwordx4 v[130:133], v[130:131], off
	s_lshl_b64 s[64:65], s[64:65], 10
	global_load_dwordx4 v[134:137], v[134:135], off
	v_lshl_add_u64 v[150:151], v[84:85], 0, s[64:65]
	s_add_i32 s64, s20, -1
	global_load_dwordx4 v[138:141], v[138:139], off
	s_ashr_i32 s65, s64, 31
	global_load_dwordx4 v[142:145], v[142:143], off
	s_lshl_b64 s[64:65], s[64:65], 10
	s_ashr_i32 s21, s20, 31
	global_load_dwordx4 v[150:153], v[150:151], off
	v_lshl_add_u64 v[154:155], v[84:85], 0, s[64:65]
	s_lshl_b64 s[20:21], s[20:21], 10
	global_load_dwordx4 v[154:157], v[154:155], off
	v_lshl_add_u64 v[158:159], v[84:85], 0, s[20:21]
	global_load_dwordx4 v[158:161], v[158:159], off
	s_add_i32 s39, s39, 2
	s_add_i32 s42, s42, 16
	s_waitcnt vmcnt(37)
	v_cvt_pk_f32_fp8_e32 v[88:89], v46
	v_cvt_pk_f32_fp8_sdwa v[90:91], v46 src0_sel:WORD_1
	v_pk_add_f32 v[88:89], v[88:89], 0 op_sel_hi:[1,0]
	s_waitcnt vmcnt(36)
	v_cvt_pk_f32_fp8_e32 v[92:93], v50
	v_cvt_pk_f32_fp8_sdwa v[94:95], v50 src0_sel:WORD_1
	v_pk_add_f32 v[88:89], v[88:89], v[92:93]
	s_waitcnt vmcnt(35)
	v_cvt_pk_f32_fp8_e32 v[96:97], v54
	v_lshlrev_b32_e32 v92, 16, v62
	v_and_b32_e32 v93, 0xffff0000, v62
	v_cvt_pk_f32_fp8_sdwa v[98:99], v54 src0_sel:WORD_1
	v_pk_add_f32 v[88:89], v[88:89], v[96:97]
	s_waitcnt vmcnt(34)
	v_cvt_pk_f32_fp8_e32 v[100:101], v58
	v_pk_mul_f32 v[92:93], v[92:93], s[78:79] op_sel_hi:[1,0]
	v_cvt_pk_f32_fp8_sdwa v[102:103], v58 src0_sel:WORD_1
	v_pk_add_f32 v[88:89], v[88:89], v[100:101]
	s_waitcnt vmcnt(33)
	v_cvt_pk_f32_fp8_e32 v[104:105], v66
	v_cvt_pk_f32_fp8_sdwa v[106:107], v66 src0_sel:WORD_1
	v_cvt_pk_f32_fp8_e32 v[96:97], v67
	v_cvt_pk_f32_fp8_sdwa v[66:67], v67 src0_sel:WORD_1
	v_pk_add_f32 v[88:89], v[88:89], v[104:105]
	s_waitcnt vmcnt(32)
	v_cvt_pk_f32_fp8_e32 v[108:109], v70
	v_cvt_pk_f32_fp8_sdwa v[110:111], v70 src0_sel:WORD_1
	v_pk_add_f32 v[88:89], v[88:89], v[108:109]
	s_waitcnt vmcnt(31)
	v_cvt_pk_f32_fp8_e32 v[112:113], v74
	v_cvt_pk_f32_fp8_sdwa v[114:115], v74 src0_sel:WORD_1
	s_waitcnt vmcnt(30)
	v_cvt_pk_f32_fp8_e32 v[116:117], v78
	v_cvt_pk_f32_fp8_sdwa v[118:119], v78 src0_sel:WORD_1
	v_pk_add_f32 v[88:89], v[88:89], v[112:113]
	v_cvt_pk_f32_fp8_e32 v[100:101], v75
	v_pk_add_f32 v[88:89], v[88:89], v[116:117]
	v_cvt_pk_f32_fp8_sdwa v[74:75], v75 src0_sel:WORD_1
	v_pk_fma_f32 v[88:89], v[88:89], s[80:81], v[92:93] op_sel_hi:[1,0,1]
	v_cvt_pk_f32_fp8_e32 v[92:93], v55
	v_cvt_pk_bf16_f32 v62, v88, v89
	v_pk_add_f32 v[88:89], v[90:91], 0 op_sel_hi:[1,0]
	v_lshlrev_b32_e32 v90, 16, v63
	v_pk_add_f32 v[88:89], v[88:89], v[94:95]
	v_and_b32_e32 v91, 0xffff0000, v63
	v_pk_add_f32 v[88:89], v[88:89], v[98:99]
	v_pk_mul_f32 v[90:91], v[90:91], s[78:79] op_sel_hi:[1,0]
	v_pk_add_f32 v[88:89], v[88:89], v[102:103]
	v_cvt_pk_f32_fp8_sdwa v[54:55], v55 src0_sel:WORD_1
	v_pk_add_f32 v[88:89], v[88:89], v[106:107]
	v_cvt_pk_f32_fp8_e32 v[94:95], v59
	v_pk_add_f32 v[88:89], v[88:89], v[110:111]
	v_cvt_pk_f32_fp8_sdwa v[58:59], v59 src0_sel:WORD_1
	v_pk_add_f32 v[88:89], v[88:89], v[114:115]
	v_cvt_pk_f32_fp8_e32 v[98:99], v71
	v_pk_add_f32 v[88:89], v[88:89], v[118:119]
	v_cvt_pk_f32_fp8_sdwa v[70:71], v71 src0_sel:WORD_1
	v_pk_fma_f32 v[88:89], v[88:89], s[80:81], v[90:91] op_sel_hi:[1,0,1]
	v_cvt_pk_f32_fp8_e32 v[90:91], v51
	v_cvt_pk_bf16_f32 v63, v88, v89
	v_cvt_pk_f32_fp8_e32 v[88:89], v47
	v_cvt_pk_f32_fp8_sdwa v[46:47], v47 src0_sel:WORD_1
	v_cvt_pk_f32_fp8_sdwa v[50:51], v51 src0_sel:WORD_1
	v_cvt_pk_f32_fp8_e32 v[102:103], v79
	v_pk_add_f32 v[88:89], v[88:89], 0 op_sel_hi:[1,0]
	v_pk_add_f32 v[46:47], v[46:47], 0 op_sel_hi:[1,0]
	v_pk_add_f32 v[88:89], v[88:89], v[90:91]
	v_pk_add_f32 v[46:47], v[46:47], v[50:51]
	v_pk_add_f32 v[88:89], v[88:89], v[92:93]
	v_pk_add_f32 v[46:47], v[46:47], v[54:55]
	v_cvt_pk_f32_fp8_sdwa v[78:79], v79 src0_sel:WORD_1
	v_pk_add_f32 v[88:89], v[88:89], v[94:95]
	v_pk_add_f32 v[46:47], v[46:47], v[58:59]
	v_pk_add_f32 v[88:89], v[88:89], v[96:97]
	v_pk_add_f32 v[46:47], v[46:47], v[66:67]
	v_pk_add_f32 v[88:89], v[88:89], v[98:99]
	v_pk_add_f32 v[46:47], v[46:47], v[70:71]
	v_pk_add_f32 v[88:89], v[88:89], v[100:101]
	v_lshlrev_b32_e32 v90, 16, v64
	v_and_b32_e32 v91, 0xffff0000, v64
	v_pk_add_f32 v[46:47], v[46:47], v[74:75]
	v_lshlrev_b32_e32 v50, 16, v65
	v_and_b32_e32 v51, 0xffff0000, v65
	v_pk_add_f32 v[88:89], v[88:89], v[102:103]
	v_pk_mul_f32 v[90:91], v[90:91], s[78:79] op_sel_hi:[1,0]
	v_pk_add_f32 v[46:47], v[46:47], v[78:79]
	v_pk_mul_f32 v[50:51], v[50:51], s[78:79] op_sel_hi:[1,0]
	v_pk_fma_f32 v[88:89], v[88:89], s[80:81], v[90:91] op_sel_hi:[1,0,1]
	v_pk_fma_f32 v[46:47], v[46:47], s[80:81], v[50:51] op_sel_hi:[1,0,1]
	v_cvt_pk_f32_fp8_e32 v[50:51], v48
	v_cvt_pk_bf16_f32 v64, v88, v89
	v_cvt_pk_bf16_f32 v65, v46, v47
	v_lshl_add_u64 v[46:47], v[86:87], 0, s[18:19]
	v_cvt_pk_f32_fp8_e32 v[58:59], v52
	global_store_dwordx4 v[46:47], v[62:65], off
	v_cvt_pk_f32_fp8_e32 v[70:71], v60
	v_cvt_pk_f32_fp8_e32 v[78:79], v68
	v_cvt_pk_f32_fp8_e32 v[64:65], v56
	v_pk_add_f32 v[50:51], v[50:51], 0 op_sel_hi:[1,0]
	v_cvt_pk_f32_fp8_e32 v[90:91], v72
	v_pk_add_f32 v[50:51], v[50:51], v[58:59]
	v_cvt_pk_f32_fp8_e32 v[94:95], v76
	v_pk_add_f32 v[50:51], v[50:51], v[64:65]
	v_cvt_pk_f32_fp8_e32 v[98:99], v80
	v_pk_add_f32 v[50:51], v[50:51], v[70:71]
	v_cvt_pk_f32_fp8_sdwa v[54:55], v48 src0_sel:WORD_1
	v_pk_add_f32 v[50:51], v[50:51], v[78:79]
	v_cvt_pk_f32_fp8_sdwa v[62:63], v52 src0_sel:WORD_1
	v_pk_add_f32 v[50:51], v[50:51], v[90:91]
	v_lshlrev_b32_e32 v58, 16, v42
	v_pk_add_f32 v[50:51], v[50:51], v[94:95]
	v_and_b32_e32 v59, 0xffff0000, v42
	v_cvt_pk_f32_fp8_sdwa v[66:67], v56 src0_sel:WORD_1
	v_pk_add_f32 v[50:51], v[50:51], v[98:99]
	v_pk_mul_f32 v[58:59], v[58:59], s[78:79] op_sel_hi:[1,0]
	v_cvt_pk_f32_fp8_sdwa v[74:75], v60 src0_sel:WORD_1
	v_pk_fma_f32 v[50:51], v[50:51], s[80:81], v[58:59] op_sel_hi:[1,0,1]
	v_cvt_pk_f32_fp8_sdwa v[88:89], v68 src0_sel:WORD_1
	v_cvt_pk_bf16_f32 v42, v50, v51
	v_pk_add_f32 v[50:51], v[54:55], 0 op_sel_hi:[1,0]
	v_cvt_pk_f32_fp8_sdwa v[92:93], v72 src0_sel:WORD_1
	v_pk_add_f32 v[50:51], v[50:51], v[62:63]
	v_cvt_pk_f32_fp8_sdwa v[96:97], v76 src0_sel:WORD_1
	v_pk_add_f32 v[50:51], v[50:51], v[66:67]
	v_cvt_pk_f32_fp8_sdwa v[100:101], v80 src0_sel:WORD_1
	v_pk_add_f32 v[50:51], v[50:51], v[74:75]
	v_lshlrev_b32_e32 v54, 16, v43
	v_pk_add_f32 v[50:51], v[50:51], v[88:89]
	v_and_b32_e32 v55, 0xffff0000, v43
	v_pk_add_f32 v[50:51], v[50:51], v[92:93]
	v_pk_mul_f32 v[54:55], v[54:55], s[78:79] op_sel_hi:[1,0]
	v_pk_add_f32 v[50:51], v[50:51], v[96:97]
	v_cvt_pk_f32_fp8_e32 v[58:59], v57
	v_pk_add_f32 v[50:51], v[50:51], v[100:101]
	v_cvt_pk_f32_fp8_e32 v[62:63], v61
	v_pk_fma_f32 v[50:51], v[50:51], s[80:81], v[54:55] op_sel_hi:[1,0,1]
	v_cvt_pk_f32_fp8_e32 v[54:55], v53
	v_cvt_pk_bf16_f32 v43, v50, v51
	v_cvt_pk_f32_fp8_e32 v[50:51], v49
	v_cvt_pk_f32_fp8_sdwa v[48:49], v49 src0_sel:WORD_1
	v_cvt_pk_f32_fp8_sdwa v[52:53], v53 src0_sel:WORD_1
	v_cvt_pk_f32_fp8_e32 v[64:65], v69
	v_pk_add_f32 v[50:51], v[50:51], 0 op_sel_hi:[1,0]
	v_cvt_pk_f32_fp8_sdwa v[56:57], v57 src0_sel:WORD_1
	v_cvt_pk_f32_fp8_sdwa v[66:67], v69 src0_sel:WORD_1
	v_cvt_pk_f32_fp8_e32 v[68:69], v73
	v_pk_add_f32 v[50:51], v[50:51], v[54:55]
	v_cvt_pk_f32_fp8_sdwa v[60:61], v61 src0_sel:WORD_1
	v_cvt_pk_f32_fp8_sdwa v[70:71], v73 src0_sel:WORD_1
	v_cvt_pk_f32_fp8_e32 v[72:73], v77
	v_pk_add_f32 v[50:51], v[50:51], v[58:59]
	v_cvt_pk_f32_fp8_sdwa v[74:75], v77 src0_sel:WORD_1
	v_cvt_pk_f32_fp8_e32 v[76:77], v81
	v_pk_add_f32 v[50:51], v[50:51], v[62:63]
	v_pk_add_f32 v[48:49], v[48:49], 0 op_sel_hi:[1,0]
	v_pk_add_f32 v[50:51], v[50:51], v[64:65]
	v_pk_add_f32 v[48:49], v[48:49], v[52:53]
	v_pk_add_f32 v[50:51], v[50:51], v[68:69]
	v_pk_add_f32 v[48:49], v[48:49], v[56:57]
	v_cvt_pk_f32_fp8_sdwa v[78:79], v81 src0_sel:WORD_1
	v_pk_add_f32 v[50:51], v[50:51], v[72:73]
	v_lshlrev_b32_e32 v54, 16, v44
	v_and_b32_e32 v55, 0xffff0000, v44
	v_pk_add_f32 v[48:49], v[48:49], v[60:61]
	v_pk_add_f32 v[50:51], v[50:51], v[76:77]
	v_pk_mul_f32 v[54:55], v[54:55], s[78:79] op_sel_hi:[1,0]
	v_pk_add_f32 v[48:49], v[48:49], v[66:67]
	v_pk_fma_f32 v[50:51], v[50:51], s[80:81], v[54:55] op_sel_hi:[1,0,1]
	v_pk_add_f32 v[48:49], v[48:49], v[70:71]
	v_cvt_pk_bf16_f32 v44, v50, v51
	v_pk_add_f32 v[48:49], v[48:49], v[74:75]
	v_lshlrev_b32_e32 v50, 16, v45
	v_and_b32_e32 v51, 0xffff0000, v45
	v_pk_add_f32 v[48:49], v[48:49], v[78:79]
	v_pk_mul_f32 v[50:51], v[50:51], s[78:79] op_sel_hi:[1,0]
	s_waitcnt vmcnt(23)
	v_cvt_pk_f32_fp8_sdwa v[52:53], v30 src0_sel:WORD_1
	v_pk_fma_f32 v[48:49], v[48:49], s[80:81], v[50:51] op_sel_hi:[1,0,1]
	v_cvt_pk_f32_fp8_sdwa v[50:51], v22 src0_sel:WORD_1
	v_cvt_pk_bf16_f32 v45, v48, v49
	global_store_dwordx4 v[46:47], v[42:45], off offset:16
	v_cvt_pk_f32_fp8_sdwa v[46:47], v14 src0_sel:WORD_1
	v_cvt_pk_f32_fp8_sdwa v[48:49], v18 src0_sel:WORD_1
	v_cvt_pk_f32_fp8_sdwa v[42:43], v6 src0_sel:WORD_1
	v_cvt_pk_f32_fp8_sdwa v[44:45], v10 src0_sel:WORD_1
	s_waitcnt vmcnt(23)
	v_cvt_pk_f32_fp8_sdwa v[54:55], v34 src0_sel:WORD_1
	s_waitcnt vmcnt(22)
	v_cvt_pk_f32_fp8_sdwa v[56:57], v38 src0_sel:WORD_1
	v_pk_add_f32 v[42:43], v[42:43], 0 op_sel_hi:[1,0]
	v_cvt_pk_f32_fp8_e32 v[58:59], v6
	v_pk_add_f32 v[42:43], v[42:43], v[44:45]
	v_lshlrev_b32_e32 v44, 16, v27
	v_pk_add_f32 v[42:43], v[42:43], v[46:47]
	v_and_b32_e32 v45, 0xffff0000, v27
	v_pk_add_f32 v[42:43], v[42:43], v[48:49]
	v_pk_mul_f32 v[44:45], v[44:45], s[78:79] op_sel_hi:[1,0]
	v_pk_add_f32 v[42:43], v[42:43], v[50:51]
	v_cvt_pk_f32_fp8_e32 v[60:61], v10
	v_pk_add_f32 v[42:43], v[42:43], v[52:53]
	v_cvt_pk_f32_fp8_e32 v[62:63], v14
	v_pk_add_f32 v[42:43], v[42:43], v[54:55]
	v_cvt_pk_f32_fp8_e32 v[46:47], v15
	v_pk_add_f32 v[42:43], v[42:43], v[56:57]
	v_cvt_pk_f32_fp8_sdwa v[14:15], v15 src0_sel:WORD_1
	v_pk_fma_f32 v[42:43], v[42:43], s[80:81], v[44:45] op_sel_hi:[1,0,1]
	v_cvt_pk_f32_fp8_e32 v[44:45], v11
	v_cvt_pk_bf16_f32 v27, v42, v43
	v_cvt_pk_f32_fp8_e32 v[42:43], v7
	v_cvt_pk_f32_fp8_sdwa v[6:7], v7 src0_sel:WORD_1
	v_cvt_pk_f32_fp8_sdwa v[10:11], v11 src0_sel:WORD_1
	v_cvt_pk_f32_fp8_e32 v[64:65], v18
	v_cvt_pk_f32_fp8_e32 v[48:49], v19
	v_cvt_pk_f32_fp8_sdwa v[18:19], v19 src0_sel:WORD_1
	v_cvt_pk_f32_fp8_e32 v[66:67], v22
	v_pk_add_f32 v[58:59], v[58:59], 0 op_sel_hi:[1,0]
	v_cvt_pk_f32_fp8_e32 v[50:51], v23
	v_cvt_pk_f32_fp8_sdwa v[22:23], v23 src0_sel:WORD_1
	v_pk_add_f32 v[42:43], v[42:43], 0 op_sel_hi:[1,0]
	v_pk_add_f32 v[6:7], v[6:7], 0 op_sel_hi:[1,0]
	v_cvt_pk_f32_fp8_e32 v[68:69], v30
	v_pk_add_f32 v[58:59], v[58:59], v[60:61]
	v_cvt_pk_f32_fp8_e32 v[52:53], v31
	v_cvt_pk_f32_fp8_sdwa v[30:31], v31 src0_sel:WORD_1
	v_pk_add_f32 v[42:43], v[42:43], v[44:45]
	v_pk_add_f32 v[6:7], v[6:7], v[10:11]
	v_cvt_pk_f32_fp8_e32 v[70:71], v34
	v_pk_add_f32 v[58:59], v[58:59], v[62:63]
	v_cvt_pk_f32_fp8_e32 v[54:55], v35
	v_cvt_pk_f32_fp8_sdwa v[34:35], v35 src0_sel:WORD_1
	v_pk_add_f32 v[42:43], v[42:43], v[46:47]
	v_pk_add_f32 v[6:7], v[6:7], v[14:15]
	v_cvt_pk_f32_fp8_e32 v[72:73], v38
	v_pk_add_f32 v[58:59], v[58:59], v[64:65]
	v_cvt_pk_f32_fp8_e32 v[56:57], v39
	v_cvt_pk_f32_fp8_sdwa v[38:39], v39 src0_sel:WORD_1
	v_pk_add_f32 v[42:43], v[42:43], v[48:49]
	v_pk_add_f32 v[6:7], v[6:7], v[18:19]
	v_pk_add_f32 v[58:59], v[58:59], v[66:67]
	v_pk_add_f32 v[42:43], v[42:43], v[50:51]
	v_pk_add_f32 v[6:7], v[6:7], v[22:23]
	v_pk_add_f32 v[58:59], v[58:59], v[68:69]
	v_pk_add_f32 v[42:43], v[42:43], v[52:53]
	v_pk_add_f32 v[6:7], v[6:7], v[30:31]
	v_pk_add_f32 v[58:59], v[58:59], v[70:71]
	v_lshlrev_b32_e32 v60, 16, v26
	v_and_b32_e32 v61, 0xffff0000, v26
	v_pk_add_f32 v[42:43], v[42:43], v[54:55]
	v_lshlrev_b32_e32 v44, 16, v28
	v_and_b32_e32 v45, 0xffff0000, v28
	v_pk_add_f32 v[6:7], v[6:7], v[34:35]
	v_lshlrev_b32_e32 v10, 16, v29
	v_and_b32_e32 v11, 0xffff0000, v29
	v_pk_add_f32 v[58:59], v[58:59], v[72:73]
	v_pk_mul_f32 v[60:61], v[60:61], s[78:79] op_sel_hi:[1,0]
	v_pk_add_f32 v[42:43], v[42:43], v[56:57]
	v_pk_mul_f32 v[44:45], v[44:45], s[78:79] op_sel_hi:[1,0]
	v_pk_add_f32 v[6:7], v[6:7], v[38:39]
	v_pk_mul_f32 v[10:11], v[10:11], s[78:79] op_sel_hi:[1,0]
	v_pk_fma_f32 v[58:59], v[58:59], s[80:81], v[60:61] op_sel_hi:[1,0,1]
	v_pk_fma_f32 v[42:43], v[42:43], s[80:81], v[44:45] op_sel_hi:[1,0,1]
	v_pk_fma_f32 v[6:7], v[6:7], s[80:81], v[10:11] op_sel_hi:[1,0,1]
	v_cvt_pk_f32_fp8_e32 v[10:11], v8
	v_cvt_pk_bf16_f32 v26, v58, v59
	v_cvt_pk_bf16_f32 v28, v42, v43
	v_cvt_pk_bf16_f32 v29, v6, v7
	v_lshl_add_u64 v[6:7], v[86:87], 0, s[16:17]
	v_cvt_pk_f32_fp8_e32 v[18:19], v12
	global_store_dwordx4 v[6:7], v[26:29], off
	v_cvt_pk_f32_fp8_e32 v[30:31], v20
	v_cvt_pk_f32_fp8_e32 v[38:39], v24
	v_cvt_pk_f32_fp8_e32 v[26:27], v16
	v_pk_add_f32 v[10:11], v[10:11], 0 op_sel_hi:[1,0]
	v_cvt_pk_f32_fp8_e32 v[44:45], v32
	v_pk_add_f32 v[10:11], v[10:11], v[18:19]
	v_cvt_pk_f32_fp8_e32 v[48:49], v36
	v_pk_add_f32 v[10:11], v[10:11], v[26:27]
	v_cvt_pk_f32_fp8_e32 v[52:53], v40
	v_pk_add_f32 v[10:11], v[10:11], v[30:31]
	v_cvt_pk_f32_fp8_sdwa v[14:15], v8 src0_sel:WORD_1
	v_pk_add_f32 v[10:11], v[10:11], v[38:39]
	v_cvt_pk_f32_fp8_sdwa v[22:23], v12 src0_sel:WORD_1
	v_pk_add_f32 v[10:11], v[10:11], v[44:45]
	v_lshlrev_b32_e32 v18, 16, v2
	v_pk_add_f32 v[10:11], v[10:11], v[48:49]
	v_and_b32_e32 v19, 0xffff0000, v2
	v_cvt_pk_f32_fp8_sdwa v[28:29], v16 src0_sel:WORD_1
	v_pk_add_f32 v[10:11], v[10:11], v[52:53]
	v_pk_mul_f32 v[18:19], v[18:19], s[78:79] op_sel_hi:[1,0]
	v_cvt_pk_f32_fp8_sdwa v[34:35], v20 src0_sel:WORD_1
	v_pk_fma_f32 v[10:11], v[10:11], s[80:81], v[18:19] op_sel_hi:[1,0,1]
	v_cvt_pk_f32_fp8_sdwa v[42:43], v24 src0_sel:WORD_1
	v_cvt_pk_bf16_f32 v2, v10, v11
	v_pk_add_f32 v[10:11], v[14:15], 0 op_sel_hi:[1,0]
	v_cvt_pk_f32_fp8_sdwa v[46:47], v32 src0_sel:WORD_1
	v_pk_add_f32 v[10:11], v[10:11], v[22:23]
	v_cvt_pk_f32_fp8_sdwa v[50:51], v36 src0_sel:WORD_1
	v_pk_add_f32 v[10:11], v[10:11], v[28:29]
	v_cvt_pk_f32_fp8_sdwa v[54:55], v40 src0_sel:WORD_1
	v_pk_add_f32 v[10:11], v[10:11], v[34:35]
	v_lshlrev_b32_e32 v14, 16, v3
	v_pk_add_f32 v[10:11], v[10:11], v[42:43]
	v_and_b32_e32 v15, 0xffff0000, v3
	v_pk_add_f32 v[10:11], v[10:11], v[46:47]
	v_pk_mul_f32 v[14:15], v[14:15], s[78:79] op_sel_hi:[1,0]
	v_pk_add_f32 v[10:11], v[10:11], v[50:51]
	v_cvt_pk_f32_fp8_e32 v[26:27], v9
	v_pk_add_f32 v[10:11], v[10:11], v[54:55]
	v_cvt_pk_f32_fp8_sdwa v[8:9], v9 src0_sel:WORD_1
	v_pk_fma_f32 v[10:11], v[10:11], s[80:81], v[14:15] op_sel_hi:[1,0,1]
	v_cvt_pk_f32_fp8_e32 v[28:29], v13
	v_cvt_pk_bf16_f32 v3, v10, v11
	v_cvt_pk_f32_fp8_sdwa v[10:11], v13 src0_sel:WORD_1
	v_cvt_pk_f32_fp8_e32 v[30:31], v17
	v_cvt_pk_f32_fp8_sdwa v[12:13], v17 src0_sel:WORD_1
	v_cvt_pk_f32_fp8_e32 v[34:35], v21
	v_cvt_pk_f32_fp8_sdwa v[14:15], v21 src0_sel:WORD_1
	v_cvt_pk_f32_fp8_e32 v[38:39], v25
	v_cvt_pk_f32_fp8_sdwa v[16:17], v25 src0_sel:WORD_1
	v_pk_add_f32 v[26:27], v[26:27], 0 op_sel_hi:[1,0]
	v_pk_add_f32 v[8:9], v[8:9], 0 op_sel_hi:[1,0]
	v_cvt_pk_f32_fp8_e32 v[24:25], v33
	v_cvt_pk_f32_fp8_sdwa v[18:19], v33 src0_sel:WORD_1
	v_pk_add_f32 v[26:27], v[26:27], v[28:29]
	v_pk_add_f32 v[8:9], v[8:9], v[10:11]
	v_cvt_pk_f32_fp8_e32 v[32:33], v37
	v_cvt_pk_f32_fp8_sdwa v[20:21], v37 src0_sel:WORD_1
	v_pk_add_f32 v[26:27], v[26:27], v[30:31]
	v_pk_add_f32 v[8:9], v[8:9], v[12:13]
	v_cvt_pk_f32_fp8_e32 v[36:37], v41
	v_cvt_pk_f32_fp8_sdwa v[22:23], v41 src0_sel:WORD_1
	v_pk_add_f32 v[26:27], v[26:27], v[34:35]
	v_pk_add_f32 v[8:9], v[8:9], v[14:15]
	v_pk_add_f32 v[26:27], v[26:27], v[38:39]
	v_pk_add_f32 v[8:9], v[8:9], v[16:17]
	v_pk_add_f32 v[24:25], v[26:27], v[24:25]
	v_pk_add_f32 v[8:9], v[8:9], v[18:19]
	v_pk_add_f32 v[24:25], v[24:25], v[32:33]
	v_lshlrev_b32_e32 v26, 16, v4
	v_and_b32_e32 v27, 0xffff0000, v4
	v_pk_add_f32 v[8:9], v[8:9], v[20:21]
	v_lshlrev_b32_e32 v10, 16, v5
	v_and_b32_e32 v11, 0xffff0000, v5
	v_pk_add_f32 v[24:25], v[24:25], v[36:37]
	v_pk_mul_f32 v[26:27], v[26:27], s[78:79] op_sel_hi:[1,0]
	v_pk_add_f32 v[8:9], v[8:9], v[22:23]
	v_pk_mul_f32 v[10:11], v[10:11], s[78:79] op_sel_hi:[1,0]
	v_pk_fma_f32 v[24:25], v[24:25], s[80:81], v[26:27] op_sel_hi:[1,0,1]
	v_pk_fma_f32 v[8:9], v[8:9], s[80:81], v[10:11] op_sel_hi:[1,0,1]
	v_cvt_pk_bf16_f32 v4, v24, v25
	v_cvt_pk_bf16_f32 v5, v8, v9
	global_store_dwordx4 v[6:7], v[2:5], off offset:16
	s_add_i32 s16, s37, s39
	s_add_i32 s18, s16, 2
	s_add_i32 s20, s23, s42
	s_ashr_i32 s19, s18, 31
	s_add_i32 s64, s20, -15
	s_lshl_b64 s[18:19], s[18:19], 11
	s_ashr_i32 s65, s64, 31
	v_lshl_add_u64 v[2:3], v[82:83], 0, s[18:19]
	s_lshl_b64 s[64:65], s[64:65], 10
	global_load_dwordx4 v[42:45], v[2:3], off offset:16
	global_load_dwordx4 v[62:65], v[2:3], off
	v_lshl_add_u64 v[2:3], v[84:85], 0, s[64:65]
	s_add_i32 s64, s20, -14
	s_ashr_i32 s65, s64, 31
	s_lshl_b64 s[64:65], s[64:65], 10
	global_load_dwordx4 v[46:49], v[2:3], off
	v_lshl_add_u64 v[2:3], v[84:85], 0, s[64:65]
	s_add_i32 s64, s20, -13
	s_ashr_i32 s65, s64, 31
	s_lshl_b64 s[64:65], s[64:65], 10
	global_load_dwordx4 v[50:53], v[2:3], off
	v_lshl_add_u64 v[2:3], v[84:85], 0, s[64:65]
	s_add_i32 s64, s20, -12
	s_ashr_i32 s65, s64, 31
	s_lshl_b64 s[64:65], s[64:65], 10
	global_load_dwordx4 v[54:57], v[2:3], off
	v_lshl_add_u64 v[2:3], v[84:85], 0, s[64:65]
	s_add_i32 s64, s20, -11
	s_ashr_i32 s65, s64, 31
	s_lshl_b64 s[64:65], s[64:65], 10
	global_load_dwordx4 v[58:61], v[2:3], off
	v_lshl_add_u64 v[2:3], v[84:85], 0, s[64:65]
	s_add_i32 s64, s20, -10
	s_ashr_i32 s65, s64, 31
	s_lshl_b64 s[64:65], s[64:65], 10
	global_load_dwordx4 v[66:69], v[2:3], off
	v_lshl_add_u64 v[2:3], v[84:85], 0, s[64:65]
	s_add_i32 s64, s20, -9
	s_ashr_i32 s65, s64, 31
	s_lshl_b64 s[64:65], s[64:65], 10
	global_load_dwordx4 v[70:73], v[2:3], off
	v_lshl_add_u64 v[2:3], v[84:85], 0, s[64:65]
	s_add_i32 s64, s20, -8
	s_ashr_i32 s65, s64, 31
	s_lshl_b64 s[64:65], s[64:65], 10
	global_load_dwordx4 v[74:77], v[2:3], off
	v_lshl_add_u64 v[2:3], v[84:85], 0, s[64:65]
	global_load_dwordx4 v[78:81], v[2:3], off
	s_add_i32 s16, s16, 3
	s_ashr_i32 s17, s16, 31
	s_add_i32 s64, s20, -7
	s_lshl_b64 s[16:17], s[16:17], 11
	s_ashr_i32 s65, s64, 31
	v_lshl_add_u64 v[6:7], v[82:83], 0, s[16:17]
	s_lshl_b64 s[64:65], s[64:65], 10
	global_load_dwordx4 v[2:5], v[6:7], off offset:16
	global_load_dwordx4 v[26:29], v[6:7], off
	v_lshl_add_u64 v[6:7], v[84:85], 0, s[64:65]
	s_add_i32 s64, s20, -6
	s_ashr_i32 s65, s64, 31
	s_lshl_b64 s[64:65], s[64:65], 10
	v_lshl_add_u64 v[10:11], v[84:85], 0, s[64:65]
	s_add_i32 s64, s20, -5
	s_ashr_i32 s65, s64, 31
	s_lshl_b64 s[64:65], s[64:65], 10
	v_lshl_add_u64 v[14:15], v[84:85], 0, s[64:65]
	s_add_i32 s64, s20, -4
	s_ashr_i32 s65, s64, 31
	s_lshl_b64 s[64:65], s[64:65], 10
	v_lshl_add_u64 v[18:19], v[84:85], 0, s[64:65]
	s_add_i32 s64, s20, -3
	s_ashr_i32 s65, s64, 31
	s_lshl_b64 s[64:65], s[64:65], 10
	v_lshl_add_u64 v[22:23], v[84:85], 0, s[64:65]
	s_add_i32 s64, s20, -2
	global_load_dwordx4 v[6:9], v[6:7], off
	s_ashr_i32 s65, s64, 31
	global_load_dwordx4 v[10:13], v[10:11], off
	s_lshl_b64 s[64:65], s[64:65], 10
	global_load_dwordx4 v[14:17], v[14:15], off
	v_lshl_add_u64 v[30:31], v[84:85], 0, s[64:65]
	s_add_i32 s64, s20, -1
	global_load_dwordx4 v[18:21], v[18:19], off
	s_ashr_i32 s65, s64, 31
	global_load_dwordx4 v[22:25], v[22:23], off
	s_lshl_b64 s[64:65], s[64:65], 10
	s_ashr_i32 s21, s20, 31
	global_load_dwordx4 v[30:33], v[30:31], off
	v_lshl_add_u64 v[34:35], v[84:85], 0, s[64:65]
	s_lshl_b64 s[20:21], s[20:21], 10
	global_load_dwordx4 v[34:37], v[34:35], off
	v_lshl_add_u64 v[38:39], v[84:85], 0, s[20:21]
	global_load_dwordx4 v[38:41], v[38:39], off
	s_add_i32 s39, s39, 2
	s_add_i32 s42, s42, 16
	s_waitcnt vmcnt(41)
	v_cvt_pk_f32_fp8_e32 v[88:89], v166
	v_cvt_pk_f32_fp8_sdwa v[90:91], v166 src0_sel:WORD_1
	v_pk_add_f32 v[88:89], v[88:89], 0 op_sel_hi:[1,0]
	s_waitcnt vmcnt(40)
	v_cvt_pk_f32_fp8_e32 v[92:93], v170
	v_cvt_pk_f32_fp8_sdwa v[94:95], v170 src0_sel:WORD_1
	v_pk_add_f32 v[88:89], v[88:89], v[92:93]
	s_waitcnt vmcnt(39)
	v_cvt_pk_f32_fp8_e32 v[96:97], v174
	v_lshlrev_b32_e32 v92, 16, v182
	v_and_b32_e32 v93, 0xffff0000, v182
	v_cvt_pk_f32_fp8_sdwa v[98:99], v174 src0_sel:WORD_1
	v_pk_add_f32 v[88:89], v[88:89], v[96:97]
	s_waitcnt vmcnt(38)
	v_cvt_pk_f32_fp8_e32 v[100:101], v178
	v_pk_mul_f32 v[92:93], v[92:93], s[78:79] op_sel_hi:[1,0]
	v_cvt_pk_f32_fp8_sdwa v[102:103], v178 src0_sel:WORD_1
	v_pk_add_f32 v[88:89], v[88:89], v[100:101]
	s_waitcnt vmcnt(37)
	v_cvt_pk_f32_fp8_e32 v[104:105], v186
	v_cvt_pk_f32_fp8_sdwa v[106:107], v186 src0_sel:WORD_1
	v_cvt_pk_f32_fp8_e32 v[96:97], v187
	v_cvt_pk_f32_fp8_sdwa v[186:187], v187 src0_sel:WORD_1
	v_pk_add_f32 v[88:89], v[88:89], v[104:105]
	s_waitcnt vmcnt(36)
	v_cvt_pk_f32_fp8_e32 v[108:109], v190
	v_cvt_pk_f32_fp8_sdwa v[110:111], v190 src0_sel:WORD_1
	v_pk_add_f32 v[88:89], v[88:89], v[108:109]
	s_waitcnt vmcnt(35)
	v_cvt_pk_f32_fp8_e32 v[112:113], v194
	v_cvt_pk_f32_fp8_sdwa v[114:115], v194 src0_sel:WORD_1
	s_waitcnt vmcnt(34)
	v_cvt_pk_f32_fp8_e32 v[116:117], v198
	v_cvt_pk_f32_fp8_sdwa v[118:119], v198 src0_sel:WORD_1
	v_pk_add_f32 v[88:89], v[88:89], v[112:113]
	v_cvt_pk_f32_fp8_e32 v[100:101], v195
	v_pk_add_f32 v[88:89], v[88:89], v[116:117]
	v_cvt_pk_f32_fp8_sdwa v[194:195], v195 src0_sel:WORD_1
	v_pk_fma_f32 v[88:89], v[88:89], s[80:81], v[92:93] op_sel_hi:[1,0,1]
	v_cvt_pk_f32_fp8_e32 v[92:93], v175
	v_cvt_pk_bf16_f32 v182, v88, v89
	v_pk_add_f32 v[88:89], v[90:91], 0 op_sel_hi:[1,0]
	v_lshlrev_b32_e32 v90, 16, v183
	v_pk_add_f32 v[88:89], v[88:89], v[94:95]
	v_and_b32_e32 v91, 0xffff0000, v183
	v_pk_add_f32 v[88:89], v[88:89], v[98:99]
	v_pk_mul_f32 v[90:91], v[90:91], s[78:79] op_sel_hi:[1,0]
	v_pk_add_f32 v[88:89], v[88:89], v[102:103]
	v_cvt_pk_f32_fp8_sdwa v[174:175], v175 src0_sel:WORD_1
	v_pk_add_f32 v[88:89], v[88:89], v[106:107]
	v_cvt_pk_f32_fp8_e32 v[94:95], v179
	v_pk_add_f32 v[88:89], v[88:89], v[110:111]
	v_cvt_pk_f32_fp8_sdwa v[178:179], v179 src0_sel:WORD_1
	v_pk_add_f32 v[88:89], v[88:89], v[114:115]
	v_cvt_pk_f32_fp8_e32 v[98:99], v191
	v_pk_add_f32 v[88:89], v[88:89], v[118:119]
	v_cvt_pk_f32_fp8_sdwa v[190:191], v191 src0_sel:WORD_1
	v_pk_fma_f32 v[88:89], v[88:89], s[80:81], v[90:91] op_sel_hi:[1,0,1]
	v_cvt_pk_f32_fp8_e32 v[90:91], v171
	v_cvt_pk_bf16_f32 v183, v88, v89
	v_cvt_pk_f32_fp8_e32 v[88:89], v167
	v_cvt_pk_f32_fp8_sdwa v[166:167], v167 src0_sel:WORD_1
	v_cvt_pk_f32_fp8_sdwa v[170:171], v171 src0_sel:WORD_1
	v_cvt_pk_f32_fp8_e32 v[102:103], v199
	v_pk_add_f32 v[88:89], v[88:89], 0 op_sel_hi:[1,0]
	v_pk_add_f32 v[166:167], v[166:167], 0 op_sel_hi:[1,0]
	v_pk_add_f32 v[88:89], v[88:89], v[90:91]
	v_pk_add_f32 v[166:167], v[166:167], v[170:171]
	v_pk_add_f32 v[88:89], v[88:89], v[92:93]
	v_pk_add_f32 v[166:167], v[166:167], v[174:175]
	v_cvt_pk_f32_fp8_sdwa v[198:199], v199 src0_sel:WORD_1
	v_pk_add_f32 v[88:89], v[88:89], v[94:95]
	v_pk_add_f32 v[166:167], v[166:167], v[178:179]
	v_pk_add_f32 v[88:89], v[88:89], v[96:97]
	v_pk_add_f32 v[166:167], v[166:167], v[186:187]
	v_pk_add_f32 v[88:89], v[88:89], v[98:99]
	v_pk_add_f32 v[166:167], v[166:167], v[190:191]
	v_pk_add_f32 v[88:89], v[88:89], v[100:101]
	v_lshlrev_b32_e32 v90, 16, v184
	v_and_b32_e32 v91, 0xffff0000, v184
	v_pk_add_f32 v[166:167], v[166:167], v[194:195]
	v_lshlrev_b32_e32 v170, 16, v185
	v_and_b32_e32 v171, 0xffff0000, v185
	v_pk_add_f32 v[88:89], v[88:89], v[102:103]
	v_pk_mul_f32 v[90:91], v[90:91], s[78:79] op_sel_hi:[1,0]
	v_pk_add_f32 v[166:167], v[166:167], v[198:199]
	v_pk_mul_f32 v[170:171], v[170:171], s[78:79] op_sel_hi:[1,0]
	v_pk_fma_f32 v[88:89], v[88:89], s[80:81], v[90:91] op_sel_hi:[1,0,1]
	v_pk_fma_f32 v[166:167], v[166:167], s[80:81], v[170:171] op_sel_hi:[1,0,1]
	v_cvt_pk_f32_fp8_e32 v[170:171], v168
	v_cvt_pk_bf16_f32 v184, v88, v89
	v_cvt_pk_bf16_f32 v185, v166, v167
	v_lshl_add_u64 v[166:167], v[86:87], 0, s[100:101]
	v_cvt_pk_f32_fp8_e32 v[178:179], v172
	global_store_dwordx4 v[166:167], v[182:185], off
	v_cvt_pk_f32_fp8_e32 v[190:191], v180
	v_cvt_pk_f32_fp8_e32 v[198:199], v188
	v_cvt_pk_f32_fp8_e32 v[184:185], v176
	v_pk_add_f32 v[170:171], v[170:171], 0 op_sel_hi:[1,0]
	v_cvt_pk_f32_fp8_e32 v[90:91], v192
	v_pk_add_f32 v[170:171], v[170:171], v[178:179]
	v_cvt_pk_f32_fp8_e32 v[94:95], v196
	v_pk_add_f32 v[170:171], v[170:171], v[184:185]
	v_cvt_pk_f32_fp8_e32 v[98:99], v200
	v_pk_add_f32 v[170:171], v[170:171], v[190:191]
	v_cvt_pk_f32_fp8_sdwa v[174:175], v168 src0_sel:WORD_1
	v_pk_add_f32 v[170:171], v[170:171], v[198:199]
	v_cvt_pk_f32_fp8_sdwa v[182:183], v172 src0_sel:WORD_1
	v_pk_add_f32 v[170:171], v[170:171], v[90:91]
	v_lshlrev_b32_e32 v178, 16, v162
	v_pk_add_f32 v[170:171], v[170:171], v[94:95]
	v_and_b32_e32 v179, 0xffff0000, v162
	v_cvt_pk_f32_fp8_sdwa v[186:187], v176 src0_sel:WORD_1
	v_pk_add_f32 v[170:171], v[170:171], v[98:99]
	v_pk_mul_f32 v[178:179], v[178:179], s[78:79] op_sel_hi:[1,0]
	v_cvt_pk_f32_fp8_sdwa v[194:195], v180 src0_sel:WORD_1
	v_pk_fma_f32 v[170:171], v[170:171], s[80:81], v[178:179] op_sel_hi:[1,0,1]
	v_cvt_pk_f32_fp8_sdwa v[88:89], v188 src0_sel:WORD_1
	v_cvt_pk_bf16_f32 v162, v170, v171
	v_pk_add_f32 v[170:171], v[174:175], 0 op_sel_hi:[1,0]
	v_cvt_pk_f32_fp8_sdwa v[92:93], v192 src0_sel:WORD_1
	v_pk_add_f32 v[170:171], v[170:171], v[182:183]
	v_cvt_pk_f32_fp8_sdwa v[96:97], v196 src0_sel:WORD_1
	v_pk_add_f32 v[170:171], v[170:171], v[186:187]
	v_cvt_pk_f32_fp8_sdwa v[100:101], v200 src0_sel:WORD_1
	v_pk_add_f32 v[170:171], v[170:171], v[194:195]
	v_lshlrev_b32_e32 v174, 16, v163
	v_pk_add_f32 v[170:171], v[170:171], v[88:89]
	v_and_b32_e32 v175, 0xffff0000, v163
	v_pk_add_f32 v[170:171], v[170:171], v[92:93]
	v_pk_mul_f32 v[174:175], v[174:175], s[78:79] op_sel_hi:[1,0]
	v_pk_add_f32 v[170:171], v[170:171], v[96:97]
	v_cvt_pk_f32_fp8_e32 v[178:179], v177
	v_pk_add_f32 v[170:171], v[170:171], v[100:101]
	v_cvt_pk_f32_fp8_e32 v[182:183], v181
	v_pk_fma_f32 v[170:171], v[170:171], s[80:81], v[174:175] op_sel_hi:[1,0,1]
	v_cvt_pk_f32_fp8_e32 v[174:175], v173
	v_cvt_pk_bf16_f32 v163, v170, v171
	v_cvt_pk_f32_fp8_e32 v[170:171], v169
	v_cvt_pk_f32_fp8_sdwa v[168:169], v169 src0_sel:WORD_1
	v_cvt_pk_f32_fp8_sdwa v[172:173], v173 src0_sel:WORD_1
	v_cvt_pk_f32_fp8_e32 v[184:185], v189
	v_pk_add_f32 v[170:171], v[170:171], 0 op_sel_hi:[1,0]
	v_cvt_pk_f32_fp8_sdwa v[176:177], v177 src0_sel:WORD_1
	v_cvt_pk_f32_fp8_sdwa v[186:187], v189 src0_sel:WORD_1
	v_cvt_pk_f32_fp8_e32 v[188:189], v193
	v_pk_add_f32 v[170:171], v[170:171], v[174:175]
	v_cvt_pk_f32_fp8_sdwa v[180:181], v181 src0_sel:WORD_1
	v_cvt_pk_f32_fp8_sdwa v[190:191], v193 src0_sel:WORD_1
	v_cvt_pk_f32_fp8_e32 v[192:193], v197
	v_pk_add_f32 v[170:171], v[170:171], v[178:179]
	v_cvt_pk_f32_fp8_sdwa v[194:195], v197 src0_sel:WORD_1
	v_cvt_pk_f32_fp8_e32 v[196:197], v201
	v_pk_add_f32 v[170:171], v[170:171], v[182:183]
	v_pk_add_f32 v[168:169], v[168:169], 0 op_sel_hi:[1,0]
	v_pk_add_f32 v[170:171], v[170:171], v[184:185]
	v_pk_add_f32 v[168:169], v[168:169], v[172:173]
	v_pk_add_f32 v[170:171], v[170:171], v[188:189]
	v_pk_add_f32 v[168:169], v[168:169], v[176:177]
	v_cvt_pk_f32_fp8_sdwa v[198:199], v201 src0_sel:WORD_1
	v_pk_add_f32 v[170:171], v[170:171], v[192:193]
	v_lshlrev_b32_e32 v174, 16, v164
	v_and_b32_e32 v175, 0xffff0000, v164
	v_pk_add_f32 v[168:169], v[168:169], v[180:181]
	v_pk_add_f32 v[170:171], v[170:171], v[196:197]
	v_pk_mul_f32 v[174:175], v[174:175], s[78:79] op_sel_hi:[1,0]
	v_pk_add_f32 v[168:169], v[168:169], v[186:187]
	v_pk_fma_f32 v[170:171], v[170:171], s[80:81], v[174:175] op_sel_hi:[1,0,1]
	v_pk_add_f32 v[168:169], v[168:169], v[190:191]
	v_cvt_pk_bf16_f32 v164, v170, v171
	v_pk_add_f32 v[168:169], v[168:169], v[194:195]
	v_lshlrev_b32_e32 v170, 16, v165
	v_and_b32_e32 v171, 0xffff0000, v165
	v_pk_add_f32 v[168:169], v[168:169], v[198:199]
	v_pk_mul_f32 v[170:171], v[170:171], s[78:79] op_sel_hi:[1,0]
	s_waitcnt vmcnt(27)
	v_cvt_pk_f32_fp8_sdwa v[172:173], v150 src0_sel:WORD_1
	v_pk_fma_f32 v[168:169], v[168:169], s[80:81], v[170:171] op_sel_hi:[1,0,1]
	v_cvt_pk_f32_fp8_sdwa v[170:171], v142 src0_sel:WORD_1
	v_cvt_pk_bf16_f32 v165, v168, v169
	global_store_dwordx4 v[166:167], v[162:165], off offset:16
	v_cvt_pk_f32_fp8_sdwa v[166:167], v134 src0_sel:WORD_1
	v_cvt_pk_f32_fp8_sdwa v[168:169], v138 src0_sel:WORD_1
	v_cvt_pk_f32_fp8_sdwa v[162:163], v126 src0_sel:WORD_1
	v_cvt_pk_f32_fp8_sdwa v[164:165], v130 src0_sel:WORD_1
	s_waitcnt vmcnt(27)
	v_cvt_pk_f32_fp8_sdwa v[174:175], v154 src0_sel:WORD_1
	s_waitcnt vmcnt(26)
	v_cvt_pk_f32_fp8_sdwa v[176:177], v158 src0_sel:WORD_1
	v_pk_add_f32 v[162:163], v[162:163], 0 op_sel_hi:[1,0]
	v_cvt_pk_f32_fp8_e32 v[178:179], v126
	v_pk_add_f32 v[162:163], v[162:163], v[164:165]
	v_lshlrev_b32_e32 v164, 16, v147
	v_pk_add_f32 v[162:163], v[162:163], v[166:167]
	v_and_b32_e32 v165, 0xffff0000, v147
	v_pk_add_f32 v[162:163], v[162:163], v[168:169]
	v_pk_mul_f32 v[164:165], v[164:165], s[78:79] op_sel_hi:[1,0]
	v_pk_add_f32 v[162:163], v[162:163], v[170:171]
	v_cvt_pk_f32_fp8_e32 v[180:181], v130
	v_pk_add_f32 v[162:163], v[162:163], v[172:173]
	v_cvt_pk_f32_fp8_e32 v[182:183], v134
	v_pk_add_f32 v[162:163], v[162:163], v[174:175]
	v_cvt_pk_f32_fp8_e32 v[166:167], v135
	v_pk_add_f32 v[162:163], v[162:163], v[176:177]
	v_cvt_pk_f32_fp8_sdwa v[134:135], v135 src0_sel:WORD_1
	v_pk_fma_f32 v[162:163], v[162:163], s[80:81], v[164:165] op_sel_hi:[1,0,1]
	v_cvt_pk_f32_fp8_e32 v[164:165], v131
	v_cvt_pk_bf16_f32 v147, v162, v163
	v_cvt_pk_f32_fp8_e32 v[162:163], v127
	v_cvt_pk_f32_fp8_sdwa v[126:127], v127 src0_sel:WORD_1
	v_cvt_pk_f32_fp8_sdwa v[130:131], v131 src0_sel:WORD_1
	v_cvt_pk_f32_fp8_e32 v[184:185], v138
	v_cvt_pk_f32_fp8_e32 v[168:169], v139
	v_cvt_pk_f32_fp8_sdwa v[138:139], v139 src0_sel:WORD_1
	v_cvt_pk_f32_fp8_e32 v[186:187], v142
	v_pk_add_f32 v[178:179], v[178:179], 0 op_sel_hi:[1,0]
	v_cvt_pk_f32_fp8_e32 v[170:171], v143
	v_cvt_pk_f32_fp8_sdwa v[142:143], v143 src0_sel:WORD_1
	v_pk_add_f32 v[162:163], v[162:163], 0 op_sel_hi:[1,0]
	v_pk_add_f32 v[126:127], v[126:127], 0 op_sel_hi:[1,0]
	v_cvt_pk_f32_fp8_e32 v[188:189], v150
	v_pk_add_f32 v[178:179], v[178:179], v[180:181]
	v_cvt_pk_f32_fp8_e32 v[172:173], v151
	v_cvt_pk_f32_fp8_sdwa v[150:151], v151 src0_sel:WORD_1
	v_pk_add_f32 v[162:163], v[162:163], v[164:165]
	v_pk_add_f32 v[126:127], v[126:127], v[130:131]
	v_cvt_pk_f32_fp8_e32 v[190:191], v154
	v_pk_add_f32 v[178:179], v[178:179], v[182:183]
	v_cvt_pk_f32_fp8_e32 v[174:175], v155
	v_cvt_pk_f32_fp8_sdwa v[154:155], v155 src0_sel:WORD_1
	v_pk_add_f32 v[162:163], v[162:163], v[166:167]
	v_pk_add_f32 v[126:127], v[126:127], v[134:135]
	v_cvt_pk_f32_fp8_e32 v[192:193], v158
	v_pk_add_f32 v[178:179], v[178:179], v[184:185]
	v_cvt_pk_f32_fp8_e32 v[176:177], v159
	v_cvt_pk_f32_fp8_sdwa v[158:159], v159 src0_sel:WORD_1
	v_pk_add_f32 v[162:163], v[162:163], v[168:169]
	v_pk_add_f32 v[126:127], v[126:127], v[138:139]
	v_pk_add_f32 v[178:179], v[178:179], v[186:187]
	v_pk_add_f32 v[162:163], v[162:163], v[170:171]
	v_pk_add_f32 v[126:127], v[126:127], v[142:143]
	v_pk_add_f32 v[178:179], v[178:179], v[188:189]
	v_pk_add_f32 v[162:163], v[162:163], v[172:173]
	v_pk_add_f32 v[126:127], v[126:127], v[150:151]
	v_pk_add_f32 v[178:179], v[178:179], v[190:191]
	v_lshlrev_b32_e32 v180, 16, v146
	v_and_b32_e32 v181, 0xffff0000, v146
	v_pk_add_f32 v[162:163], v[162:163], v[174:175]
	v_lshlrev_b32_e32 v164, 16, v148
	v_and_b32_e32 v165, 0xffff0000, v148
	v_pk_add_f32 v[126:127], v[126:127], v[154:155]
	v_lshlrev_b32_e32 v130, 16, v149
	v_and_b32_e32 v131, 0xffff0000, v149
	v_pk_add_f32 v[178:179], v[178:179], v[192:193]
	v_pk_mul_f32 v[180:181], v[180:181], s[78:79] op_sel_hi:[1,0]
	v_pk_add_f32 v[162:163], v[162:163], v[176:177]
	v_pk_mul_f32 v[164:165], v[164:165], s[78:79] op_sel_hi:[1,0]
	v_pk_add_f32 v[126:127], v[126:127], v[158:159]
	v_pk_mul_f32 v[130:131], v[130:131], s[78:79] op_sel_hi:[1,0]
	v_pk_fma_f32 v[178:179], v[178:179], s[80:81], v[180:181] op_sel_hi:[1,0,1]
	v_pk_fma_f32 v[162:163], v[162:163], s[80:81], v[164:165] op_sel_hi:[1,0,1]
	v_pk_fma_f32 v[126:127], v[126:127], s[80:81], v[130:131] op_sel_hi:[1,0,1]
	v_cvt_pk_f32_fp8_e32 v[130:131], v128
	v_cvt_pk_bf16_f32 v146, v178, v179
	v_cvt_pk_bf16_f32 v148, v162, v163
	v_cvt_pk_bf16_f32 v149, v126, v127
	v_lshl_add_u64 v[126:127], v[86:87], 0, s[98:99]
	v_cvt_pk_f32_fp8_e32 v[138:139], v132
	global_store_dwordx4 v[126:127], v[146:149], off
	v_cvt_pk_f32_fp8_e32 v[150:151], v140
	v_cvt_pk_f32_fp8_e32 v[158:159], v144
	v_cvt_pk_f32_fp8_e32 v[146:147], v136
	v_pk_add_f32 v[130:131], v[130:131], 0 op_sel_hi:[1,0]
	v_cvt_pk_f32_fp8_e32 v[164:165], v152
	v_pk_add_f32 v[130:131], v[130:131], v[138:139]
	v_cvt_pk_f32_fp8_e32 v[168:169], v156
	v_pk_add_f32 v[130:131], v[130:131], v[146:147]
	v_cvt_pk_f32_fp8_e32 v[172:173], v160
	v_pk_add_f32 v[130:131], v[130:131], v[150:151]
	v_cvt_pk_f32_fp8_sdwa v[134:135], v128 src0_sel:WORD_1
	v_pk_add_f32 v[130:131], v[130:131], v[158:159]
	v_cvt_pk_f32_fp8_sdwa v[142:143], v132 src0_sel:WORD_1
	v_pk_add_f32 v[130:131], v[130:131], v[164:165]
	v_lshlrev_b32_e32 v138, 16, v122
	v_pk_add_f32 v[130:131], v[130:131], v[168:169]
	v_and_b32_e32 v139, 0xffff0000, v122
	v_cvt_pk_f32_fp8_sdwa v[148:149], v136 src0_sel:WORD_1
	v_pk_add_f32 v[130:131], v[130:131], v[172:173]
	v_pk_mul_f32 v[138:139], v[138:139], s[78:79] op_sel_hi:[1,0]
	v_cvt_pk_f32_fp8_sdwa v[154:155], v140 src0_sel:WORD_1
	v_pk_fma_f32 v[130:131], v[130:131], s[80:81], v[138:139] op_sel_hi:[1,0,1]
	v_cvt_pk_f32_fp8_sdwa v[162:163], v144 src0_sel:WORD_1
	v_cvt_pk_bf16_f32 v122, v130, v131
	v_pk_add_f32 v[130:131], v[134:135], 0 op_sel_hi:[1,0]
	v_cvt_pk_f32_fp8_sdwa v[166:167], v152 src0_sel:WORD_1
	v_pk_add_f32 v[130:131], v[130:131], v[142:143]
	v_cvt_pk_f32_fp8_sdwa v[170:171], v156 src0_sel:WORD_1
	v_pk_add_f32 v[130:131], v[130:131], v[148:149]
	v_cvt_pk_f32_fp8_sdwa v[174:175], v160 src0_sel:WORD_1
	v_pk_add_f32 v[130:131], v[130:131], v[154:155]
	v_lshlrev_b32_e32 v134, 16, v123
	v_pk_add_f32 v[130:131], v[130:131], v[162:163]
	v_and_b32_e32 v135, 0xffff0000, v123
	v_pk_add_f32 v[130:131], v[130:131], v[166:167]
	v_pk_mul_f32 v[134:135], v[134:135], s[78:79] op_sel_hi:[1,0]
	v_pk_add_f32 v[130:131], v[130:131], v[170:171]
	v_cvt_pk_f32_fp8_e32 v[146:147], v129
	v_pk_add_f32 v[130:131], v[130:131], v[174:175]
	v_cvt_pk_f32_fp8_sdwa v[128:129], v129 src0_sel:WORD_1
	v_pk_fma_f32 v[130:131], v[130:131], s[80:81], v[134:135] op_sel_hi:[1,0,1]
	v_cvt_pk_f32_fp8_e32 v[148:149], v133
	v_cvt_pk_bf16_f32 v123, v130, v131
	v_cvt_pk_f32_fp8_sdwa v[130:131], v133 src0_sel:WORD_1
	v_cvt_pk_f32_fp8_e32 v[150:151], v137
	v_cvt_pk_f32_fp8_sdwa v[132:133], v137 src0_sel:WORD_1
	v_cvt_pk_f32_fp8_e32 v[154:155], v141
	v_cvt_pk_f32_fp8_sdwa v[134:135], v141 src0_sel:WORD_1
	v_cvt_pk_f32_fp8_e32 v[158:159], v145
	v_cvt_pk_f32_fp8_sdwa v[136:137], v145 src0_sel:WORD_1
	v_pk_add_f32 v[146:147], v[146:147], 0 op_sel_hi:[1,0]
	v_pk_add_f32 v[128:129], v[128:129], 0 op_sel_hi:[1,0]
	v_cvt_pk_f32_fp8_e32 v[144:145], v153
	v_cvt_pk_f32_fp8_sdwa v[138:139], v153 src0_sel:WORD_1
	v_pk_add_f32 v[146:147], v[146:147], v[148:149]
	v_pk_add_f32 v[128:129], v[128:129], v[130:131]
	v_cvt_pk_f32_fp8_e32 v[152:153], v157
	v_cvt_pk_f32_fp8_sdwa v[140:141], v157 src0_sel:WORD_1
	v_pk_add_f32 v[146:147], v[146:147], v[150:151]
	v_pk_add_f32 v[128:129], v[128:129], v[132:133]
	v_cvt_pk_f32_fp8_e32 v[156:157], v161
	v_cvt_pk_f32_fp8_sdwa v[142:143], v161 src0_sel:WORD_1
	v_pk_add_f32 v[146:147], v[146:147], v[154:155]
	v_pk_add_f32 v[128:129], v[128:129], v[134:135]
	v_pk_add_f32 v[146:147], v[146:147], v[158:159]
	v_pk_add_f32 v[128:129], v[128:129], v[136:137]
	v_pk_add_f32 v[144:145], v[146:147], v[144:145]
	v_pk_add_f32 v[128:129], v[128:129], v[138:139]
	v_pk_add_f32 v[144:145], v[144:145], v[152:153]
	v_lshlrev_b32_e32 v146, 16, v124
	v_and_b32_e32 v147, 0xffff0000, v124
	v_pk_add_f32 v[128:129], v[128:129], v[140:141]
	v_lshlrev_b32_e32 v130, 16, v125
	v_and_b32_e32 v131, 0xffff0000, v125
	v_pk_add_f32 v[144:145], v[144:145], v[156:157]
	v_pk_mul_f32 v[146:147], v[146:147], s[78:79] op_sel_hi:[1,0]
	v_pk_add_f32 v[128:129], v[128:129], v[142:143]
	v_pk_mul_f32 v[130:131], v[130:131], s[78:79] op_sel_hi:[1,0]
	v_pk_fma_f32 v[144:145], v[144:145], s[80:81], v[146:147] op_sel_hi:[1,0,1]
	v_pk_fma_f32 v[128:129], v[128:129], s[80:81], v[130:131] op_sel_hi:[1,0,1]
	v_cvt_pk_bf16_f32 v124, v144, v145
	v_cvt_pk_bf16_f32 v125, v128, v129
	global_store_dwordx4 v[126:127], v[122:125], off offset:16
	s_add_i32 s98, s37, s39
	s_add_i32 s100, s98, 2
	s_add_i32 s20, s23, s42
	s_ashr_i32 s101, s100, 31
	s_add_i32 s64, s20, -15
	s_lshl_b64 s[100:101], s[100:101], 11
	s_ashr_i32 s65, s64, 31
	v_lshl_add_u64 v[122:123], v[82:83], 0, s[100:101]
	s_lshl_b64 s[64:65], s[64:65], 10
	global_load_dwordx4 v[162:165], v[122:123], off offset:16
	global_load_dwordx4 v[182:185], v[122:123], off
	v_lshl_add_u64 v[122:123], v[84:85], 0, s[64:65]
	s_add_i32 s64, s20, -14
	s_ashr_i32 s65, s64, 31
	s_lshl_b64 s[64:65], s[64:65], 10
	global_load_dwordx4 v[166:169], v[122:123], off
	v_lshl_add_u64 v[122:123], v[84:85], 0, s[64:65]
	s_add_i32 s64, s20, -13
	s_ashr_i32 s65, s64, 31
	s_lshl_b64 s[64:65], s[64:65], 10
	global_load_dwordx4 v[170:173], v[122:123], off
	v_lshl_add_u64 v[122:123], v[84:85], 0, s[64:65]
	s_add_i32 s64, s20, -12
	s_ashr_i32 s65, s64, 31
	s_lshl_b64 s[64:65], s[64:65], 10
	global_load_dwordx4 v[174:177], v[122:123], off
	v_lshl_add_u64 v[122:123], v[84:85], 0, s[64:65]
	s_add_i32 s64, s20, -11
	s_ashr_i32 s65, s64, 31
	s_lshl_b64 s[64:65], s[64:65], 10
	global_load_dwordx4 v[178:181], v[122:123], off
	v_lshl_add_u64 v[122:123], v[84:85], 0, s[64:65]
	s_add_i32 s64, s20, -10
	s_ashr_i32 s65, s64, 31
	s_lshl_b64 s[64:65], s[64:65], 10
	global_load_dwordx4 v[186:189], v[122:123], off
	v_lshl_add_u64 v[122:123], v[84:85], 0, s[64:65]
	s_add_i32 s64, s20, -9
	s_ashr_i32 s65, s64, 31
	s_lshl_b64 s[64:65], s[64:65], 10
	global_load_dwordx4 v[190:193], v[122:123], off
	v_lshl_add_u64 v[122:123], v[84:85], 0, s[64:65]
	s_add_i32 s64, s20, -8
	s_ashr_i32 s65, s64, 31
	s_lshl_b64 s[64:65], s[64:65], 10
	global_load_dwordx4 v[194:197], v[122:123], off
	v_lshl_add_u64 v[122:123], v[84:85], 0, s[64:65]
	global_load_dwordx4 v[198:201], v[122:123], off
	s_add_i32 s98, s98, 3
	s_ashr_i32 s99, s98, 31
	s_add_i32 s64, s20, -7
	s_lshl_b64 s[98:99], s[98:99], 11
	s_ashr_i32 s65, s64, 31
	v_lshl_add_u64 v[126:127], v[82:83], 0, s[98:99]
	s_lshl_b64 s[64:65], s[64:65], 10
	global_load_dwordx4 v[122:125], v[126:127], off offset:16
	global_load_dwordx4 v[146:149], v[126:127], off
	v_lshl_add_u64 v[126:127], v[84:85], 0, s[64:65]
	s_add_i32 s64, s20, -6
	s_ashr_i32 s65, s64, 31
	s_lshl_b64 s[64:65], s[64:65], 10
	v_lshl_add_u64 v[130:131], v[84:85], 0, s[64:65]
	s_add_i32 s64, s20, -5
	s_ashr_i32 s65, s64, 31
	s_lshl_b64 s[64:65], s[64:65], 10
	v_lshl_add_u64 v[134:135], v[84:85], 0, s[64:65]
	s_add_i32 s64, s20, -4
	s_ashr_i32 s65, s64, 31
	s_lshl_b64 s[64:65], s[64:65], 10
	v_lshl_add_u64 v[138:139], v[84:85], 0, s[64:65]
	s_add_i32 s64, s20, -3
	s_ashr_i32 s65, s64, 31
	s_lshl_b64 s[64:65], s[64:65], 10
	v_lshl_add_u64 v[142:143], v[84:85], 0, s[64:65]
	s_add_i32 s64, s20, -2
	global_load_dwordx4 v[126:129], v[126:127], off
	s_ashr_i32 s65, s64, 31
	global_load_dwordx4 v[130:133], v[130:131], off
	s_lshl_b64 s[64:65], s[64:65], 10
	global_load_dwordx4 v[134:137], v[134:135], off
	v_lshl_add_u64 v[150:151], v[84:85], 0, s[64:65]
	s_add_i32 s64, s20, -1
	global_load_dwordx4 v[138:141], v[138:139], off
	s_ashr_i32 s65, s64, 31
	global_load_dwordx4 v[142:145], v[142:143], off
	s_lshl_b64 s[64:65], s[64:65], 10
	s_ashr_i32 s21, s20, 31
	global_load_dwordx4 v[150:153], v[150:151], off
	v_lshl_add_u64 v[154:155], v[84:85], 0, s[64:65]
	s_lshl_b64 s[20:21], s[20:21], 10
	global_load_dwordx4 v[154:157], v[154:155], off
	v_lshl_add_u64 v[158:159], v[84:85], 0, s[20:21]
	global_load_dwordx4 v[158:161], v[158:159], off
	s_add_i32 s39, s39, 2
	s_add_i32 s42, s42, 16
	s_waitcnt vmcnt(41)
	v_cvt_pk_f32_fp8_e32 v[88:89], v46
	v_cvt_pk_f32_fp8_sdwa v[90:91], v46 src0_sel:WORD_1
	v_pk_add_f32 v[88:89], v[88:89], 0 op_sel_hi:[1,0]
	s_waitcnt vmcnt(40)
	v_cvt_pk_f32_fp8_e32 v[92:93], v50
	v_cvt_pk_f32_fp8_sdwa v[94:95], v50 src0_sel:WORD_1
	v_pk_add_f32 v[88:89], v[88:89], v[92:93]
	s_waitcnt vmcnt(39)
	v_cvt_pk_f32_fp8_e32 v[96:97], v54
	v_lshlrev_b32_e32 v92, 16, v62
	v_and_b32_e32 v93, 0xffff0000, v62
	v_cvt_pk_f32_fp8_sdwa v[98:99], v54 src0_sel:WORD_1
	v_pk_add_f32 v[88:89], v[88:89], v[96:97]
	s_waitcnt vmcnt(38)
	v_cvt_pk_f32_fp8_e32 v[100:101], v58
	v_pk_mul_f32 v[92:93], v[92:93], s[78:79] op_sel_hi:[1,0]
	v_cvt_pk_f32_fp8_sdwa v[102:103], v58 src0_sel:WORD_1
	v_pk_add_f32 v[88:89], v[88:89], v[100:101]
	s_waitcnt vmcnt(37)
	v_cvt_pk_f32_fp8_e32 v[104:105], v66
	v_cvt_pk_f32_fp8_sdwa v[106:107], v66 src0_sel:WORD_1
	v_cvt_pk_f32_fp8_e32 v[96:97], v67
	v_cvt_pk_f32_fp8_sdwa v[66:67], v67 src0_sel:WORD_1
	v_pk_add_f32 v[88:89], v[88:89], v[104:105]
	s_waitcnt vmcnt(36)
	v_cvt_pk_f32_fp8_e32 v[108:109], v70
	v_cvt_pk_f32_fp8_sdwa v[110:111], v70 src0_sel:WORD_1
	v_pk_add_f32 v[88:89], v[88:89], v[108:109]
	s_waitcnt vmcnt(35)
	v_cvt_pk_f32_fp8_e32 v[112:113], v74
	v_cvt_pk_f32_fp8_sdwa v[114:115], v74 src0_sel:WORD_1
	s_waitcnt vmcnt(34)
	v_cvt_pk_f32_fp8_e32 v[116:117], v78
	v_cvt_pk_f32_fp8_sdwa v[118:119], v78 src0_sel:WORD_1
	v_pk_add_f32 v[88:89], v[88:89], v[112:113]
	v_cvt_pk_f32_fp8_e32 v[100:101], v75
	v_pk_add_f32 v[88:89], v[88:89], v[116:117]
	v_cvt_pk_f32_fp8_sdwa v[74:75], v75 src0_sel:WORD_1
	v_pk_fma_f32 v[88:89], v[88:89], s[80:81], v[92:93] op_sel_hi:[1,0,1]
	v_cvt_pk_f32_fp8_e32 v[92:93], v55
	v_cvt_pk_bf16_f32 v62, v88, v89
	v_pk_add_f32 v[88:89], v[90:91], 0 op_sel_hi:[1,0]
	v_lshlrev_b32_e32 v90, 16, v63
	v_pk_add_f32 v[88:89], v[88:89], v[94:95]
	v_and_b32_e32 v91, 0xffff0000, v63
	v_pk_add_f32 v[88:89], v[88:89], v[98:99]
	v_pk_mul_f32 v[90:91], v[90:91], s[78:79] op_sel_hi:[1,0]
	v_pk_add_f32 v[88:89], v[88:89], v[102:103]
	v_cvt_pk_f32_fp8_sdwa v[54:55], v55 src0_sel:WORD_1
	v_pk_add_f32 v[88:89], v[88:89], v[106:107]
	v_cvt_pk_f32_fp8_e32 v[94:95], v59
	v_pk_add_f32 v[88:89], v[88:89], v[110:111]
	v_cvt_pk_f32_fp8_sdwa v[58:59], v59 src0_sel:WORD_1
	v_pk_add_f32 v[88:89], v[88:89], v[114:115]
	v_cvt_pk_f32_fp8_e32 v[98:99], v71
	v_pk_add_f32 v[88:89], v[88:89], v[118:119]
	v_cvt_pk_f32_fp8_sdwa v[70:71], v71 src0_sel:WORD_1
	v_pk_fma_f32 v[88:89], v[88:89], s[80:81], v[90:91] op_sel_hi:[1,0,1]
	v_cvt_pk_f32_fp8_e32 v[90:91], v51
	v_cvt_pk_bf16_f32 v63, v88, v89
	v_cvt_pk_f32_fp8_e32 v[88:89], v47
	v_cvt_pk_f32_fp8_sdwa v[46:47], v47 src0_sel:WORD_1
	v_cvt_pk_f32_fp8_sdwa v[50:51], v51 src0_sel:WORD_1
	v_cvt_pk_f32_fp8_e32 v[102:103], v79
	v_pk_add_f32 v[88:89], v[88:89], 0 op_sel_hi:[1,0]
	v_pk_add_f32 v[46:47], v[46:47], 0 op_sel_hi:[1,0]
	v_pk_add_f32 v[88:89], v[88:89], v[90:91]
	v_pk_add_f32 v[46:47], v[46:47], v[50:51]
	v_pk_add_f32 v[88:89], v[88:89], v[92:93]
	v_pk_add_f32 v[46:47], v[46:47], v[54:55]
	v_cvt_pk_f32_fp8_sdwa v[78:79], v79 src0_sel:WORD_1
	v_pk_add_f32 v[88:89], v[88:89], v[94:95]
	v_pk_add_f32 v[46:47], v[46:47], v[58:59]
	v_pk_add_f32 v[88:89], v[88:89], v[96:97]
	v_pk_add_f32 v[46:47], v[46:47], v[66:67]
	v_pk_add_f32 v[88:89], v[88:89], v[98:99]
	v_pk_add_f32 v[46:47], v[46:47], v[70:71]
	v_pk_add_f32 v[88:89], v[88:89], v[100:101]
	v_lshlrev_b32_e32 v90, 16, v64
	v_and_b32_e32 v91, 0xffff0000, v64
	v_pk_add_f32 v[46:47], v[46:47], v[74:75]
	v_lshlrev_b32_e32 v50, 16, v65
	v_and_b32_e32 v51, 0xffff0000, v65
	v_pk_add_f32 v[88:89], v[88:89], v[102:103]
	v_pk_mul_f32 v[90:91], v[90:91], s[78:79] op_sel_hi:[1,0]
	v_pk_add_f32 v[46:47], v[46:47], v[78:79]
	v_pk_mul_f32 v[50:51], v[50:51], s[78:79] op_sel_hi:[1,0]
	v_pk_fma_f32 v[88:89], v[88:89], s[80:81], v[90:91] op_sel_hi:[1,0,1]
	v_pk_fma_f32 v[46:47], v[46:47], s[80:81], v[50:51] op_sel_hi:[1,0,1]
	v_cvt_pk_f32_fp8_e32 v[50:51], v48
	v_cvt_pk_bf16_f32 v64, v88, v89
	v_cvt_pk_bf16_f32 v65, v46, v47
	v_lshl_add_u64 v[46:47], v[86:87], 0, s[18:19]
	v_cvt_pk_f32_fp8_e32 v[58:59], v52
	global_store_dwordx4 v[46:47], v[62:65], off
	v_cvt_pk_f32_fp8_e32 v[70:71], v60
	v_cvt_pk_f32_fp8_e32 v[78:79], v68
	v_cvt_pk_f32_fp8_e32 v[64:65], v56
	v_pk_add_f32 v[50:51], v[50:51], 0 op_sel_hi:[1,0]
	v_cvt_pk_f32_fp8_e32 v[90:91], v72
	v_pk_add_f32 v[50:51], v[50:51], v[58:59]
	v_cvt_pk_f32_fp8_e32 v[94:95], v76
	v_pk_add_f32 v[50:51], v[50:51], v[64:65]
	v_cvt_pk_f32_fp8_e32 v[98:99], v80
	v_pk_add_f32 v[50:51], v[50:51], v[70:71]
	v_cvt_pk_f32_fp8_sdwa v[54:55], v48 src0_sel:WORD_1
	v_pk_add_f32 v[50:51], v[50:51], v[78:79]
	v_cvt_pk_f32_fp8_sdwa v[62:63], v52 src0_sel:WORD_1
	v_pk_add_f32 v[50:51], v[50:51], v[90:91]
	v_lshlrev_b32_e32 v58, 16, v42
	v_pk_add_f32 v[50:51], v[50:51], v[94:95]
	v_and_b32_e32 v59, 0xffff0000, v42
	v_cvt_pk_f32_fp8_sdwa v[66:67], v56 src0_sel:WORD_1
	v_pk_add_f32 v[50:51], v[50:51], v[98:99]
	v_pk_mul_f32 v[58:59], v[58:59], s[78:79] op_sel_hi:[1,0]
	v_cvt_pk_f32_fp8_sdwa v[74:75], v60 src0_sel:WORD_1
	v_pk_fma_f32 v[50:51], v[50:51], s[80:81], v[58:59] op_sel_hi:[1,0,1]
	v_cvt_pk_f32_fp8_sdwa v[88:89], v68 src0_sel:WORD_1
	v_cvt_pk_bf16_f32 v42, v50, v51
	v_pk_add_f32 v[50:51], v[54:55], 0 op_sel_hi:[1,0]
	v_cvt_pk_f32_fp8_sdwa v[92:93], v72 src0_sel:WORD_1
	v_pk_add_f32 v[50:51], v[50:51], v[62:63]
	v_cvt_pk_f32_fp8_sdwa v[96:97], v76 src0_sel:WORD_1
	v_pk_add_f32 v[50:51], v[50:51], v[66:67]
	v_cvt_pk_f32_fp8_sdwa v[100:101], v80 src0_sel:WORD_1
	v_pk_add_f32 v[50:51], v[50:51], v[74:75]
	v_lshlrev_b32_e32 v54, 16, v43
	v_pk_add_f32 v[50:51], v[50:51], v[88:89]
	v_and_b32_e32 v55, 0xffff0000, v43
	v_pk_add_f32 v[50:51], v[50:51], v[92:93]
	v_pk_mul_f32 v[54:55], v[54:55], s[78:79] op_sel_hi:[1,0]
	v_pk_add_f32 v[50:51], v[50:51], v[96:97]
	v_cvt_pk_f32_fp8_e32 v[58:59], v57
	v_pk_add_f32 v[50:51], v[50:51], v[100:101]
	v_cvt_pk_f32_fp8_e32 v[62:63], v61
	v_pk_fma_f32 v[50:51], v[50:51], s[80:81], v[54:55] op_sel_hi:[1,0,1]
	v_cvt_pk_f32_fp8_e32 v[54:55], v53
	v_cvt_pk_bf16_f32 v43, v50, v51
	v_cvt_pk_f32_fp8_e32 v[50:51], v49
	v_cvt_pk_f32_fp8_sdwa v[48:49], v49 src0_sel:WORD_1
	v_cvt_pk_f32_fp8_sdwa v[52:53], v53 src0_sel:WORD_1
	v_cvt_pk_f32_fp8_e32 v[64:65], v69
	v_pk_add_f32 v[50:51], v[50:51], 0 op_sel_hi:[1,0]
	v_cvt_pk_f32_fp8_sdwa v[56:57], v57 src0_sel:WORD_1
	v_cvt_pk_f32_fp8_sdwa v[66:67], v69 src0_sel:WORD_1
	v_cvt_pk_f32_fp8_e32 v[68:69], v73
	v_pk_add_f32 v[50:51], v[50:51], v[54:55]
	v_cvt_pk_f32_fp8_sdwa v[60:61], v61 src0_sel:WORD_1
	v_cvt_pk_f32_fp8_sdwa v[70:71], v73 src0_sel:WORD_1
	v_cvt_pk_f32_fp8_e32 v[72:73], v77
	v_pk_add_f32 v[50:51], v[50:51], v[58:59]
	v_cvt_pk_f32_fp8_sdwa v[74:75], v77 src0_sel:WORD_1
	v_cvt_pk_f32_fp8_e32 v[76:77], v81
	v_pk_add_f32 v[50:51], v[50:51], v[62:63]
	v_pk_add_f32 v[48:49], v[48:49], 0 op_sel_hi:[1,0]
	v_pk_add_f32 v[50:51], v[50:51], v[64:65]
	v_pk_add_f32 v[48:49], v[48:49], v[52:53]
	v_pk_add_f32 v[50:51], v[50:51], v[68:69]
	v_pk_add_f32 v[48:49], v[48:49], v[56:57]
	v_cvt_pk_f32_fp8_sdwa v[78:79], v81 src0_sel:WORD_1
	v_pk_add_f32 v[50:51], v[50:51], v[72:73]
	v_lshlrev_b32_e32 v54, 16, v44
	v_and_b32_e32 v55, 0xffff0000, v44
	v_pk_add_f32 v[48:49], v[48:49], v[60:61]
	v_pk_add_f32 v[50:51], v[50:51], v[76:77]
	v_pk_mul_f32 v[54:55], v[54:55], s[78:79] op_sel_hi:[1,0]
	v_pk_add_f32 v[48:49], v[48:49], v[66:67]
	v_pk_fma_f32 v[50:51], v[50:51], s[80:81], v[54:55] op_sel_hi:[1,0,1]
	v_pk_add_f32 v[48:49], v[48:49], v[70:71]
	v_cvt_pk_bf16_f32 v44, v50, v51
	v_pk_add_f32 v[48:49], v[48:49], v[74:75]
	v_lshlrev_b32_e32 v50, 16, v45
	v_and_b32_e32 v51, 0xffff0000, v45
	v_pk_add_f32 v[48:49], v[48:49], v[78:79]
	v_pk_mul_f32 v[50:51], v[50:51], s[78:79] op_sel_hi:[1,0]
	s_waitcnt vmcnt(27)
	v_cvt_pk_f32_fp8_sdwa v[52:53], v30 src0_sel:WORD_1
	v_pk_fma_f32 v[48:49], v[48:49], s[80:81], v[50:51] op_sel_hi:[1,0,1]
	v_cvt_pk_f32_fp8_sdwa v[50:51], v22 src0_sel:WORD_1
	v_cvt_pk_bf16_f32 v45, v48, v49
	global_store_dwordx4 v[46:47], v[42:45], off offset:16
	v_cvt_pk_f32_fp8_sdwa v[46:47], v14 src0_sel:WORD_1
	v_cvt_pk_f32_fp8_sdwa v[48:49], v18 src0_sel:WORD_1
	v_cvt_pk_f32_fp8_sdwa v[42:43], v6 src0_sel:WORD_1
	v_cvt_pk_f32_fp8_sdwa v[44:45], v10 src0_sel:WORD_1
	s_waitcnt vmcnt(27)
	v_cvt_pk_f32_fp8_sdwa v[54:55], v34 src0_sel:WORD_1
	s_waitcnt vmcnt(26)
	v_cvt_pk_f32_fp8_sdwa v[56:57], v38 src0_sel:WORD_1
	v_pk_add_f32 v[42:43], v[42:43], 0 op_sel_hi:[1,0]
	v_cvt_pk_f32_fp8_e32 v[58:59], v6
	v_pk_add_f32 v[42:43], v[42:43], v[44:45]
	v_lshlrev_b32_e32 v44, 16, v27
	v_pk_add_f32 v[42:43], v[42:43], v[46:47]
	v_and_b32_e32 v45, 0xffff0000, v27
	v_pk_add_f32 v[42:43], v[42:43], v[48:49]
	v_pk_mul_f32 v[44:45], v[44:45], s[78:79] op_sel_hi:[1,0]
	v_pk_add_f32 v[42:43], v[42:43], v[50:51]
	v_cvt_pk_f32_fp8_e32 v[60:61], v10
	v_pk_add_f32 v[42:43], v[42:43], v[52:53]
	v_cvt_pk_f32_fp8_e32 v[62:63], v14
	v_pk_add_f32 v[42:43], v[42:43], v[54:55]
	v_cvt_pk_f32_fp8_e32 v[46:47], v15
	v_pk_add_f32 v[42:43], v[42:43], v[56:57]
	v_cvt_pk_f32_fp8_sdwa v[14:15], v15 src0_sel:WORD_1
	v_pk_fma_f32 v[42:43], v[42:43], s[80:81], v[44:45] op_sel_hi:[1,0,1]
	v_cvt_pk_f32_fp8_e32 v[44:45], v11
	v_cvt_pk_bf16_f32 v27, v42, v43
	v_cvt_pk_f32_fp8_e32 v[42:43], v7
	v_cvt_pk_f32_fp8_sdwa v[6:7], v7 src0_sel:WORD_1
	v_cvt_pk_f32_fp8_sdwa v[10:11], v11 src0_sel:WORD_1
	v_cvt_pk_f32_fp8_e32 v[64:65], v18
	v_cvt_pk_f32_fp8_e32 v[48:49], v19
	v_cvt_pk_f32_fp8_sdwa v[18:19], v19 src0_sel:WORD_1
	v_cvt_pk_f32_fp8_e32 v[66:67], v22
	v_pk_add_f32 v[58:59], v[58:59], 0 op_sel_hi:[1,0]
	v_cvt_pk_f32_fp8_e32 v[50:51], v23
	v_cvt_pk_f32_fp8_sdwa v[22:23], v23 src0_sel:WORD_1
	v_pk_add_f32 v[42:43], v[42:43], 0 op_sel_hi:[1,0]
	v_pk_add_f32 v[6:7], v[6:7], 0 op_sel_hi:[1,0]
	v_cvt_pk_f32_fp8_e32 v[68:69], v30
	v_pk_add_f32 v[58:59], v[58:59], v[60:61]
	v_cvt_pk_f32_fp8_e32 v[52:53], v31
	v_cvt_pk_f32_fp8_sdwa v[30:31], v31 src0_sel:WORD_1
	v_pk_add_f32 v[42:43], v[42:43], v[44:45]
	v_pk_add_f32 v[6:7], v[6:7], v[10:11]
	v_cvt_pk_f32_fp8_e32 v[70:71], v34
	v_pk_add_f32 v[58:59], v[58:59], v[62:63]
	v_cvt_pk_f32_fp8_e32 v[54:55], v35
	v_cvt_pk_f32_fp8_sdwa v[34:35], v35 src0_sel:WORD_1
	v_pk_add_f32 v[42:43], v[42:43], v[46:47]
	v_pk_add_f32 v[6:7], v[6:7], v[14:15]
	v_cvt_pk_f32_fp8_e32 v[72:73], v38
	v_pk_add_f32 v[58:59], v[58:59], v[64:65]
	v_cvt_pk_f32_fp8_e32 v[56:57], v39
	v_cvt_pk_f32_fp8_sdwa v[38:39], v39 src0_sel:WORD_1
	v_pk_add_f32 v[42:43], v[42:43], v[48:49]
	v_pk_add_f32 v[6:7], v[6:7], v[18:19]
	v_pk_add_f32 v[58:59], v[58:59], v[66:67]
	v_pk_add_f32 v[42:43], v[42:43], v[50:51]
	v_pk_add_f32 v[6:7], v[6:7], v[22:23]
	v_pk_add_f32 v[58:59], v[58:59], v[68:69]
	v_pk_add_f32 v[42:43], v[42:43], v[52:53]
	v_pk_add_f32 v[6:7], v[6:7], v[30:31]
	v_pk_add_f32 v[58:59], v[58:59], v[70:71]
	v_lshlrev_b32_e32 v60, 16, v26
	v_and_b32_e32 v61, 0xffff0000, v26
	v_pk_add_f32 v[42:43], v[42:43], v[54:55]
	v_lshlrev_b32_e32 v44, 16, v28
	v_and_b32_e32 v45, 0xffff0000, v28
	v_pk_add_f32 v[6:7], v[6:7], v[34:35]
	v_lshlrev_b32_e32 v10, 16, v29
	v_and_b32_e32 v11, 0xffff0000, v29
	v_pk_add_f32 v[58:59], v[58:59], v[72:73]
	v_pk_mul_f32 v[60:61], v[60:61], s[78:79] op_sel_hi:[1,0]
	v_pk_add_f32 v[42:43], v[42:43], v[56:57]
	v_pk_mul_f32 v[44:45], v[44:45], s[78:79] op_sel_hi:[1,0]
	v_pk_add_f32 v[6:7], v[6:7], v[38:39]
	v_pk_mul_f32 v[10:11], v[10:11], s[78:79] op_sel_hi:[1,0]
	v_pk_fma_f32 v[58:59], v[58:59], s[80:81], v[60:61] op_sel_hi:[1,0,1]
	v_pk_fma_f32 v[42:43], v[42:43], s[80:81], v[44:45] op_sel_hi:[1,0,1]
	v_pk_fma_f32 v[6:7], v[6:7], s[80:81], v[10:11] op_sel_hi:[1,0,1]
	v_cvt_pk_f32_fp8_e32 v[10:11], v8
	v_cvt_pk_bf16_f32 v26, v58, v59
	v_cvt_pk_bf16_f32 v28, v42, v43
	v_cvt_pk_bf16_f32 v29, v6, v7
	v_lshl_add_u64 v[6:7], v[86:87], 0, s[16:17]
	v_cvt_pk_f32_fp8_e32 v[18:19], v12
	global_store_dwordx4 v[6:7], v[26:29], off
	v_cvt_pk_f32_fp8_e32 v[30:31], v20
	v_cvt_pk_f32_fp8_e32 v[38:39], v24
	v_cvt_pk_f32_fp8_e32 v[26:27], v16
	v_pk_add_f32 v[10:11], v[10:11], 0 op_sel_hi:[1,0]
	v_cvt_pk_f32_fp8_e32 v[44:45], v32
	v_pk_add_f32 v[10:11], v[10:11], v[18:19]
	v_cvt_pk_f32_fp8_e32 v[48:49], v36
	v_pk_add_f32 v[10:11], v[10:11], v[26:27]
	v_cvt_pk_f32_fp8_e32 v[52:53], v40
	v_pk_add_f32 v[10:11], v[10:11], v[30:31]
	v_cvt_pk_f32_fp8_sdwa v[14:15], v8 src0_sel:WORD_1
	v_pk_add_f32 v[10:11], v[10:11], v[38:39]
	v_cvt_pk_f32_fp8_sdwa v[22:23], v12 src0_sel:WORD_1
	v_pk_add_f32 v[10:11], v[10:11], v[44:45]
	v_lshlrev_b32_e32 v18, 16, v2
	v_pk_add_f32 v[10:11], v[10:11], v[48:49]
	v_and_b32_e32 v19, 0xffff0000, v2
	v_cvt_pk_f32_fp8_sdwa v[28:29], v16 src0_sel:WORD_1
	v_pk_add_f32 v[10:11], v[10:11], v[52:53]
	v_pk_mul_f32 v[18:19], v[18:19], s[78:79] op_sel_hi:[1,0]
	v_cvt_pk_f32_fp8_sdwa v[34:35], v20 src0_sel:WORD_1
	v_pk_fma_f32 v[10:11], v[10:11], s[80:81], v[18:19] op_sel_hi:[1,0,1]
	v_cvt_pk_f32_fp8_sdwa v[42:43], v24 src0_sel:WORD_1
	v_cvt_pk_bf16_f32 v2, v10, v11
	v_pk_add_f32 v[10:11], v[14:15], 0 op_sel_hi:[1,0]
	v_cvt_pk_f32_fp8_sdwa v[46:47], v32 src0_sel:WORD_1
	v_pk_add_f32 v[10:11], v[10:11], v[22:23]
	v_cvt_pk_f32_fp8_sdwa v[50:51], v36 src0_sel:WORD_1
	v_pk_add_f32 v[10:11], v[10:11], v[28:29]
	v_cvt_pk_f32_fp8_sdwa v[54:55], v40 src0_sel:WORD_1
	v_pk_add_f32 v[10:11], v[10:11], v[34:35]
	v_lshlrev_b32_e32 v14, 16, v3
	v_pk_add_f32 v[10:11], v[10:11], v[42:43]
	v_and_b32_e32 v15, 0xffff0000, v3
	v_pk_add_f32 v[10:11], v[10:11], v[46:47]
	v_pk_mul_f32 v[14:15], v[14:15], s[78:79] op_sel_hi:[1,0]
	v_pk_add_f32 v[10:11], v[10:11], v[50:51]
	v_cvt_pk_f32_fp8_e32 v[26:27], v9
	v_pk_add_f32 v[10:11], v[10:11], v[54:55]
	v_cvt_pk_f32_fp8_sdwa v[8:9], v9 src0_sel:WORD_1
	v_pk_fma_f32 v[10:11], v[10:11], s[80:81], v[14:15] op_sel_hi:[1,0,1]
	v_cvt_pk_f32_fp8_e32 v[28:29], v13
	v_cvt_pk_bf16_f32 v3, v10, v11
	v_cvt_pk_f32_fp8_sdwa v[10:11], v13 src0_sel:WORD_1
	v_cvt_pk_f32_fp8_e32 v[30:31], v17
	v_cvt_pk_f32_fp8_sdwa v[12:13], v17 src0_sel:WORD_1
	v_cvt_pk_f32_fp8_e32 v[34:35], v21
	v_cvt_pk_f32_fp8_sdwa v[14:15], v21 src0_sel:WORD_1
	v_cvt_pk_f32_fp8_e32 v[38:39], v25
	v_cvt_pk_f32_fp8_sdwa v[16:17], v25 src0_sel:WORD_1
	v_pk_add_f32 v[26:27], v[26:27], 0 op_sel_hi:[1,0]
	v_pk_add_f32 v[8:9], v[8:9], 0 op_sel_hi:[1,0]
	v_cvt_pk_f32_fp8_e32 v[24:25], v33
	v_cvt_pk_f32_fp8_sdwa v[18:19], v33 src0_sel:WORD_1
	v_pk_add_f32 v[26:27], v[26:27], v[28:29]
	v_pk_add_f32 v[8:9], v[8:9], v[10:11]
	v_cvt_pk_f32_fp8_e32 v[32:33], v37
	v_cvt_pk_f32_fp8_sdwa v[20:21], v37 src0_sel:WORD_1
	v_pk_add_f32 v[26:27], v[26:27], v[30:31]
	v_pk_add_f32 v[8:9], v[8:9], v[12:13]
	v_cvt_pk_f32_fp8_e32 v[36:37], v41
	v_cvt_pk_f32_fp8_sdwa v[22:23], v41 src0_sel:WORD_1
	v_pk_add_f32 v[26:27], v[26:27], v[34:35]
	v_pk_add_f32 v[8:9], v[8:9], v[14:15]
	v_pk_add_f32 v[26:27], v[26:27], v[38:39]
	v_pk_add_f32 v[8:9], v[8:9], v[16:17]
	v_pk_add_f32 v[24:25], v[26:27], v[24:25]
	v_pk_add_f32 v[8:9], v[8:9], v[18:19]
	v_pk_add_f32 v[24:25], v[24:25], v[32:33]
	v_lshlrev_b32_e32 v26, 16, v4
	v_and_b32_e32 v27, 0xffff0000, v4
	v_pk_add_f32 v[8:9], v[8:9], v[20:21]
	v_lshlrev_b32_e32 v10, 16, v5
	v_and_b32_e32 v11, 0xffff0000, v5
	v_pk_add_f32 v[24:25], v[24:25], v[36:37]
	v_pk_mul_f32 v[26:27], v[26:27], s[78:79] op_sel_hi:[1,0]
	v_pk_add_f32 v[8:9], v[8:9], v[22:23]
	v_pk_mul_f32 v[10:11], v[10:11], s[78:79] op_sel_hi:[1,0]
	v_pk_fma_f32 v[24:25], v[24:25], s[80:81], v[26:27] op_sel_hi:[1,0,1]
	v_pk_fma_f32 v[8:9], v[8:9], s[80:81], v[10:11] op_sel_hi:[1,0,1]
	v_cvt_pk_bf16_f32 v4, v24, v25
	v_cvt_pk_bf16_f32 v5, v8, v9
	global_store_dwordx4 v[6:7], v[2:5], off offset:16
	s_waitcnt vmcnt(21)
	v_cvt_pk_f32_fp8_e32 v[88:89], v166
	v_cvt_pk_f32_fp8_sdwa v[90:91], v166 src0_sel:WORD_1
	v_pk_add_f32 v[88:89], v[88:89], 0 op_sel_hi:[1,0]
	s_waitcnt vmcnt(20)
	v_cvt_pk_f32_fp8_e32 v[92:93], v170
	v_cvt_pk_f32_fp8_sdwa v[94:95], v170 src0_sel:WORD_1
	v_pk_add_f32 v[88:89], v[88:89], v[92:93]
	s_waitcnt vmcnt(19)
	v_cvt_pk_f32_fp8_e32 v[96:97], v174
	v_lshlrev_b32_e32 v92, 16, v182
	v_and_b32_e32 v93, 0xffff0000, v182
	v_cvt_pk_f32_fp8_sdwa v[98:99], v174 src0_sel:WORD_1
	v_pk_add_f32 v[88:89], v[88:89], v[96:97]
	s_waitcnt vmcnt(18)
	v_cvt_pk_f32_fp8_e32 v[100:101], v178
	v_pk_mul_f32 v[92:93], v[92:93], s[78:79] op_sel_hi:[1,0]
	v_cvt_pk_f32_fp8_sdwa v[102:103], v178 src0_sel:WORD_1
	v_pk_add_f32 v[88:89], v[88:89], v[100:101]
	s_waitcnt vmcnt(17)
	v_cvt_pk_f32_fp8_e32 v[104:105], v186
	v_cvt_pk_f32_fp8_sdwa v[106:107], v186 src0_sel:WORD_1
	v_cvt_pk_f32_fp8_e32 v[96:97], v187
	v_cvt_pk_f32_fp8_sdwa v[186:187], v187 src0_sel:WORD_1
	v_pk_add_f32 v[88:89], v[88:89], v[104:105]
	s_waitcnt vmcnt(16)
	v_cvt_pk_f32_fp8_e32 v[108:109], v190
	v_cvt_pk_f32_fp8_sdwa v[110:111], v190 src0_sel:WORD_1
	v_pk_add_f32 v[88:89], v[88:89], v[108:109]
	s_waitcnt vmcnt(15)
	v_cvt_pk_f32_fp8_e32 v[112:113], v194
	v_cvt_pk_f32_fp8_sdwa v[114:115], v194 src0_sel:WORD_1
	s_waitcnt vmcnt(14)
	v_cvt_pk_f32_fp8_e32 v[116:117], v198
	v_cvt_pk_f32_fp8_sdwa v[118:119], v198 src0_sel:WORD_1
	v_pk_add_f32 v[88:89], v[88:89], v[112:113]
	v_cvt_pk_f32_fp8_e32 v[100:101], v195
	v_pk_add_f32 v[88:89], v[88:89], v[116:117]
	v_cvt_pk_f32_fp8_sdwa v[194:195], v195 src0_sel:WORD_1
	v_pk_fma_f32 v[88:89], v[88:89], s[80:81], v[92:93] op_sel_hi:[1,0,1]
	v_cvt_pk_f32_fp8_e32 v[92:93], v175
	v_cvt_pk_bf16_f32 v182, v88, v89
	v_pk_add_f32 v[88:89], v[90:91], 0 op_sel_hi:[1,0]
	v_lshlrev_b32_e32 v90, 16, v183
	v_pk_add_f32 v[88:89], v[88:89], v[94:95]
	v_and_b32_e32 v91, 0xffff0000, v183
	v_pk_add_f32 v[88:89], v[88:89], v[98:99]
	v_pk_mul_f32 v[90:91], v[90:91], s[78:79] op_sel_hi:[1,0]
	v_pk_add_f32 v[88:89], v[88:89], v[102:103]
	v_cvt_pk_f32_fp8_sdwa v[174:175], v175 src0_sel:WORD_1
	v_pk_add_f32 v[88:89], v[88:89], v[106:107]
	v_cvt_pk_f32_fp8_e32 v[94:95], v179
	v_pk_add_f32 v[88:89], v[88:89], v[110:111]
	v_cvt_pk_f32_fp8_sdwa v[178:179], v179 src0_sel:WORD_1
	v_pk_add_f32 v[88:89], v[88:89], v[114:115]
	v_cvt_pk_f32_fp8_e32 v[98:99], v191
	v_pk_add_f32 v[88:89], v[88:89], v[118:119]
	v_cvt_pk_f32_fp8_sdwa v[190:191], v191 src0_sel:WORD_1
	v_pk_fma_f32 v[88:89], v[88:89], s[80:81], v[90:91] op_sel_hi:[1,0,1]
	v_cvt_pk_f32_fp8_e32 v[90:91], v171
	v_cvt_pk_bf16_f32 v183, v88, v89
	v_cvt_pk_f32_fp8_e32 v[88:89], v167
	v_cvt_pk_f32_fp8_sdwa v[166:167], v167 src0_sel:WORD_1
	v_cvt_pk_f32_fp8_sdwa v[170:171], v171 src0_sel:WORD_1
	v_cvt_pk_f32_fp8_e32 v[102:103], v199
	v_pk_add_f32 v[88:89], v[88:89], 0 op_sel_hi:[1,0]
	v_pk_add_f32 v[166:167], v[166:167], 0 op_sel_hi:[1,0]
	v_pk_add_f32 v[88:89], v[88:89], v[90:91]
	v_pk_add_f32 v[166:167], v[166:167], v[170:171]
	v_pk_add_f32 v[88:89], v[88:89], v[92:93]
	v_pk_add_f32 v[166:167], v[166:167], v[174:175]
	v_cvt_pk_f32_fp8_sdwa v[198:199], v199 src0_sel:WORD_1
	v_pk_add_f32 v[88:89], v[88:89], v[94:95]
	v_pk_add_f32 v[166:167], v[166:167], v[178:179]
	v_pk_add_f32 v[88:89], v[88:89], v[96:97]
	v_pk_add_f32 v[166:167], v[166:167], v[186:187]
	v_pk_add_f32 v[88:89], v[88:89], v[98:99]
	v_pk_add_f32 v[166:167], v[166:167], v[190:191]
	v_pk_add_f32 v[88:89], v[88:89], v[100:101]
	v_lshlrev_b32_e32 v90, 16, v184
	v_and_b32_e32 v91, 0xffff0000, v184
	v_pk_add_f32 v[166:167], v[166:167], v[194:195]
	v_lshlrev_b32_e32 v170, 16, v185
	v_and_b32_e32 v171, 0xffff0000, v185
	v_pk_add_f32 v[88:89], v[88:89], v[102:103]
	v_pk_mul_f32 v[90:91], v[90:91], s[78:79] op_sel_hi:[1,0]
	v_pk_add_f32 v[166:167], v[166:167], v[198:199]
	v_pk_mul_f32 v[170:171], v[170:171], s[78:79] op_sel_hi:[1,0]
	v_pk_fma_f32 v[88:89], v[88:89], s[80:81], v[90:91] op_sel_hi:[1,0,1]
	v_pk_fma_f32 v[166:167], v[166:167], s[80:81], v[170:171] op_sel_hi:[1,0,1]
	v_cvt_pk_f32_fp8_e32 v[170:171], v168
	v_cvt_pk_bf16_f32 v184, v88, v89
	v_cvt_pk_bf16_f32 v185, v166, v167
	v_lshl_add_u64 v[166:167], v[86:87], 0, s[100:101]
	v_cvt_pk_f32_fp8_e32 v[178:179], v172
	global_store_dwordx4 v[166:167], v[182:185], off
	v_cvt_pk_f32_fp8_e32 v[190:191], v180
	v_cvt_pk_f32_fp8_e32 v[198:199], v188
	v_cvt_pk_f32_fp8_e32 v[184:185], v176
	v_pk_add_f32 v[170:171], v[170:171], 0 op_sel_hi:[1,0]
	v_cvt_pk_f32_fp8_e32 v[90:91], v192
	v_pk_add_f32 v[170:171], v[170:171], v[178:179]
	v_cvt_pk_f32_fp8_e32 v[94:95], v196
	v_pk_add_f32 v[170:171], v[170:171], v[184:185]
	v_cvt_pk_f32_fp8_e32 v[98:99], v200
	v_pk_add_f32 v[170:171], v[170:171], v[190:191]
	v_cvt_pk_f32_fp8_sdwa v[174:175], v168 src0_sel:WORD_1
	v_pk_add_f32 v[170:171], v[170:171], v[198:199]
	v_cvt_pk_f32_fp8_sdwa v[182:183], v172 src0_sel:WORD_1
	v_pk_add_f32 v[170:171], v[170:171], v[90:91]
	v_lshlrev_b32_e32 v178, 16, v162
	v_pk_add_f32 v[170:171], v[170:171], v[94:95]
	v_and_b32_e32 v179, 0xffff0000, v162
	v_cvt_pk_f32_fp8_sdwa v[186:187], v176 src0_sel:WORD_1
	v_pk_add_f32 v[170:171], v[170:171], v[98:99]
	v_pk_mul_f32 v[178:179], v[178:179], s[78:79] op_sel_hi:[1,0]
	v_cvt_pk_f32_fp8_sdwa v[194:195], v180 src0_sel:WORD_1
	v_pk_fma_f32 v[170:171], v[170:171], s[80:81], v[178:179] op_sel_hi:[1,0,1]
	v_cvt_pk_f32_fp8_sdwa v[88:89], v188 src0_sel:WORD_1
	v_cvt_pk_bf16_f32 v162, v170, v171
	v_pk_add_f32 v[170:171], v[174:175], 0 op_sel_hi:[1,0]
	v_cvt_pk_f32_fp8_sdwa v[92:93], v192 src0_sel:WORD_1
	v_pk_add_f32 v[170:171], v[170:171], v[182:183]
	v_cvt_pk_f32_fp8_sdwa v[96:97], v196 src0_sel:WORD_1
	v_pk_add_f32 v[170:171], v[170:171], v[186:187]
	v_cvt_pk_f32_fp8_sdwa v[100:101], v200 src0_sel:WORD_1
	v_pk_add_f32 v[170:171], v[170:171], v[194:195]
	v_lshlrev_b32_e32 v174, 16, v163
	v_pk_add_f32 v[170:171], v[170:171], v[88:89]
	v_and_b32_e32 v175, 0xffff0000, v163
	v_pk_add_f32 v[170:171], v[170:171], v[92:93]
	v_pk_mul_f32 v[174:175], v[174:175], s[78:79] op_sel_hi:[1,0]
	v_pk_add_f32 v[170:171], v[170:171], v[96:97]
	v_cvt_pk_f32_fp8_e32 v[178:179], v177
	v_pk_add_f32 v[170:171], v[170:171], v[100:101]
	v_cvt_pk_f32_fp8_e32 v[182:183], v181
	v_pk_fma_f32 v[170:171], v[170:171], s[80:81], v[174:175] op_sel_hi:[1,0,1]
	v_cvt_pk_f32_fp8_e32 v[174:175], v173
	v_cvt_pk_bf16_f32 v163, v170, v171
	v_cvt_pk_f32_fp8_e32 v[170:171], v169
	v_cvt_pk_f32_fp8_sdwa v[168:169], v169 src0_sel:WORD_1
	v_cvt_pk_f32_fp8_sdwa v[172:173], v173 src0_sel:WORD_1
	v_cvt_pk_f32_fp8_e32 v[184:185], v189
	v_pk_add_f32 v[170:171], v[170:171], 0 op_sel_hi:[1,0]
	v_cvt_pk_f32_fp8_sdwa v[176:177], v177 src0_sel:WORD_1
	v_cvt_pk_f32_fp8_sdwa v[186:187], v189 src0_sel:WORD_1
	v_cvt_pk_f32_fp8_e32 v[188:189], v193
	v_pk_add_f32 v[170:171], v[170:171], v[174:175]
	v_cvt_pk_f32_fp8_sdwa v[180:181], v181 src0_sel:WORD_1
	v_cvt_pk_f32_fp8_sdwa v[190:191], v193 src0_sel:WORD_1
	v_cvt_pk_f32_fp8_e32 v[192:193], v197
	v_pk_add_f32 v[170:171], v[170:171], v[178:179]
	v_cvt_pk_f32_fp8_sdwa v[194:195], v197 src0_sel:WORD_1
	v_cvt_pk_f32_fp8_e32 v[196:197], v201
	v_pk_add_f32 v[170:171], v[170:171], v[182:183]
	v_pk_add_f32 v[168:169], v[168:169], 0 op_sel_hi:[1,0]
	v_pk_add_f32 v[170:171], v[170:171], v[184:185]
	v_pk_add_f32 v[168:169], v[168:169], v[172:173]
	v_pk_add_f32 v[170:171], v[170:171], v[188:189]
	v_pk_add_f32 v[168:169], v[168:169], v[176:177]
	v_cvt_pk_f32_fp8_sdwa v[198:199], v201 src0_sel:WORD_1
	v_pk_add_f32 v[170:171], v[170:171], v[192:193]
	v_lshlrev_b32_e32 v174, 16, v164
	v_and_b32_e32 v175, 0xffff0000, v164
	v_pk_add_f32 v[168:169], v[168:169], v[180:181]
	v_pk_add_f32 v[170:171], v[170:171], v[196:197]
	v_pk_mul_f32 v[174:175], v[174:175], s[78:79] op_sel_hi:[1,0]
	v_pk_add_f32 v[168:169], v[168:169], v[186:187]
	v_pk_fma_f32 v[170:171], v[170:171], s[80:81], v[174:175] op_sel_hi:[1,0,1]
	v_pk_add_f32 v[168:169], v[168:169], v[190:191]
	v_cvt_pk_bf16_f32 v164, v170, v171
	v_pk_add_f32 v[168:169], v[168:169], v[194:195]
	v_lshlrev_b32_e32 v170, 16, v165
	v_and_b32_e32 v171, 0xffff0000, v165
	v_pk_add_f32 v[168:169], v[168:169], v[198:199]
	v_pk_mul_f32 v[170:171], v[170:171], s[78:79] op_sel_hi:[1,0]
	s_waitcnt vmcnt(7)
	v_cvt_pk_f32_fp8_sdwa v[172:173], v150 src0_sel:WORD_1
	v_pk_fma_f32 v[168:169], v[168:169], s[80:81], v[170:171] op_sel_hi:[1,0,1]
	v_cvt_pk_f32_fp8_sdwa v[170:171], v142 src0_sel:WORD_1
	v_cvt_pk_bf16_f32 v165, v168, v169
	global_store_dwordx4 v[166:167], v[162:165], off offset:16
	v_cvt_pk_f32_fp8_sdwa v[166:167], v134 src0_sel:WORD_1
	v_cvt_pk_f32_fp8_sdwa v[168:169], v138 src0_sel:WORD_1
	v_cvt_pk_f32_fp8_sdwa v[162:163], v126 src0_sel:WORD_1
	v_cvt_pk_f32_fp8_sdwa v[164:165], v130 src0_sel:WORD_1
	s_waitcnt vmcnt(7)
	v_cvt_pk_f32_fp8_sdwa v[174:175], v154 src0_sel:WORD_1
	s_waitcnt vmcnt(6)
	v_cvt_pk_f32_fp8_sdwa v[176:177], v158 src0_sel:WORD_1
	v_pk_add_f32 v[162:163], v[162:163], 0 op_sel_hi:[1,0]
	v_cvt_pk_f32_fp8_e32 v[178:179], v126
	v_pk_add_f32 v[162:163], v[162:163], v[164:165]
	v_lshlrev_b32_e32 v164, 16, v147
	v_pk_add_f32 v[162:163], v[162:163], v[166:167]
	v_and_b32_e32 v165, 0xffff0000, v147
	v_pk_add_f32 v[162:163], v[162:163], v[168:169]
	v_pk_mul_f32 v[164:165], v[164:165], s[78:79] op_sel_hi:[1,0]
	v_pk_add_f32 v[162:163], v[162:163], v[170:171]
	v_cvt_pk_f32_fp8_e32 v[180:181], v130
	v_pk_add_f32 v[162:163], v[162:163], v[172:173]
	v_cvt_pk_f32_fp8_e32 v[182:183], v134
	v_pk_add_f32 v[162:163], v[162:163], v[174:175]
	v_cvt_pk_f32_fp8_e32 v[166:167], v135
	v_pk_add_f32 v[162:163], v[162:163], v[176:177]
	v_cvt_pk_f32_fp8_sdwa v[134:135], v135 src0_sel:WORD_1
	v_pk_fma_f32 v[162:163], v[162:163], s[80:81], v[164:165] op_sel_hi:[1,0,1]
	v_cvt_pk_f32_fp8_e32 v[164:165], v131
	v_cvt_pk_bf16_f32 v147, v162, v163
	v_cvt_pk_f32_fp8_e32 v[162:163], v127
	v_cvt_pk_f32_fp8_sdwa v[126:127], v127 src0_sel:WORD_1
	v_cvt_pk_f32_fp8_sdwa v[130:131], v131 src0_sel:WORD_1
	v_cvt_pk_f32_fp8_e32 v[184:185], v138
	v_cvt_pk_f32_fp8_e32 v[168:169], v139
	v_cvt_pk_f32_fp8_sdwa v[138:139], v139 src0_sel:WORD_1
	v_cvt_pk_f32_fp8_e32 v[186:187], v142
	v_pk_add_f32 v[178:179], v[178:179], 0 op_sel_hi:[1,0]
	v_cvt_pk_f32_fp8_e32 v[170:171], v143
	v_cvt_pk_f32_fp8_sdwa v[142:143], v143 src0_sel:WORD_1
	v_pk_add_f32 v[162:163], v[162:163], 0 op_sel_hi:[1,0]
	v_pk_add_f32 v[126:127], v[126:127], 0 op_sel_hi:[1,0]
	v_cvt_pk_f32_fp8_e32 v[188:189], v150
	v_pk_add_f32 v[178:179], v[178:179], v[180:181]
	v_cvt_pk_f32_fp8_e32 v[172:173], v151
	v_cvt_pk_f32_fp8_sdwa v[150:151], v151 src0_sel:WORD_1
	v_pk_add_f32 v[162:163], v[162:163], v[164:165]
	v_pk_add_f32 v[126:127], v[126:127], v[130:131]
	v_cvt_pk_f32_fp8_e32 v[190:191], v154
	v_pk_add_f32 v[178:179], v[178:179], v[182:183]
	v_cvt_pk_f32_fp8_e32 v[174:175], v155
	v_cvt_pk_f32_fp8_sdwa v[154:155], v155 src0_sel:WORD_1
	v_pk_add_f32 v[162:163], v[162:163], v[166:167]
	v_pk_add_f32 v[126:127], v[126:127], v[134:135]
	v_cvt_pk_f32_fp8_e32 v[192:193], v158
	v_pk_add_f32 v[178:179], v[178:179], v[184:185]
	v_cvt_pk_f32_fp8_e32 v[176:177], v159
	v_cvt_pk_f32_fp8_sdwa v[158:159], v159 src0_sel:WORD_1
	v_pk_add_f32 v[162:163], v[162:163], v[168:169]
	v_pk_add_f32 v[126:127], v[126:127], v[138:139]
	v_pk_add_f32 v[178:179], v[178:179], v[186:187]
	v_pk_add_f32 v[162:163], v[162:163], v[170:171]
	v_pk_add_f32 v[126:127], v[126:127], v[142:143]
	v_pk_add_f32 v[178:179], v[178:179], v[188:189]
	v_pk_add_f32 v[162:163], v[162:163], v[172:173]
	v_pk_add_f32 v[126:127], v[126:127], v[150:151]
	v_pk_add_f32 v[178:179], v[178:179], v[190:191]
	v_lshlrev_b32_e32 v180, 16, v146
	v_and_b32_e32 v181, 0xffff0000, v146
	v_pk_add_f32 v[162:163], v[162:163], v[174:175]
	v_lshlrev_b32_e32 v164, 16, v148
	v_and_b32_e32 v165, 0xffff0000, v148
	v_pk_add_f32 v[126:127], v[126:127], v[154:155]
	v_lshlrev_b32_e32 v130, 16, v149
	v_and_b32_e32 v131, 0xffff0000, v149
	v_pk_add_f32 v[178:179], v[178:179], v[192:193]
	v_pk_mul_f32 v[180:181], v[180:181], s[78:79] op_sel_hi:[1,0]
	v_pk_add_f32 v[162:163], v[162:163], v[176:177]
	v_pk_mul_f32 v[164:165], v[164:165], s[78:79] op_sel_hi:[1,0]
	v_pk_add_f32 v[126:127], v[126:127], v[158:159]
	v_pk_mul_f32 v[130:131], v[130:131], s[78:79] op_sel_hi:[1,0]
	v_pk_fma_f32 v[178:179], v[178:179], s[80:81], v[180:181] op_sel_hi:[1,0,1]
	v_pk_fma_f32 v[162:163], v[162:163], s[80:81], v[164:165] op_sel_hi:[1,0,1]
	v_pk_fma_f32 v[126:127], v[126:127], s[80:81], v[130:131] op_sel_hi:[1,0,1]
	v_cvt_pk_f32_fp8_e32 v[130:131], v128
	v_cvt_pk_bf16_f32 v146, v178, v179
	v_cvt_pk_bf16_f32 v148, v162, v163
	v_cvt_pk_bf16_f32 v149, v126, v127
	v_lshl_add_u64 v[126:127], v[86:87], 0, s[98:99]
	v_cvt_pk_f32_fp8_e32 v[138:139], v132
	global_store_dwordx4 v[126:127], v[146:149], off
	v_cvt_pk_f32_fp8_e32 v[150:151], v140
	v_cvt_pk_f32_fp8_e32 v[158:159], v144
	v_cvt_pk_f32_fp8_e32 v[146:147], v136
	v_pk_add_f32 v[130:131], v[130:131], 0 op_sel_hi:[1,0]
	v_cvt_pk_f32_fp8_e32 v[164:165], v152
	v_pk_add_f32 v[130:131], v[130:131], v[138:139]
	v_cvt_pk_f32_fp8_e32 v[168:169], v156
	v_pk_add_f32 v[130:131], v[130:131], v[146:147]
	v_cvt_pk_f32_fp8_e32 v[172:173], v160
	v_pk_add_f32 v[130:131], v[130:131], v[150:151]
	v_cvt_pk_f32_fp8_sdwa v[134:135], v128 src0_sel:WORD_1
	v_pk_add_f32 v[130:131], v[130:131], v[158:159]
	v_cvt_pk_f32_fp8_sdwa v[142:143], v132 src0_sel:WORD_1
	v_pk_add_f32 v[130:131], v[130:131], v[164:165]
	v_lshlrev_b32_e32 v138, 16, v122
	v_pk_add_f32 v[130:131], v[130:131], v[168:169]
	v_and_b32_e32 v139, 0xffff0000, v122
	v_cvt_pk_f32_fp8_sdwa v[148:149], v136 src0_sel:WORD_1
	v_pk_add_f32 v[130:131], v[130:131], v[172:173]
	v_pk_mul_f32 v[138:139], v[138:139], s[78:79] op_sel_hi:[1,0]
	v_cvt_pk_f32_fp8_sdwa v[154:155], v140 src0_sel:WORD_1
	v_pk_fma_f32 v[130:131], v[130:131], s[80:81], v[138:139] op_sel_hi:[1,0,1]
	v_cvt_pk_f32_fp8_sdwa v[162:163], v144 src0_sel:WORD_1
	v_cvt_pk_bf16_f32 v122, v130, v131
	v_pk_add_f32 v[130:131], v[134:135], 0 op_sel_hi:[1,0]
	v_cvt_pk_f32_fp8_sdwa v[166:167], v152 src0_sel:WORD_1
	v_pk_add_f32 v[130:131], v[130:131], v[142:143]
	v_cvt_pk_f32_fp8_sdwa v[170:171], v156 src0_sel:WORD_1
	v_pk_add_f32 v[130:131], v[130:131], v[148:149]
	v_cvt_pk_f32_fp8_sdwa v[174:175], v160 src0_sel:WORD_1
	v_pk_add_f32 v[130:131], v[130:131], v[154:155]
	v_lshlrev_b32_e32 v134, 16, v123
	v_pk_add_f32 v[130:131], v[130:131], v[162:163]
	v_and_b32_e32 v135, 0xffff0000, v123
	v_pk_add_f32 v[130:131], v[130:131], v[166:167]
	v_pk_mul_f32 v[134:135], v[134:135], s[78:79] op_sel_hi:[1,0]
	v_pk_add_f32 v[130:131], v[130:131], v[170:171]
	v_cvt_pk_f32_fp8_e32 v[146:147], v129
	v_pk_add_f32 v[130:131], v[130:131], v[174:175]
	v_cvt_pk_f32_fp8_sdwa v[128:129], v129 src0_sel:WORD_1
	v_pk_fma_f32 v[130:131], v[130:131], s[80:81], v[134:135] op_sel_hi:[1,0,1]
	v_cvt_pk_f32_fp8_e32 v[148:149], v133
	v_cvt_pk_bf16_f32 v123, v130, v131
	v_cvt_pk_f32_fp8_sdwa v[130:131], v133 src0_sel:WORD_1
	v_cvt_pk_f32_fp8_e32 v[150:151], v137
	v_cvt_pk_f32_fp8_sdwa v[132:133], v137 src0_sel:WORD_1
	v_cvt_pk_f32_fp8_e32 v[154:155], v141
	v_cvt_pk_f32_fp8_sdwa v[134:135], v141 src0_sel:WORD_1
	v_cvt_pk_f32_fp8_e32 v[158:159], v145
	v_cvt_pk_f32_fp8_sdwa v[136:137], v145 src0_sel:WORD_1
	v_pk_add_f32 v[146:147], v[146:147], 0 op_sel_hi:[1,0]
	v_pk_add_f32 v[128:129], v[128:129], 0 op_sel_hi:[1,0]
	v_cvt_pk_f32_fp8_e32 v[144:145], v153
	v_cvt_pk_f32_fp8_sdwa v[138:139], v153 src0_sel:WORD_1
	v_pk_add_f32 v[146:147], v[146:147], v[148:149]
	v_pk_add_f32 v[128:129], v[128:129], v[130:131]
	v_cvt_pk_f32_fp8_e32 v[152:153], v157
	v_cvt_pk_f32_fp8_sdwa v[140:141], v157 src0_sel:WORD_1
	v_pk_add_f32 v[146:147], v[146:147], v[150:151]
	v_pk_add_f32 v[128:129], v[128:129], v[132:133]
	v_cvt_pk_f32_fp8_e32 v[156:157], v161
	v_cvt_pk_f32_fp8_sdwa v[142:143], v161 src0_sel:WORD_1
	v_pk_add_f32 v[146:147], v[146:147], v[154:155]
	v_pk_add_f32 v[128:129], v[128:129], v[134:135]
	v_pk_add_f32 v[146:147], v[146:147], v[158:159]
	v_pk_add_f32 v[128:129], v[128:129], v[136:137]
	v_pk_add_f32 v[144:145], v[146:147], v[144:145]
	v_pk_add_f32 v[128:129], v[128:129], v[138:139]
	v_pk_add_f32 v[144:145], v[144:145], v[152:153]
	v_lshlrev_b32_e32 v146, 16, v124
	v_and_b32_e32 v147, 0xffff0000, v124
	v_pk_add_f32 v[128:129], v[128:129], v[140:141]
	v_lshlrev_b32_e32 v130, 16, v125
	v_and_b32_e32 v131, 0xffff0000, v125
	v_pk_add_f32 v[144:145], v[144:145], v[156:157]
	v_pk_mul_f32 v[146:147], v[146:147], s[78:79] op_sel_hi:[1,0]
	v_pk_add_f32 v[128:129], v[128:129], v[142:143]
	v_pk_mul_f32 v[130:131], v[130:131], s[78:79] op_sel_hi:[1,0]
	v_pk_fma_f32 v[144:145], v[144:145], s[80:81], v[146:147] op_sel_hi:[1,0,1]
	v_pk_fma_f32 v[128:129], v[128:129], s[80:81], v[130:131] op_sel_hi:[1,0,1]
	v_cvt_pk_bf16_f32 v124, v144, v145
	v_cvt_pk_bf16_f32 v125, v128, v129
	global_store_dwordx4 v[126:127], v[122:125], off offset:16
	s_mov_b64 s[30:31], 0

.LBB0_1068:
	s_add_i32 s43, s37, s39
	s_add_i32 s6, s43, 2
	s_ashr_i32 s7, s6, 31
	s_add_i32 s76, s35, s41
	s_lshl_b64 s[8:9], s[6:7], 11
	s_add_i32 s6, s76, -15
	s_ashr_i32 s7, s6, 31
	v_lshl_add_u64 v[2:3], v[82:83], 0, s[8:9]
	s_lshl_b64 s[6:7], s[6:7], 10
	global_load_dwordx4 v[42:45], v[2:3], off offset:16
	global_load_dwordx4 v[58:61], v[2:3], off
	v_lshl_add_u64 v[2:3], v[84:85], 0, s[6:7]
	s_add_i32 s6, s76, -14
	s_ashr_i32 s7, s6, 31
	s_lshl_b64 s[6:7], s[6:7], 10
	global_load_dwordx4 v[46:49], v[2:3], off
	v_lshl_add_u64 v[2:3], v[84:85], 0, s[6:7]
	s_add_i32 s6, s76, -13
	s_ashr_i32 s7, s6, 31
	s_lshl_b64 s[6:7], s[6:7], 10
	global_load_dwordx4 v[50:53], v[2:3], off
	v_lshl_add_u64 v[2:3], v[84:85], 0, s[6:7]
	s_add_i32 s6, s76, -12
	s_ashr_i32 s7, s6, 31
	s_lshl_b64 s[6:7], s[6:7], 10
	global_load_dwordx4 v[54:57], v[2:3], off
	v_lshl_add_u64 v[2:3], v[84:85], 0, s[6:7]
	s_add_i32 s6, s76, -11
	s_ashr_i32 s7, s6, 31
	s_lshl_b64 s[6:7], s[6:7], 10
	global_load_dwordx4 v[62:65], v[2:3], off
	v_lshl_add_u64 v[2:3], v[84:85], 0, s[6:7]
	s_add_i32 s6, s76, -10
	s_ashr_i32 s7, s6, 31
	s_lshl_b64 s[6:7], s[6:7], 10
	global_load_dwordx4 v[66:69], v[2:3], off
	v_lshl_add_u64 v[2:3], v[84:85], 0, s[6:7]
	s_add_i32 s6, s76, -9
	s_ashr_i32 s7, s6, 31
	s_lshl_b64 s[6:7], s[6:7], 10
	global_load_dwordx4 v[70:73], v[2:3], off
	v_lshl_add_u64 v[2:3], v[84:85], 0, s[6:7]
	s_add_i32 s6, s76, -8
	s_ashr_i32 s7, s6, 31
	s_lshl_b64 s[6:7], s[6:7], 10
	global_load_dwordx4 v[74:77], v[2:3], off
	v_lshl_add_u64 v[2:3], v[84:85], 0, s[6:7]
	global_load_dwordx4 v[78:81], v[2:3], off
	s_add_i32 s6, s43, 3
	s_ashr_i32 s7, s6, 31
	s_add_i32 s78, s76, -7
	s_lshl_b64 s[6:7], s[6:7], 11
	s_ashr_i32 s79, s78, 31
	v_lshl_add_u64 v[6:7], v[82:83], 0, s[6:7]
	s_lshl_b64 s[78:79], s[78:79], 10
	global_load_dwordx4 v[2:5], v[6:7], off offset:16
	global_load_dwordx4 v[38:41], v[6:7], off
	v_lshl_add_u64 v[6:7], v[84:85], 0, s[78:79]
	s_add_i32 s78, s76, -6
	s_ashr_i32 s79, s78, 31
	s_lshl_b64 s[78:79], s[78:79], 10
	v_lshl_add_u64 v[10:11], v[84:85], 0, s[78:79]
	s_add_i32 s78, s76, -5
	s_ashr_i32 s79, s78, 31
	s_lshl_b64 s[78:79], s[78:79], 10
	v_lshl_add_u64 v[14:15], v[84:85], 0, s[78:79]
	s_add_i32 s78, s76, -4
	s_ashr_i32 s79, s78, 31
	s_lshl_b64 s[78:79], s[78:79], 10
	v_lshl_add_u64 v[18:19], v[84:85], 0, s[78:79]
	s_add_i32 s78, s76, -3
	s_ashr_i32 s79, s78, 31
	s_lshl_b64 s[78:79], s[78:79], 10
	v_lshl_add_u64 v[22:23], v[84:85], 0, s[78:79]
	s_add_i32 s78, s76, -2
	global_load_dwordx4 v[6:9], v[6:7], off
	s_ashr_i32 s79, s78, 31
	global_load_dwordx4 v[10:13], v[10:11], off
	s_lshl_b64 s[78:79], s[78:79], 10
	global_load_dwordx4 v[14:17], v[14:15], off
	v_lshl_add_u64 v[26:27], v[84:85], 0, s[78:79]
	s_add_i32 s78, s76, -1
	global_load_dwordx4 v[18:21], v[18:19], off
	s_ashr_i32 s79, s78, 31
	global_load_dwordx4 v[22:25], v[22:23], off
	s_lshl_b64 s[78:79], s[78:79], 10
	s_ashr_i32 s77, s76, 31
	global_load_dwordx4 v[26:29], v[26:27], off
	v_lshl_add_u64 v[30:31], v[84:85], 0, s[78:79]
	s_lshl_b64 s[76:77], s[76:77], 10
	global_load_dwordx4 v[30:33], v[30:31], off
	v_lshl_add_u64 v[34:35], v[84:85], 0, s[76:77]
	global_load_dwordx4 v[34:37], v[34:35], off
	s_add_i32 s39, s39, 2
	s_add_i32 s41, s41, 16
	s_add_i32 s43, s37, s39
	s_add_i32 s98, s43, 2
	s_ashr_i32 s99, s98, 31
	s_add_i32 s76, s35, s41
	s_lshl_b64 s[100:101], s[98:99], 11
	s_add_i32 s98, s76, -15
	s_ashr_i32 s99, s98, 31
	v_lshl_add_u64 v[122:123], v[82:83], 0, s[100:101]
	s_lshl_b64 s[98:99], s[98:99], 10
	global_load_dwordx4 v[162:165], v[122:123], off offset:16
	global_load_dwordx4 v[178:181], v[122:123], off
	v_lshl_add_u64 v[122:123], v[84:85], 0, s[98:99]
	s_add_i32 s98, s76, -14
	s_ashr_i32 s99, s98, 31
	s_lshl_b64 s[98:99], s[98:99], 10
	global_load_dwordx4 v[166:169], v[122:123], off
	v_lshl_add_u64 v[122:123], v[84:85], 0, s[98:99]
	s_add_i32 s98, s76, -13
	s_ashr_i32 s99, s98, 31
	s_lshl_b64 s[98:99], s[98:99], 10
	global_load_dwordx4 v[170:173], v[122:123], off
	v_lshl_add_u64 v[122:123], v[84:85], 0, s[98:99]
	s_add_i32 s98, s76, -12
	s_ashr_i32 s99, s98, 31
	s_lshl_b64 s[98:99], s[98:99], 10
	global_load_dwordx4 v[174:177], v[122:123], off
	v_lshl_add_u64 v[122:123], v[84:85], 0, s[98:99]
	s_add_i32 s98, s76, -11
	s_ashr_i32 s99, s98, 31
	s_lshl_b64 s[98:99], s[98:99], 10
	global_load_dwordx4 v[182:185], v[122:123], off
	v_lshl_add_u64 v[122:123], v[84:85], 0, s[98:99]
	s_add_i32 s98, s76, -10
	s_ashr_i32 s99, s98, 31
	s_lshl_b64 s[98:99], s[98:99], 10
	global_load_dwordx4 v[186:189], v[122:123], off
	v_lshl_add_u64 v[122:123], v[84:85], 0, s[98:99]
	s_add_i32 s98, s76, -9
	s_ashr_i32 s99, s98, 31
	s_lshl_b64 s[98:99], s[98:99], 10
	global_load_dwordx4 v[190:193], v[122:123], off
	v_lshl_add_u64 v[122:123], v[84:85], 0, s[98:99]
	s_add_i32 s98, s76, -8
	s_ashr_i32 s99, s98, 31
	s_lshl_b64 s[98:99], s[98:99], 10
	global_load_dwordx4 v[194:197], v[122:123], off
	v_lshl_add_u64 v[122:123], v[84:85], 0, s[98:99]
	global_load_dwordx4 v[198:201], v[122:123], off
	s_add_i32 s98, s43, 3
	s_ashr_i32 s99, s98, 31
	s_add_i32 s78, s76, -7
	s_lshl_b64 s[98:99], s[98:99], 11
	s_ashr_i32 s79, s78, 31
	v_lshl_add_u64 v[126:127], v[82:83], 0, s[98:99]
	s_lshl_b64 s[78:79], s[78:79], 10
	global_load_dwordx4 v[122:125], v[126:127], off offset:16
	global_load_dwordx4 v[158:161], v[126:127], off
	v_lshl_add_u64 v[126:127], v[84:85], 0, s[78:79]
	s_add_i32 s78, s76, -6
	s_ashr_i32 s79, s78, 31
	s_lshl_b64 s[78:79], s[78:79], 10
	v_lshl_add_u64 v[130:131], v[84:85], 0, s[78:79]
	s_add_i32 s78, s76, -5
	s_ashr_i32 s79, s78, 31
	s_lshl_b64 s[78:79], s[78:79], 10
	v_lshl_add_u64 v[134:135], v[84:85], 0, s[78:79]
	s_add_i32 s78, s76, -4
	s_ashr_i32 s79, s78, 31
	s_lshl_b64 s[78:79], s[78:79], 10
	v_lshl_add_u64 v[138:139], v[84:85], 0, s[78:79]
	s_add_i32 s78, s76, -3
	s_ashr_i32 s79, s78, 31
	s_lshl_b64 s[78:79], s[78:79], 10
	v_lshl_add_u64 v[142:143], v[84:85], 0, s[78:79]
	s_add_i32 s78, s76, -2
	global_load_dwordx4 v[126:129], v[126:127], off
	s_ashr_i32 s79, s78, 31
	global_load_dwordx4 v[130:133], v[130:131], off
	s_lshl_b64 s[78:79], s[78:79], 10
	global_load_dwordx4 v[134:137], v[134:135], off
	v_lshl_add_u64 v[146:147], v[84:85], 0, s[78:79]
	s_add_i32 s78, s76, -1
	global_load_dwordx4 v[138:141], v[138:139], off
	s_ashr_i32 s79, s78, 31
	global_load_dwordx4 v[142:145], v[142:143], off
	s_lshl_b64 s[78:79], s[78:79], 10
	s_ashr_i32 s77, s76, 31
	global_load_dwordx4 v[146:149], v[146:147], off
	v_lshl_add_u64 v[150:151], v[84:85], 0, s[78:79]
	s_lshl_b64 s[76:77], s[76:77], 10
	global_load_dwordx4 v[150:153], v[150:151], off
	v_lshl_add_u64 v[154:155], v[84:85], 0, s[76:77]
	global_load_dwordx4 v[154:157], v[154:155], off
	s_add_i32 s39, s39, 2
	s_add_i32 s41, s41, 16
	s_waitcnt vmcnt(37)
	v_cvt_pk_f32_fp8_e32 v[88:89], v46
	v_cvt_pk_f32_fp8_sdwa v[90:91], v46 src0_sel:WORD_1
	v_pk_add_f32 v[88:89], v[88:89], 0 op_sel_hi:[1,0]
	s_waitcnt vmcnt(36)
	v_cvt_pk_f32_fp8_e32 v[92:93], v50
	v_cvt_pk_f32_fp8_sdwa v[94:95], v50 src0_sel:WORD_1
	v_pk_add_f32 v[88:89], v[88:89], v[92:93]
	s_waitcnt vmcnt(35)
	v_cvt_pk_f32_fp8_e32 v[96:97], v54
	v_lshlrev_b32_e32 v92, 16, v58
	v_and_b32_e32 v93, 0xffff0000, v58
	v_cvt_pk_f32_fp8_sdwa v[98:99], v54 src0_sel:WORD_1
	v_pk_add_f32 v[88:89], v[88:89], v[96:97]
	s_waitcnt vmcnt(34)
	v_cvt_pk_f32_fp8_e32 v[100:101], v62
	v_pk_mul_f32 v[92:93], v[92:93], s[26:27] op_sel_hi:[1,0]
	v_cvt_pk_f32_fp8_sdwa v[102:103], v62 src0_sel:WORD_1
	v_pk_add_f32 v[88:89], v[88:89], v[100:101]
	s_waitcnt vmcnt(33)
	v_cvt_pk_f32_fp8_e32 v[104:105], v66
	v_cvt_pk_f32_fp8_sdwa v[106:107], v66 src0_sel:WORD_1
	v_cvt_pk_f32_fp8_e32 v[96:97], v67
	v_cvt_pk_f32_fp8_sdwa v[66:67], v67 src0_sel:WORD_1
	v_pk_add_f32 v[88:89], v[88:89], v[104:105]
	s_waitcnt vmcnt(32)
	v_cvt_pk_f32_fp8_e32 v[108:109], v70
	v_cvt_pk_f32_fp8_sdwa v[110:111], v70 src0_sel:WORD_1
	v_pk_add_f32 v[88:89], v[88:89], v[108:109]
	s_waitcnt vmcnt(31)
	v_cvt_pk_f32_fp8_e32 v[112:113], v74
	v_cvt_pk_f32_fp8_sdwa v[114:115], v74 src0_sel:WORD_1
	s_waitcnt vmcnt(30)
	v_cvt_pk_f32_fp8_e32 v[116:117], v78
	v_cvt_pk_f32_fp8_sdwa v[118:119], v78 src0_sel:WORD_1
	v_pk_add_f32 v[88:89], v[88:89], v[112:113]
	v_cvt_pk_f32_fp8_e32 v[100:101], v75
	v_pk_add_f32 v[88:89], v[88:89], v[116:117]
	v_cvt_pk_f32_fp8_sdwa v[74:75], v75 src0_sel:WORD_1
	v_pk_fma_f32 v[88:89], v[88:89], s[28:29], v[92:93] op_sel_hi:[1,0,1]
	v_cvt_pk_f32_fp8_e32 v[92:93], v55
	v_cvt_pk_bf16_f32 v58, v88, v89
	v_pk_add_f32 v[88:89], v[90:91], 0 op_sel_hi:[1,0]
	v_lshlrev_b32_e32 v90, 16, v59
	v_pk_add_f32 v[88:89], v[88:89], v[94:95]
	v_and_b32_e32 v91, 0xffff0000, v59
	v_pk_add_f32 v[88:89], v[88:89], v[98:99]
	v_pk_mul_f32 v[90:91], v[90:91], s[26:27] op_sel_hi:[1,0]
	v_pk_add_f32 v[88:89], v[88:89], v[102:103]
	v_cvt_pk_f32_fp8_sdwa v[54:55], v55 src0_sel:WORD_1
	v_pk_add_f32 v[88:89], v[88:89], v[106:107]
	v_cvt_pk_f32_fp8_e32 v[94:95], v63
	v_pk_add_f32 v[88:89], v[88:89], v[110:111]
	v_cvt_pk_f32_fp8_sdwa v[62:63], v63 src0_sel:WORD_1
	v_pk_add_f32 v[88:89], v[88:89], v[114:115]
	v_cvt_pk_f32_fp8_e32 v[98:99], v71
	v_pk_add_f32 v[88:89], v[88:89], v[118:119]
	v_cvt_pk_f32_fp8_sdwa v[70:71], v71 src0_sel:WORD_1
	v_pk_fma_f32 v[88:89], v[88:89], s[28:29], v[90:91] op_sel_hi:[1,0,1]
	v_cvt_pk_f32_fp8_e32 v[90:91], v51
	v_cvt_pk_bf16_f32 v59, v88, v89
	v_cvt_pk_f32_fp8_e32 v[88:89], v47
	v_cvt_pk_f32_fp8_sdwa v[46:47], v47 src0_sel:WORD_1
	v_cvt_pk_f32_fp8_sdwa v[50:51], v51 src0_sel:WORD_1
	v_cvt_pk_f32_fp8_e32 v[102:103], v79
	v_pk_add_f32 v[88:89], v[88:89], 0 op_sel_hi:[1,0]
	v_pk_add_f32 v[46:47], v[46:47], 0 op_sel_hi:[1,0]
	v_pk_add_f32 v[88:89], v[88:89], v[90:91]
	v_pk_add_f32 v[46:47], v[46:47], v[50:51]
	v_pk_add_f32 v[88:89], v[88:89], v[92:93]
	v_pk_add_f32 v[46:47], v[46:47], v[54:55]
	v_cvt_pk_f32_fp8_sdwa v[78:79], v79 src0_sel:WORD_1
	v_pk_add_f32 v[88:89], v[88:89], v[94:95]
	v_pk_add_f32 v[46:47], v[46:47], v[62:63]
	v_pk_add_f32 v[88:89], v[88:89], v[96:97]
	v_pk_add_f32 v[46:47], v[46:47], v[66:67]
	v_pk_add_f32 v[88:89], v[88:89], v[98:99]
	v_pk_add_f32 v[46:47], v[46:47], v[70:71]
	v_pk_add_f32 v[88:89], v[88:89], v[100:101]
	v_lshlrev_b32_e32 v90, 16, v60
	v_and_b32_e32 v91, 0xffff0000, v60
	v_pk_add_f32 v[46:47], v[46:47], v[74:75]
	v_lshlrev_b32_e32 v50, 16, v61
	v_and_b32_e32 v51, 0xffff0000, v61
	v_pk_add_f32 v[88:89], v[88:89], v[102:103]
	v_pk_mul_f32 v[90:91], v[90:91], s[26:27] op_sel_hi:[1,0]
	v_pk_add_f32 v[46:47], v[46:47], v[78:79]
	v_pk_mul_f32 v[50:51], v[50:51], s[26:27] op_sel_hi:[1,0]
	v_pk_fma_f32 v[88:89], v[88:89], s[28:29], v[90:91] op_sel_hi:[1,0,1]
	v_pk_fma_f32 v[46:47], v[46:47], s[28:29], v[50:51] op_sel_hi:[1,0,1]
	v_cvt_pk_bf16_f32 v60, v88, v89
	v_cvt_pk_bf16_f32 v61, v46, v47
	v_lshl_add_u64 v[46:47], v[86:87], 0, s[8:9]
	v_cvt_pk_f32_fp8_e32 v[50:51], v48
	global_store_dwordx4 v[46:47], v[58:61], off
	v_cvt_pk_f32_fp8_e32 v[62:63], v56
	v_cvt_pk_f32_fp8_e32 v[70:71], v64
	v_cvt_pk_f32_fp8_e32 v[58:59], v52
	v_cvt_pk_f32_fp8_e32 v[78:79], v68
	v_pk_add_f32 v[50:51], v[50:51], 0 op_sel_hi:[1,0]
	v_cvt_pk_f32_fp8_e32 v[90:91], v72
	v_pk_add_f32 v[50:51], v[50:51], v[58:59]
	v_cvt_pk_f32_fp8_e32 v[94:95], v76
	v_pk_add_f32 v[50:51], v[50:51], v[62:63]
	v_cvt_pk_f32_fp8_e32 v[98:99], v80
	v_pk_add_f32 v[50:51], v[50:51], v[70:71]
	v_cvt_pk_f32_fp8_sdwa v[54:55], v48 src0_sel:WORD_1
	v_pk_add_f32 v[50:51], v[50:51], v[78:79]
	v_cvt_pk_f32_fp8_sdwa v[60:61], v52 src0_sel:WORD_1
	v_pk_add_f32 v[50:51], v[50:51], v[90:91]
	v_lshlrev_b32_e32 v58, 16, v42
	v_pk_add_f32 v[50:51], v[50:51], v[94:95]
	v_and_b32_e32 v59, 0xffff0000, v42
	v_cvt_pk_f32_fp8_sdwa v[66:67], v56 src0_sel:WORD_1
	v_pk_add_f32 v[50:51], v[50:51], v[98:99]
	v_pk_mul_f32 v[58:59], v[58:59], s[26:27] op_sel_hi:[1,0]
	v_cvt_pk_f32_fp8_sdwa v[74:75], v64 src0_sel:WORD_1
	v_pk_fma_f32 v[50:51], v[50:51], s[28:29], v[58:59] op_sel_hi:[1,0,1]
	v_cvt_pk_f32_fp8_sdwa v[88:89], v68 src0_sel:WORD_1
	v_cvt_pk_bf16_f32 v42, v50, v51
	v_pk_add_f32 v[50:51], v[54:55], 0 op_sel_hi:[1,0]
	v_cvt_pk_f32_fp8_sdwa v[92:93], v72 src0_sel:WORD_1
	v_pk_add_f32 v[50:51], v[50:51], v[60:61]
	v_cvt_pk_f32_fp8_sdwa v[96:97], v76 src0_sel:WORD_1
	v_pk_add_f32 v[50:51], v[50:51], v[66:67]
	v_cvt_pk_f32_fp8_sdwa v[100:101], v80 src0_sel:WORD_1
	v_pk_add_f32 v[50:51], v[50:51], v[74:75]
	v_lshlrev_b32_e32 v54, 16, v43
	v_pk_add_f32 v[50:51], v[50:51], v[88:89]
	v_and_b32_e32 v55, 0xffff0000, v43
	v_pk_add_f32 v[50:51], v[50:51], v[92:93]
	v_pk_mul_f32 v[54:55], v[54:55], s[26:27] op_sel_hi:[1,0]
	v_pk_add_f32 v[50:51], v[50:51], v[96:97]
	v_cvt_pk_f32_fp8_e32 v[58:59], v57
	v_pk_add_f32 v[50:51], v[50:51], v[100:101]
	v_cvt_pk_f32_fp8_e32 v[60:61], v65
	v_pk_fma_f32 v[50:51], v[50:51], s[28:29], v[54:55] op_sel_hi:[1,0,1]
	v_cvt_pk_f32_fp8_e32 v[54:55], v53
	v_cvt_pk_bf16_f32 v43, v50, v51
	v_cvt_pk_f32_fp8_e32 v[50:51], v49
	v_cvt_pk_f32_fp8_sdwa v[48:49], v49 src0_sel:WORD_1
	v_cvt_pk_f32_fp8_sdwa v[52:53], v53 src0_sel:WORD_1
	v_cvt_pk_f32_fp8_sdwa v[62:63], v65 src0_sel:WORD_1
	v_cvt_pk_f32_fp8_e32 v[64:65], v69
	v_pk_add_f32 v[50:51], v[50:51], 0 op_sel_hi:[1,0]
	v_cvt_pk_f32_fp8_sdwa v[56:57], v57 src0_sel:WORD_1
	v_cvt_pk_f32_fp8_sdwa v[66:67], v69 src0_sel:WORD_1
	v_cvt_pk_f32_fp8_e32 v[68:69], v73
	v_pk_add_f32 v[50:51], v[50:51], v[54:55]
	v_cvt_pk_f32_fp8_sdwa v[70:71], v73 src0_sel:WORD_1
	v_cvt_pk_f32_fp8_e32 v[72:73], v77
	v_pk_add_f32 v[50:51], v[50:51], v[58:59]
	v_cvt_pk_f32_fp8_sdwa v[74:75], v77 src0_sel:WORD_1
	v_cvt_pk_f32_fp8_e32 v[76:77], v81
	v_pk_add_f32 v[50:51], v[50:51], v[60:61]
	v_pk_add_f32 v[48:49], v[48:49], 0 op_sel_hi:[1,0]
	v_pk_add_f32 v[50:51], v[50:51], v[64:65]
	v_pk_add_f32 v[48:49], v[48:49], v[52:53]
	v_pk_add_f32 v[50:51], v[50:51], v[68:69]
	v_pk_add_f32 v[48:49], v[48:49], v[56:57]
	v_cvt_pk_f32_fp8_sdwa v[78:79], v81 src0_sel:WORD_1
	v_pk_add_f32 v[50:51], v[50:51], v[72:73]
	v_lshlrev_b32_e32 v54, 16, v44
	v_and_b32_e32 v55, 0xffff0000, v44
	v_pk_add_f32 v[48:49], v[48:49], v[62:63]
	v_pk_add_f32 v[50:51], v[50:51], v[76:77]
	v_pk_mul_f32 v[54:55], v[54:55], s[26:27] op_sel_hi:[1,0]
	v_pk_add_f32 v[48:49], v[48:49], v[66:67]
	v_pk_fma_f32 v[50:51], v[50:51], s[28:29], v[54:55] op_sel_hi:[1,0,1]
	v_pk_add_f32 v[48:49], v[48:49], v[70:71]
	v_cvt_pk_bf16_f32 v44, v50, v51
	v_pk_add_f32 v[48:49], v[48:49], v[74:75]
	v_lshlrev_b32_e32 v50, 16, v45
	v_and_b32_e32 v51, 0xffff0000, v45
	v_pk_add_f32 v[48:49], v[48:49], v[78:79]
	v_pk_mul_f32 v[50:51], v[50:51], s[26:27] op_sel_hi:[1,0]
	s_waitcnt vmcnt(23)
	v_cvt_pk_f32_fp8_sdwa v[52:53], v26 src0_sel:WORD_1
	v_pk_fma_f32 v[48:49], v[48:49], s[28:29], v[50:51] op_sel_hi:[1,0,1]
	v_cvt_pk_f32_fp8_sdwa v[50:51], v22 src0_sel:WORD_1
	v_cvt_pk_bf16_f32 v45, v48, v49
	global_store_dwordx4 v[46:47], v[42:45], off offset:16
	v_cvt_pk_f32_fp8_sdwa v[46:47], v14 src0_sel:WORD_1
	v_cvt_pk_f32_fp8_sdwa v[48:49], v18 src0_sel:WORD_1
	v_cvt_pk_f32_fp8_sdwa v[42:43], v6 src0_sel:WORD_1
	v_cvt_pk_f32_fp8_sdwa v[44:45], v10 src0_sel:WORD_1
	s_waitcnt vmcnt(23)
	v_cvt_pk_f32_fp8_sdwa v[54:55], v30 src0_sel:WORD_1
	s_waitcnt vmcnt(22)
	v_cvt_pk_f32_fp8_sdwa v[56:57], v34 src0_sel:WORD_1
	v_pk_add_f32 v[42:43], v[42:43], 0 op_sel_hi:[1,0]
	v_cvt_pk_f32_fp8_e32 v[58:59], v6
	v_pk_add_f32 v[42:43], v[42:43], v[44:45]
	v_lshlrev_b32_e32 v44, 16, v39
	v_pk_add_f32 v[42:43], v[42:43], v[46:47]
	v_and_b32_e32 v45, 0xffff0000, v39
	v_pk_add_f32 v[42:43], v[42:43], v[48:49]
	v_pk_mul_f32 v[44:45], v[44:45], s[26:27] op_sel_hi:[1,0]
	v_pk_add_f32 v[42:43], v[42:43], v[50:51]
	v_cvt_pk_f32_fp8_e32 v[60:61], v10
	v_pk_add_f32 v[42:43], v[42:43], v[52:53]
	v_cvt_pk_f32_fp8_e32 v[62:63], v14
	v_pk_add_f32 v[42:43], v[42:43], v[54:55]
	v_cvt_pk_f32_fp8_e32 v[46:47], v15
	v_pk_add_f32 v[42:43], v[42:43], v[56:57]
	v_cvt_pk_f32_fp8_sdwa v[14:15], v15 src0_sel:WORD_1
	v_pk_fma_f32 v[42:43], v[42:43], s[28:29], v[44:45] op_sel_hi:[1,0,1]
	v_cvt_pk_f32_fp8_e32 v[44:45], v11
	v_cvt_pk_bf16_f32 v39, v42, v43
	v_cvt_pk_f32_fp8_e32 v[42:43], v7
	v_cvt_pk_f32_fp8_sdwa v[6:7], v7 src0_sel:WORD_1
	v_cvt_pk_f32_fp8_sdwa v[10:11], v11 src0_sel:WORD_1
	v_cvt_pk_f32_fp8_e32 v[64:65], v18
	v_cvt_pk_f32_fp8_e32 v[48:49], v19
	v_cvt_pk_f32_fp8_sdwa v[18:19], v19 src0_sel:WORD_1
	v_cvt_pk_f32_fp8_e32 v[66:67], v22
	v_cvt_pk_f32_fp8_e32 v[50:51], v23
	v_cvt_pk_f32_fp8_sdwa v[22:23], v23 src0_sel:WORD_1
	v_pk_add_f32 v[6:7], v[6:7], 0 op_sel_hi:[1,0]
	v_cvt_pk_f32_fp8_e32 v[68:69], v26
	v_cvt_pk_f32_fp8_e32 v[52:53], v27
	v_cvt_pk_f32_fp8_sdwa v[26:27], v27 src0_sel:WORD_1
	v_pk_add_f32 v[6:7], v[6:7], v[10:11]
	v_cvt_pk_f32_fp8_e32 v[70:71], v30
	v_pk_add_f32 v[58:59], v[58:59], 0 op_sel_hi:[1,0]
	v_cvt_pk_f32_fp8_e32 v[54:55], v31
	v_cvt_pk_f32_fp8_sdwa v[30:31], v31 src0_sel:WORD_1
	v_pk_add_f32 v[42:43], v[42:43], 0 op_sel_hi:[1,0]
	v_pk_add_f32 v[6:7], v[6:7], v[14:15]
	v_cvt_pk_f32_fp8_e32 v[72:73], v34
	v_pk_add_f32 v[58:59], v[58:59], v[60:61]
	v_cvt_pk_f32_fp8_e32 v[56:57], v35
	v_cvt_pk_f32_fp8_sdwa v[34:35], v35 src0_sel:WORD_1
	v_pk_add_f32 v[42:43], v[42:43], v[44:45]
	v_pk_add_f32 v[6:7], v[6:7], v[18:19]
	v_pk_add_f32 v[58:59], v[58:59], v[62:63]
	v_pk_add_f32 v[42:43], v[42:43], v[46:47]
	v_pk_add_f32 v[6:7], v[6:7], v[22:23]
	v_pk_add_f32 v[58:59], v[58:59], v[64:65]
	v_pk_add_f32 v[42:43], v[42:43], v[48:49]
	v_pk_add_f32 v[6:7], v[6:7], v[26:27]
	v_pk_add_f32 v[58:59], v[58:59], v[66:67]
	v_pk_add_f32 v[42:43], v[42:43], v[50:51]
	v_pk_add_f32 v[6:7], v[6:7], v[30:31]
	v_lshlrev_b32_e32 v10, 16, v41
	v_and_b32_e32 v11, 0xffff0000, v41
	v_pk_add_f32 v[58:59], v[58:59], v[68:69]
	v_pk_add_f32 v[42:43], v[42:43], v[52:53]
	v_pk_add_f32 v[6:7], v[6:7], v[34:35]
	v_pk_mul_f32 v[10:11], v[10:11], s[26:27] op_sel_hi:[1,0]
	v_pk_add_f32 v[58:59], v[58:59], v[70:71]
	v_lshlrev_b32_e32 v60, 16, v38
	v_and_b32_e32 v61, 0xffff0000, v38
	v_pk_add_f32 v[42:43], v[42:43], v[54:55]
	v_lshlrev_b32_e32 v44, 16, v40
	v_and_b32_e32 v45, 0xffff0000, v40
	v_pk_fma_f32 v[6:7], v[6:7], s[28:29], v[10:11] op_sel_hi:[1,0,1]
	v_cvt_pk_f32_fp8_e32 v[10:11], v8
	v_pk_add_f32 v[58:59], v[58:59], v[72:73]
	v_pk_mul_f32 v[60:61], v[60:61], s[26:27] op_sel_hi:[1,0]
	v_pk_add_f32 v[42:43], v[42:43], v[56:57]
	v_pk_mul_f32 v[44:45], v[44:45], s[26:27] op_sel_hi:[1,0]
	v_cvt_pk_f32_fp8_e32 v[18:19], v12
	v_pk_fma_f32 v[58:59], v[58:59], s[28:29], v[60:61] op_sel_hi:[1,0,1]
	v_pk_fma_f32 v[42:43], v[42:43], s[28:29], v[44:45] op_sel_hi:[1,0,1]
	v_cvt_pk_f32_fp8_e32 v[26:27], v16
	v_cvt_pk_bf16_f32 v38, v58, v59
	v_cvt_pk_bf16_f32 v40, v42, v43
	v_cvt_pk_bf16_f32 v41, v6, v7
	v_lshl_add_u64 v[6:7], v[86:87], 0, s[6:7]
	v_cvt_pk_f32_fp8_e32 v[34:35], v20
	global_store_dwordx4 v[6:7], v[38:41], off
	v_pk_add_f32 v[10:11], v[10:11], 0 op_sel_hi:[1,0]
	v_cvt_pk_f32_fp8_e32 v[44:45], v28
	v_cvt_pk_f32_fp8_e32 v[40:41], v24
	v_pk_add_f32 v[10:11], v[10:11], v[18:19]
	v_cvt_pk_f32_fp8_e32 v[48:49], v32
	v_pk_add_f32 v[10:11], v[10:11], v[26:27]
	v_cvt_pk_f32_fp8_e32 v[52:53], v36
	v_pk_add_f32 v[10:11], v[10:11], v[34:35]
	v_cvt_pk_f32_fp8_sdwa v[14:15], v8 src0_sel:WORD_1
	v_pk_add_f32 v[10:11], v[10:11], v[40:41]
	v_cvt_pk_f32_fp8_sdwa v[22:23], v12 src0_sel:WORD_1
	v_pk_add_f32 v[10:11], v[10:11], v[44:45]
	v_lshlrev_b32_e32 v18, 16, v2
	v_pk_add_f32 v[10:11], v[10:11], v[48:49]
	v_and_b32_e32 v19, 0xffff0000, v2
	v_cvt_pk_f32_fp8_sdwa v[30:31], v16 src0_sel:WORD_1
	v_pk_add_f32 v[10:11], v[10:11], v[52:53]
	v_pk_mul_f32 v[18:19], v[18:19], s[26:27] op_sel_hi:[1,0]
	v_cvt_pk_f32_fp8_sdwa v[38:39], v20 src0_sel:WORD_1
	v_pk_fma_f32 v[10:11], v[10:11], s[28:29], v[18:19] op_sel_hi:[1,0,1]
	v_cvt_pk_f32_fp8_sdwa v[42:43], v24 src0_sel:WORD_1
	v_cvt_pk_bf16_f32 v2, v10, v11
	v_pk_add_f32 v[10:11], v[14:15], 0 op_sel_hi:[1,0]
	v_cvt_pk_f32_fp8_sdwa v[46:47], v28 src0_sel:WORD_1
	v_pk_add_f32 v[10:11], v[10:11], v[22:23]
	v_cvt_pk_f32_fp8_sdwa v[50:51], v32 src0_sel:WORD_1
	v_pk_add_f32 v[10:11], v[10:11], v[30:31]
	v_cvt_pk_f32_fp8_sdwa v[54:55], v36 src0_sel:WORD_1
	v_pk_add_f32 v[10:11], v[10:11], v[38:39]
	v_lshlrev_b32_e32 v14, 16, v3
	v_pk_add_f32 v[10:11], v[10:11], v[42:43]
	v_and_b32_e32 v15, 0xffff0000, v3
	v_pk_add_f32 v[10:11], v[10:11], v[46:47]
	v_pk_mul_f32 v[14:15], v[14:15], s[26:27] op_sel_hi:[1,0]
	v_pk_add_f32 v[10:11], v[10:11], v[50:51]
	v_cvt_pk_f32_fp8_e32 v[26:27], v9
	v_pk_add_f32 v[10:11], v[10:11], v[54:55]
	v_cvt_pk_f32_fp8_sdwa v[8:9], v9 src0_sel:WORD_1
	v_pk_fma_f32 v[10:11], v[10:11], s[28:29], v[14:15] op_sel_hi:[1,0,1]
	v_cvt_pk_f32_fp8_e32 v[30:31], v13
	v_cvt_pk_bf16_f32 v3, v10, v11
	v_cvt_pk_f32_fp8_sdwa v[10:11], v13 src0_sel:WORD_1
	v_cvt_pk_f32_fp8_e32 v[34:35], v17
	v_cvt_pk_f32_fp8_sdwa v[12:13], v17 src0_sel:WORD_1
	v_cvt_pk_f32_fp8_e32 v[38:39], v21
	v_cvt_pk_f32_fp8_sdwa v[14:15], v21 src0_sel:WORD_1
	v_cvt_pk_f32_fp8_e32 v[40:41], v25
	v_cvt_pk_f32_fp8_sdwa v[16:17], v25 src0_sel:WORD_1
	v_pk_add_f32 v[26:27], v[26:27], 0 op_sel_hi:[1,0]
	v_pk_add_f32 v[8:9], v[8:9], 0 op_sel_hi:[1,0]
	v_cvt_pk_f32_fp8_e32 v[24:25], v29
	v_cvt_pk_f32_fp8_sdwa v[18:19], v29 src0_sel:WORD_1
	v_pk_add_f32 v[26:27], v[26:27], v[30:31]
	v_pk_add_f32 v[8:9], v[8:9], v[10:11]
	v_cvt_pk_f32_fp8_e32 v[28:29], v33
	v_cvt_pk_f32_fp8_sdwa v[20:21], v33 src0_sel:WORD_1
	v_pk_add_f32 v[26:27], v[26:27], v[34:35]
	v_pk_add_f32 v[8:9], v[8:9], v[12:13]
	v_cvt_pk_f32_fp8_e32 v[32:33], v37
	v_cvt_pk_f32_fp8_sdwa v[22:23], v37 src0_sel:WORD_1
	v_pk_add_f32 v[26:27], v[26:27], v[38:39]
	v_pk_add_f32 v[8:9], v[8:9], v[14:15]
	v_pk_add_f32 v[26:27], v[26:27], v[40:41]
	v_pk_add_f32 v[8:9], v[8:9], v[16:17]
	v_pk_add_f32 v[24:25], v[26:27], v[24:25]
	v_pk_add_f32 v[8:9], v[8:9], v[18:19]
	v_pk_add_f32 v[24:25], v[24:25], v[28:29]
	v_lshlrev_b32_e32 v26, 16, v4
	v_and_b32_e32 v27, 0xffff0000, v4
	v_pk_add_f32 v[8:9], v[8:9], v[20:21]
	v_lshlrev_b32_e32 v10, 16, v5
	v_and_b32_e32 v11, 0xffff0000, v5
	v_pk_add_f32 v[24:25], v[24:25], v[32:33]
	v_pk_mul_f32 v[26:27], v[26:27], s[26:27] op_sel_hi:[1,0]
	v_pk_add_f32 v[8:9], v[8:9], v[22:23]
	v_pk_mul_f32 v[10:11], v[10:11], s[26:27] op_sel_hi:[1,0]
	v_pk_fma_f32 v[24:25], v[24:25], s[28:29], v[26:27] op_sel_hi:[1,0,1]
	v_pk_fma_f32 v[8:9], v[8:9], s[28:29], v[10:11] op_sel_hi:[1,0,1]
	v_cvt_pk_bf16_f32 v4, v24, v25
	v_cvt_pk_bf16_f32 v5, v8, v9
	global_store_dwordx4 v[6:7], v[2:5], off offset:16
	s_add_i32 s43, s37, s39
	s_add_i32 s6, s43, 2
	s_ashr_i32 s7, s6, 31
	s_add_i32 s76, s35, s41
	s_lshl_b64 s[8:9], s[6:7], 11
	s_add_i32 s6, s76, -15
	s_ashr_i32 s7, s6, 31
	v_lshl_add_u64 v[2:3], v[82:83], 0, s[8:9]
	s_lshl_b64 s[6:7], s[6:7], 10
	global_load_dwordx4 v[42:45], v[2:3], off offset:16
	global_load_dwordx4 v[58:61], v[2:3], off
	v_lshl_add_u64 v[2:3], v[84:85], 0, s[6:7]
	s_add_i32 s6, s76, -14
	s_ashr_i32 s7, s6, 31
	s_lshl_b64 s[6:7], s[6:7], 10
	global_load_dwordx4 v[46:49], v[2:3], off
	v_lshl_add_u64 v[2:3], v[84:85], 0, s[6:7]
	s_add_i32 s6, s76, -13
	s_ashr_i32 s7, s6, 31
	s_lshl_b64 s[6:7], s[6:7], 10
	global_load_dwordx4 v[50:53], v[2:3], off
	v_lshl_add_u64 v[2:3], v[84:85], 0, s[6:7]
	s_add_i32 s6, s76, -12
	s_ashr_i32 s7, s6, 31
	s_lshl_b64 s[6:7], s[6:7], 10
	global_load_dwordx4 v[54:57], v[2:3], off
	v_lshl_add_u64 v[2:3], v[84:85], 0, s[6:7]
	s_add_i32 s6, s76, -11
	s_ashr_i32 s7, s6, 31
	s_lshl_b64 s[6:7], s[6:7], 10
	global_load_dwordx4 v[62:65], v[2:3], off
	v_lshl_add_u64 v[2:3], v[84:85], 0, s[6:7]
	s_add_i32 s6, s76, -10
	s_ashr_i32 s7, s6, 31
	s_lshl_b64 s[6:7], s[6:7], 10
	global_load_dwordx4 v[66:69], v[2:3], off
	v_lshl_add_u64 v[2:3], v[84:85], 0, s[6:7]
	s_add_i32 s6, s76, -9
	s_ashr_i32 s7, s6, 31
	s_lshl_b64 s[6:7], s[6:7], 10
	global_load_dwordx4 v[70:73], v[2:3], off
	v_lshl_add_u64 v[2:3], v[84:85], 0, s[6:7]
	s_add_i32 s6, s76, -8
	s_ashr_i32 s7, s6, 31
	s_lshl_b64 s[6:7], s[6:7], 10
	global_load_dwordx4 v[74:77], v[2:3], off
	v_lshl_add_u64 v[2:3], v[84:85], 0, s[6:7]
	global_load_dwordx4 v[78:81], v[2:3], off
	s_add_i32 s6, s43, 3
	s_ashr_i32 s7, s6, 31
	s_add_i32 s78, s76, -7
	s_lshl_b64 s[6:7], s[6:7], 11
	s_ashr_i32 s79, s78, 31
	v_lshl_add_u64 v[6:7], v[82:83], 0, s[6:7]
	s_lshl_b64 s[78:79], s[78:79], 10
	global_load_dwordx4 v[2:5], v[6:7], off offset:16
	global_load_dwordx4 v[38:41], v[6:7], off
	v_lshl_add_u64 v[6:7], v[84:85], 0, s[78:79]
	s_add_i32 s78, s76, -6
	s_ashr_i32 s79, s78, 31
	s_lshl_b64 s[78:79], s[78:79], 10
	v_lshl_add_u64 v[10:11], v[84:85], 0, s[78:79]
	s_add_i32 s78, s76, -5
	s_ashr_i32 s79, s78, 31
	s_lshl_b64 s[78:79], s[78:79], 10
	v_lshl_add_u64 v[14:15], v[84:85], 0, s[78:79]
	s_add_i32 s78, s76, -4
	s_ashr_i32 s79, s78, 31
	s_lshl_b64 s[78:79], s[78:79], 10
	v_lshl_add_u64 v[18:19], v[84:85], 0, s[78:79]
	s_add_i32 s78, s76, -3
	s_ashr_i32 s79, s78, 31
	s_lshl_b64 s[78:79], s[78:79], 10
	v_lshl_add_u64 v[22:23], v[84:85], 0, s[78:79]
	s_add_i32 s78, s76, -2
	global_load_dwordx4 v[6:9], v[6:7], off
	s_ashr_i32 s79, s78, 31
	global_load_dwordx4 v[10:13], v[10:11], off
	s_lshl_b64 s[78:79], s[78:79], 10
	global_load_dwordx4 v[14:17], v[14:15], off
	v_lshl_add_u64 v[26:27], v[84:85], 0, s[78:79]
	s_add_i32 s78, s76, -1
	global_load_dwordx4 v[18:21], v[18:19], off
	s_ashr_i32 s79, s78, 31
	global_load_dwordx4 v[22:25], v[22:23], off
	s_lshl_b64 s[78:79], s[78:79], 10
	s_ashr_i32 s77, s76, 31
	global_load_dwordx4 v[26:29], v[26:27], off
	v_lshl_add_u64 v[30:31], v[84:85], 0, s[78:79]
	s_lshl_b64 s[76:77], s[76:77], 10
	global_load_dwordx4 v[30:33], v[30:31], off
	v_lshl_add_u64 v[34:35], v[84:85], 0, s[76:77]
	global_load_dwordx4 v[34:37], v[34:35], off
	s_add_i32 s39, s39, 2
	s_add_i32 s41, s41, 16
	s_waitcnt vmcnt(41)
	v_cvt_pk_f32_fp8_e32 v[88:89], v166
	v_cvt_pk_f32_fp8_sdwa v[90:91], v166 src0_sel:WORD_1
	v_pk_add_f32 v[88:89], v[88:89], 0 op_sel_hi:[1,0]
	s_waitcnt vmcnt(40)
	v_cvt_pk_f32_fp8_e32 v[92:93], v170
	v_cvt_pk_f32_fp8_sdwa v[94:95], v170 src0_sel:WORD_1
	v_pk_add_f32 v[88:89], v[88:89], v[92:93]
	s_waitcnt vmcnt(39)
	v_cvt_pk_f32_fp8_e32 v[96:97], v174
	v_lshlrev_b32_e32 v92, 16, v178
	v_and_b32_e32 v93, 0xffff0000, v178
	v_cvt_pk_f32_fp8_sdwa v[98:99], v174 src0_sel:WORD_1
	v_pk_add_f32 v[88:89], v[88:89], v[96:97]
	s_waitcnt vmcnt(38)
	v_cvt_pk_f32_fp8_e32 v[100:101], v182
	v_pk_mul_f32 v[92:93], v[92:93], s[26:27] op_sel_hi:[1,0]
	v_cvt_pk_f32_fp8_sdwa v[102:103], v182 src0_sel:WORD_1
	v_pk_add_f32 v[88:89], v[88:89], v[100:101]
	s_waitcnt vmcnt(37)
	v_cvt_pk_f32_fp8_e32 v[104:105], v186
	v_cvt_pk_f32_fp8_sdwa v[106:107], v186 src0_sel:WORD_1
	v_cvt_pk_f32_fp8_e32 v[96:97], v187
	v_cvt_pk_f32_fp8_sdwa v[186:187], v187 src0_sel:WORD_1
	v_pk_add_f32 v[88:89], v[88:89], v[104:105]
	s_waitcnt vmcnt(36)
	v_cvt_pk_f32_fp8_e32 v[108:109], v190
	v_cvt_pk_f32_fp8_sdwa v[110:111], v190 src0_sel:WORD_1
	v_pk_add_f32 v[88:89], v[88:89], v[108:109]
	s_waitcnt vmcnt(35)
	v_cvt_pk_f32_fp8_e32 v[112:113], v194
	v_cvt_pk_f32_fp8_sdwa v[114:115], v194 src0_sel:WORD_1
	s_waitcnt vmcnt(34)
	v_cvt_pk_f32_fp8_e32 v[116:117], v198
	v_cvt_pk_f32_fp8_sdwa v[118:119], v198 src0_sel:WORD_1
	v_pk_add_f32 v[88:89], v[88:89], v[112:113]
	v_cvt_pk_f32_fp8_e32 v[100:101], v195
	v_pk_add_f32 v[88:89], v[88:89], v[116:117]
	v_cvt_pk_f32_fp8_sdwa v[194:195], v195 src0_sel:WORD_1
	v_pk_fma_f32 v[88:89], v[88:89], s[28:29], v[92:93] op_sel_hi:[1,0,1]
	v_cvt_pk_f32_fp8_e32 v[92:93], v175
	v_cvt_pk_bf16_f32 v178, v88, v89
	v_pk_add_f32 v[88:89], v[90:91], 0 op_sel_hi:[1,0]
	v_lshlrev_b32_e32 v90, 16, v179
	v_pk_add_f32 v[88:89], v[88:89], v[94:95]
	v_and_b32_e32 v91, 0xffff0000, v179
	v_pk_add_f32 v[88:89], v[88:89], v[98:99]
	v_pk_mul_f32 v[90:91], v[90:91], s[26:27] op_sel_hi:[1,0]
	v_pk_add_f32 v[88:89], v[88:89], v[102:103]
	v_cvt_pk_f32_fp8_sdwa v[174:175], v175 src0_sel:WORD_1
	v_pk_add_f32 v[88:89], v[88:89], v[106:107]
	v_cvt_pk_f32_fp8_e32 v[94:95], v183
	v_pk_add_f32 v[88:89], v[88:89], v[110:111]
	v_cvt_pk_f32_fp8_sdwa v[182:183], v183 src0_sel:WORD_1
	v_pk_add_f32 v[88:89], v[88:89], v[114:115]
	v_cvt_pk_f32_fp8_e32 v[98:99], v191
	v_pk_add_f32 v[88:89], v[88:89], v[118:119]
	v_cvt_pk_f32_fp8_sdwa v[190:191], v191 src0_sel:WORD_1
	v_pk_fma_f32 v[88:89], v[88:89], s[28:29], v[90:91] op_sel_hi:[1,0,1]
	v_cvt_pk_f32_fp8_e32 v[90:91], v171
	v_cvt_pk_bf16_f32 v179, v88, v89
	v_cvt_pk_f32_fp8_e32 v[88:89], v167
	v_cvt_pk_f32_fp8_sdwa v[166:167], v167 src0_sel:WORD_1
	v_cvt_pk_f32_fp8_sdwa v[170:171], v171 src0_sel:WORD_1
	v_cvt_pk_f32_fp8_e32 v[102:103], v199
	v_pk_add_f32 v[88:89], v[88:89], 0 op_sel_hi:[1,0]
	v_pk_add_f32 v[166:167], v[166:167], 0 op_sel_hi:[1,0]
	v_pk_add_f32 v[88:89], v[88:89], v[90:91]
	v_pk_add_f32 v[166:167], v[166:167], v[170:171]
	v_pk_add_f32 v[88:89], v[88:89], v[92:93]
	v_pk_add_f32 v[166:167], v[166:167], v[174:175]
	v_cvt_pk_f32_fp8_sdwa v[198:199], v199 src0_sel:WORD_1
	v_pk_add_f32 v[88:89], v[88:89], v[94:95]
	v_pk_add_f32 v[166:167], v[166:167], v[182:183]
	v_pk_add_f32 v[88:89], v[88:89], v[96:97]
	v_pk_add_f32 v[166:167], v[166:167], v[186:187]
	v_pk_add_f32 v[88:89], v[88:89], v[98:99]
	v_pk_add_f32 v[166:167], v[166:167], v[190:191]
	v_pk_add_f32 v[88:89], v[88:89], v[100:101]
	v_lshlrev_b32_e32 v90, 16, v180
	v_and_b32_e32 v91, 0xffff0000, v180
	v_pk_add_f32 v[166:167], v[166:167], v[194:195]
	v_lshlrev_b32_e32 v170, 16, v181
	v_and_b32_e32 v171, 0xffff0000, v181
	v_pk_add_f32 v[88:89], v[88:89], v[102:103]
	v_pk_mul_f32 v[90:91], v[90:91], s[26:27] op_sel_hi:[1,0]
	v_pk_add_f32 v[166:167], v[166:167], v[198:199]
	v_pk_mul_f32 v[170:171], v[170:171], s[26:27] op_sel_hi:[1,0]
	v_pk_fma_f32 v[88:89], v[88:89], s[28:29], v[90:91] op_sel_hi:[1,0,1]
	v_pk_fma_f32 v[166:167], v[166:167], s[28:29], v[170:171] op_sel_hi:[1,0,1]
	v_cvt_pk_bf16_f32 v180, v88, v89
	v_cvt_pk_bf16_f32 v181, v166, v167
	v_lshl_add_u64 v[166:167], v[86:87], 0, s[100:101]
	v_cvt_pk_f32_fp8_e32 v[170:171], v168
	global_store_dwordx4 v[166:167], v[178:181], off
	v_cvt_pk_f32_fp8_e32 v[182:183], v176
	v_cvt_pk_f32_fp8_e32 v[190:191], v184
	v_cvt_pk_f32_fp8_e32 v[178:179], v172
	v_cvt_pk_f32_fp8_e32 v[198:199], v188
	v_pk_add_f32 v[170:171], v[170:171], 0 op_sel_hi:[1,0]
	v_cvt_pk_f32_fp8_e32 v[90:91], v192
	v_pk_add_f32 v[170:171], v[170:171], v[178:179]
	v_cvt_pk_f32_fp8_e32 v[94:95], v196
	v_pk_add_f32 v[170:171], v[170:171], v[182:183]
	v_cvt_pk_f32_fp8_e32 v[98:99], v200
	v_pk_add_f32 v[170:171], v[170:171], v[190:191]
	v_cvt_pk_f32_fp8_sdwa v[174:175], v168 src0_sel:WORD_1
	v_pk_add_f32 v[170:171], v[170:171], v[198:199]
	v_cvt_pk_f32_fp8_sdwa v[180:181], v172 src0_sel:WORD_1
	v_pk_add_f32 v[170:171], v[170:171], v[90:91]
	v_lshlrev_b32_e32 v178, 16, v162
	v_pk_add_f32 v[170:171], v[170:171], v[94:95]
	v_and_b32_e32 v179, 0xffff0000, v162
	v_cvt_pk_f32_fp8_sdwa v[186:187], v176 src0_sel:WORD_1
	v_pk_add_f32 v[170:171], v[170:171], v[98:99]
	v_pk_mul_f32 v[178:179], v[178:179], s[26:27] op_sel_hi:[1,0]
	v_cvt_pk_f32_fp8_sdwa v[194:195], v184 src0_sel:WORD_1
	v_pk_fma_f32 v[170:171], v[170:171], s[28:29], v[178:179] op_sel_hi:[1,0,1]
	v_cvt_pk_f32_fp8_sdwa v[88:89], v188 src0_sel:WORD_1
	v_cvt_pk_bf16_f32 v162, v170, v171
	v_pk_add_f32 v[170:171], v[174:175], 0 op_sel_hi:[1,0]
	v_cvt_pk_f32_fp8_sdwa v[92:93], v192 src0_sel:WORD_1
	v_pk_add_f32 v[170:171], v[170:171], v[180:181]
	v_cvt_pk_f32_fp8_sdwa v[96:97], v196 src0_sel:WORD_1
	v_pk_add_f32 v[170:171], v[170:171], v[186:187]
	v_cvt_pk_f32_fp8_sdwa v[100:101], v200 src0_sel:WORD_1
	v_pk_add_f32 v[170:171], v[170:171], v[194:195]
	v_lshlrev_b32_e32 v174, 16, v163
	v_pk_add_f32 v[170:171], v[170:171], v[88:89]
	v_and_b32_e32 v175, 0xffff0000, v163
	v_pk_add_f32 v[170:171], v[170:171], v[92:93]
	v_pk_mul_f32 v[174:175], v[174:175], s[26:27] op_sel_hi:[1,0]
	v_pk_add_f32 v[170:171], v[170:171], v[96:97]
	v_cvt_pk_f32_fp8_e32 v[178:179], v177
	v_pk_add_f32 v[170:171], v[170:171], v[100:101]
	v_cvt_pk_f32_fp8_e32 v[180:181], v185
	v_pk_fma_f32 v[170:171], v[170:171], s[28:29], v[174:175] op_sel_hi:[1,0,1]
	v_cvt_pk_f32_fp8_e32 v[174:175], v173
	v_cvt_pk_bf16_f32 v163, v170, v171
	v_cvt_pk_f32_fp8_e32 v[170:171], v169
	v_cvt_pk_f32_fp8_sdwa v[168:169], v169 src0_sel:WORD_1
	v_cvt_pk_f32_fp8_sdwa v[172:173], v173 src0_sel:WORD_1
	v_cvt_pk_f32_fp8_sdwa v[182:183], v185 src0_sel:WORD_1
	v_cvt_pk_f32_fp8_e32 v[184:185], v189
	v_pk_add_f32 v[170:171], v[170:171], 0 op_sel_hi:[1,0]
	v_cvt_pk_f32_fp8_sdwa v[176:177], v177 src0_sel:WORD_1
	v_cvt_pk_f32_fp8_sdwa v[186:187], v189 src0_sel:WORD_1
	v_cvt_pk_f32_fp8_e32 v[188:189], v193
	v_pk_add_f32 v[170:171], v[170:171], v[174:175]
	v_cvt_pk_f32_fp8_sdwa v[190:191], v193 src0_sel:WORD_1
	v_cvt_pk_f32_fp8_e32 v[192:193], v197
	v_pk_add_f32 v[170:171], v[170:171], v[178:179]
	v_cvt_pk_f32_fp8_sdwa v[194:195], v197 src0_sel:WORD_1
	v_cvt_pk_f32_fp8_e32 v[196:197], v201
	v_pk_add_f32 v[170:171], v[170:171], v[180:181]
	v_pk_add_f32 v[168:169], v[168:169], 0 op_sel_hi:[1,0]
	v_pk_add_f32 v[170:171], v[170:171], v[184:185]
	v_pk_add_f32 v[168:169], v[168:169], v[172:173]
	v_pk_add_f32 v[170:171], v[170:171], v[188:189]
	v_pk_add_f32 v[168:169], v[168:169], v[176:177]
	v_cvt_pk_f32_fp8_sdwa v[198:199], v201 src0_sel:WORD_1
	v_pk_add_f32 v[170:171], v[170:171], v[192:193]
	v_lshlrev_b32_e32 v174, 16, v164
	v_and_b32_e32 v175, 0xffff0000, v164
	v_pk_add_f32 v[168:169], v[168:169], v[182:183]
	v_pk_add_f32 v[170:171], v[170:171], v[196:197]
	v_pk_mul_f32 v[174:175], v[174:175], s[26:27] op_sel_hi:[1,0]
	v_pk_add_f32 v[168:169], v[168:169], v[186:187]
	v_pk_fma_f32 v[170:171], v[170:171], s[28:29], v[174:175] op_sel_hi:[1,0,1]
	v_pk_add_f32 v[168:169], v[168:169], v[190:191]
	v_cvt_pk_bf16_f32 v164, v170, v171
	v_pk_add_f32 v[168:169], v[168:169], v[194:195]
	v_lshlrev_b32_e32 v170, 16, v165
	v_and_b32_e32 v171, 0xffff0000, v165
	v_pk_add_f32 v[168:169], v[168:169], v[198:199]
	v_pk_mul_f32 v[170:171], v[170:171], s[26:27] op_sel_hi:[1,0]
	s_waitcnt vmcnt(27)
	v_cvt_pk_f32_fp8_sdwa v[172:173], v146 src0_sel:WORD_1
	v_pk_fma_f32 v[168:169], v[168:169], s[28:29], v[170:171] op_sel_hi:[1,0,1]
	v_cvt_pk_f32_fp8_sdwa v[170:171], v142 src0_sel:WORD_1
	v_cvt_pk_bf16_f32 v165, v168, v169
	global_store_dwordx4 v[166:167], v[162:165], off offset:16
	v_cvt_pk_f32_fp8_sdwa v[166:167], v134 src0_sel:WORD_1
	v_cvt_pk_f32_fp8_sdwa v[168:169], v138 src0_sel:WORD_1
	v_cvt_pk_f32_fp8_sdwa v[162:163], v126 src0_sel:WORD_1
	v_cvt_pk_f32_fp8_sdwa v[164:165], v130 src0_sel:WORD_1
	s_waitcnt vmcnt(27)
	v_cvt_pk_f32_fp8_sdwa v[174:175], v150 src0_sel:WORD_1
	s_waitcnt vmcnt(26)
	v_cvt_pk_f32_fp8_sdwa v[176:177], v154 src0_sel:WORD_1
	v_pk_add_f32 v[162:163], v[162:163], 0 op_sel_hi:[1,0]
	v_cvt_pk_f32_fp8_e32 v[178:179], v126
	v_pk_add_f32 v[162:163], v[162:163], v[164:165]
	v_lshlrev_b32_e32 v164, 16, v159
	v_pk_add_f32 v[162:163], v[162:163], v[166:167]
	v_and_b32_e32 v165, 0xffff0000, v159
	v_pk_add_f32 v[162:163], v[162:163], v[168:169]
	v_pk_mul_f32 v[164:165], v[164:165], s[26:27] op_sel_hi:[1,0]
	v_pk_add_f32 v[162:163], v[162:163], v[170:171]
	v_cvt_pk_f32_fp8_e32 v[180:181], v130
	v_pk_add_f32 v[162:163], v[162:163], v[172:173]
	v_cvt_pk_f32_fp8_e32 v[182:183], v134
	v_pk_add_f32 v[162:163], v[162:163], v[174:175]
	v_cvt_pk_f32_fp8_e32 v[166:167], v135
	v_pk_add_f32 v[162:163], v[162:163], v[176:177]
	v_cvt_pk_f32_fp8_sdwa v[134:135], v135 src0_sel:WORD_1
	v_pk_fma_f32 v[162:163], v[162:163], s[28:29], v[164:165] op_sel_hi:[1,0,1]
	v_cvt_pk_f32_fp8_e32 v[164:165], v131
	v_cvt_pk_bf16_f32 v159, v162, v163
	v_cvt_pk_f32_fp8_e32 v[162:163], v127
	v_cvt_pk_f32_fp8_sdwa v[126:127], v127 src0_sel:WORD_1
	v_cvt_pk_f32_fp8_sdwa v[130:131], v131 src0_sel:WORD_1
	v_cvt_pk_f32_fp8_e32 v[184:185], v138
	v_cvt_pk_f32_fp8_e32 v[168:169], v139
	v_cvt_pk_f32_fp8_sdwa v[138:139], v139 src0_sel:WORD_1
	v_cvt_pk_f32_fp8_e32 v[186:187], v142
	v_cvt_pk_f32_fp8_e32 v[170:171], v143
	v_cvt_pk_f32_fp8_sdwa v[142:143], v143 src0_sel:WORD_1
	v_pk_add_f32 v[126:127], v[126:127], 0 op_sel_hi:[1,0]
	v_cvt_pk_f32_fp8_e32 v[188:189], v146
	v_cvt_pk_f32_fp8_e32 v[172:173], v147
	v_cvt_pk_f32_fp8_sdwa v[146:147], v147 src0_sel:WORD_1
	v_pk_add_f32 v[126:127], v[126:127], v[130:131]
	v_cvt_pk_f32_fp8_e32 v[190:191], v150
	v_pk_add_f32 v[178:179], v[178:179], 0 op_sel_hi:[1,0]
	v_cvt_pk_f32_fp8_e32 v[174:175], v151
	v_cvt_pk_f32_fp8_sdwa v[150:151], v151 src0_sel:WORD_1
	v_pk_add_f32 v[162:163], v[162:163], 0 op_sel_hi:[1,0]
	v_pk_add_f32 v[126:127], v[126:127], v[134:135]
	v_cvt_pk_f32_fp8_e32 v[192:193], v154
	v_pk_add_f32 v[178:179], v[178:179], v[180:181]
	v_cvt_pk_f32_fp8_e32 v[176:177], v155
	v_cvt_pk_f32_fp8_sdwa v[154:155], v155 src0_sel:WORD_1
	v_pk_add_f32 v[162:163], v[162:163], v[164:165]
	v_pk_add_f32 v[126:127], v[126:127], v[138:139]
	v_pk_add_f32 v[178:179], v[178:179], v[182:183]
	v_pk_add_f32 v[162:163], v[162:163], v[166:167]
	v_pk_add_f32 v[126:127], v[126:127], v[142:143]
	v_pk_add_f32 v[178:179], v[178:179], v[184:185]
	v_pk_add_f32 v[162:163], v[162:163], v[168:169]
	v_pk_add_f32 v[126:127], v[126:127], v[146:147]
	v_pk_add_f32 v[178:179], v[178:179], v[186:187]
	v_pk_add_f32 v[162:163], v[162:163], v[170:171]
	v_pk_add_f32 v[126:127], v[126:127], v[150:151]
	v_lshlrev_b32_e32 v130, 16, v161
	v_and_b32_e32 v131, 0xffff0000, v161
	v_pk_add_f32 v[178:179], v[178:179], v[188:189]
	v_pk_add_f32 v[162:163], v[162:163], v[172:173]
	v_pk_add_f32 v[126:127], v[126:127], v[154:155]
	v_pk_mul_f32 v[130:131], v[130:131], s[26:27] op_sel_hi:[1,0]
	v_pk_add_f32 v[178:179], v[178:179], v[190:191]
	v_lshlrev_b32_e32 v180, 16, v158
	v_and_b32_e32 v181, 0xffff0000, v158
	v_pk_add_f32 v[162:163], v[162:163], v[174:175]
	v_lshlrev_b32_e32 v164, 16, v160
	v_and_b32_e32 v165, 0xffff0000, v160
	v_pk_fma_f32 v[126:127], v[126:127], s[28:29], v[130:131] op_sel_hi:[1,0,1]
	v_cvt_pk_f32_fp8_e32 v[130:131], v128
	v_pk_add_f32 v[178:179], v[178:179], v[192:193]
	v_pk_mul_f32 v[180:181], v[180:181], s[26:27] op_sel_hi:[1,0]
	v_pk_add_f32 v[162:163], v[162:163], v[176:177]
	v_pk_mul_f32 v[164:165], v[164:165], s[26:27] op_sel_hi:[1,0]
	v_cvt_pk_f32_fp8_e32 v[138:139], v132
	v_pk_fma_f32 v[178:179], v[178:179], s[28:29], v[180:181] op_sel_hi:[1,0,1]
	v_pk_fma_f32 v[162:163], v[162:163], s[28:29], v[164:165] op_sel_hi:[1,0,1]
	v_cvt_pk_f32_fp8_e32 v[146:147], v136
	v_cvt_pk_bf16_f32 v158, v178, v179
	v_cvt_pk_bf16_f32 v160, v162, v163
	v_cvt_pk_bf16_f32 v161, v126, v127
	v_lshl_add_u64 v[126:127], v[86:87], 0, s[98:99]
	v_cvt_pk_f32_fp8_e32 v[154:155], v140
	global_store_dwordx4 v[126:127], v[158:161], off
	v_pk_add_f32 v[130:131], v[130:131], 0 op_sel_hi:[1,0]
	v_cvt_pk_f32_fp8_e32 v[164:165], v148
	v_cvt_pk_f32_fp8_e32 v[160:161], v144
	v_pk_add_f32 v[130:131], v[130:131], v[138:139]
	v_cvt_pk_f32_fp8_e32 v[168:169], v152
	v_pk_add_f32 v[130:131], v[130:131], v[146:147]
	v_cvt_pk_f32_fp8_e32 v[172:173], v156
	v_pk_add_f32 v[130:131], v[130:131], v[154:155]
	v_cvt_pk_f32_fp8_sdwa v[134:135], v128 src0_sel:WORD_1
	v_pk_add_f32 v[130:131], v[130:131], v[160:161]
	v_cvt_pk_f32_fp8_sdwa v[142:143], v132 src0_sel:WORD_1
	v_pk_add_f32 v[130:131], v[130:131], v[164:165]
	v_lshlrev_b32_e32 v138, 16, v122
	v_pk_add_f32 v[130:131], v[130:131], v[168:169]
	v_and_b32_e32 v139, 0xffff0000, v122
	v_cvt_pk_f32_fp8_sdwa v[150:151], v136 src0_sel:WORD_1
	v_pk_add_f32 v[130:131], v[130:131], v[172:173]
	v_pk_mul_f32 v[138:139], v[138:139], s[26:27] op_sel_hi:[1,0]
	v_cvt_pk_f32_fp8_sdwa v[158:159], v140 src0_sel:WORD_1
	v_pk_fma_f32 v[130:131], v[130:131], s[28:29], v[138:139] op_sel_hi:[1,0,1]
	v_cvt_pk_f32_fp8_sdwa v[162:163], v144 src0_sel:WORD_1
	v_cvt_pk_bf16_f32 v122, v130, v131
	v_pk_add_f32 v[130:131], v[134:135], 0 op_sel_hi:[1,0]
	v_cvt_pk_f32_fp8_sdwa v[166:167], v148 src0_sel:WORD_1
	v_pk_add_f32 v[130:131], v[130:131], v[142:143]
	v_cvt_pk_f32_fp8_sdwa v[170:171], v152 src0_sel:WORD_1
	v_pk_add_f32 v[130:131], v[130:131], v[150:151]
	v_cvt_pk_f32_fp8_sdwa v[174:175], v156 src0_sel:WORD_1
	v_pk_add_f32 v[130:131], v[130:131], v[158:159]
	v_lshlrev_b32_e32 v134, 16, v123
	v_pk_add_f32 v[130:131], v[130:131], v[162:163]
	v_and_b32_e32 v135, 0xffff0000, v123
	v_pk_add_f32 v[130:131], v[130:131], v[166:167]
	v_pk_mul_f32 v[134:135], v[134:135], s[26:27] op_sel_hi:[1,0]
	v_pk_add_f32 v[130:131], v[130:131], v[170:171]
	v_cvt_pk_f32_fp8_e32 v[146:147], v129
	v_pk_add_f32 v[130:131], v[130:131], v[174:175]
	v_cvt_pk_f32_fp8_sdwa v[128:129], v129 src0_sel:WORD_1
	v_pk_fma_f32 v[130:131], v[130:131], s[28:29], v[134:135] op_sel_hi:[1,0,1]
	v_cvt_pk_f32_fp8_e32 v[150:151], v133
	v_cvt_pk_bf16_f32 v123, v130, v131
	v_cvt_pk_f32_fp8_sdwa v[130:131], v133 src0_sel:WORD_1
	v_cvt_pk_f32_fp8_e32 v[154:155], v137
	v_cvt_pk_f32_fp8_sdwa v[132:133], v137 src0_sel:WORD_1
	v_cvt_pk_f32_fp8_e32 v[158:159], v141
	v_cvt_pk_f32_fp8_sdwa v[134:135], v141 src0_sel:WORD_1
	v_cvt_pk_f32_fp8_e32 v[160:161], v145
	v_cvt_pk_f32_fp8_sdwa v[136:137], v145 src0_sel:WORD_1
	v_pk_add_f32 v[146:147], v[146:147], 0 op_sel_hi:[1,0]
	v_pk_add_f32 v[128:129], v[128:129], 0 op_sel_hi:[1,0]
	v_cvt_pk_f32_fp8_e32 v[144:145], v149
	v_cvt_pk_f32_fp8_sdwa v[138:139], v149 src0_sel:WORD_1
	v_pk_add_f32 v[146:147], v[146:147], v[150:151]
	v_pk_add_f32 v[128:129], v[128:129], v[130:131]
	v_cvt_pk_f32_fp8_e32 v[148:149], v153
	v_cvt_pk_f32_fp8_sdwa v[140:141], v153 src0_sel:WORD_1
	v_pk_add_f32 v[146:147], v[146:147], v[154:155]
	v_pk_add_f32 v[128:129], v[128:129], v[132:133]
	v_cvt_pk_f32_fp8_e32 v[152:153], v157
	v_cvt_pk_f32_fp8_sdwa v[142:143], v157 src0_sel:WORD_1
	v_pk_add_f32 v[146:147], v[146:147], v[158:159]
	v_pk_add_f32 v[128:129], v[128:129], v[134:135]
	v_pk_add_f32 v[146:147], v[146:147], v[160:161]
	v_pk_add_f32 v[128:129], v[128:129], v[136:137]
	v_pk_add_f32 v[144:145], v[146:147], v[144:145]
	v_pk_add_f32 v[128:129], v[128:129], v[138:139]
	v_pk_add_f32 v[144:145], v[144:145], v[148:149]
	v_lshlrev_b32_e32 v146, 16, v124
	v_and_b32_e32 v147, 0xffff0000, v124
	v_pk_add_f32 v[128:129], v[128:129], v[140:141]
	v_lshlrev_b32_e32 v130, 16, v125
	v_and_b32_e32 v131, 0xffff0000, v125
	v_pk_add_f32 v[144:145], v[144:145], v[152:153]
	v_pk_mul_f32 v[146:147], v[146:147], s[26:27] op_sel_hi:[1,0]
	v_pk_add_f32 v[128:129], v[128:129], v[142:143]
	v_pk_mul_f32 v[130:131], v[130:131], s[26:27] op_sel_hi:[1,0]
	v_pk_fma_f32 v[144:145], v[144:145], s[28:29], v[146:147] op_sel_hi:[1,0,1]
	v_pk_fma_f32 v[128:129], v[128:129], s[28:29], v[130:131] op_sel_hi:[1,0,1]
	v_cvt_pk_bf16_f32 v124, v144, v145
	v_cvt_pk_bf16_f32 v125, v128, v129
	global_store_dwordx4 v[126:127], v[122:125], off offset:16
	s_add_i32 s43, s37, s39
	s_add_i32 s98, s43, 2
	s_ashr_i32 s99, s98, 31
	s_add_i32 s76, s35, s41
	s_lshl_b64 s[100:101], s[98:99], 11
	s_add_i32 s98, s76, -15
	s_ashr_i32 s99, s98, 31
	v_lshl_add_u64 v[122:123], v[82:83], 0, s[100:101]
	s_lshl_b64 s[98:99], s[98:99], 10
	global_load_dwordx4 v[162:165], v[122:123], off offset:16
	global_load_dwordx4 v[178:181], v[122:123], off
	v_lshl_add_u64 v[122:123], v[84:85], 0, s[98:99]
	s_add_i32 s98, s76, -14
	s_ashr_i32 s99, s98, 31
	s_lshl_b64 s[98:99], s[98:99], 10
	global_load_dwordx4 v[166:169], v[122:123], off
	v_lshl_add_u64 v[122:123], v[84:85], 0, s[98:99]
	s_add_i32 s98, s76, -13
	s_ashr_i32 s99, s98, 31
	s_lshl_b64 s[98:99], s[98:99], 10
	global_load_dwordx4 v[170:173], v[122:123], off
	v_lshl_add_u64 v[122:123], v[84:85], 0, s[98:99]
	s_add_i32 s98, s76, -12
	s_ashr_i32 s99, s98, 31
	s_lshl_b64 s[98:99], s[98:99], 10
	global_load_dwordx4 v[174:177], v[122:123], off
	v_lshl_add_u64 v[122:123], v[84:85], 0, s[98:99]
	s_add_i32 s98, s76, -11
	s_ashr_i32 s99, s98, 31
	s_lshl_b64 s[98:99], s[98:99], 10
	global_load_dwordx4 v[182:185], v[122:123], off
	v_lshl_add_u64 v[122:123], v[84:85], 0, s[98:99]
	s_add_i32 s98, s76, -10
	s_ashr_i32 s99, s98, 31
	s_lshl_b64 s[98:99], s[98:99], 10
	global_load_dwordx4 v[186:189], v[122:123], off
	v_lshl_add_u64 v[122:123], v[84:85], 0, s[98:99]
	s_add_i32 s98, s76, -9
	s_ashr_i32 s99, s98, 31
	s_lshl_b64 s[98:99], s[98:99], 10
	global_load_dwordx4 v[190:193], v[122:123], off
	v_lshl_add_u64 v[122:123], v[84:85], 0, s[98:99]
	s_add_i32 s98, s76, -8
	s_ashr_i32 s99, s98, 31
	s_lshl_b64 s[98:99], s[98:99], 10
	global_load_dwordx4 v[194:197], v[122:123], off
	v_lshl_add_u64 v[122:123], v[84:85], 0, s[98:99]
	global_load_dwordx4 v[198:201], v[122:123], off
	s_add_i32 s98, s43, 3
	s_ashr_i32 s99, s98, 31
	s_add_i32 s78, s76, -7
	s_lshl_b64 s[98:99], s[98:99], 11
	s_ashr_i32 s79, s78, 31
	v_lshl_add_u64 v[126:127], v[82:83], 0, s[98:99]
	s_lshl_b64 s[78:79], s[78:79], 10
	global_load_dwordx4 v[122:125], v[126:127], off offset:16
	global_load_dwordx4 v[158:161], v[126:127], off
	v_lshl_add_u64 v[126:127], v[84:85], 0, s[78:79]
	s_add_i32 s78, s76, -6
	s_ashr_i32 s79, s78, 31
	s_lshl_b64 s[78:79], s[78:79], 10
	v_lshl_add_u64 v[130:131], v[84:85], 0, s[78:79]
	s_add_i32 s78, s76, -5
	s_ashr_i32 s79, s78, 31
	s_lshl_b64 s[78:79], s[78:79], 10
	v_lshl_add_u64 v[134:135], v[84:85], 0, s[78:79]
	s_add_i32 s78, s76, -4
	s_ashr_i32 s79, s78, 31
	s_lshl_b64 s[78:79], s[78:79], 10
	v_lshl_add_u64 v[138:139], v[84:85], 0, s[78:79]
	s_add_i32 s78, s76, -3
	s_ashr_i32 s79, s78, 31
	s_lshl_b64 s[78:79], s[78:79], 10
	v_lshl_add_u64 v[142:143], v[84:85], 0, s[78:79]
	s_add_i32 s78, s76, -2
	global_load_dwordx4 v[126:129], v[126:127], off
	s_ashr_i32 s79, s78, 31
	global_load_dwordx4 v[130:133], v[130:131], off
	s_lshl_b64 s[78:79], s[78:79], 10
	global_load_dwordx4 v[134:137], v[134:135], off
	v_lshl_add_u64 v[146:147], v[84:85], 0, s[78:79]
	s_add_i32 s78, s76, -1
	global_load_dwordx4 v[138:141], v[138:139], off
	s_ashr_i32 s79, s78, 31
	global_load_dwordx4 v[142:145], v[142:143], off
	s_lshl_b64 s[78:79], s[78:79], 10
	s_ashr_i32 s77, s76, 31
	global_load_dwordx4 v[146:149], v[146:147], off
	v_lshl_add_u64 v[150:151], v[84:85], 0, s[78:79]
	s_lshl_b64 s[76:77], s[76:77], 10
	global_load_dwordx4 v[150:153], v[150:151], off
	v_lshl_add_u64 v[154:155], v[84:85], 0, s[76:77]
	global_load_dwordx4 v[154:157], v[154:155], off
	s_add_i32 s39, s39, 2
	s_add_i32 s41, s41, 16
	s_waitcnt vmcnt(41)
	v_cvt_pk_f32_fp8_e32 v[88:89], v46
	v_cvt_pk_f32_fp8_sdwa v[90:91], v46 src0_sel:WORD_1
	v_pk_add_f32 v[88:89], v[88:89], 0 op_sel_hi:[1,0]
	s_waitcnt vmcnt(40)
	v_cvt_pk_f32_fp8_e32 v[92:93], v50
	v_cvt_pk_f32_fp8_sdwa v[94:95], v50 src0_sel:WORD_1
	v_pk_add_f32 v[88:89], v[88:89], v[92:93]
	s_waitcnt vmcnt(39)
	v_cvt_pk_f32_fp8_e32 v[96:97], v54
	v_lshlrev_b32_e32 v92, 16, v58
	v_and_b32_e32 v93, 0xffff0000, v58
	v_cvt_pk_f32_fp8_sdwa v[98:99], v54 src0_sel:WORD_1
	v_pk_add_f32 v[88:89], v[88:89], v[96:97]
	s_waitcnt vmcnt(38)
	v_cvt_pk_f32_fp8_e32 v[100:101], v62
	v_pk_mul_f32 v[92:93], v[92:93], s[26:27] op_sel_hi:[1,0]
	v_cvt_pk_f32_fp8_sdwa v[102:103], v62 src0_sel:WORD_1
	v_pk_add_f32 v[88:89], v[88:89], v[100:101]
	s_waitcnt vmcnt(37)
	v_cvt_pk_f32_fp8_e32 v[104:105], v66
	v_cvt_pk_f32_fp8_sdwa v[106:107], v66 src0_sel:WORD_1
	v_cvt_pk_f32_fp8_e32 v[96:97], v67
	v_cvt_pk_f32_fp8_sdwa v[66:67], v67 src0_sel:WORD_1
	v_pk_add_f32 v[88:89], v[88:89], v[104:105]
	s_waitcnt vmcnt(36)
	v_cvt_pk_f32_fp8_e32 v[108:109], v70
	v_cvt_pk_f32_fp8_sdwa v[110:111], v70 src0_sel:WORD_1
	v_pk_add_f32 v[88:89], v[88:89], v[108:109]
	s_waitcnt vmcnt(35)
	v_cvt_pk_f32_fp8_e32 v[112:113], v74
	v_cvt_pk_f32_fp8_sdwa v[114:115], v74 src0_sel:WORD_1
	s_waitcnt vmcnt(34)
	v_cvt_pk_f32_fp8_e32 v[116:117], v78
	v_cvt_pk_f32_fp8_sdwa v[118:119], v78 src0_sel:WORD_1
	v_pk_add_f32 v[88:89], v[88:89], v[112:113]
	v_cvt_pk_f32_fp8_e32 v[100:101], v75
	v_pk_add_f32 v[88:89], v[88:89], v[116:117]
	v_cvt_pk_f32_fp8_sdwa v[74:75], v75 src0_sel:WORD_1
	v_pk_fma_f32 v[88:89], v[88:89], s[28:29], v[92:93] op_sel_hi:[1,0,1]
	v_cvt_pk_f32_fp8_e32 v[92:93], v55
	v_cvt_pk_bf16_f32 v58, v88, v89
	v_pk_add_f32 v[88:89], v[90:91], 0 op_sel_hi:[1,0]
	v_lshlrev_b32_e32 v90, 16, v59
	v_pk_add_f32 v[88:89], v[88:89], v[94:95]
	v_and_b32_e32 v91, 0xffff0000, v59
	v_pk_add_f32 v[88:89], v[88:89], v[98:99]
	v_pk_mul_f32 v[90:91], v[90:91], s[26:27] op_sel_hi:[1,0]
	v_pk_add_f32 v[88:89], v[88:89], v[102:103]
	v_cvt_pk_f32_fp8_sdwa v[54:55], v55 src0_sel:WORD_1
	v_pk_add_f32 v[88:89], v[88:89], v[106:107]
	v_cvt_pk_f32_fp8_e32 v[94:95], v63
	v_pk_add_f32 v[88:89], v[88:89], v[110:111]
	v_cvt_pk_f32_fp8_sdwa v[62:63], v63 src0_sel:WORD_1
	v_pk_add_f32 v[88:89], v[88:89], v[114:115]
	v_cvt_pk_f32_fp8_e32 v[98:99], v71
	v_pk_add_f32 v[88:89], v[88:89], v[118:119]
	v_cvt_pk_f32_fp8_sdwa v[70:71], v71 src0_sel:WORD_1
	v_pk_fma_f32 v[88:89], v[88:89], s[28:29], v[90:91] op_sel_hi:[1,0,1]
	v_cvt_pk_f32_fp8_e32 v[90:91], v51
	v_cvt_pk_bf16_f32 v59, v88, v89
	v_cvt_pk_f32_fp8_e32 v[88:89], v47
	v_cvt_pk_f32_fp8_sdwa v[46:47], v47 src0_sel:WORD_1
	v_cvt_pk_f32_fp8_sdwa v[50:51], v51 src0_sel:WORD_1
	v_cvt_pk_f32_fp8_e32 v[102:103], v79
	v_pk_add_f32 v[88:89], v[88:89], 0 op_sel_hi:[1,0]
	v_pk_add_f32 v[46:47], v[46:47], 0 op_sel_hi:[1,0]
	v_pk_add_f32 v[88:89], v[88:89], v[90:91]
	v_pk_add_f32 v[46:47], v[46:47], v[50:51]
	v_pk_add_f32 v[88:89], v[88:89], v[92:93]
	v_pk_add_f32 v[46:47], v[46:47], v[54:55]
	v_cvt_pk_f32_fp8_sdwa v[78:79], v79 src0_sel:WORD_1
	v_pk_add_f32 v[88:89], v[88:89], v[94:95]
	v_pk_add_f32 v[46:47], v[46:47], v[62:63]
	v_pk_add_f32 v[88:89], v[88:89], v[96:97]
	v_pk_add_f32 v[46:47], v[46:47], v[66:67]
	v_pk_add_f32 v[88:89], v[88:89], v[98:99]
	v_pk_add_f32 v[46:47], v[46:47], v[70:71]
	v_pk_add_f32 v[88:89], v[88:89], v[100:101]
	v_lshlrev_b32_e32 v90, 16, v60
	v_and_b32_e32 v91, 0xffff0000, v60
	v_pk_add_f32 v[46:47], v[46:47], v[74:75]
	v_lshlrev_b32_e32 v50, 16, v61
	v_and_b32_e32 v51, 0xffff0000, v61
	v_pk_add_f32 v[88:89], v[88:89], v[102:103]
	v_pk_mul_f32 v[90:91], v[90:91], s[26:27] op_sel_hi:[1,0]
	v_pk_add_f32 v[46:47], v[46:47], v[78:79]
	v_pk_mul_f32 v[50:51], v[50:51], s[26:27] op_sel_hi:[1,0]
	v_pk_fma_f32 v[88:89], v[88:89], s[28:29], v[90:91] op_sel_hi:[1,0,1]
	v_pk_fma_f32 v[46:47], v[46:47], s[28:29], v[50:51] op_sel_hi:[1,0,1]
	v_cvt_pk_bf16_f32 v60, v88, v89
	v_cvt_pk_bf16_f32 v61, v46, v47
	v_lshl_add_u64 v[46:47], v[86:87], 0, s[8:9]
	v_cvt_pk_f32_fp8_e32 v[50:51], v48
	global_store_dwordx4 v[46:47], v[58:61], off
	v_cvt_pk_f32_fp8_e32 v[62:63], v56
	v_cvt_pk_f32_fp8_e32 v[70:71], v64
	v_cvt_pk_f32_fp8_e32 v[58:59], v52
	v_cvt_pk_f32_fp8_e32 v[78:79], v68
	v_pk_add_f32 v[50:51], v[50:51], 0 op_sel_hi:[1,0]
	v_cvt_pk_f32_fp8_e32 v[90:91], v72
	v_pk_add_f32 v[50:51], v[50:51], v[58:59]
	v_cvt_pk_f32_fp8_e32 v[94:95], v76
	v_pk_add_f32 v[50:51], v[50:51], v[62:63]
	v_cvt_pk_f32_fp8_e32 v[98:99], v80
	v_pk_add_f32 v[50:51], v[50:51], v[70:71]
	v_cvt_pk_f32_fp8_sdwa v[54:55], v48 src0_sel:WORD_1
	v_pk_add_f32 v[50:51], v[50:51], v[78:79]
	v_cvt_pk_f32_fp8_sdwa v[60:61], v52 src0_sel:WORD_1
	v_pk_add_f32 v[50:51], v[50:51], v[90:91]
	v_lshlrev_b32_e32 v58, 16, v42
	v_pk_add_f32 v[50:51], v[50:51], v[94:95]
	v_and_b32_e32 v59, 0xffff0000, v42
	v_cvt_pk_f32_fp8_sdwa v[66:67], v56 src0_sel:WORD_1
	v_pk_add_f32 v[50:51], v[50:51], v[98:99]
	v_pk_mul_f32 v[58:59], v[58:59], s[26:27] op_sel_hi:[1,0]
	v_cvt_pk_f32_fp8_sdwa v[74:75], v64 src0_sel:WORD_1
	v_pk_fma_f32 v[50:51], v[50:51], s[28:29], v[58:59] op_sel_hi:[1,0,1]
	v_cvt_pk_f32_fp8_sdwa v[88:89], v68 src0_sel:WORD_1
	v_cvt_pk_bf16_f32 v42, v50, v51
	v_pk_add_f32 v[50:51], v[54:55], 0 op_sel_hi:[1,0]
	v_cvt_pk_f32_fp8_sdwa v[92:93], v72 src0_sel:WORD_1
	v_pk_add_f32 v[50:51], v[50:51], v[60:61]
	v_cvt_pk_f32_fp8_sdwa v[96:97], v76 src0_sel:WORD_1
	v_pk_add_f32 v[50:51], v[50:51], v[66:67]
	v_cvt_pk_f32_fp8_sdwa v[100:101], v80 src0_sel:WORD_1
	v_pk_add_f32 v[50:51], v[50:51], v[74:75]
	v_lshlrev_b32_e32 v54, 16, v43
	v_pk_add_f32 v[50:51], v[50:51], v[88:89]
	v_and_b32_e32 v55, 0xffff0000, v43
	v_pk_add_f32 v[50:51], v[50:51], v[92:93]
	v_pk_mul_f32 v[54:55], v[54:55], s[26:27] op_sel_hi:[1,0]
	v_pk_add_f32 v[50:51], v[50:51], v[96:97]
	v_cvt_pk_f32_fp8_e32 v[58:59], v57
	v_pk_add_f32 v[50:51], v[50:51], v[100:101]
	v_cvt_pk_f32_fp8_e32 v[60:61], v65
	v_pk_fma_f32 v[50:51], v[50:51], s[28:29], v[54:55] op_sel_hi:[1,0,1]
	v_cvt_pk_f32_fp8_e32 v[54:55], v53
	v_cvt_pk_bf16_f32 v43, v50, v51
	v_cvt_pk_f32_fp8_e32 v[50:51], v49
	v_cvt_pk_f32_fp8_sdwa v[48:49], v49 src0_sel:WORD_1
	v_cvt_pk_f32_fp8_sdwa v[52:53], v53 src0_sel:WORD_1
	v_cvt_pk_f32_fp8_sdwa v[62:63], v65 src0_sel:WORD_1
	v_cvt_pk_f32_fp8_e32 v[64:65], v69
	v_pk_add_f32 v[50:51], v[50:51], 0 op_sel_hi:[1,0]
	v_cvt_pk_f32_fp8_sdwa v[56:57], v57 src0_sel:WORD_1
	v_cvt_pk_f32_fp8_sdwa v[66:67], v69 src0_sel:WORD_1
	v_cvt_pk_f32_fp8_e32 v[68:69], v73
	v_pk_add_f32 v[50:51], v[50:51], v[54:55]
	v_cvt_pk_f32_fp8_sdwa v[70:71], v73 src0_sel:WORD_1
	v_cvt_pk_f32_fp8_e32 v[72:73], v77
	v_pk_add_f32 v[50:51], v[50:51], v[58:59]
	v_cvt_pk_f32_fp8_sdwa v[74:75], v77 src0_sel:WORD_1
	v_cvt_pk_f32_fp8_e32 v[76:77], v81
	v_pk_add_f32 v[50:51], v[50:51], v[60:61]
	v_pk_add_f32 v[48:49], v[48:49], 0 op_sel_hi:[1,0]
	v_pk_add_f32 v[50:51], v[50:51], v[64:65]
	v_pk_add_f32 v[48:49], v[48:49], v[52:53]
	v_pk_add_f32 v[50:51], v[50:51], v[68:69]
	v_pk_add_f32 v[48:49], v[48:49], v[56:57]
	v_cvt_pk_f32_fp8_sdwa v[78:79], v81 src0_sel:WORD_1
	v_pk_add_f32 v[50:51], v[50:51], v[72:73]
	v_lshlrev_b32_e32 v54, 16, v44
	v_and_b32_e32 v55, 0xffff0000, v44
	v_pk_add_f32 v[48:49], v[48:49], v[62:63]
	v_pk_add_f32 v[50:51], v[50:51], v[76:77]
	v_pk_mul_f32 v[54:55], v[54:55], s[26:27] op_sel_hi:[1,0]
	v_pk_add_f32 v[48:49], v[48:49], v[66:67]
	v_pk_fma_f32 v[50:51], v[50:51], s[28:29], v[54:55] op_sel_hi:[1,0,1]
	v_pk_add_f32 v[48:49], v[48:49], v[70:71]
	v_cvt_pk_bf16_f32 v44, v50, v51
	v_pk_add_f32 v[48:49], v[48:49], v[74:75]
	v_lshlrev_b32_e32 v50, 16, v45
	v_and_b32_e32 v51, 0xffff0000, v45
	v_pk_add_f32 v[48:49], v[48:49], v[78:79]
	v_pk_mul_f32 v[50:51], v[50:51], s[26:27] op_sel_hi:[1,0]
	s_waitcnt vmcnt(27)
	v_cvt_pk_f32_fp8_sdwa v[52:53], v26 src0_sel:WORD_1
	v_pk_fma_f32 v[48:49], v[48:49], s[28:29], v[50:51] op_sel_hi:[1,0,1]
	v_cvt_pk_f32_fp8_sdwa v[50:51], v22 src0_sel:WORD_1
	v_cvt_pk_bf16_f32 v45, v48, v49
	global_store_dwordx4 v[46:47], v[42:45], off offset:16
	v_cvt_pk_f32_fp8_sdwa v[46:47], v14 src0_sel:WORD_1
	v_cvt_pk_f32_fp8_sdwa v[48:49], v18 src0_sel:WORD_1
	v_cvt_pk_f32_fp8_sdwa v[42:43], v6 src0_sel:WORD_1
	v_cvt_pk_f32_fp8_sdwa v[44:45], v10 src0_sel:WORD_1
	s_waitcnt vmcnt(27)
	v_cvt_pk_f32_fp8_sdwa v[54:55], v30 src0_sel:WORD_1
	s_waitcnt vmcnt(26)
	v_cvt_pk_f32_fp8_sdwa v[56:57], v34 src0_sel:WORD_1
	v_pk_add_f32 v[42:43], v[42:43], 0 op_sel_hi:[1,0]
	v_cvt_pk_f32_fp8_e32 v[58:59], v6
	v_pk_add_f32 v[42:43], v[42:43], v[44:45]
	v_lshlrev_b32_e32 v44, 16, v39
	v_pk_add_f32 v[42:43], v[42:43], v[46:47]
	v_and_b32_e32 v45, 0xffff0000, v39
	v_pk_add_f32 v[42:43], v[42:43], v[48:49]
	v_pk_mul_f32 v[44:45], v[44:45], s[26:27] op_sel_hi:[1,0]
	v_pk_add_f32 v[42:43], v[42:43], v[50:51]
	v_cvt_pk_f32_fp8_e32 v[60:61], v10
	v_pk_add_f32 v[42:43], v[42:43], v[52:53]
	v_cvt_pk_f32_fp8_e32 v[62:63], v14
	v_pk_add_f32 v[42:43], v[42:43], v[54:55]
	v_cvt_pk_f32_fp8_e32 v[46:47], v15
	v_pk_add_f32 v[42:43], v[42:43], v[56:57]
	v_cvt_pk_f32_fp8_sdwa v[14:15], v15 src0_sel:WORD_1
	v_pk_fma_f32 v[42:43], v[42:43], s[28:29], v[44:45] op_sel_hi:[1,0,1]
	v_cvt_pk_f32_fp8_e32 v[44:45], v11
	v_cvt_pk_bf16_f32 v39, v42, v43
	v_cvt_pk_f32_fp8_e32 v[42:43], v7
	v_cvt_pk_f32_fp8_sdwa v[6:7], v7 src0_sel:WORD_1
	v_cvt_pk_f32_fp8_sdwa v[10:11], v11 src0_sel:WORD_1
	v_cvt_pk_f32_fp8_e32 v[64:65], v18
	v_cvt_pk_f32_fp8_e32 v[48:49], v19
	v_cvt_pk_f32_fp8_sdwa v[18:19], v19 src0_sel:WORD_1
	v_cvt_pk_f32_fp8_e32 v[66:67], v22
	v_cvt_pk_f32_fp8_e32 v[50:51], v23
	v_cvt_pk_f32_fp8_sdwa v[22:23], v23 src0_sel:WORD_1
	v_pk_add_f32 v[6:7], v[6:7], 0 op_sel_hi:[1,0]
	v_cvt_pk_f32_fp8_e32 v[68:69], v26
	v_cvt_pk_f32_fp8_e32 v[52:53], v27
	v_cvt_pk_f32_fp8_sdwa v[26:27], v27 src0_sel:WORD_1
	v_pk_add_f32 v[6:7], v[6:7], v[10:11]
	v_cvt_pk_f32_fp8_e32 v[70:71], v30
	v_pk_add_f32 v[58:59], v[58:59], 0 op_sel_hi:[1,0]
	v_cvt_pk_f32_fp8_e32 v[54:55], v31
	v_cvt_pk_f32_fp8_sdwa v[30:31], v31 src0_sel:WORD_1
	v_pk_add_f32 v[42:43], v[42:43], 0 op_sel_hi:[1,0]
	v_pk_add_f32 v[6:7], v[6:7], v[14:15]
	v_cvt_pk_f32_fp8_e32 v[72:73], v34
	v_pk_add_f32 v[58:59], v[58:59], v[60:61]
	v_cvt_pk_f32_fp8_e32 v[56:57], v35
	v_cvt_pk_f32_fp8_sdwa v[34:35], v35 src0_sel:WORD_1
	v_pk_add_f32 v[42:43], v[42:43], v[44:45]
	v_pk_add_f32 v[6:7], v[6:7], v[18:19]
	v_pk_add_f32 v[58:59], v[58:59], v[62:63]
	v_pk_add_f32 v[42:43], v[42:43], v[46:47]
	v_pk_add_f32 v[6:7], v[6:7], v[22:23]
	v_pk_add_f32 v[58:59], v[58:59], v[64:65]
	v_pk_add_f32 v[42:43], v[42:43], v[48:49]
	v_pk_add_f32 v[6:7], v[6:7], v[26:27]
	v_pk_add_f32 v[58:59], v[58:59], v[66:67]
	v_pk_add_f32 v[42:43], v[42:43], v[50:51]
	v_pk_add_f32 v[6:7], v[6:7], v[30:31]
	v_lshlrev_b32_e32 v10, 16, v41
	v_and_b32_e32 v11, 0xffff0000, v41
	v_pk_add_f32 v[58:59], v[58:59], v[68:69]
	v_pk_add_f32 v[42:43], v[42:43], v[52:53]
	v_pk_add_f32 v[6:7], v[6:7], v[34:35]
	v_pk_mul_f32 v[10:11], v[10:11], s[26:27] op_sel_hi:[1,0]
	v_pk_add_f32 v[58:59], v[58:59], v[70:71]
	v_lshlrev_b32_e32 v60, 16, v38
	v_and_b32_e32 v61, 0xffff0000, v38
	v_pk_add_f32 v[42:43], v[42:43], v[54:55]
	v_lshlrev_b32_e32 v44, 16, v40
	v_and_b32_e32 v45, 0xffff0000, v40
	v_pk_fma_f32 v[6:7], v[6:7], s[28:29], v[10:11] op_sel_hi:[1,0,1]
	v_cvt_pk_f32_fp8_e32 v[10:11], v8
	v_pk_add_f32 v[58:59], v[58:59], v[72:73]
	v_pk_mul_f32 v[60:61], v[60:61], s[26:27] op_sel_hi:[1,0]
	v_pk_add_f32 v[42:43], v[42:43], v[56:57]
	v_pk_mul_f32 v[44:45], v[44:45], s[26:27] op_sel_hi:[1,0]
	v_cvt_pk_f32_fp8_e32 v[18:19], v12
	v_pk_fma_f32 v[58:59], v[58:59], s[28:29], v[60:61] op_sel_hi:[1,0,1]
	v_pk_fma_f32 v[42:43], v[42:43], s[28:29], v[44:45] op_sel_hi:[1,0,1]
	v_cvt_pk_f32_fp8_e32 v[26:27], v16
	v_cvt_pk_bf16_f32 v38, v58, v59
	v_cvt_pk_bf16_f32 v40, v42, v43
	v_cvt_pk_bf16_f32 v41, v6, v7
	v_lshl_add_u64 v[6:7], v[86:87], 0, s[6:7]
	v_cvt_pk_f32_fp8_e32 v[34:35], v20
	global_store_dwordx4 v[6:7], v[38:41], off
	v_pk_add_f32 v[10:11], v[10:11], 0 op_sel_hi:[1,0]
	v_cvt_pk_f32_fp8_e32 v[44:45], v28
	v_cvt_pk_f32_fp8_e32 v[40:41], v24
	v_pk_add_f32 v[10:11], v[10:11], v[18:19]
	v_cvt_pk_f32_fp8_e32 v[48:49], v32
	v_pk_add_f32 v[10:11], v[10:11], v[26:27]
	v_cvt_pk_f32_fp8_e32 v[52:53], v36
	v_pk_add_f32 v[10:11], v[10:11], v[34:35]
	v_cvt_pk_f32_fp8_sdwa v[14:15], v8 src0_sel:WORD_1
	v_pk_add_f32 v[10:11], v[10:11], v[40:41]
	v_cvt_pk_f32_fp8_sdwa v[22:23], v12 src0_sel:WORD_1
	v_pk_add_f32 v[10:11], v[10:11], v[44:45]
	v_lshlrev_b32_e32 v18, 16, v2
	v_pk_add_f32 v[10:11], v[10:11], v[48:49]
	v_and_b32_e32 v19, 0xffff0000, v2
	v_cvt_pk_f32_fp8_sdwa v[30:31], v16 src0_sel:WORD_1
	v_pk_add_f32 v[10:11], v[10:11], v[52:53]
	v_pk_mul_f32 v[18:19], v[18:19], s[26:27] op_sel_hi:[1,0]
	v_cvt_pk_f32_fp8_sdwa v[38:39], v20 src0_sel:WORD_1
	v_pk_fma_f32 v[10:11], v[10:11], s[28:29], v[18:19] op_sel_hi:[1,0,1]
	v_cvt_pk_f32_fp8_sdwa v[42:43], v24 src0_sel:WORD_1
	v_cvt_pk_bf16_f32 v2, v10, v11
	v_pk_add_f32 v[10:11], v[14:15], 0 op_sel_hi:[1,0]
	v_cvt_pk_f32_fp8_sdwa v[46:47], v28 src0_sel:WORD_1
	v_pk_add_f32 v[10:11], v[10:11], v[22:23]
	v_cvt_pk_f32_fp8_sdwa v[50:51], v32 src0_sel:WORD_1
	v_pk_add_f32 v[10:11], v[10:11], v[30:31]
	v_cvt_pk_f32_fp8_sdwa v[54:55], v36 src0_sel:WORD_1
	v_pk_add_f32 v[10:11], v[10:11], v[38:39]
	v_lshlrev_b32_e32 v14, 16, v3
	v_pk_add_f32 v[10:11], v[10:11], v[42:43]
	v_and_b32_e32 v15, 0xffff0000, v3
	v_pk_add_f32 v[10:11], v[10:11], v[46:47]
	v_pk_mul_f32 v[14:15], v[14:15], s[26:27] op_sel_hi:[1,0]
	v_pk_add_f32 v[10:11], v[10:11], v[50:51]
	v_cvt_pk_f32_fp8_e32 v[26:27], v9
	v_pk_add_f32 v[10:11], v[10:11], v[54:55]
	v_cvt_pk_f32_fp8_sdwa v[8:9], v9 src0_sel:WORD_1
	v_pk_fma_f32 v[10:11], v[10:11], s[28:29], v[14:15] op_sel_hi:[1,0,1]
	v_cvt_pk_f32_fp8_e32 v[30:31], v13
	v_cvt_pk_bf16_f32 v3, v10, v11
	v_cvt_pk_f32_fp8_sdwa v[10:11], v13 src0_sel:WORD_1
	v_cvt_pk_f32_fp8_e32 v[34:35], v17
	v_cvt_pk_f32_fp8_sdwa v[12:13], v17 src0_sel:WORD_1
	v_cvt_pk_f32_fp8_e32 v[38:39], v21
	v_cvt_pk_f32_fp8_sdwa v[14:15], v21 src0_sel:WORD_1
	v_cvt_pk_f32_fp8_e32 v[40:41], v25
	v_cvt_pk_f32_fp8_sdwa v[16:17], v25 src0_sel:WORD_1
	v_pk_add_f32 v[26:27], v[26:27], 0 op_sel_hi:[1,0]
	v_pk_add_f32 v[8:9], v[8:9], 0 op_sel_hi:[1,0]
	v_cvt_pk_f32_fp8_e32 v[24:25], v29
	v_cvt_pk_f32_fp8_sdwa v[18:19], v29 src0_sel:WORD_1
	v_pk_add_f32 v[26:27], v[26:27], v[30:31]
	v_pk_add_f32 v[8:9], v[8:9], v[10:11]
	v_cvt_pk_f32_fp8_e32 v[28:29], v33
	v_cvt_pk_f32_fp8_sdwa v[20:21], v33 src0_sel:WORD_1
	v_pk_add_f32 v[26:27], v[26:27], v[34:35]
	v_pk_add_f32 v[8:9], v[8:9], v[12:13]
	v_cvt_pk_f32_fp8_e32 v[32:33], v37
	v_cvt_pk_f32_fp8_sdwa v[22:23], v37 src0_sel:WORD_1
	v_pk_add_f32 v[26:27], v[26:27], v[38:39]
	v_pk_add_f32 v[8:9], v[8:9], v[14:15]
	v_pk_add_f32 v[26:27], v[26:27], v[40:41]
	v_pk_add_f32 v[8:9], v[8:9], v[16:17]
	v_pk_add_f32 v[24:25], v[26:27], v[24:25]
	v_pk_add_f32 v[8:9], v[8:9], v[18:19]
	v_pk_add_f32 v[24:25], v[24:25], v[28:29]
	v_lshlrev_b32_e32 v26, 16, v4
	v_and_b32_e32 v27, 0xffff0000, v4
	v_pk_add_f32 v[8:9], v[8:9], v[20:21]
	v_lshlrev_b32_e32 v10, 16, v5
	v_and_b32_e32 v11, 0xffff0000, v5
	v_pk_add_f32 v[24:25], v[24:25], v[32:33]
	v_pk_mul_f32 v[26:27], v[26:27], s[26:27] op_sel_hi:[1,0]
	v_pk_add_f32 v[8:9], v[8:9], v[22:23]
	v_pk_mul_f32 v[10:11], v[10:11], s[26:27] op_sel_hi:[1,0]
	v_pk_fma_f32 v[24:25], v[24:25], s[28:29], v[26:27] op_sel_hi:[1,0,1]
	v_pk_fma_f32 v[8:9], v[8:9], s[28:29], v[10:11] op_sel_hi:[1,0,1]
	v_cvt_pk_bf16_f32 v4, v24, v25
	v_cvt_pk_bf16_f32 v5, v8, v9
	global_store_dwordx4 v[6:7], v[2:5], off offset:16
	s_waitcnt vmcnt(21)
	v_cvt_pk_f32_fp8_e32 v[88:89], v166
	v_cvt_pk_f32_fp8_sdwa v[90:91], v166 src0_sel:WORD_1
	v_pk_add_f32 v[88:89], v[88:89], 0 op_sel_hi:[1,0]
	s_waitcnt vmcnt(20)
	v_cvt_pk_f32_fp8_e32 v[92:93], v170
	v_cvt_pk_f32_fp8_sdwa v[94:95], v170 src0_sel:WORD_1
	v_pk_add_f32 v[88:89], v[88:89], v[92:93]
	s_waitcnt vmcnt(19)
	v_cvt_pk_f32_fp8_e32 v[96:97], v174
	v_lshlrev_b32_e32 v92, 16, v178
	v_and_b32_e32 v93, 0xffff0000, v178
	v_cvt_pk_f32_fp8_sdwa v[98:99], v174 src0_sel:WORD_1
	v_pk_add_f32 v[88:89], v[88:89], v[96:97]
	s_waitcnt vmcnt(18)
	v_cvt_pk_f32_fp8_e32 v[100:101], v182
	v_pk_mul_f32 v[92:93], v[92:93], s[26:27] op_sel_hi:[1,0]
	v_cvt_pk_f32_fp8_sdwa v[102:103], v182 src0_sel:WORD_1
	v_pk_add_f32 v[88:89], v[88:89], v[100:101]
	s_waitcnt vmcnt(17)
	v_cvt_pk_f32_fp8_e32 v[104:105], v186
	v_cvt_pk_f32_fp8_sdwa v[106:107], v186 src0_sel:WORD_1
	v_cvt_pk_f32_fp8_e32 v[96:97], v187
	v_cvt_pk_f32_fp8_sdwa v[186:187], v187 src0_sel:WORD_1
	v_pk_add_f32 v[88:89], v[88:89], v[104:105]
	s_waitcnt vmcnt(16)
	v_cvt_pk_f32_fp8_e32 v[108:109], v190
	v_cvt_pk_f32_fp8_sdwa v[110:111], v190 src0_sel:WORD_1
	v_pk_add_f32 v[88:89], v[88:89], v[108:109]
	s_waitcnt vmcnt(15)
	v_cvt_pk_f32_fp8_e32 v[112:113], v194
	v_cvt_pk_f32_fp8_sdwa v[114:115], v194 src0_sel:WORD_1
	s_waitcnt vmcnt(14)
	v_cvt_pk_f32_fp8_e32 v[116:117], v198
	v_cvt_pk_f32_fp8_sdwa v[118:119], v198 src0_sel:WORD_1
	v_pk_add_f32 v[88:89], v[88:89], v[112:113]
	v_cvt_pk_f32_fp8_e32 v[100:101], v195
	v_pk_add_f32 v[88:89], v[88:89], v[116:117]
	v_cvt_pk_f32_fp8_sdwa v[194:195], v195 src0_sel:WORD_1
	v_pk_fma_f32 v[88:89], v[88:89], s[28:29], v[92:93] op_sel_hi:[1,0,1]
	v_cvt_pk_f32_fp8_e32 v[92:93], v175
	v_cvt_pk_bf16_f32 v178, v88, v89
	v_pk_add_f32 v[88:89], v[90:91], 0 op_sel_hi:[1,0]
	v_lshlrev_b32_e32 v90, 16, v179
	v_pk_add_f32 v[88:89], v[88:89], v[94:95]
	v_and_b32_e32 v91, 0xffff0000, v179
	v_pk_add_f32 v[88:89], v[88:89], v[98:99]
	v_pk_mul_f32 v[90:91], v[90:91], s[26:27] op_sel_hi:[1,0]
	v_pk_add_f32 v[88:89], v[88:89], v[102:103]
	v_cvt_pk_f32_fp8_sdwa v[174:175], v175 src0_sel:WORD_1
	v_pk_add_f32 v[88:89], v[88:89], v[106:107]
	v_cvt_pk_f32_fp8_e32 v[94:95], v183
	v_pk_add_f32 v[88:89], v[88:89], v[110:111]
	v_cvt_pk_f32_fp8_sdwa v[182:183], v183 src0_sel:WORD_1
	v_pk_add_f32 v[88:89], v[88:89], v[114:115]
	v_cvt_pk_f32_fp8_e32 v[98:99], v191
	v_pk_add_f32 v[88:89], v[88:89], v[118:119]
	v_cvt_pk_f32_fp8_sdwa v[190:191], v191 src0_sel:WORD_1
	v_pk_fma_f32 v[88:89], v[88:89], s[28:29], v[90:91] op_sel_hi:[1,0,1]
	v_cvt_pk_f32_fp8_e32 v[90:91], v171
	v_cvt_pk_bf16_f32 v179, v88, v89
	v_cvt_pk_f32_fp8_e32 v[88:89], v167
	v_cvt_pk_f32_fp8_sdwa v[166:167], v167 src0_sel:WORD_1
	v_cvt_pk_f32_fp8_sdwa v[170:171], v171 src0_sel:WORD_1
	v_cvt_pk_f32_fp8_e32 v[102:103], v199
	v_pk_add_f32 v[88:89], v[88:89], 0 op_sel_hi:[1,0]
	v_pk_add_f32 v[166:167], v[166:167], 0 op_sel_hi:[1,0]
	v_pk_add_f32 v[88:89], v[88:89], v[90:91]
	v_pk_add_f32 v[166:167], v[166:167], v[170:171]
	v_pk_add_f32 v[88:89], v[88:89], v[92:93]
	v_pk_add_f32 v[166:167], v[166:167], v[174:175]
	v_cvt_pk_f32_fp8_sdwa v[198:199], v199 src0_sel:WORD_1
	v_pk_add_f32 v[88:89], v[88:89], v[94:95]
	v_pk_add_f32 v[166:167], v[166:167], v[182:183]
	v_pk_add_f32 v[88:89], v[88:89], v[96:97]
	v_pk_add_f32 v[166:167], v[166:167], v[186:187]
	v_pk_add_f32 v[88:89], v[88:89], v[98:99]
	v_pk_add_f32 v[166:167], v[166:167], v[190:191]
	v_pk_add_f32 v[88:89], v[88:89], v[100:101]
	v_lshlrev_b32_e32 v90, 16, v180
	v_and_b32_e32 v91, 0xffff0000, v180
	v_pk_add_f32 v[166:167], v[166:167], v[194:195]
	v_lshlrev_b32_e32 v170, 16, v181
	v_and_b32_e32 v171, 0xffff0000, v181
	v_pk_add_f32 v[88:89], v[88:89], v[102:103]
	v_pk_mul_f32 v[90:91], v[90:91], s[26:27] op_sel_hi:[1,0]
	v_pk_add_f32 v[166:167], v[166:167], v[198:199]
	v_pk_mul_f32 v[170:171], v[170:171], s[26:27] op_sel_hi:[1,0]
	v_pk_fma_f32 v[88:89], v[88:89], s[28:29], v[90:91] op_sel_hi:[1,0,1]
	v_pk_fma_f32 v[166:167], v[166:167], s[28:29], v[170:171] op_sel_hi:[1,0,1]
	v_cvt_pk_bf16_f32 v180, v88, v89
	v_cvt_pk_bf16_f32 v181, v166, v167
	v_lshl_add_u64 v[166:167], v[86:87], 0, s[100:101]
	v_cvt_pk_f32_fp8_e32 v[170:171], v168
	global_store_dwordx4 v[166:167], v[178:181], off
	v_cvt_pk_f32_fp8_e32 v[182:183], v176
	v_cvt_pk_f32_fp8_e32 v[190:191], v184
	v_cvt_pk_f32_fp8_e32 v[178:179], v172
	v_cvt_pk_f32_fp8_e32 v[198:199], v188
	v_pk_add_f32 v[170:171], v[170:171], 0 op_sel_hi:[1,0]
	v_cvt_pk_f32_fp8_e32 v[90:91], v192
	v_pk_add_f32 v[170:171], v[170:171], v[178:179]
	v_cvt_pk_f32_fp8_e32 v[94:95], v196
	v_pk_add_f32 v[170:171], v[170:171], v[182:183]
	v_cvt_pk_f32_fp8_e32 v[98:99], v200
	v_pk_add_f32 v[170:171], v[170:171], v[190:191]
	v_cvt_pk_f32_fp8_sdwa v[174:175], v168 src0_sel:WORD_1
	v_pk_add_f32 v[170:171], v[170:171], v[198:199]
	v_cvt_pk_f32_fp8_sdwa v[180:181], v172 src0_sel:WORD_1
	v_pk_add_f32 v[170:171], v[170:171], v[90:91]
	v_lshlrev_b32_e32 v178, 16, v162
	v_pk_add_f32 v[170:171], v[170:171], v[94:95]
	v_and_b32_e32 v179, 0xffff0000, v162
	v_cvt_pk_f32_fp8_sdwa v[186:187], v176 src0_sel:WORD_1
	v_pk_add_f32 v[170:171], v[170:171], v[98:99]
	v_pk_mul_f32 v[178:179], v[178:179], s[26:27] op_sel_hi:[1,0]
	v_cvt_pk_f32_fp8_sdwa v[194:195], v184 src0_sel:WORD_1
	v_pk_fma_f32 v[170:171], v[170:171], s[28:29], v[178:179] op_sel_hi:[1,0,1]
	v_cvt_pk_f32_fp8_sdwa v[88:89], v188 src0_sel:WORD_1
	v_cvt_pk_bf16_f32 v162, v170, v171
	v_pk_add_f32 v[170:171], v[174:175], 0 op_sel_hi:[1,0]
	v_cvt_pk_f32_fp8_sdwa v[92:93], v192 src0_sel:WORD_1
	v_pk_add_f32 v[170:171], v[170:171], v[180:181]
	v_cvt_pk_f32_fp8_sdwa v[96:97], v196 src0_sel:WORD_1
	v_pk_add_f32 v[170:171], v[170:171], v[186:187]
	v_cvt_pk_f32_fp8_sdwa v[100:101], v200 src0_sel:WORD_1
	v_pk_add_f32 v[170:171], v[170:171], v[194:195]
	v_lshlrev_b32_e32 v174, 16, v163
	v_pk_add_f32 v[170:171], v[170:171], v[88:89]
	v_and_b32_e32 v175, 0xffff0000, v163
	v_pk_add_f32 v[170:171], v[170:171], v[92:93]
	v_pk_mul_f32 v[174:175], v[174:175], s[26:27] op_sel_hi:[1,0]
	v_pk_add_f32 v[170:171], v[170:171], v[96:97]
	v_cvt_pk_f32_fp8_e32 v[178:179], v177
	v_pk_add_f32 v[170:171], v[170:171], v[100:101]
	v_cvt_pk_f32_fp8_e32 v[180:181], v185
	v_pk_fma_f32 v[170:171], v[170:171], s[28:29], v[174:175] op_sel_hi:[1,0,1]
	v_cvt_pk_f32_fp8_e32 v[174:175], v173
	v_cvt_pk_bf16_f32 v163, v170, v171
	v_cvt_pk_f32_fp8_e32 v[170:171], v169
	v_cvt_pk_f32_fp8_sdwa v[168:169], v169 src0_sel:WORD_1
	v_cvt_pk_f32_fp8_sdwa v[172:173], v173 src0_sel:WORD_1
	v_cvt_pk_f32_fp8_sdwa v[182:183], v185 src0_sel:WORD_1
	v_cvt_pk_f32_fp8_e32 v[184:185], v189
	v_pk_add_f32 v[170:171], v[170:171], 0 op_sel_hi:[1,0]
	v_cvt_pk_f32_fp8_sdwa v[176:177], v177 src0_sel:WORD_1
	v_cvt_pk_f32_fp8_sdwa v[186:187], v189 src0_sel:WORD_1
	v_cvt_pk_f32_fp8_e32 v[188:189], v193
	v_pk_add_f32 v[170:171], v[170:171], v[174:175]
	v_cvt_pk_f32_fp8_sdwa v[190:191], v193 src0_sel:WORD_1
	v_cvt_pk_f32_fp8_e32 v[192:193], v197
	v_pk_add_f32 v[170:171], v[170:171], v[178:179]
	v_cvt_pk_f32_fp8_sdwa v[194:195], v197 src0_sel:WORD_1
	v_cvt_pk_f32_fp8_e32 v[196:197], v201
	v_pk_add_f32 v[170:171], v[170:171], v[180:181]
	v_pk_add_f32 v[168:169], v[168:169], 0 op_sel_hi:[1,0]
	v_pk_add_f32 v[170:171], v[170:171], v[184:185]
	v_pk_add_f32 v[168:169], v[168:169], v[172:173]
	v_pk_add_f32 v[170:171], v[170:171], v[188:189]
	v_pk_add_f32 v[168:169], v[168:169], v[176:177]
	v_cvt_pk_f32_fp8_sdwa v[198:199], v201 src0_sel:WORD_1
	v_pk_add_f32 v[170:171], v[170:171], v[192:193]
	v_lshlrev_b32_e32 v174, 16, v164
	v_and_b32_e32 v175, 0xffff0000, v164
	v_pk_add_f32 v[168:169], v[168:169], v[182:183]
	v_pk_add_f32 v[170:171], v[170:171], v[196:197]
	v_pk_mul_f32 v[174:175], v[174:175], s[26:27] op_sel_hi:[1,0]
	v_pk_add_f32 v[168:169], v[168:169], v[186:187]
	v_pk_fma_f32 v[170:171], v[170:171], s[28:29], v[174:175] op_sel_hi:[1,0,1]
	v_pk_add_f32 v[168:169], v[168:169], v[190:191]
	v_cvt_pk_bf16_f32 v164, v170, v171
	v_pk_add_f32 v[168:169], v[168:169], v[194:195]
	v_lshlrev_b32_e32 v170, 16, v165
	v_and_b32_e32 v171, 0xffff0000, v165
	v_pk_add_f32 v[168:169], v[168:169], v[198:199]
	v_pk_mul_f32 v[170:171], v[170:171], s[26:27] op_sel_hi:[1,0]
	s_waitcnt vmcnt(7)
	v_cvt_pk_f32_fp8_sdwa v[172:173], v146 src0_sel:WORD_1
	v_pk_fma_f32 v[168:169], v[168:169], s[28:29], v[170:171] op_sel_hi:[1,0,1]
	v_cvt_pk_f32_fp8_sdwa v[170:171], v142 src0_sel:WORD_1
	v_cvt_pk_bf16_f32 v165, v168, v169
	global_store_dwordx4 v[166:167], v[162:165], off offset:16
	v_cvt_pk_f32_fp8_sdwa v[166:167], v134 src0_sel:WORD_1
	v_cvt_pk_f32_fp8_sdwa v[168:169], v138 src0_sel:WORD_1
	v_cvt_pk_f32_fp8_sdwa v[162:163], v126 src0_sel:WORD_1
	v_cvt_pk_f32_fp8_sdwa v[164:165], v130 src0_sel:WORD_1
	s_waitcnt vmcnt(7)
	v_cvt_pk_f32_fp8_sdwa v[174:175], v150 src0_sel:WORD_1
	s_waitcnt vmcnt(6)
	v_cvt_pk_f32_fp8_sdwa v[176:177], v154 src0_sel:WORD_1
	v_pk_add_f32 v[162:163], v[162:163], 0 op_sel_hi:[1,0]
	v_cvt_pk_f32_fp8_e32 v[178:179], v126
	v_pk_add_f32 v[162:163], v[162:163], v[164:165]
	v_lshlrev_b32_e32 v164, 16, v159
	v_pk_add_f32 v[162:163], v[162:163], v[166:167]
	v_and_b32_e32 v165, 0xffff0000, v159
	v_pk_add_f32 v[162:163], v[162:163], v[168:169]
	v_pk_mul_f32 v[164:165], v[164:165], s[26:27] op_sel_hi:[1,0]
	v_pk_add_f32 v[162:163], v[162:163], v[170:171]
	v_cvt_pk_f32_fp8_e32 v[180:181], v130
	v_pk_add_f32 v[162:163], v[162:163], v[172:173]
	v_cvt_pk_f32_fp8_e32 v[182:183], v134
	v_pk_add_f32 v[162:163], v[162:163], v[174:175]
	v_cvt_pk_f32_fp8_e32 v[166:167], v135
	v_pk_add_f32 v[162:163], v[162:163], v[176:177]
	v_cvt_pk_f32_fp8_sdwa v[134:135], v135 src0_sel:WORD_1
	v_pk_fma_f32 v[162:163], v[162:163], s[28:29], v[164:165] op_sel_hi:[1,0,1]
	v_cvt_pk_f32_fp8_e32 v[164:165], v131
	v_cvt_pk_bf16_f32 v159, v162, v163
	v_cvt_pk_f32_fp8_e32 v[162:163], v127
	v_cvt_pk_f32_fp8_sdwa v[126:127], v127 src0_sel:WORD_1
	v_cvt_pk_f32_fp8_sdwa v[130:131], v131 src0_sel:WORD_1
	v_cvt_pk_f32_fp8_e32 v[184:185], v138
	v_cvt_pk_f32_fp8_e32 v[168:169], v139
	v_cvt_pk_f32_fp8_sdwa v[138:139], v139 src0_sel:WORD_1
	v_cvt_pk_f32_fp8_e32 v[186:187], v142
	v_cvt_pk_f32_fp8_e32 v[170:171], v143
	v_cvt_pk_f32_fp8_sdwa v[142:143], v143 src0_sel:WORD_1
	v_pk_add_f32 v[126:127], v[126:127], 0 op_sel_hi:[1,0]
	v_cvt_pk_f32_fp8_e32 v[188:189], v146
	v_cvt_pk_f32_fp8_e32 v[172:173], v147
	v_cvt_pk_f32_fp8_sdwa v[146:147], v147 src0_sel:WORD_1
	v_pk_add_f32 v[126:127], v[126:127], v[130:131]
	v_cvt_pk_f32_fp8_e32 v[190:191], v150
	v_pk_add_f32 v[178:179], v[178:179], 0 op_sel_hi:[1,0]
	v_cvt_pk_f32_fp8_e32 v[174:175], v151
	v_cvt_pk_f32_fp8_sdwa v[150:151], v151 src0_sel:WORD_1
	v_pk_add_f32 v[162:163], v[162:163], 0 op_sel_hi:[1,0]
	v_pk_add_f32 v[126:127], v[126:127], v[134:135]
	v_cvt_pk_f32_fp8_e32 v[192:193], v154
	v_pk_add_f32 v[178:179], v[178:179], v[180:181]
	v_cvt_pk_f32_fp8_e32 v[176:177], v155
	v_cvt_pk_f32_fp8_sdwa v[154:155], v155 src0_sel:WORD_1
	v_pk_add_f32 v[162:163], v[162:163], v[164:165]
	v_pk_add_f32 v[126:127], v[126:127], v[138:139]
	v_pk_add_f32 v[178:179], v[178:179], v[182:183]
	v_pk_add_f32 v[162:163], v[162:163], v[166:167]
	v_pk_add_f32 v[126:127], v[126:127], v[142:143]
	v_pk_add_f32 v[178:179], v[178:179], v[184:185]
	v_pk_add_f32 v[162:163], v[162:163], v[168:169]
	v_pk_add_f32 v[126:127], v[126:127], v[146:147]
	v_pk_add_f32 v[178:179], v[178:179], v[186:187]
	v_pk_add_f32 v[162:163], v[162:163], v[170:171]
	v_pk_add_f32 v[126:127], v[126:127], v[150:151]
	v_lshlrev_b32_e32 v130, 16, v161
	v_and_b32_e32 v131, 0xffff0000, v161
	v_pk_add_f32 v[178:179], v[178:179], v[188:189]
	v_pk_add_f32 v[162:163], v[162:163], v[172:173]
	v_pk_add_f32 v[126:127], v[126:127], v[154:155]
	v_pk_mul_f32 v[130:131], v[130:131], s[26:27] op_sel_hi:[1,0]
	v_pk_add_f32 v[178:179], v[178:179], v[190:191]
	v_lshlrev_b32_e32 v180, 16, v158
	v_and_b32_e32 v181, 0xffff0000, v158
	v_pk_add_f32 v[162:163], v[162:163], v[174:175]
	v_lshlrev_b32_e32 v164, 16, v160
	v_and_b32_e32 v165, 0xffff0000, v160
	v_pk_fma_f32 v[126:127], v[126:127], s[28:29], v[130:131] op_sel_hi:[1,0,1]
	v_cvt_pk_f32_fp8_e32 v[130:131], v128
	v_pk_add_f32 v[178:179], v[178:179], v[192:193]
	v_pk_mul_f32 v[180:181], v[180:181], s[26:27] op_sel_hi:[1,0]
	v_pk_add_f32 v[162:163], v[162:163], v[176:177]
	v_pk_mul_f32 v[164:165], v[164:165], s[26:27] op_sel_hi:[1,0]
	v_cvt_pk_f32_fp8_e32 v[138:139], v132
	v_pk_fma_f32 v[178:179], v[178:179], s[28:29], v[180:181] op_sel_hi:[1,0,1]
	v_pk_fma_f32 v[162:163], v[162:163], s[28:29], v[164:165] op_sel_hi:[1,0,1]
	v_cvt_pk_f32_fp8_e32 v[146:147], v136
	v_cvt_pk_bf16_f32 v158, v178, v179
	v_cvt_pk_bf16_f32 v160, v162, v163
	v_cvt_pk_bf16_f32 v161, v126, v127
	v_lshl_add_u64 v[126:127], v[86:87], 0, s[98:99]
	v_cvt_pk_f32_fp8_e32 v[154:155], v140
	global_store_dwordx4 v[126:127], v[158:161], off
	v_pk_add_f32 v[130:131], v[130:131], 0 op_sel_hi:[1,0]
	v_cvt_pk_f32_fp8_e32 v[164:165], v148
	v_cvt_pk_f32_fp8_e32 v[160:161], v144
	v_pk_add_f32 v[130:131], v[130:131], v[138:139]
	v_cvt_pk_f32_fp8_e32 v[168:169], v152
	v_pk_add_f32 v[130:131], v[130:131], v[146:147]
	v_cvt_pk_f32_fp8_e32 v[172:173], v156
	v_pk_add_f32 v[130:131], v[130:131], v[154:155]
	v_cvt_pk_f32_fp8_sdwa v[134:135], v128 src0_sel:WORD_1
	v_pk_add_f32 v[130:131], v[130:131], v[160:161]
	v_cvt_pk_f32_fp8_sdwa v[142:143], v132 src0_sel:WORD_1
	v_pk_add_f32 v[130:131], v[130:131], v[164:165]
	v_lshlrev_b32_e32 v138, 16, v122
	v_pk_add_f32 v[130:131], v[130:131], v[168:169]
	v_and_b32_e32 v139, 0xffff0000, v122
	v_cvt_pk_f32_fp8_sdwa v[150:151], v136 src0_sel:WORD_1
	v_pk_add_f32 v[130:131], v[130:131], v[172:173]
	v_pk_mul_f32 v[138:139], v[138:139], s[26:27] op_sel_hi:[1,0]
	v_cvt_pk_f32_fp8_sdwa v[158:159], v140 src0_sel:WORD_1
	v_pk_fma_f32 v[130:131], v[130:131], s[28:29], v[138:139] op_sel_hi:[1,0,1]
	v_cvt_pk_f32_fp8_sdwa v[162:163], v144 src0_sel:WORD_1
	v_cvt_pk_bf16_f32 v122, v130, v131
	v_pk_add_f32 v[130:131], v[134:135], 0 op_sel_hi:[1,0]
	v_cvt_pk_f32_fp8_sdwa v[166:167], v148 src0_sel:WORD_1
	v_pk_add_f32 v[130:131], v[130:131], v[142:143]
	v_cvt_pk_f32_fp8_sdwa v[170:171], v152 src0_sel:WORD_1
	v_pk_add_f32 v[130:131], v[130:131], v[150:151]
	v_cvt_pk_f32_fp8_sdwa v[174:175], v156 src0_sel:WORD_1
	v_pk_add_f32 v[130:131], v[130:131], v[158:159]
	v_lshlrev_b32_e32 v134, 16, v123
	v_pk_add_f32 v[130:131], v[130:131], v[162:163]
	v_and_b32_e32 v135, 0xffff0000, v123
	v_pk_add_f32 v[130:131], v[130:131], v[166:167]
	v_pk_mul_f32 v[134:135], v[134:135], s[26:27] op_sel_hi:[1,0]
	v_pk_add_f32 v[130:131], v[130:131], v[170:171]
	v_cvt_pk_f32_fp8_e32 v[146:147], v129
	v_pk_add_f32 v[130:131], v[130:131], v[174:175]
	v_cvt_pk_f32_fp8_sdwa v[128:129], v129 src0_sel:WORD_1
	v_pk_fma_f32 v[130:131], v[130:131], s[28:29], v[134:135] op_sel_hi:[1,0,1]
	v_cvt_pk_f32_fp8_e32 v[150:151], v133
	v_cvt_pk_bf16_f32 v123, v130, v131
	v_cvt_pk_f32_fp8_sdwa v[130:131], v133 src0_sel:WORD_1
	v_cvt_pk_f32_fp8_e32 v[154:155], v137
	v_cvt_pk_f32_fp8_sdwa v[132:133], v137 src0_sel:WORD_1
	v_cvt_pk_f32_fp8_e32 v[158:159], v141
	v_cvt_pk_f32_fp8_sdwa v[134:135], v141 src0_sel:WORD_1
	v_cvt_pk_f32_fp8_e32 v[160:161], v145
	v_cvt_pk_f32_fp8_sdwa v[136:137], v145 src0_sel:WORD_1
	v_pk_add_f32 v[146:147], v[146:147], 0 op_sel_hi:[1,0]
	v_pk_add_f32 v[128:129], v[128:129], 0 op_sel_hi:[1,0]
	v_cvt_pk_f32_fp8_e32 v[144:145], v149
	v_cvt_pk_f32_fp8_sdwa v[138:139], v149 src0_sel:WORD_1
	v_pk_add_f32 v[146:147], v[146:147], v[150:151]
	v_pk_add_f32 v[128:129], v[128:129], v[130:131]
	v_cvt_pk_f32_fp8_e32 v[148:149], v153
	v_cvt_pk_f32_fp8_sdwa v[140:141], v153 src0_sel:WORD_1
	v_pk_add_f32 v[146:147], v[146:147], v[154:155]
	v_pk_add_f32 v[128:129], v[128:129], v[132:133]
	v_cvt_pk_f32_fp8_e32 v[152:153], v157
	v_cvt_pk_f32_fp8_sdwa v[142:143], v157 src0_sel:WORD_1
	v_pk_add_f32 v[146:147], v[146:147], v[158:159]
	v_pk_add_f32 v[128:129], v[128:129], v[134:135]
	v_pk_add_f32 v[146:147], v[146:147], v[160:161]
	v_pk_add_f32 v[128:129], v[128:129], v[136:137]
	v_pk_add_f32 v[144:145], v[146:147], v[144:145]
	v_pk_add_f32 v[128:129], v[128:129], v[138:139]
	v_pk_add_f32 v[144:145], v[144:145], v[148:149]
	v_lshlrev_b32_e32 v146, 16, v124
	v_and_b32_e32 v147, 0xffff0000, v124
	v_pk_add_f32 v[128:129], v[128:129], v[140:141]
	v_lshlrev_b32_e32 v130, 16, v125
	v_and_b32_e32 v131, 0xffff0000, v125
	v_pk_add_f32 v[144:145], v[144:145], v[152:153]
	v_pk_mul_f32 v[146:147], v[146:147], s[26:27] op_sel_hi:[1,0]
	v_pk_add_f32 v[128:129], v[128:129], v[142:143]
	v_pk_mul_f32 v[130:131], v[130:131], s[26:27] op_sel_hi:[1,0]
	v_pk_fma_f32 v[144:145], v[144:145], s[28:29], v[146:147] op_sel_hi:[1,0,1]
	v_pk_fma_f32 v[128:129], v[128:129], s[28:29], v[130:131] op_sel_hi:[1,0,1]
	v_cvt_pk_bf16_f32 v124, v144, v145
	v_cvt_pk_bf16_f32 v125, v128, v129
	global_store_dwordx4 v[126:127], v[122:125], off offset:16
	s_mov_b64 s[76:77], 0

.LBB0_1093:
	s_add_i32 s41, s35, s37
	s_add_i32 s6, s41, 2
	s_ashr_i32 s7, s6, 31
	s_add_i32 s80, s31, s39
	s_lshl_b64 s[76:77], s[6:7], 11
	s_add_i32 s6, s80, -15
	s_ashr_i32 s7, s6, 31
	v_lshl_add_u64 v[2:3], v[82:83], 0, s[76:77]
	s_lshl_b64 s[6:7], s[6:7], 10
	global_load_dwordx4 v[42:45], v[2:3], off offset:16
	global_load_dwordx4 v[58:61], v[2:3], off
	v_lshl_add_u64 v[2:3], v[84:85], 0, s[6:7]
	s_add_i32 s6, s80, -14
	s_ashr_i32 s7, s6, 31
	s_lshl_b64 s[6:7], s[6:7], 10
	global_load_dwordx4 v[46:49], v[2:3], off
	v_lshl_add_u64 v[2:3], v[84:85], 0, s[6:7]
	s_add_i32 s6, s80, -13
	s_ashr_i32 s7, s6, 31
	s_lshl_b64 s[6:7], s[6:7], 10
	global_load_dwordx4 v[50:53], v[2:3], off
	v_lshl_add_u64 v[2:3], v[84:85], 0, s[6:7]
	s_add_i32 s6, s80, -12
	s_ashr_i32 s7, s6, 31
	s_lshl_b64 s[6:7], s[6:7], 10
	global_load_dwordx4 v[54:57], v[2:3], off
	v_lshl_add_u64 v[2:3], v[84:85], 0, s[6:7]
	s_add_i32 s6, s80, -11
	s_ashr_i32 s7, s6, 31
	s_lshl_b64 s[6:7], s[6:7], 10
	global_load_dwordx4 v[62:65], v[2:3], off
	v_lshl_add_u64 v[2:3], v[84:85], 0, s[6:7]
	s_add_i32 s6, s80, -10
	s_ashr_i32 s7, s6, 31
	s_lshl_b64 s[6:7], s[6:7], 10
	global_load_dwordx4 v[66:69], v[2:3], off
	v_lshl_add_u64 v[2:3], v[84:85], 0, s[6:7]
	s_add_i32 s6, s80, -9
	s_ashr_i32 s7, s6, 31
	s_lshl_b64 s[6:7], s[6:7], 10
	global_load_dwordx4 v[70:73], v[2:3], off
	v_lshl_add_u64 v[2:3], v[84:85], 0, s[6:7]
	s_add_i32 s6, s80, -8
	s_ashr_i32 s7, s6, 31
	s_lshl_b64 s[6:7], s[6:7], 10
	global_load_dwordx4 v[74:77], v[2:3], off
	v_lshl_add_u64 v[2:3], v[84:85], 0, s[6:7]
	global_load_dwordx4 v[78:81], v[2:3], off
	s_add_i32 s6, s41, 3
	s_ashr_i32 s7, s6, 31
	s_add_i32 s82, s80, -7
	s_lshl_b64 s[6:7], s[6:7], 11
	s_ashr_i32 s83, s82, 31
	v_lshl_add_u64 v[6:7], v[82:83], 0, s[6:7]
	s_lshl_b64 s[82:83], s[82:83], 10
	global_load_dwordx4 v[2:5], v[6:7], off offset:16
	global_load_dwordx4 v[38:41], v[6:7], off
	v_lshl_add_u64 v[6:7], v[84:85], 0, s[82:83]
	s_add_i32 s82, s80, -6
	s_ashr_i32 s83, s82, 31
	s_lshl_b64 s[82:83], s[82:83], 10
	v_lshl_add_u64 v[10:11], v[84:85], 0, s[82:83]
	s_add_i32 s82, s80, -5
	s_ashr_i32 s83, s82, 31
	s_lshl_b64 s[82:83], s[82:83], 10
	v_lshl_add_u64 v[14:15], v[84:85], 0, s[82:83]
	s_add_i32 s82, s80, -4
	s_ashr_i32 s83, s82, 31
	s_lshl_b64 s[82:83], s[82:83], 10
	v_lshl_add_u64 v[18:19], v[84:85], 0, s[82:83]
	s_add_i32 s82, s80, -3
	s_ashr_i32 s83, s82, 31
	s_lshl_b64 s[82:83], s[82:83], 10
	v_lshl_add_u64 v[22:23], v[84:85], 0, s[82:83]
	s_add_i32 s82, s80, -2
	global_load_dwordx4 v[6:9], v[6:7], off
	s_ashr_i32 s83, s82, 31
	global_load_dwordx4 v[10:13], v[10:11], off
	s_lshl_b64 s[82:83], s[82:83], 10
	global_load_dwordx4 v[14:17], v[14:15], off
	v_lshl_add_u64 v[26:27], v[84:85], 0, s[82:83]
	s_add_i32 s82, s80, -1
	global_load_dwordx4 v[18:21], v[18:19], off
	s_ashr_i32 s83, s82, 31
	global_load_dwordx4 v[22:25], v[22:23], off
	s_lshl_b64 s[82:83], s[82:83], 10
	s_ashr_i32 s81, s80, 31
	global_load_dwordx4 v[26:29], v[26:27], off
	v_lshl_add_u64 v[30:31], v[84:85], 0, s[82:83]
	s_lshl_b64 s[80:81], s[80:81], 10
	global_load_dwordx4 v[30:33], v[30:31], off
	v_lshl_add_u64 v[34:35], v[84:85], 0, s[80:81]
	global_load_dwordx4 v[34:37], v[34:35], off
	s_add_i32 s37, s37, 2
	s_add_i32 s39, s39, 16
	s_add_i32 s41, s35, s37
	s_add_i32 s98, s41, 2
	s_ashr_i32 s99, s98, 31
	s_add_i32 s80, s31, s39
	s_lshl_b64 s[100:101], s[98:99], 11
	s_add_i32 s98, s80, -15
	s_ashr_i32 s99, s98, 31
	v_lshl_add_u64 v[122:123], v[82:83], 0, s[100:101]
	s_lshl_b64 s[98:99], s[98:99], 10
	global_load_dwordx4 v[166:169], v[122:123], off offset:16
	global_load_dwordx4 v[182:185], v[122:123], off
	v_lshl_add_u64 v[122:123], v[84:85], 0, s[98:99]
	s_add_i32 s98, s80, -14
	s_ashr_i32 s99, s98, 31
	s_lshl_b64 s[98:99], s[98:99], 10
	global_load_dwordx4 v[170:173], v[122:123], off
	v_lshl_add_u64 v[122:123], v[84:85], 0, s[98:99]
	s_add_i32 s98, s80, -13
	s_ashr_i32 s99, s98, 31
	s_lshl_b64 s[98:99], s[98:99], 10
	global_load_dwordx4 v[174:177], v[122:123], off
	v_lshl_add_u64 v[122:123], v[84:85], 0, s[98:99]
	s_add_i32 s98, s80, -12
	s_ashr_i32 s99, s98, 31
	s_lshl_b64 s[98:99], s[98:99], 10
	global_load_dwordx4 v[178:181], v[122:123], off
	v_lshl_add_u64 v[122:123], v[84:85], 0, s[98:99]
	s_add_i32 s98, s80, -11
	s_ashr_i32 s99, s98, 31
	s_lshl_b64 s[98:99], s[98:99], 10
	global_load_dwordx4 v[186:189], v[122:123], off
	v_lshl_add_u64 v[122:123], v[84:85], 0, s[98:99]
	s_add_i32 s98, s80, -10
	s_ashr_i32 s99, s98, 31
	s_lshl_b64 s[98:99], s[98:99], 10
	global_load_dwordx4 v[190:193], v[122:123], off
	v_lshl_add_u64 v[122:123], v[84:85], 0, s[98:99]
	s_add_i32 s98, s80, -9
	s_ashr_i32 s99, s98, 31
	s_lshl_b64 s[98:99], s[98:99], 10
	global_load_dwordx4 v[194:197], v[122:123], off
	v_lshl_add_u64 v[122:123], v[84:85], 0, s[98:99]
	s_add_i32 s98, s80, -8
	s_ashr_i32 s99, s98, 31
	s_lshl_b64 s[98:99], s[98:99], 10
	global_load_dwordx4 v[198:201], v[122:123], off
	v_lshl_add_u64 v[122:123], v[84:85], 0, s[98:99]
	global_load_dwordx4 v[202:205], v[122:123], off
	s_add_i32 s98, s41, 3
	s_ashr_i32 s99, s98, 31
	s_add_i32 s82, s80, -7
	s_lshl_b64 s[98:99], s[98:99], 11
	s_ashr_i32 s83, s82, 31
	v_lshl_add_u64 v[126:127], v[82:83], 0, s[98:99]
	s_lshl_b64 s[82:83], s[82:83], 10
	global_load_dwordx4 v[122:125], v[126:127], off offset:16
	global_load_dwordx4 v[162:165], v[126:127], off
	v_lshl_add_u64 v[126:127], v[84:85], 0, s[82:83]
	s_add_i32 s82, s80, -6
	s_ashr_i32 s83, s82, 31
	s_lshl_b64 s[82:83], s[82:83], 10
	v_lshl_add_u64 v[130:131], v[84:85], 0, s[82:83]
	s_add_i32 s82, s80, -5
	s_ashr_i32 s83, s82, 31
	s_lshl_b64 s[82:83], s[82:83], 10
	v_lshl_add_u64 v[134:135], v[84:85], 0, s[82:83]
	s_add_i32 s82, s80, -4
	s_ashr_i32 s83, s82, 31
	s_lshl_b64 s[82:83], s[82:83], 10
	v_lshl_add_u64 v[138:139], v[84:85], 0, s[82:83]
	s_add_i32 s82, s80, -3
	s_ashr_i32 s83, s82, 31
	s_lshl_b64 s[82:83], s[82:83], 10
	v_lshl_add_u64 v[142:143], v[84:85], 0, s[82:83]
	s_add_i32 s82, s80, -2
	global_load_dwordx4 v[126:129], v[126:127], off
	s_ashr_i32 s83, s82, 31
	global_load_dwordx4 v[130:133], v[130:131], off
	s_lshl_b64 s[82:83], s[82:83], 10
	global_load_dwordx4 v[134:137], v[134:135], off
	v_lshl_add_u64 v[150:151], v[84:85], 0, s[82:83]
	s_add_i32 s82, s80, -1
	global_load_dwordx4 v[138:141], v[138:139], off
	s_ashr_i32 s83, s82, 31
	global_load_dwordx4 v[142:145], v[142:143], off
	s_lshl_b64 s[82:83], s[82:83], 10
	s_ashr_i32 s81, s80, 31
	global_load_dwordx4 v[150:153], v[150:151], off
	v_lshl_add_u64 v[154:155], v[84:85], 0, s[82:83]
	s_lshl_b64 s[80:81], s[80:81], 10
	global_load_dwordx4 v[154:157], v[154:155], off
	v_lshl_add_u64 v[158:159], v[84:85], 0, s[80:81]
	global_load_dwordx4 v[158:161], v[158:159], off
	s_add_i32 s37, s37, 2
	s_add_i32 s39, s39, 16
	s_waitcnt vmcnt(37)
	v_cvt_pk_f32_fp8_e32 v[88:89], v46
	v_cvt_pk_f32_fp8_sdwa v[90:91], v46 src0_sel:WORD_1
	v_pk_add_f32 v[88:89], v[88:89], 0 op_sel_hi:[1,0]
	s_waitcnt vmcnt(36)
	v_cvt_pk_f32_fp8_e32 v[92:93], v50
	v_cvt_pk_f32_fp8_sdwa v[94:95], v50 src0_sel:WORD_1
	v_pk_add_f32 v[88:89], v[88:89], v[92:93]
	s_waitcnt vmcnt(35)
	v_cvt_pk_f32_fp8_e32 v[96:97], v54
	v_lshlrev_b32_e32 v92, 16, v58
	v_and_b32_e32 v93, 0xffff0000, v58
	v_cvt_pk_f32_fp8_sdwa v[98:99], v54 src0_sel:WORD_1
	v_pk_add_f32 v[88:89], v[88:89], v[96:97]
	s_waitcnt vmcnt(34)
	v_cvt_pk_f32_fp8_e32 v[100:101], v62
	v_pk_mul_f32 v[92:93], v[92:93], s[26:27] op_sel_hi:[1,0]
	v_cvt_pk_f32_fp8_sdwa v[102:103], v62 src0_sel:WORD_1
	v_pk_add_f32 v[88:89], v[88:89], v[100:101]
	s_waitcnt vmcnt(33)
	v_cvt_pk_f32_fp8_e32 v[104:105], v66
	v_cvt_pk_f32_fp8_sdwa v[106:107], v66 src0_sel:WORD_1
	v_cvt_pk_f32_fp8_e32 v[96:97], v67
	v_cvt_pk_f32_fp8_sdwa v[66:67], v67 src0_sel:WORD_1
	v_pk_add_f32 v[88:89], v[88:89], v[104:105]
	s_waitcnt vmcnt(32)
	v_cvt_pk_f32_fp8_e32 v[108:109], v70
	v_cvt_pk_f32_fp8_sdwa v[110:111], v70 src0_sel:WORD_1
	v_pk_add_f32 v[88:89], v[88:89], v[108:109]
	s_waitcnt vmcnt(31)
	v_cvt_pk_f32_fp8_e32 v[112:113], v74
	v_cvt_pk_f32_fp8_sdwa v[114:115], v74 src0_sel:WORD_1
	s_waitcnt vmcnt(30)
	v_cvt_pk_f32_fp8_e32 v[116:117], v78
	v_cvt_pk_f32_fp8_sdwa v[118:119], v78 src0_sel:WORD_1
	v_pk_add_f32 v[88:89], v[88:89], v[112:113]
	v_cvt_pk_f32_fp8_e32 v[100:101], v75
	v_pk_add_f32 v[88:89], v[88:89], v[116:117]
	v_cvt_pk_f32_fp8_sdwa v[74:75], v75 src0_sel:WORD_1
	v_pk_fma_f32 v[88:89], v[88:89], s[28:29], v[92:93] op_sel_hi:[1,0,1]
	v_cvt_pk_f32_fp8_e32 v[92:93], v55
	v_cvt_pk_bf16_f32 v58, v88, v89
	v_pk_add_f32 v[88:89], v[90:91], 0 op_sel_hi:[1,0]
	v_lshlrev_b32_e32 v90, 16, v59
	v_pk_add_f32 v[88:89], v[88:89], v[94:95]
	v_and_b32_e32 v91, 0xffff0000, v59
	v_pk_add_f32 v[88:89], v[88:89], v[98:99]
	v_pk_mul_f32 v[90:91], v[90:91], s[26:27] op_sel_hi:[1,0]
	v_pk_add_f32 v[88:89], v[88:89], v[102:103]
	v_cvt_pk_f32_fp8_sdwa v[54:55], v55 src0_sel:WORD_1
	v_pk_add_f32 v[88:89], v[88:89], v[106:107]
	v_cvt_pk_f32_fp8_e32 v[94:95], v63
	v_pk_add_f32 v[88:89], v[88:89], v[110:111]
	v_cvt_pk_f32_fp8_sdwa v[62:63], v63 src0_sel:WORD_1
	v_pk_add_f32 v[88:89], v[88:89], v[114:115]
	v_cvt_pk_f32_fp8_e32 v[98:99], v71
	v_pk_add_f32 v[88:89], v[88:89], v[118:119]
	v_cvt_pk_f32_fp8_sdwa v[70:71], v71 src0_sel:WORD_1
	v_pk_fma_f32 v[88:89], v[88:89], s[28:29], v[90:91] op_sel_hi:[1,0,1]
	v_cvt_pk_f32_fp8_e32 v[90:91], v51
	v_cvt_pk_bf16_f32 v59, v88, v89
	v_cvt_pk_f32_fp8_e32 v[88:89], v47
	v_cvt_pk_f32_fp8_sdwa v[46:47], v47 src0_sel:WORD_1
	v_cvt_pk_f32_fp8_sdwa v[50:51], v51 src0_sel:WORD_1
	v_cvt_pk_f32_fp8_e32 v[102:103], v79
	v_pk_add_f32 v[88:89], v[88:89], 0 op_sel_hi:[1,0]
	v_pk_add_f32 v[46:47], v[46:47], 0 op_sel_hi:[1,0]
	v_pk_add_f32 v[88:89], v[88:89], v[90:91]
	v_pk_add_f32 v[46:47], v[46:47], v[50:51]
	v_pk_add_f32 v[88:89], v[88:89], v[92:93]
	v_pk_add_f32 v[46:47], v[46:47], v[54:55]
	v_cvt_pk_f32_fp8_sdwa v[78:79], v79 src0_sel:WORD_1
	v_pk_add_f32 v[88:89], v[88:89], v[94:95]
	v_pk_add_f32 v[46:47], v[46:47], v[62:63]
	v_pk_add_f32 v[88:89], v[88:89], v[96:97]
	v_pk_add_f32 v[46:47], v[46:47], v[66:67]
	v_pk_add_f32 v[88:89], v[88:89], v[98:99]
	v_pk_add_f32 v[46:47], v[46:47], v[70:71]
	v_pk_add_f32 v[88:89], v[88:89], v[100:101]
	v_lshlrev_b32_e32 v90, 16, v60
	v_and_b32_e32 v91, 0xffff0000, v60
	v_pk_add_f32 v[46:47], v[46:47], v[74:75]
	v_lshlrev_b32_e32 v50, 16, v61
	v_and_b32_e32 v51, 0xffff0000, v61
	v_pk_add_f32 v[88:89], v[88:89], v[102:103]
	v_pk_mul_f32 v[90:91], v[90:91], s[26:27] op_sel_hi:[1,0]
	v_pk_add_f32 v[46:47], v[46:47], v[78:79]
	v_pk_mul_f32 v[50:51], v[50:51], s[26:27] op_sel_hi:[1,0]
	v_pk_fma_f32 v[88:89], v[88:89], s[28:29], v[90:91] op_sel_hi:[1,0,1]
	v_pk_fma_f32 v[46:47], v[46:47], s[28:29], v[50:51] op_sel_hi:[1,0,1]
	v_cvt_pk_bf16_f32 v60, v88, v89
	v_cvt_pk_bf16_f32 v61, v46, v47
	v_lshl_add_u64 v[46:47], v[86:87], 0, s[76:77]
	v_cvt_pk_f32_fp8_e32 v[50:51], v48
	global_store_dwordx4 v[46:47], v[58:61], off
	v_cvt_pk_f32_fp8_e32 v[62:63], v56
	v_cvt_pk_f32_fp8_e32 v[70:71], v64
	v_cvt_pk_f32_fp8_e32 v[58:59], v52
	v_cvt_pk_f32_fp8_e32 v[78:79], v68
	v_pk_add_f32 v[50:51], v[50:51], 0 op_sel_hi:[1,0]
	v_cvt_pk_f32_fp8_e32 v[90:91], v72
	v_pk_add_f32 v[50:51], v[50:51], v[58:59]
	v_cvt_pk_f32_fp8_e32 v[94:95], v76
	v_pk_add_f32 v[50:51], v[50:51], v[62:63]
	v_cvt_pk_f32_fp8_e32 v[98:99], v80
	v_pk_add_f32 v[50:51], v[50:51], v[70:71]
	v_cvt_pk_f32_fp8_sdwa v[54:55], v48 src0_sel:WORD_1
	v_pk_add_f32 v[50:51], v[50:51], v[78:79]
	v_cvt_pk_f32_fp8_sdwa v[60:61], v52 src0_sel:WORD_1
	v_pk_add_f32 v[50:51], v[50:51], v[90:91]
	v_lshlrev_b32_e32 v58, 16, v42
	v_pk_add_f32 v[50:51], v[50:51], v[94:95]
	v_and_b32_e32 v59, 0xffff0000, v42
	v_cvt_pk_f32_fp8_sdwa v[66:67], v56 src0_sel:WORD_1
	v_pk_add_f32 v[50:51], v[50:51], v[98:99]
	v_pk_mul_f32 v[58:59], v[58:59], s[26:27] op_sel_hi:[1,0]
	v_cvt_pk_f32_fp8_sdwa v[74:75], v64 src0_sel:WORD_1
	v_pk_fma_f32 v[50:51], v[50:51], s[28:29], v[58:59] op_sel_hi:[1,0,1]
	v_cvt_pk_f32_fp8_sdwa v[88:89], v68 src0_sel:WORD_1
	v_cvt_pk_bf16_f32 v42, v50, v51
	v_pk_add_f32 v[50:51], v[54:55], 0 op_sel_hi:[1,0]
	v_cvt_pk_f32_fp8_sdwa v[92:93], v72 src0_sel:WORD_1
	v_pk_add_f32 v[50:51], v[50:51], v[60:61]
	v_cvt_pk_f32_fp8_sdwa v[96:97], v76 src0_sel:WORD_1
	v_pk_add_f32 v[50:51], v[50:51], v[66:67]
	v_cvt_pk_f32_fp8_sdwa v[100:101], v80 src0_sel:WORD_1
	v_pk_add_f32 v[50:51], v[50:51], v[74:75]
	v_lshlrev_b32_e32 v54, 16, v43
	v_pk_add_f32 v[50:51], v[50:51], v[88:89]
	v_and_b32_e32 v55, 0xffff0000, v43
	v_pk_add_f32 v[50:51], v[50:51], v[92:93]
	v_pk_mul_f32 v[54:55], v[54:55], s[26:27] op_sel_hi:[1,0]
	v_pk_add_f32 v[50:51], v[50:51], v[96:97]
	v_cvt_pk_f32_fp8_e32 v[58:59], v57
	v_pk_add_f32 v[50:51], v[50:51], v[100:101]
	v_cvt_pk_f32_fp8_e32 v[60:61], v65
	v_pk_fma_f32 v[50:51], v[50:51], s[28:29], v[54:55] op_sel_hi:[1,0,1]
	v_cvt_pk_f32_fp8_e32 v[54:55], v53
	v_cvt_pk_bf16_f32 v43, v50, v51
	v_cvt_pk_f32_fp8_e32 v[50:51], v49
	v_cvt_pk_f32_fp8_sdwa v[48:49], v49 src0_sel:WORD_1
	v_cvt_pk_f32_fp8_sdwa v[52:53], v53 src0_sel:WORD_1
	v_cvt_pk_f32_fp8_sdwa v[62:63], v65 src0_sel:WORD_1
	v_cvt_pk_f32_fp8_e32 v[64:65], v69
	v_pk_add_f32 v[50:51], v[50:51], 0 op_sel_hi:[1,0]
	v_cvt_pk_f32_fp8_sdwa v[56:57], v57 src0_sel:WORD_1
	v_cvt_pk_f32_fp8_sdwa v[66:67], v69 src0_sel:WORD_1
	v_cvt_pk_f32_fp8_e32 v[68:69], v73
	v_pk_add_f32 v[50:51], v[50:51], v[54:55]
	v_cvt_pk_f32_fp8_sdwa v[70:71], v73 src0_sel:WORD_1
	v_cvt_pk_f32_fp8_e32 v[72:73], v77
	v_pk_add_f32 v[50:51], v[50:51], v[58:59]
	v_cvt_pk_f32_fp8_sdwa v[74:75], v77 src0_sel:WORD_1
	v_cvt_pk_f32_fp8_e32 v[76:77], v81
	v_pk_add_f32 v[50:51], v[50:51], v[60:61]
	v_pk_add_f32 v[48:49], v[48:49], 0 op_sel_hi:[1,0]
	v_pk_add_f32 v[50:51], v[50:51], v[64:65]
	v_pk_add_f32 v[48:49], v[48:49], v[52:53]
	v_pk_add_f32 v[50:51], v[50:51], v[68:69]
	v_pk_add_f32 v[48:49], v[48:49], v[56:57]
	v_cvt_pk_f32_fp8_sdwa v[78:79], v81 src0_sel:WORD_1
	v_pk_add_f32 v[50:51], v[50:51], v[72:73]
	v_lshlrev_b32_e32 v54, 16, v44
	v_and_b32_e32 v55, 0xffff0000, v44
	v_pk_add_f32 v[48:49], v[48:49], v[62:63]
	v_pk_add_f32 v[50:51], v[50:51], v[76:77]
	v_pk_mul_f32 v[54:55], v[54:55], s[26:27] op_sel_hi:[1,0]
	v_pk_add_f32 v[48:49], v[48:49], v[66:67]
	v_pk_fma_f32 v[50:51], v[50:51], s[28:29], v[54:55] op_sel_hi:[1,0,1]
	v_pk_add_f32 v[48:49], v[48:49], v[70:71]
	v_cvt_pk_bf16_f32 v44, v50, v51
	v_pk_add_f32 v[48:49], v[48:49], v[74:75]
	v_lshlrev_b32_e32 v50, 16, v45
	v_and_b32_e32 v51, 0xffff0000, v45
	v_pk_add_f32 v[48:49], v[48:49], v[78:79]
	v_pk_mul_f32 v[50:51], v[50:51], s[26:27] op_sel_hi:[1,0]
	s_waitcnt vmcnt(23)
	v_cvt_pk_f32_fp8_sdwa v[52:53], v26 src0_sel:WORD_1
	v_pk_fma_f32 v[48:49], v[48:49], s[28:29], v[50:51] op_sel_hi:[1,0,1]
	v_cvt_pk_f32_fp8_sdwa v[50:51], v22 src0_sel:WORD_1
	v_cvt_pk_bf16_f32 v45, v48, v49
	global_store_dwordx4 v[46:47], v[42:45], off offset:16
	v_cvt_pk_f32_fp8_sdwa v[46:47], v14 src0_sel:WORD_1
	v_cvt_pk_f32_fp8_sdwa v[48:49], v18 src0_sel:WORD_1
	v_cvt_pk_f32_fp8_sdwa v[42:43], v6 src0_sel:WORD_1
	v_cvt_pk_f32_fp8_sdwa v[44:45], v10 src0_sel:WORD_1
	s_waitcnt vmcnt(23)
	v_cvt_pk_f32_fp8_sdwa v[54:55], v30 src0_sel:WORD_1
	s_waitcnt vmcnt(22)
	v_cvt_pk_f32_fp8_sdwa v[56:57], v34 src0_sel:WORD_1
	v_pk_add_f32 v[42:43], v[42:43], 0 op_sel_hi:[1,0]
	v_cvt_pk_f32_fp8_e32 v[58:59], v6
	v_pk_add_f32 v[42:43], v[42:43], v[44:45]
	v_lshlrev_b32_e32 v44, 16, v39
	v_pk_add_f32 v[42:43], v[42:43], v[46:47]
	v_and_b32_e32 v45, 0xffff0000, v39
	v_pk_add_f32 v[42:43], v[42:43], v[48:49]
	v_pk_mul_f32 v[44:45], v[44:45], s[26:27] op_sel_hi:[1,0]
	v_pk_add_f32 v[42:43], v[42:43], v[50:51]
	v_cvt_pk_f32_fp8_e32 v[60:61], v10
	v_pk_add_f32 v[42:43], v[42:43], v[52:53]
	v_cvt_pk_f32_fp8_e32 v[62:63], v14
	v_pk_add_f32 v[42:43], v[42:43], v[54:55]
	v_cvt_pk_f32_fp8_e32 v[46:47], v15
	v_pk_add_f32 v[42:43], v[42:43], v[56:57]
	v_cvt_pk_f32_fp8_sdwa v[14:15], v15 src0_sel:WORD_1
	v_pk_fma_f32 v[42:43], v[42:43], s[28:29], v[44:45] op_sel_hi:[1,0,1]
	v_cvt_pk_f32_fp8_e32 v[44:45], v11
	v_cvt_pk_bf16_f32 v39, v42, v43
	v_cvt_pk_f32_fp8_e32 v[42:43], v7
	v_cvt_pk_f32_fp8_sdwa v[6:7], v7 src0_sel:WORD_1
	v_cvt_pk_f32_fp8_sdwa v[10:11], v11 src0_sel:WORD_1
	v_cvt_pk_f32_fp8_e32 v[64:65], v18
	v_cvt_pk_f32_fp8_e32 v[48:49], v19
	v_cvt_pk_f32_fp8_sdwa v[18:19], v19 src0_sel:WORD_1
	v_cvt_pk_f32_fp8_e32 v[66:67], v22
	v_cvt_pk_f32_fp8_e32 v[50:51], v23
	v_cvt_pk_f32_fp8_sdwa v[22:23], v23 src0_sel:WORD_1
	v_pk_add_f32 v[6:7], v[6:7], 0 op_sel_hi:[1,0]
	v_cvt_pk_f32_fp8_e32 v[68:69], v26
	v_cvt_pk_f32_fp8_e32 v[52:53], v27
	v_cvt_pk_f32_fp8_sdwa v[26:27], v27 src0_sel:WORD_1
	v_pk_add_f32 v[6:7], v[6:7], v[10:11]
	v_cvt_pk_f32_fp8_e32 v[70:71], v30
	v_pk_add_f32 v[58:59], v[58:59], 0 op_sel_hi:[1,0]
	v_cvt_pk_f32_fp8_e32 v[54:55], v31
	v_cvt_pk_f32_fp8_sdwa v[30:31], v31 src0_sel:WORD_1
	v_pk_add_f32 v[42:43], v[42:43], 0 op_sel_hi:[1,0]
	v_pk_add_f32 v[6:7], v[6:7], v[14:15]
	v_cvt_pk_f32_fp8_e32 v[72:73], v34
	v_pk_add_f32 v[58:59], v[58:59], v[60:61]
	v_cvt_pk_f32_fp8_e32 v[56:57], v35
	v_cvt_pk_f32_fp8_sdwa v[34:35], v35 src0_sel:WORD_1
	v_pk_add_f32 v[42:43], v[42:43], v[44:45]
	v_pk_add_f32 v[6:7], v[6:7], v[18:19]
	v_pk_add_f32 v[58:59], v[58:59], v[62:63]
	v_pk_add_f32 v[42:43], v[42:43], v[46:47]
	v_pk_add_f32 v[6:7], v[6:7], v[22:23]
	v_pk_add_f32 v[58:59], v[58:59], v[64:65]
	v_pk_add_f32 v[42:43], v[42:43], v[48:49]
	v_pk_add_f32 v[6:7], v[6:7], v[26:27]
	v_pk_add_f32 v[58:59], v[58:59], v[66:67]
	v_pk_add_f32 v[42:43], v[42:43], v[50:51]
	v_pk_add_f32 v[6:7], v[6:7], v[30:31]
	v_lshlrev_b32_e32 v10, 16, v41
	v_and_b32_e32 v11, 0xffff0000, v41
	v_pk_add_f32 v[58:59], v[58:59], v[68:69]
	v_pk_add_f32 v[42:43], v[42:43], v[52:53]
	v_pk_add_f32 v[6:7], v[6:7], v[34:35]
	v_pk_mul_f32 v[10:11], v[10:11], s[26:27] op_sel_hi:[1,0]
	v_pk_add_f32 v[58:59], v[58:59], v[70:71]
	v_lshlrev_b32_e32 v60, 16, v38
	v_and_b32_e32 v61, 0xffff0000, v38
	v_pk_add_f32 v[42:43], v[42:43], v[54:55]
	v_lshlrev_b32_e32 v44, 16, v40
	v_and_b32_e32 v45, 0xffff0000, v40
	v_pk_fma_f32 v[6:7], v[6:7], s[28:29], v[10:11] op_sel_hi:[1,0,1]
	v_cvt_pk_f32_fp8_e32 v[10:11], v8
	v_pk_add_f32 v[58:59], v[58:59], v[72:73]
	v_pk_mul_f32 v[60:61], v[60:61], s[26:27] op_sel_hi:[1,0]
	v_pk_add_f32 v[42:43], v[42:43], v[56:57]
	v_pk_mul_f32 v[44:45], v[44:45], s[26:27] op_sel_hi:[1,0]
	v_cvt_pk_f32_fp8_e32 v[18:19], v12
	v_pk_fma_f32 v[58:59], v[58:59], s[28:29], v[60:61] op_sel_hi:[1,0,1]
	v_pk_fma_f32 v[42:43], v[42:43], s[28:29], v[44:45] op_sel_hi:[1,0,1]
	v_cvt_pk_f32_fp8_e32 v[26:27], v16
	v_cvt_pk_bf16_f32 v38, v58, v59
	v_cvt_pk_bf16_f32 v40, v42, v43
	v_cvt_pk_bf16_f32 v41, v6, v7
	v_lshl_add_u64 v[6:7], v[86:87], 0, s[6:7]
	v_cvt_pk_f32_fp8_e32 v[34:35], v20
	global_store_dwordx4 v[6:7], v[38:41], off
	v_pk_add_f32 v[10:11], v[10:11], 0 op_sel_hi:[1,0]
	v_cvt_pk_f32_fp8_e32 v[44:45], v28
	v_cvt_pk_f32_fp8_e32 v[40:41], v24
	v_pk_add_f32 v[10:11], v[10:11], v[18:19]
	v_cvt_pk_f32_fp8_e32 v[48:49], v32
	v_pk_add_f32 v[10:11], v[10:11], v[26:27]
	v_cvt_pk_f32_fp8_e32 v[52:53], v36
	v_pk_add_f32 v[10:11], v[10:11], v[34:35]
	v_cvt_pk_f32_fp8_sdwa v[14:15], v8 src0_sel:WORD_1
	v_pk_add_f32 v[10:11], v[10:11], v[40:41]
	v_cvt_pk_f32_fp8_sdwa v[22:23], v12 src0_sel:WORD_1
	v_pk_add_f32 v[10:11], v[10:11], v[44:45]
	v_lshlrev_b32_e32 v18, 16, v2
	v_pk_add_f32 v[10:11], v[10:11], v[48:49]
	v_and_b32_e32 v19, 0xffff0000, v2
	v_cvt_pk_f32_fp8_sdwa v[30:31], v16 src0_sel:WORD_1
	v_pk_add_f32 v[10:11], v[10:11], v[52:53]
	v_pk_mul_f32 v[18:19], v[18:19], s[26:27] op_sel_hi:[1,0]
	v_cvt_pk_f32_fp8_sdwa v[38:39], v20 src0_sel:WORD_1
	v_pk_fma_f32 v[10:11], v[10:11], s[28:29], v[18:19] op_sel_hi:[1,0,1]
	v_cvt_pk_f32_fp8_sdwa v[42:43], v24 src0_sel:WORD_1
	v_cvt_pk_bf16_f32 v2, v10, v11
	v_pk_add_f32 v[10:11], v[14:15], 0 op_sel_hi:[1,0]
	v_cvt_pk_f32_fp8_sdwa v[46:47], v28 src0_sel:WORD_1
	v_pk_add_f32 v[10:11], v[10:11], v[22:23]
	v_cvt_pk_f32_fp8_sdwa v[50:51], v32 src0_sel:WORD_1
	v_pk_add_f32 v[10:11], v[10:11], v[30:31]
	v_cvt_pk_f32_fp8_sdwa v[54:55], v36 src0_sel:WORD_1
	v_pk_add_f32 v[10:11], v[10:11], v[38:39]
	v_lshlrev_b32_e32 v14, 16, v3
	v_pk_add_f32 v[10:11], v[10:11], v[42:43]
	v_and_b32_e32 v15, 0xffff0000, v3
	v_pk_add_f32 v[10:11], v[10:11], v[46:47]
	v_pk_mul_f32 v[14:15], v[14:15], s[26:27] op_sel_hi:[1,0]
	v_pk_add_f32 v[10:11], v[10:11], v[50:51]
	v_cvt_pk_f32_fp8_e32 v[26:27], v9
	v_pk_add_f32 v[10:11], v[10:11], v[54:55]
	v_cvt_pk_f32_fp8_sdwa v[8:9], v9 src0_sel:WORD_1
	v_pk_fma_f32 v[10:11], v[10:11], s[28:29], v[14:15] op_sel_hi:[1,0,1]
	v_cvt_pk_f32_fp8_e32 v[30:31], v13
	v_cvt_pk_bf16_f32 v3, v10, v11
	v_cvt_pk_f32_fp8_sdwa v[10:11], v13 src0_sel:WORD_1
	v_cvt_pk_f32_fp8_e32 v[34:35], v17
	v_cvt_pk_f32_fp8_sdwa v[12:13], v17 src0_sel:WORD_1
	v_cvt_pk_f32_fp8_e32 v[38:39], v21
	v_cvt_pk_f32_fp8_sdwa v[14:15], v21 src0_sel:WORD_1
	v_cvt_pk_f32_fp8_e32 v[40:41], v25
	v_cvt_pk_f32_fp8_sdwa v[16:17], v25 src0_sel:WORD_1
	v_pk_add_f32 v[26:27], v[26:27], 0 op_sel_hi:[1,0]
	v_pk_add_f32 v[8:9], v[8:9], 0 op_sel_hi:[1,0]
	v_cvt_pk_f32_fp8_e32 v[24:25], v29
	v_cvt_pk_f32_fp8_sdwa v[18:19], v29 src0_sel:WORD_1
	v_pk_add_f32 v[26:27], v[26:27], v[30:31]
	v_pk_add_f32 v[8:9], v[8:9], v[10:11]
	v_cvt_pk_f32_fp8_e32 v[28:29], v33
	v_cvt_pk_f32_fp8_sdwa v[20:21], v33 src0_sel:WORD_1
	v_pk_add_f32 v[26:27], v[26:27], v[34:35]
	v_pk_add_f32 v[8:9], v[8:9], v[12:13]
	v_cvt_pk_f32_fp8_e32 v[32:33], v37
	v_cvt_pk_f32_fp8_sdwa v[22:23], v37 src0_sel:WORD_1
	v_pk_add_f32 v[26:27], v[26:27], v[38:39]
	v_pk_add_f32 v[8:9], v[8:9], v[14:15]
	v_pk_add_f32 v[26:27], v[26:27], v[40:41]
	v_pk_add_f32 v[8:9], v[8:9], v[16:17]
	v_pk_add_f32 v[24:25], v[26:27], v[24:25]
	v_pk_add_f32 v[8:9], v[8:9], v[18:19]
	v_pk_add_f32 v[24:25], v[24:25], v[28:29]
	v_lshlrev_b32_e32 v26, 16, v4
	v_and_b32_e32 v27, 0xffff0000, v4
	v_pk_add_f32 v[8:9], v[8:9], v[20:21]
	v_lshlrev_b32_e32 v10, 16, v5
	v_and_b32_e32 v11, 0xffff0000, v5
	v_pk_add_f32 v[24:25], v[24:25], v[32:33]
	v_pk_mul_f32 v[26:27], v[26:27], s[26:27] op_sel_hi:[1,0]
	v_pk_add_f32 v[8:9], v[8:9], v[22:23]
	v_pk_mul_f32 v[10:11], v[10:11], s[26:27] op_sel_hi:[1,0]
	v_pk_fma_f32 v[24:25], v[24:25], s[28:29], v[26:27] op_sel_hi:[1,0,1]
	v_pk_fma_f32 v[8:9], v[8:9], s[28:29], v[10:11] op_sel_hi:[1,0,1]
	v_cvt_pk_bf16_f32 v4, v24, v25
	v_cvt_pk_bf16_f32 v5, v8, v9
	global_store_dwordx4 v[6:7], v[2:5], off offset:16
	s_add_i32 s41, s35, s37
	s_add_i32 s6, s41, 2
	s_ashr_i32 s7, s6, 31
	s_add_i32 s80, s31, s39
	s_lshl_b64 s[76:77], s[6:7], 11
	s_add_i32 s6, s80, -15
	s_ashr_i32 s7, s6, 31
	v_lshl_add_u64 v[2:3], v[82:83], 0, s[76:77]
	s_lshl_b64 s[6:7], s[6:7], 10
	global_load_dwordx4 v[42:45], v[2:3], off offset:16
	global_load_dwordx4 v[58:61], v[2:3], off
	v_lshl_add_u64 v[2:3], v[84:85], 0, s[6:7]
	s_add_i32 s6, s80, -14
	s_ashr_i32 s7, s6, 31
	s_lshl_b64 s[6:7], s[6:7], 10
	global_load_dwordx4 v[46:49], v[2:3], off
	v_lshl_add_u64 v[2:3], v[84:85], 0, s[6:7]
	s_add_i32 s6, s80, -13
	s_ashr_i32 s7, s6, 31
	s_lshl_b64 s[6:7], s[6:7], 10
	global_load_dwordx4 v[50:53], v[2:3], off
	v_lshl_add_u64 v[2:3], v[84:85], 0, s[6:7]
	s_add_i32 s6, s80, -12
	s_ashr_i32 s7, s6, 31
	s_lshl_b64 s[6:7], s[6:7], 10
	global_load_dwordx4 v[54:57], v[2:3], off
	v_lshl_add_u64 v[2:3], v[84:85], 0, s[6:7]
	s_add_i32 s6, s80, -11
	s_ashr_i32 s7, s6, 31
	s_lshl_b64 s[6:7], s[6:7], 10
	global_load_dwordx4 v[62:65], v[2:3], off
	v_lshl_add_u64 v[2:3], v[84:85], 0, s[6:7]
	s_add_i32 s6, s80, -10
	s_ashr_i32 s7, s6, 31
	s_lshl_b64 s[6:7], s[6:7], 10
	global_load_dwordx4 v[66:69], v[2:3], off
	v_lshl_add_u64 v[2:3], v[84:85], 0, s[6:7]
	s_add_i32 s6, s80, -9
	s_ashr_i32 s7, s6, 31
	s_lshl_b64 s[6:7], s[6:7], 10
	global_load_dwordx4 v[70:73], v[2:3], off
	v_lshl_add_u64 v[2:3], v[84:85], 0, s[6:7]
	s_add_i32 s6, s80, -8
	s_ashr_i32 s7, s6, 31
	s_lshl_b64 s[6:7], s[6:7], 10
	global_load_dwordx4 v[74:77], v[2:3], off
	v_lshl_add_u64 v[2:3], v[84:85], 0, s[6:7]
	global_load_dwordx4 v[78:81], v[2:3], off
	s_add_i32 s6, s41, 3
	s_ashr_i32 s7, s6, 31
	s_add_i32 s82, s80, -7
	s_lshl_b64 s[6:7], s[6:7], 11
	s_ashr_i32 s83, s82, 31
	v_lshl_add_u64 v[6:7], v[82:83], 0, s[6:7]
	s_lshl_b64 s[82:83], s[82:83], 10
	global_load_dwordx4 v[2:5], v[6:7], off offset:16
	global_load_dwordx4 v[38:41], v[6:7], off
	v_lshl_add_u64 v[6:7], v[84:85], 0, s[82:83]
	s_add_i32 s82, s80, -6
	s_ashr_i32 s83, s82, 31
	s_lshl_b64 s[82:83], s[82:83], 10
	v_lshl_add_u64 v[10:11], v[84:85], 0, s[82:83]
	s_add_i32 s82, s80, -5
	s_ashr_i32 s83, s82, 31
	s_lshl_b64 s[82:83], s[82:83], 10
	v_lshl_add_u64 v[14:15], v[84:85], 0, s[82:83]
	s_add_i32 s82, s80, -4
	s_ashr_i32 s83, s82, 31
	s_lshl_b64 s[82:83], s[82:83], 10
	v_lshl_add_u64 v[18:19], v[84:85], 0, s[82:83]
	s_add_i32 s82, s80, -3
	s_ashr_i32 s83, s82, 31
	s_lshl_b64 s[82:83], s[82:83], 10
	v_lshl_add_u64 v[22:23], v[84:85], 0, s[82:83]
	s_add_i32 s82, s80, -2
	global_load_dwordx4 v[6:9], v[6:7], off
	s_ashr_i32 s83, s82, 31
	global_load_dwordx4 v[10:13], v[10:11], off
	s_lshl_b64 s[82:83], s[82:83], 10
	global_load_dwordx4 v[14:17], v[14:15], off
	v_lshl_add_u64 v[26:27], v[84:85], 0, s[82:83]
	s_add_i32 s82, s80, -1
	global_load_dwordx4 v[18:21], v[18:19], off
	s_ashr_i32 s83, s82, 31
	global_load_dwordx4 v[22:25], v[22:23], off
	s_lshl_b64 s[82:83], s[82:83], 10
	s_ashr_i32 s81, s80, 31
	global_load_dwordx4 v[26:29], v[26:27], off
	v_lshl_add_u64 v[30:31], v[84:85], 0, s[82:83]
	s_lshl_b64 s[80:81], s[80:81], 10
	global_load_dwordx4 v[30:33], v[30:31], off
	v_lshl_add_u64 v[34:35], v[84:85], 0, s[80:81]
	global_load_dwordx4 v[34:37], v[34:35], off
	s_add_i32 s37, s37, 2
	s_add_i32 s39, s39, 16
	s_waitcnt vmcnt(41)
	v_cvt_pk_f32_fp8_e32 v[88:89], v170
	v_cvt_pk_f32_fp8_sdwa v[90:91], v170 src0_sel:WORD_1
	v_pk_add_f32 v[88:89], v[88:89], 0 op_sel_hi:[1,0]
	s_waitcnt vmcnt(40)
	v_cvt_pk_f32_fp8_e32 v[92:93], v174
	v_cvt_pk_f32_fp8_sdwa v[94:95], v174 src0_sel:WORD_1
	v_pk_add_f32 v[88:89], v[88:89], v[92:93]
	s_waitcnt vmcnt(39)
	v_cvt_pk_f32_fp8_e32 v[96:97], v178
	v_lshlrev_b32_e32 v92, 16, v182
	v_and_b32_e32 v93, 0xffff0000, v182
	v_cvt_pk_f32_fp8_sdwa v[98:99], v178 src0_sel:WORD_1
	v_pk_add_f32 v[88:89], v[88:89], v[96:97]
	s_waitcnt vmcnt(38)
	v_cvt_pk_f32_fp8_e32 v[100:101], v186
	v_pk_mul_f32 v[92:93], v[92:93], s[26:27] op_sel_hi:[1,0]
	v_cvt_pk_f32_fp8_sdwa v[102:103], v186 src0_sel:WORD_1
	v_pk_add_f32 v[88:89], v[88:89], v[100:101]
	s_waitcnt vmcnt(37)
	v_cvt_pk_f32_fp8_e32 v[104:105], v190
	v_cvt_pk_f32_fp8_sdwa v[106:107], v190 src0_sel:WORD_1
	v_cvt_pk_f32_fp8_e32 v[96:97], v191
	v_cvt_pk_f32_fp8_sdwa v[190:191], v191 src0_sel:WORD_1
	v_pk_add_f32 v[88:89], v[88:89], v[104:105]
	s_waitcnt vmcnt(36)
	v_cvt_pk_f32_fp8_e32 v[108:109], v194
	v_cvt_pk_f32_fp8_sdwa v[110:111], v194 src0_sel:WORD_1
	v_pk_add_f32 v[88:89], v[88:89], v[108:109]
	s_waitcnt vmcnt(35)
	v_cvt_pk_f32_fp8_e32 v[112:113], v198
	v_cvt_pk_f32_fp8_sdwa v[114:115], v198 src0_sel:WORD_1
	s_waitcnt vmcnt(34)
	v_cvt_pk_f32_fp8_e32 v[116:117], v202
	v_cvt_pk_f32_fp8_sdwa v[118:119], v202 src0_sel:WORD_1
	v_pk_add_f32 v[88:89], v[88:89], v[112:113]
	v_cvt_pk_f32_fp8_e32 v[100:101], v199
	v_pk_add_f32 v[88:89], v[88:89], v[116:117]
	v_cvt_pk_f32_fp8_sdwa v[198:199], v199 src0_sel:WORD_1
	v_pk_fma_f32 v[88:89], v[88:89], s[28:29], v[92:93] op_sel_hi:[1,0,1]
	v_cvt_pk_f32_fp8_e32 v[92:93], v179
	v_cvt_pk_bf16_f32 v182, v88, v89
	v_pk_add_f32 v[88:89], v[90:91], 0 op_sel_hi:[1,0]
	v_lshlrev_b32_e32 v90, 16, v183
	v_pk_add_f32 v[88:89], v[88:89], v[94:95]
	v_and_b32_e32 v91, 0xffff0000, v183
	v_pk_add_f32 v[88:89], v[88:89], v[98:99]
	v_pk_mul_f32 v[90:91], v[90:91], s[26:27] op_sel_hi:[1,0]
	v_pk_add_f32 v[88:89], v[88:89], v[102:103]
	v_cvt_pk_f32_fp8_sdwa v[178:179], v179 src0_sel:WORD_1
	v_pk_add_f32 v[88:89], v[88:89], v[106:107]
	v_cvt_pk_f32_fp8_e32 v[94:95], v187
	v_pk_add_f32 v[88:89], v[88:89], v[110:111]
	v_cvt_pk_f32_fp8_sdwa v[186:187], v187 src0_sel:WORD_1
	v_pk_add_f32 v[88:89], v[88:89], v[114:115]
	v_cvt_pk_f32_fp8_e32 v[98:99], v195
	v_pk_add_f32 v[88:89], v[88:89], v[118:119]
	v_cvt_pk_f32_fp8_sdwa v[194:195], v195 src0_sel:WORD_1
	v_pk_fma_f32 v[88:89], v[88:89], s[28:29], v[90:91] op_sel_hi:[1,0,1]
	v_cvt_pk_f32_fp8_e32 v[90:91], v175
	v_cvt_pk_bf16_f32 v183, v88, v89
	v_cvt_pk_f32_fp8_e32 v[88:89], v171
	v_cvt_pk_f32_fp8_sdwa v[170:171], v171 src0_sel:WORD_1
	v_cvt_pk_f32_fp8_sdwa v[174:175], v175 src0_sel:WORD_1
	v_cvt_pk_f32_fp8_e32 v[102:103], v203
	v_pk_add_f32 v[88:89], v[88:89], 0 op_sel_hi:[1,0]
	v_pk_add_f32 v[170:171], v[170:171], 0 op_sel_hi:[1,0]
	v_pk_add_f32 v[88:89], v[88:89], v[90:91]
	v_pk_add_f32 v[170:171], v[170:171], v[174:175]
	v_pk_add_f32 v[88:89], v[88:89], v[92:93]
	v_pk_add_f32 v[170:171], v[170:171], v[178:179]
	v_cvt_pk_f32_fp8_sdwa v[202:203], v203 src0_sel:WORD_1
	v_pk_add_f32 v[88:89], v[88:89], v[94:95]
	v_pk_add_f32 v[170:171], v[170:171], v[186:187]
	v_pk_add_f32 v[88:89], v[88:89], v[96:97]
	v_pk_add_f32 v[170:171], v[170:171], v[190:191]
	v_pk_add_f32 v[88:89], v[88:89], v[98:99]
	v_pk_add_f32 v[170:171], v[170:171], v[194:195]
	v_pk_add_f32 v[88:89], v[88:89], v[100:101]
	v_lshlrev_b32_e32 v90, 16, v184
	v_and_b32_e32 v91, 0xffff0000, v184
	v_pk_add_f32 v[170:171], v[170:171], v[198:199]
	v_lshlrev_b32_e32 v174, 16, v185
	v_and_b32_e32 v175, 0xffff0000, v185
	v_pk_add_f32 v[88:89], v[88:89], v[102:103]
	v_pk_mul_f32 v[90:91], v[90:91], s[26:27] op_sel_hi:[1,0]
	v_pk_add_f32 v[170:171], v[170:171], v[202:203]
	v_pk_mul_f32 v[174:175], v[174:175], s[26:27] op_sel_hi:[1,0]
	v_pk_fma_f32 v[88:89], v[88:89], s[28:29], v[90:91] op_sel_hi:[1,0,1]
	v_pk_fma_f32 v[170:171], v[170:171], s[28:29], v[174:175] op_sel_hi:[1,0,1]
	v_cvt_pk_bf16_f32 v184, v88, v89
	v_cvt_pk_bf16_f32 v185, v170, v171
	v_lshl_add_u64 v[170:171], v[86:87], 0, s[100:101]
	v_cvt_pk_f32_fp8_e32 v[174:175], v172
	global_store_dwordx4 v[170:171], v[182:185], off
	v_cvt_pk_f32_fp8_e32 v[186:187], v180
	v_cvt_pk_f32_fp8_e32 v[194:195], v188
	v_cvt_pk_f32_fp8_e32 v[182:183], v176
	v_cvt_pk_f32_fp8_e32 v[202:203], v192
	v_pk_add_f32 v[174:175], v[174:175], 0 op_sel_hi:[1,0]
	v_cvt_pk_f32_fp8_e32 v[90:91], v196
	v_pk_add_f32 v[174:175], v[174:175], v[182:183]
	v_cvt_pk_f32_fp8_e32 v[94:95], v200
	v_pk_add_f32 v[174:175], v[174:175], v[186:187]
	v_cvt_pk_f32_fp8_e32 v[98:99], v204
	v_pk_add_f32 v[174:175], v[174:175], v[194:195]
	v_cvt_pk_f32_fp8_sdwa v[178:179], v172 src0_sel:WORD_1
	v_pk_add_f32 v[174:175], v[174:175], v[202:203]
	v_cvt_pk_f32_fp8_sdwa v[184:185], v176 src0_sel:WORD_1
	v_pk_add_f32 v[174:175], v[174:175], v[90:91]
	v_lshlrev_b32_e32 v182, 16, v166
	v_pk_add_f32 v[174:175], v[174:175], v[94:95]
	v_and_b32_e32 v183, 0xffff0000, v166
	v_cvt_pk_f32_fp8_sdwa v[190:191], v180 src0_sel:WORD_1
	v_pk_add_f32 v[174:175], v[174:175], v[98:99]
	v_pk_mul_f32 v[182:183], v[182:183], s[26:27] op_sel_hi:[1,0]
	v_cvt_pk_f32_fp8_sdwa v[198:199], v188 src0_sel:WORD_1
	v_pk_fma_f32 v[174:175], v[174:175], s[28:29], v[182:183] op_sel_hi:[1,0,1]
	v_cvt_pk_f32_fp8_sdwa v[88:89], v192 src0_sel:WORD_1
	v_cvt_pk_bf16_f32 v166, v174, v175
	v_pk_add_f32 v[174:175], v[178:179], 0 op_sel_hi:[1,0]
	v_cvt_pk_f32_fp8_sdwa v[92:93], v196 src0_sel:WORD_1
	v_pk_add_f32 v[174:175], v[174:175], v[184:185]
	v_cvt_pk_f32_fp8_sdwa v[96:97], v200 src0_sel:WORD_1
	v_pk_add_f32 v[174:175], v[174:175], v[190:191]
	v_cvt_pk_f32_fp8_sdwa v[100:101], v204 src0_sel:WORD_1
	v_pk_add_f32 v[174:175], v[174:175], v[198:199]
	v_lshlrev_b32_e32 v178, 16, v167
	v_pk_add_f32 v[174:175], v[174:175], v[88:89]
	v_and_b32_e32 v179, 0xffff0000, v167
	v_pk_add_f32 v[174:175], v[174:175], v[92:93]
	v_pk_mul_f32 v[178:179], v[178:179], s[26:27] op_sel_hi:[1,0]
	v_pk_add_f32 v[174:175], v[174:175], v[96:97]
	v_cvt_pk_f32_fp8_e32 v[182:183], v181
	v_pk_add_f32 v[174:175], v[174:175], v[100:101]
	v_cvt_pk_f32_fp8_e32 v[184:185], v189
	v_pk_fma_f32 v[174:175], v[174:175], s[28:29], v[178:179] op_sel_hi:[1,0,1]
	v_cvt_pk_f32_fp8_e32 v[178:179], v177
	v_cvt_pk_bf16_f32 v167, v174, v175
	v_cvt_pk_f32_fp8_e32 v[174:175], v173
	v_cvt_pk_f32_fp8_sdwa v[172:173], v173 src0_sel:WORD_1
	v_cvt_pk_f32_fp8_sdwa v[176:177], v177 src0_sel:WORD_1
	v_cvt_pk_f32_fp8_sdwa v[186:187], v189 src0_sel:WORD_1
	v_cvt_pk_f32_fp8_e32 v[188:189], v193
	v_pk_add_f32 v[174:175], v[174:175], 0 op_sel_hi:[1,0]
	v_cvt_pk_f32_fp8_sdwa v[180:181], v181 src0_sel:WORD_1
	v_cvt_pk_f32_fp8_sdwa v[190:191], v193 src0_sel:WORD_1
	v_cvt_pk_f32_fp8_e32 v[192:193], v197
	v_pk_add_f32 v[174:175], v[174:175], v[178:179]
	v_cvt_pk_f32_fp8_sdwa v[194:195], v197 src0_sel:WORD_1
	v_cvt_pk_f32_fp8_e32 v[196:197], v201
	v_pk_add_f32 v[174:175], v[174:175], v[182:183]
	v_cvt_pk_f32_fp8_sdwa v[198:199], v201 src0_sel:WORD_1
	v_cvt_pk_f32_fp8_e32 v[200:201], v205
	v_pk_add_f32 v[174:175], v[174:175], v[184:185]
	v_pk_add_f32 v[172:173], v[172:173], 0 op_sel_hi:[1,0]
	v_pk_add_f32 v[174:175], v[174:175], v[188:189]
	v_pk_add_f32 v[172:173], v[172:173], v[176:177]
	v_pk_add_f32 v[174:175], v[174:175], v[192:193]
	v_pk_add_f32 v[172:173], v[172:173], v[180:181]
	v_cvt_pk_f32_fp8_sdwa v[202:203], v205 src0_sel:WORD_1
	v_pk_add_f32 v[174:175], v[174:175], v[196:197]
	v_lshlrev_b32_e32 v178, 16, v168
	v_and_b32_e32 v179, 0xffff0000, v168
	v_pk_add_f32 v[172:173], v[172:173], v[186:187]
	v_pk_add_f32 v[174:175], v[174:175], v[200:201]
	v_pk_mul_f32 v[178:179], v[178:179], s[26:27] op_sel_hi:[1,0]
	v_pk_add_f32 v[172:173], v[172:173], v[190:191]
	v_pk_fma_f32 v[174:175], v[174:175], s[28:29], v[178:179] op_sel_hi:[1,0,1]
	v_pk_add_f32 v[172:173], v[172:173], v[194:195]
	v_cvt_pk_bf16_f32 v168, v174, v175
	v_pk_add_f32 v[172:173], v[172:173], v[198:199]
	v_lshlrev_b32_e32 v174, 16, v169
	v_and_b32_e32 v175, 0xffff0000, v169
	v_pk_add_f32 v[172:173], v[172:173], v[202:203]
	v_pk_mul_f32 v[174:175], v[174:175], s[26:27] op_sel_hi:[1,0]
	s_waitcnt vmcnt(27)
	v_cvt_pk_f32_fp8_sdwa v[176:177], v150 src0_sel:WORD_1
	v_pk_fma_f32 v[172:173], v[172:173], s[28:29], v[174:175] op_sel_hi:[1,0,1]
	v_cvt_pk_f32_fp8_sdwa v[174:175], v142 src0_sel:WORD_1
	v_cvt_pk_bf16_f32 v169, v172, v173
	global_store_dwordx4 v[170:171], v[166:169], off offset:16
	v_cvt_pk_f32_fp8_sdwa v[170:171], v134 src0_sel:WORD_1
	v_cvt_pk_f32_fp8_sdwa v[172:173], v138 src0_sel:WORD_1
	v_cvt_pk_f32_fp8_sdwa v[166:167], v126 src0_sel:WORD_1
	v_cvt_pk_f32_fp8_sdwa v[168:169], v130 src0_sel:WORD_1
	s_waitcnt vmcnt(27)
	v_cvt_pk_f32_fp8_sdwa v[178:179], v154 src0_sel:WORD_1
	s_waitcnt vmcnt(26)
	v_cvt_pk_f32_fp8_sdwa v[180:181], v158 src0_sel:WORD_1
	v_pk_add_f32 v[166:167], v[166:167], 0 op_sel_hi:[1,0]
	v_cvt_pk_f32_fp8_e32 v[182:183], v126
	v_pk_add_f32 v[166:167], v[166:167], v[168:169]
	v_lshlrev_b32_e32 v168, 16, v163
	v_pk_add_f32 v[166:167], v[166:167], v[170:171]
	v_and_b32_e32 v169, 0xffff0000, v163
	v_pk_add_f32 v[166:167], v[166:167], v[172:173]
	v_pk_mul_f32 v[168:169], v[168:169], s[26:27] op_sel_hi:[1,0]
	v_pk_add_f32 v[166:167], v[166:167], v[174:175]
	v_cvt_pk_f32_fp8_e32 v[184:185], v130
	v_pk_add_f32 v[166:167], v[166:167], v[176:177]
	v_cvt_pk_f32_fp8_e32 v[186:187], v134
	v_pk_add_f32 v[166:167], v[166:167], v[178:179]
	v_cvt_pk_f32_fp8_e32 v[170:171], v135
	v_pk_add_f32 v[166:167], v[166:167], v[180:181]
	v_cvt_pk_f32_fp8_sdwa v[134:135], v135 src0_sel:WORD_1
	v_pk_fma_f32 v[166:167], v[166:167], s[28:29], v[168:169] op_sel_hi:[1,0,1]
	v_cvt_pk_f32_fp8_e32 v[168:169], v131
	v_cvt_pk_bf16_f32 v163, v166, v167
	v_cvt_pk_f32_fp8_e32 v[166:167], v127
	v_cvt_pk_f32_fp8_sdwa v[126:127], v127 src0_sel:WORD_1
	v_cvt_pk_f32_fp8_sdwa v[130:131], v131 src0_sel:WORD_1
	v_cvt_pk_f32_fp8_e32 v[188:189], v138
	v_cvt_pk_f32_fp8_e32 v[172:173], v139
	v_cvt_pk_f32_fp8_sdwa v[138:139], v139 src0_sel:WORD_1
	v_cvt_pk_f32_fp8_e32 v[190:191], v142
	v_cvt_pk_f32_fp8_e32 v[174:175], v143
	v_cvt_pk_f32_fp8_sdwa v[142:143], v143 src0_sel:WORD_1
	v_pk_add_f32 v[126:127], v[126:127], 0 op_sel_hi:[1,0]
	v_cvt_pk_f32_fp8_e32 v[192:193], v150
	v_cvt_pk_f32_fp8_e32 v[176:177], v151
	v_cvt_pk_f32_fp8_sdwa v[150:151], v151 src0_sel:WORD_1
	v_pk_add_f32 v[126:127], v[126:127], v[130:131]
	v_cvt_pk_f32_fp8_e32 v[194:195], v154
	v_pk_add_f32 v[182:183], v[182:183], 0 op_sel_hi:[1,0]
	v_cvt_pk_f32_fp8_e32 v[178:179], v155
	v_cvt_pk_f32_fp8_sdwa v[154:155], v155 src0_sel:WORD_1
	v_pk_add_f32 v[166:167], v[166:167], 0 op_sel_hi:[1,0]
	v_pk_add_f32 v[126:127], v[126:127], v[134:135]
	v_cvt_pk_f32_fp8_e32 v[196:197], v158
	v_pk_add_f32 v[182:183], v[182:183], v[184:185]
	v_cvt_pk_f32_fp8_e32 v[180:181], v159
	v_cvt_pk_f32_fp8_sdwa v[158:159], v159 src0_sel:WORD_1
	v_pk_add_f32 v[166:167], v[166:167], v[168:169]
	v_pk_add_f32 v[126:127], v[126:127], v[138:139]
	v_pk_add_f32 v[182:183], v[182:183], v[186:187]
	v_pk_add_f32 v[166:167], v[166:167], v[170:171]
	v_pk_add_f32 v[126:127], v[126:127], v[142:143]
	v_pk_add_f32 v[182:183], v[182:183], v[188:189]
	v_pk_add_f32 v[166:167], v[166:167], v[172:173]
	v_pk_add_f32 v[126:127], v[126:127], v[150:151]
	v_pk_add_f32 v[182:183], v[182:183], v[190:191]
	v_pk_add_f32 v[166:167], v[166:167], v[174:175]
	v_pk_add_f32 v[126:127], v[126:127], v[154:155]
	v_lshlrev_b32_e32 v130, 16, v165
	v_and_b32_e32 v131, 0xffff0000, v165
	v_pk_add_f32 v[182:183], v[182:183], v[192:193]
	v_pk_add_f32 v[166:167], v[166:167], v[176:177]
	v_pk_add_f32 v[126:127], v[126:127], v[158:159]
	v_pk_mul_f32 v[130:131], v[130:131], s[26:27] op_sel_hi:[1,0]
	v_pk_add_f32 v[182:183], v[182:183], v[194:195]
	v_lshlrev_b32_e32 v184, 16, v162
	v_and_b32_e32 v185, 0xffff0000, v162
	v_pk_add_f32 v[166:167], v[166:167], v[178:179]
	v_lshlrev_b32_e32 v168, 16, v164
	v_and_b32_e32 v169, 0xffff0000, v164
	v_pk_fma_f32 v[126:127], v[126:127], s[28:29], v[130:131] op_sel_hi:[1,0,1]
	v_cvt_pk_f32_fp8_e32 v[130:131], v128
	v_pk_add_f32 v[182:183], v[182:183], v[196:197]
	v_pk_mul_f32 v[184:185], v[184:185], s[26:27] op_sel_hi:[1,0]
	v_pk_add_f32 v[166:167], v[166:167], v[180:181]
	v_pk_mul_f32 v[168:169], v[168:169], s[26:27] op_sel_hi:[1,0]
	v_cvt_pk_f32_fp8_e32 v[138:139], v132
	v_pk_fma_f32 v[182:183], v[182:183], s[28:29], v[184:185] op_sel_hi:[1,0,1]
	v_pk_fma_f32 v[166:167], v[166:167], s[28:29], v[168:169] op_sel_hi:[1,0,1]
	v_cvt_pk_f32_fp8_e32 v[150:151], v136
	v_cvt_pk_bf16_f32 v162, v182, v183
	v_cvt_pk_bf16_f32 v164, v166, v167
	v_cvt_pk_bf16_f32 v165, v126, v127
	v_lshl_add_u64 v[126:127], v[86:87], 0, s[98:99]
	v_cvt_pk_f32_fp8_e32 v[158:159], v140
	global_store_dwordx4 v[126:127], v[162:165], off
	v_pk_add_f32 v[130:131], v[130:131], 0 op_sel_hi:[1,0]
	v_cvt_pk_f32_fp8_e32 v[168:169], v152
	v_cvt_pk_f32_fp8_e32 v[164:165], v144
	v_pk_add_f32 v[130:131], v[130:131], v[138:139]
	v_cvt_pk_f32_fp8_e32 v[172:173], v156
	v_pk_add_f32 v[130:131], v[130:131], v[150:151]
	v_cvt_pk_f32_fp8_e32 v[176:177], v160
	v_pk_add_f32 v[130:131], v[130:131], v[158:159]
	v_cvt_pk_f32_fp8_sdwa v[134:135], v128 src0_sel:WORD_1
	v_pk_add_f32 v[130:131], v[130:131], v[164:165]
	v_cvt_pk_f32_fp8_sdwa v[142:143], v132 src0_sel:WORD_1
	v_pk_add_f32 v[130:131], v[130:131], v[168:169]
	v_lshlrev_b32_e32 v138, 16, v122
	v_pk_add_f32 v[130:131], v[130:131], v[172:173]
	v_and_b32_e32 v139, 0xffff0000, v122
	v_cvt_pk_f32_fp8_sdwa v[154:155], v136 src0_sel:WORD_1
	v_pk_add_f32 v[130:131], v[130:131], v[176:177]
	v_pk_mul_f32 v[138:139], v[138:139], s[26:27] op_sel_hi:[1,0]
	v_cvt_pk_f32_fp8_sdwa v[162:163], v140 src0_sel:WORD_1
	v_pk_fma_f32 v[130:131], v[130:131], s[28:29], v[138:139] op_sel_hi:[1,0,1]
	v_cvt_pk_f32_fp8_sdwa v[166:167], v144 src0_sel:WORD_1
	v_cvt_pk_bf16_f32 v122, v130, v131
	v_pk_add_f32 v[130:131], v[134:135], 0 op_sel_hi:[1,0]
	v_cvt_pk_f32_fp8_sdwa v[170:171], v152 src0_sel:WORD_1
	v_pk_add_f32 v[130:131], v[130:131], v[142:143]
	v_cvt_pk_f32_fp8_sdwa v[174:175], v156 src0_sel:WORD_1
	v_pk_add_f32 v[130:131], v[130:131], v[154:155]
	v_cvt_pk_f32_fp8_sdwa v[178:179], v160 src0_sel:WORD_1
	v_pk_add_f32 v[130:131], v[130:131], v[162:163]
	v_lshlrev_b32_e32 v134, 16, v123
	v_pk_add_f32 v[130:131], v[130:131], v[166:167]
	v_and_b32_e32 v135, 0xffff0000, v123
	v_pk_add_f32 v[130:131], v[130:131], v[170:171]
	v_pk_mul_f32 v[134:135], v[134:135], s[26:27] op_sel_hi:[1,0]
	v_pk_add_f32 v[130:131], v[130:131], v[174:175]
	v_cvt_pk_f32_fp8_e32 v[150:151], v129
	v_pk_add_f32 v[130:131], v[130:131], v[178:179]
	v_cvt_pk_f32_fp8_sdwa v[128:129], v129 src0_sel:WORD_1
	v_pk_fma_f32 v[130:131], v[130:131], s[28:29], v[134:135] op_sel_hi:[1,0,1]
	v_cvt_pk_f32_fp8_e32 v[154:155], v133
	v_cvt_pk_bf16_f32 v123, v130, v131
	v_cvt_pk_f32_fp8_sdwa v[130:131], v133 src0_sel:WORD_1
	v_cvt_pk_f32_fp8_e32 v[158:159], v137
	v_cvt_pk_f32_fp8_sdwa v[132:133], v137 src0_sel:WORD_1
	v_cvt_pk_f32_fp8_e32 v[162:163], v141
	v_cvt_pk_f32_fp8_sdwa v[134:135], v141 src0_sel:WORD_1
	v_cvt_pk_f32_fp8_e32 v[164:165], v145
	v_cvt_pk_f32_fp8_sdwa v[136:137], v145 src0_sel:WORD_1
	v_pk_add_f32 v[150:151], v[150:151], 0 op_sel_hi:[1,0]
	v_pk_add_f32 v[128:129], v[128:129], 0 op_sel_hi:[1,0]
	v_cvt_pk_f32_fp8_e32 v[144:145], v153
	v_cvt_pk_f32_fp8_sdwa v[138:139], v153 src0_sel:WORD_1
	v_pk_add_f32 v[150:151], v[150:151], v[154:155]
	v_pk_add_f32 v[128:129], v[128:129], v[130:131]
	v_cvt_pk_f32_fp8_e32 v[152:153], v157
	v_cvt_pk_f32_fp8_sdwa v[140:141], v157 src0_sel:WORD_1
	v_pk_add_f32 v[150:151], v[150:151], v[158:159]
	v_pk_add_f32 v[128:129], v[128:129], v[132:133]
	v_cvt_pk_f32_fp8_e32 v[156:157], v161
	v_cvt_pk_f32_fp8_sdwa v[142:143], v161 src0_sel:WORD_1
	v_pk_add_f32 v[150:151], v[150:151], v[162:163]
	v_pk_add_f32 v[128:129], v[128:129], v[134:135]
	v_pk_add_f32 v[150:151], v[150:151], v[164:165]
	v_pk_add_f32 v[128:129], v[128:129], v[136:137]
	v_pk_add_f32 v[144:145], v[150:151], v[144:145]
	v_pk_add_f32 v[128:129], v[128:129], v[138:139]
	v_pk_add_f32 v[144:145], v[144:145], v[152:153]
	v_lshlrev_b32_e32 v150, 16, v124
	v_and_b32_e32 v151, 0xffff0000, v124
	v_pk_add_f32 v[128:129], v[128:129], v[140:141]
	v_lshlrev_b32_e32 v130, 16, v125
	v_and_b32_e32 v131, 0xffff0000, v125
	v_pk_add_f32 v[144:145], v[144:145], v[156:157]
	v_pk_mul_f32 v[150:151], v[150:151], s[26:27] op_sel_hi:[1,0]
	v_pk_add_f32 v[128:129], v[128:129], v[142:143]
	v_pk_mul_f32 v[130:131], v[130:131], s[26:27] op_sel_hi:[1,0]
	v_pk_fma_f32 v[144:145], v[144:145], s[28:29], v[150:151] op_sel_hi:[1,0,1]
	v_pk_fma_f32 v[128:129], v[128:129], s[28:29], v[130:131] op_sel_hi:[1,0,1]
	v_cvt_pk_bf16_f32 v124, v144, v145
	v_cvt_pk_bf16_f32 v125, v128, v129
	global_store_dwordx4 v[126:127], v[122:125], off offset:16
	s_add_i32 s41, s35, s37
	s_add_i32 s98, s41, 2
	s_ashr_i32 s99, s98, 31
	s_add_i32 s80, s31, s39
	s_lshl_b64 s[100:101], s[98:99], 11
	s_add_i32 s98, s80, -15
	s_ashr_i32 s99, s98, 31
	v_lshl_add_u64 v[122:123], v[82:83], 0, s[100:101]
	s_lshl_b64 s[98:99], s[98:99], 10
	global_load_dwordx4 v[166:169], v[122:123], off offset:16
	global_load_dwordx4 v[182:185], v[122:123], off
	v_lshl_add_u64 v[122:123], v[84:85], 0, s[98:99]
	s_add_i32 s98, s80, -14
	s_ashr_i32 s99, s98, 31
	s_lshl_b64 s[98:99], s[98:99], 10
	global_load_dwordx4 v[170:173], v[122:123], off
	v_lshl_add_u64 v[122:123], v[84:85], 0, s[98:99]
	s_add_i32 s98, s80, -13
	s_ashr_i32 s99, s98, 31
	s_lshl_b64 s[98:99], s[98:99], 10
	global_load_dwordx4 v[174:177], v[122:123], off
	v_lshl_add_u64 v[122:123], v[84:85], 0, s[98:99]
	s_add_i32 s98, s80, -12
	s_ashr_i32 s99, s98, 31
	s_lshl_b64 s[98:99], s[98:99], 10
	global_load_dwordx4 v[178:181], v[122:123], off
	v_lshl_add_u64 v[122:123], v[84:85], 0, s[98:99]
	s_add_i32 s98, s80, -11
	s_ashr_i32 s99, s98, 31
	s_lshl_b64 s[98:99], s[98:99], 10
	global_load_dwordx4 v[186:189], v[122:123], off
	v_lshl_add_u64 v[122:123], v[84:85], 0, s[98:99]
	s_add_i32 s98, s80, -10
	s_ashr_i32 s99, s98, 31
	s_lshl_b64 s[98:99], s[98:99], 10
	global_load_dwordx4 v[190:193], v[122:123], off
	v_lshl_add_u64 v[122:123], v[84:85], 0, s[98:99]
	s_add_i32 s98, s80, -9
	s_ashr_i32 s99, s98, 31
	s_lshl_b64 s[98:99], s[98:99], 10
	global_load_dwordx4 v[194:197], v[122:123], off
	v_lshl_add_u64 v[122:123], v[84:85], 0, s[98:99]
	s_add_i32 s98, s80, -8
	s_ashr_i32 s99, s98, 31
	s_lshl_b64 s[98:99], s[98:99], 10
	global_load_dwordx4 v[198:201], v[122:123], off
	v_lshl_add_u64 v[122:123], v[84:85], 0, s[98:99]
	global_load_dwordx4 v[202:205], v[122:123], off
	s_add_i32 s98, s41, 3
	s_ashr_i32 s99, s98, 31
	s_add_i32 s82, s80, -7
	s_lshl_b64 s[98:99], s[98:99], 11
	s_ashr_i32 s83, s82, 31
	v_lshl_add_u64 v[126:127], v[82:83], 0, s[98:99]
	s_lshl_b64 s[82:83], s[82:83], 10
	global_load_dwordx4 v[122:125], v[126:127], off offset:16
	global_load_dwordx4 v[162:165], v[126:127], off
	v_lshl_add_u64 v[126:127], v[84:85], 0, s[82:83]
	s_add_i32 s82, s80, -6
	s_ashr_i32 s83, s82, 31
	s_lshl_b64 s[82:83], s[82:83], 10
	v_lshl_add_u64 v[130:131], v[84:85], 0, s[82:83]
	s_add_i32 s82, s80, -5
	s_ashr_i32 s83, s82, 31
	s_lshl_b64 s[82:83], s[82:83], 10
	v_lshl_add_u64 v[134:135], v[84:85], 0, s[82:83]
	s_add_i32 s82, s80, -4
	s_ashr_i32 s83, s82, 31
	s_lshl_b64 s[82:83], s[82:83], 10
	v_lshl_add_u64 v[138:139], v[84:85], 0, s[82:83]
	s_add_i32 s82, s80, -3
	s_ashr_i32 s83, s82, 31
	s_lshl_b64 s[82:83], s[82:83], 10
	v_lshl_add_u64 v[142:143], v[84:85], 0, s[82:83]
	s_add_i32 s82, s80, -2
	global_load_dwordx4 v[126:129], v[126:127], off
	s_ashr_i32 s83, s82, 31
	global_load_dwordx4 v[130:133], v[130:131], off
	s_lshl_b64 s[82:83], s[82:83], 10
	global_load_dwordx4 v[134:137], v[134:135], off
	v_lshl_add_u64 v[150:151], v[84:85], 0, s[82:83]
	s_add_i32 s82, s80, -1
	global_load_dwordx4 v[138:141], v[138:139], off
	s_ashr_i32 s83, s82, 31
	global_load_dwordx4 v[142:145], v[142:143], off
	s_lshl_b64 s[82:83], s[82:83], 10
	s_ashr_i32 s81, s80, 31
	global_load_dwordx4 v[150:153], v[150:151], off
	v_lshl_add_u64 v[154:155], v[84:85], 0, s[82:83]
	s_lshl_b64 s[80:81], s[80:81], 10
	global_load_dwordx4 v[154:157], v[154:155], off
	v_lshl_add_u64 v[158:159], v[84:85], 0, s[80:81]
	global_load_dwordx4 v[158:161], v[158:159], off
	s_add_i32 s37, s37, 2
	s_add_i32 s39, s39, 16
	s_waitcnt vmcnt(41)
	v_cvt_pk_f32_fp8_e32 v[88:89], v46
	v_cvt_pk_f32_fp8_sdwa v[90:91], v46 src0_sel:WORD_1
	v_pk_add_f32 v[88:89], v[88:89], 0 op_sel_hi:[1,0]
	s_waitcnt vmcnt(40)
	v_cvt_pk_f32_fp8_e32 v[92:93], v50
	v_cvt_pk_f32_fp8_sdwa v[94:95], v50 src0_sel:WORD_1
	v_pk_add_f32 v[88:89], v[88:89], v[92:93]
	s_waitcnt vmcnt(39)
	v_cvt_pk_f32_fp8_e32 v[96:97], v54
	v_lshlrev_b32_e32 v92, 16, v58
	v_and_b32_e32 v93, 0xffff0000, v58
	v_cvt_pk_f32_fp8_sdwa v[98:99], v54 src0_sel:WORD_1
	v_pk_add_f32 v[88:89], v[88:89], v[96:97]
	s_waitcnt vmcnt(38)
	v_cvt_pk_f32_fp8_e32 v[100:101], v62
	v_pk_mul_f32 v[92:93], v[92:93], s[26:27] op_sel_hi:[1,0]
	v_cvt_pk_f32_fp8_sdwa v[102:103], v62 src0_sel:WORD_1
	v_pk_add_f32 v[88:89], v[88:89], v[100:101]
	s_waitcnt vmcnt(37)
	v_cvt_pk_f32_fp8_e32 v[104:105], v66
	v_cvt_pk_f32_fp8_sdwa v[106:107], v66 src0_sel:WORD_1
	v_cvt_pk_f32_fp8_e32 v[96:97], v67
	v_cvt_pk_f32_fp8_sdwa v[66:67], v67 src0_sel:WORD_1
	v_pk_add_f32 v[88:89], v[88:89], v[104:105]
	s_waitcnt vmcnt(36)
	v_cvt_pk_f32_fp8_e32 v[108:109], v70
	v_cvt_pk_f32_fp8_sdwa v[110:111], v70 src0_sel:WORD_1
	v_pk_add_f32 v[88:89], v[88:89], v[108:109]
	s_waitcnt vmcnt(35)
	v_cvt_pk_f32_fp8_e32 v[112:113], v74
	v_cvt_pk_f32_fp8_sdwa v[114:115], v74 src0_sel:WORD_1
	s_waitcnt vmcnt(34)
	v_cvt_pk_f32_fp8_e32 v[116:117], v78
	v_cvt_pk_f32_fp8_sdwa v[118:119], v78 src0_sel:WORD_1
	v_pk_add_f32 v[88:89], v[88:89], v[112:113]
	v_cvt_pk_f32_fp8_e32 v[100:101], v75
	v_pk_add_f32 v[88:89], v[88:89], v[116:117]
	v_cvt_pk_f32_fp8_sdwa v[74:75], v75 src0_sel:WORD_1
	v_pk_fma_f32 v[88:89], v[88:89], s[28:29], v[92:93] op_sel_hi:[1,0,1]
	v_cvt_pk_f32_fp8_e32 v[92:93], v55
	v_cvt_pk_bf16_f32 v58, v88, v89
	v_pk_add_f32 v[88:89], v[90:91], 0 op_sel_hi:[1,0]
	v_lshlrev_b32_e32 v90, 16, v59
	v_pk_add_f32 v[88:89], v[88:89], v[94:95]
	v_and_b32_e32 v91, 0xffff0000, v59
	v_pk_add_f32 v[88:89], v[88:89], v[98:99]
	v_pk_mul_f32 v[90:91], v[90:91], s[26:27] op_sel_hi:[1,0]
	v_pk_add_f32 v[88:89], v[88:89], v[102:103]
	v_cvt_pk_f32_fp8_sdwa v[54:55], v55 src0_sel:WORD_1
	v_pk_add_f32 v[88:89], v[88:89], v[106:107]
	v_cvt_pk_f32_fp8_e32 v[94:95], v63
	v_pk_add_f32 v[88:89], v[88:89], v[110:111]
	v_cvt_pk_f32_fp8_sdwa v[62:63], v63 src0_sel:WORD_1
	v_pk_add_f32 v[88:89], v[88:89], v[114:115]
	v_cvt_pk_f32_fp8_e32 v[98:99], v71
	v_pk_add_f32 v[88:89], v[88:89], v[118:119]
	v_cvt_pk_f32_fp8_sdwa v[70:71], v71 src0_sel:WORD_1
	v_pk_fma_f32 v[88:89], v[88:89], s[28:29], v[90:91] op_sel_hi:[1,0,1]
	v_cvt_pk_f32_fp8_e32 v[90:91], v51
	v_cvt_pk_bf16_f32 v59, v88, v89
	v_cvt_pk_f32_fp8_e32 v[88:89], v47
	v_cvt_pk_f32_fp8_sdwa v[46:47], v47 src0_sel:WORD_1
	v_cvt_pk_f32_fp8_sdwa v[50:51], v51 src0_sel:WORD_1
	v_cvt_pk_f32_fp8_e32 v[102:103], v79
	v_pk_add_f32 v[88:89], v[88:89], 0 op_sel_hi:[1,0]
	v_pk_add_f32 v[46:47], v[46:47], 0 op_sel_hi:[1,0]
	v_pk_add_f32 v[88:89], v[88:89], v[90:91]
	v_pk_add_f32 v[46:47], v[46:47], v[50:51]
	v_pk_add_f32 v[88:89], v[88:89], v[92:93]
	v_pk_add_f32 v[46:47], v[46:47], v[54:55]
	v_cvt_pk_f32_fp8_sdwa v[78:79], v79 src0_sel:WORD_1
	v_pk_add_f32 v[88:89], v[88:89], v[94:95]
	v_pk_add_f32 v[46:47], v[46:47], v[62:63]
	v_pk_add_f32 v[88:89], v[88:89], v[96:97]
	v_pk_add_f32 v[46:47], v[46:47], v[66:67]
	v_pk_add_f32 v[88:89], v[88:89], v[98:99]
	v_pk_add_f32 v[46:47], v[46:47], v[70:71]
	v_pk_add_f32 v[88:89], v[88:89], v[100:101]
	v_lshlrev_b32_e32 v90, 16, v60
	v_and_b32_e32 v91, 0xffff0000, v60
	v_pk_add_f32 v[46:47], v[46:47], v[74:75]
	v_lshlrev_b32_e32 v50, 16, v61
	v_and_b32_e32 v51, 0xffff0000, v61
	v_pk_add_f32 v[88:89], v[88:89], v[102:103]
	v_pk_mul_f32 v[90:91], v[90:91], s[26:27] op_sel_hi:[1,0]
	v_pk_add_f32 v[46:47], v[46:47], v[78:79]
	v_pk_mul_f32 v[50:51], v[50:51], s[26:27] op_sel_hi:[1,0]
	v_pk_fma_f32 v[88:89], v[88:89], s[28:29], v[90:91] op_sel_hi:[1,0,1]
	v_pk_fma_f32 v[46:47], v[46:47], s[28:29], v[50:51] op_sel_hi:[1,0,1]
	v_cvt_pk_bf16_f32 v60, v88, v89
	v_cvt_pk_bf16_f32 v61, v46, v47
	v_lshl_add_u64 v[46:47], v[86:87], 0, s[76:77]
	v_cvt_pk_f32_fp8_e32 v[50:51], v48
	global_store_dwordx4 v[46:47], v[58:61], off
	v_cvt_pk_f32_fp8_e32 v[62:63], v56
	v_cvt_pk_f32_fp8_e32 v[70:71], v64
	v_cvt_pk_f32_fp8_e32 v[58:59], v52
	v_cvt_pk_f32_fp8_e32 v[78:79], v68
	v_pk_add_f32 v[50:51], v[50:51], 0 op_sel_hi:[1,0]
	v_cvt_pk_f32_fp8_e32 v[90:91], v72
	v_pk_add_f32 v[50:51], v[50:51], v[58:59]
	v_cvt_pk_f32_fp8_e32 v[94:95], v76
	v_pk_add_f32 v[50:51], v[50:51], v[62:63]
	v_cvt_pk_f32_fp8_e32 v[98:99], v80
	v_pk_add_f32 v[50:51], v[50:51], v[70:71]
	v_cvt_pk_f32_fp8_sdwa v[54:55], v48 src0_sel:WORD_1
	v_pk_add_f32 v[50:51], v[50:51], v[78:79]
	v_cvt_pk_f32_fp8_sdwa v[60:61], v52 src0_sel:WORD_1
	v_pk_add_f32 v[50:51], v[50:51], v[90:91]
	v_lshlrev_b32_e32 v58, 16, v42
	v_pk_add_f32 v[50:51], v[50:51], v[94:95]
	v_and_b32_e32 v59, 0xffff0000, v42
	v_cvt_pk_f32_fp8_sdwa v[66:67], v56 src0_sel:WORD_1
	v_pk_add_f32 v[50:51], v[50:51], v[98:99]
	v_pk_mul_f32 v[58:59], v[58:59], s[26:27] op_sel_hi:[1,0]
	v_cvt_pk_f32_fp8_sdwa v[74:75], v64 src0_sel:WORD_1
	v_pk_fma_f32 v[50:51], v[50:51], s[28:29], v[58:59] op_sel_hi:[1,0,1]
	v_cvt_pk_f32_fp8_sdwa v[88:89], v68 src0_sel:WORD_1
	v_cvt_pk_bf16_f32 v42, v50, v51
	v_pk_add_f32 v[50:51], v[54:55], 0 op_sel_hi:[1,0]
	v_cvt_pk_f32_fp8_sdwa v[92:93], v72 src0_sel:WORD_1
	v_pk_add_f32 v[50:51], v[50:51], v[60:61]
	v_cvt_pk_f32_fp8_sdwa v[96:97], v76 src0_sel:WORD_1
	v_pk_add_f32 v[50:51], v[50:51], v[66:67]
	v_cvt_pk_f32_fp8_sdwa v[100:101], v80 src0_sel:WORD_1
	v_pk_add_f32 v[50:51], v[50:51], v[74:75]
	v_lshlrev_b32_e32 v54, 16, v43
	v_pk_add_f32 v[50:51], v[50:51], v[88:89]
	v_and_b32_e32 v55, 0xffff0000, v43
	v_pk_add_f32 v[50:51], v[50:51], v[92:93]
	v_pk_mul_f32 v[54:55], v[54:55], s[26:27] op_sel_hi:[1,0]
	v_pk_add_f32 v[50:51], v[50:51], v[96:97]
	v_cvt_pk_f32_fp8_e32 v[58:59], v57
	v_pk_add_f32 v[50:51], v[50:51], v[100:101]
	v_cvt_pk_f32_fp8_e32 v[60:61], v65
	v_pk_fma_f32 v[50:51], v[50:51], s[28:29], v[54:55] op_sel_hi:[1,0,1]
	v_cvt_pk_f32_fp8_e32 v[54:55], v53
	v_cvt_pk_bf16_f32 v43, v50, v51
	v_cvt_pk_f32_fp8_e32 v[50:51], v49
	v_cvt_pk_f32_fp8_sdwa v[48:49], v49 src0_sel:WORD_1
	v_cvt_pk_f32_fp8_sdwa v[52:53], v53 src0_sel:WORD_1
	v_cvt_pk_f32_fp8_sdwa v[62:63], v65 src0_sel:WORD_1
	v_cvt_pk_f32_fp8_e32 v[64:65], v69
	v_pk_add_f32 v[50:51], v[50:51], 0 op_sel_hi:[1,0]
	v_cvt_pk_f32_fp8_sdwa v[56:57], v57 src0_sel:WORD_1
	v_cvt_pk_f32_fp8_sdwa v[66:67], v69 src0_sel:WORD_1
	v_cvt_pk_f32_fp8_e32 v[68:69], v73
	v_pk_add_f32 v[50:51], v[50:51], v[54:55]
	v_cvt_pk_f32_fp8_sdwa v[70:71], v73 src0_sel:WORD_1
	v_cvt_pk_f32_fp8_e32 v[72:73], v77
	v_pk_add_f32 v[50:51], v[50:51], v[58:59]
	v_cvt_pk_f32_fp8_sdwa v[74:75], v77 src0_sel:WORD_1
	v_cvt_pk_f32_fp8_e32 v[76:77], v81
	v_pk_add_f32 v[50:51], v[50:51], v[60:61]
	v_pk_add_f32 v[48:49], v[48:49], 0 op_sel_hi:[1,0]
	v_pk_add_f32 v[50:51], v[50:51], v[64:65]
	v_pk_add_f32 v[48:49], v[48:49], v[52:53]
	v_pk_add_f32 v[50:51], v[50:51], v[68:69]
	v_pk_add_f32 v[48:49], v[48:49], v[56:57]
	v_cvt_pk_f32_fp8_sdwa v[78:79], v81 src0_sel:WORD_1
	v_pk_add_f32 v[50:51], v[50:51], v[72:73]
	v_lshlrev_b32_e32 v54, 16, v44
	v_and_b32_e32 v55, 0xffff0000, v44
	v_pk_add_f32 v[48:49], v[48:49], v[62:63]
	v_pk_add_f32 v[50:51], v[50:51], v[76:77]
	v_pk_mul_f32 v[54:55], v[54:55], s[26:27] op_sel_hi:[1,0]
	v_pk_add_f32 v[48:49], v[48:49], v[66:67]
	v_pk_fma_f32 v[50:51], v[50:51], s[28:29], v[54:55] op_sel_hi:[1,0,1]
	v_pk_add_f32 v[48:49], v[48:49], v[70:71]
	v_cvt_pk_bf16_f32 v44, v50, v51
	v_pk_add_f32 v[48:49], v[48:49], v[74:75]
	v_lshlrev_b32_e32 v50, 16, v45
	v_and_b32_e32 v51, 0xffff0000, v45
	v_pk_add_f32 v[48:49], v[48:49], v[78:79]
	v_pk_mul_f32 v[50:51], v[50:51], s[26:27] op_sel_hi:[1,0]
	s_waitcnt vmcnt(27)
	v_cvt_pk_f32_fp8_sdwa v[52:53], v26 src0_sel:WORD_1
	v_pk_fma_f32 v[48:49], v[48:49], s[28:29], v[50:51] op_sel_hi:[1,0,1]
	v_cvt_pk_f32_fp8_sdwa v[50:51], v22 src0_sel:WORD_1
	v_cvt_pk_bf16_f32 v45, v48, v49
	global_store_dwordx4 v[46:47], v[42:45], off offset:16
	v_cvt_pk_f32_fp8_sdwa v[46:47], v14 src0_sel:WORD_1
	v_cvt_pk_f32_fp8_sdwa v[48:49], v18 src0_sel:WORD_1
	v_cvt_pk_f32_fp8_sdwa v[42:43], v6 src0_sel:WORD_1
	v_cvt_pk_f32_fp8_sdwa v[44:45], v10 src0_sel:WORD_1
	s_waitcnt vmcnt(27)
	v_cvt_pk_f32_fp8_sdwa v[54:55], v30 src0_sel:WORD_1
	s_waitcnt vmcnt(26)
	v_cvt_pk_f32_fp8_sdwa v[56:57], v34 src0_sel:WORD_1
	v_pk_add_f32 v[42:43], v[42:43], 0 op_sel_hi:[1,0]
	v_cvt_pk_f32_fp8_e32 v[58:59], v6
	v_pk_add_f32 v[42:43], v[42:43], v[44:45]
	v_lshlrev_b32_e32 v44, 16, v39
	v_pk_add_f32 v[42:43], v[42:43], v[46:47]
	v_and_b32_e32 v45, 0xffff0000, v39
	v_pk_add_f32 v[42:43], v[42:43], v[48:49]
	v_pk_mul_f32 v[44:45], v[44:45], s[26:27] op_sel_hi:[1,0]
	v_pk_add_f32 v[42:43], v[42:43], v[50:51]
	v_cvt_pk_f32_fp8_e32 v[60:61], v10
	v_pk_add_f32 v[42:43], v[42:43], v[52:53]
	v_cvt_pk_f32_fp8_e32 v[62:63], v14
	v_pk_add_f32 v[42:43], v[42:43], v[54:55]
	v_cvt_pk_f32_fp8_e32 v[46:47], v15
	v_pk_add_f32 v[42:43], v[42:43], v[56:57]
	v_cvt_pk_f32_fp8_sdwa v[14:15], v15 src0_sel:WORD_1
	v_pk_fma_f32 v[42:43], v[42:43], s[28:29], v[44:45] op_sel_hi:[1,0,1]
	v_cvt_pk_f32_fp8_e32 v[44:45], v11
	v_cvt_pk_bf16_f32 v39, v42, v43
	v_cvt_pk_f32_fp8_e32 v[42:43], v7
	v_cvt_pk_f32_fp8_sdwa v[6:7], v7 src0_sel:WORD_1
	v_cvt_pk_f32_fp8_sdwa v[10:11], v11 src0_sel:WORD_1
	v_cvt_pk_f32_fp8_e32 v[64:65], v18
	v_cvt_pk_f32_fp8_e32 v[48:49], v19
	v_cvt_pk_f32_fp8_sdwa v[18:19], v19 src0_sel:WORD_1
	v_cvt_pk_f32_fp8_e32 v[66:67], v22
	v_cvt_pk_f32_fp8_e32 v[50:51], v23
	v_cvt_pk_f32_fp8_sdwa v[22:23], v23 src0_sel:WORD_1
	v_pk_add_f32 v[6:7], v[6:7], 0 op_sel_hi:[1,0]
	v_cvt_pk_f32_fp8_e32 v[68:69], v26
	v_cvt_pk_f32_fp8_e32 v[52:53], v27
	v_cvt_pk_f32_fp8_sdwa v[26:27], v27 src0_sel:WORD_1
	v_pk_add_f32 v[6:7], v[6:7], v[10:11]
	v_cvt_pk_f32_fp8_e32 v[70:71], v30
	v_pk_add_f32 v[58:59], v[58:59], 0 op_sel_hi:[1,0]
	v_cvt_pk_f32_fp8_e32 v[54:55], v31
	v_cvt_pk_f32_fp8_sdwa v[30:31], v31 src0_sel:WORD_1
	v_pk_add_f32 v[42:43], v[42:43], 0 op_sel_hi:[1,0]
	v_pk_add_f32 v[6:7], v[6:7], v[14:15]
	v_cvt_pk_f32_fp8_e32 v[72:73], v34
	v_pk_add_f32 v[58:59], v[58:59], v[60:61]
	v_cvt_pk_f32_fp8_e32 v[56:57], v35
	v_cvt_pk_f32_fp8_sdwa v[34:35], v35 src0_sel:WORD_1
	v_pk_add_f32 v[42:43], v[42:43], v[44:45]
	v_pk_add_f32 v[6:7], v[6:7], v[18:19]
	v_pk_add_f32 v[58:59], v[58:59], v[62:63]
	v_pk_add_f32 v[42:43], v[42:43], v[46:47]
	v_pk_add_f32 v[6:7], v[6:7], v[22:23]
	v_pk_add_f32 v[58:59], v[58:59], v[64:65]
	v_pk_add_f32 v[42:43], v[42:43], v[48:49]
	v_pk_add_f32 v[6:7], v[6:7], v[26:27]
	v_pk_add_f32 v[58:59], v[58:59], v[66:67]
	v_pk_add_f32 v[42:43], v[42:43], v[50:51]
	v_pk_add_f32 v[6:7], v[6:7], v[30:31]
	v_lshlrev_b32_e32 v10, 16, v41
	v_and_b32_e32 v11, 0xffff0000, v41
	v_pk_add_f32 v[58:59], v[58:59], v[68:69]
	v_pk_add_f32 v[42:43], v[42:43], v[52:53]
	v_pk_add_f32 v[6:7], v[6:7], v[34:35]
	v_pk_mul_f32 v[10:11], v[10:11], s[26:27] op_sel_hi:[1,0]
	v_pk_add_f32 v[58:59], v[58:59], v[70:71]
	v_lshlrev_b32_e32 v60, 16, v38
	v_and_b32_e32 v61, 0xffff0000, v38
	v_pk_add_f32 v[42:43], v[42:43], v[54:55]
	v_lshlrev_b32_e32 v44, 16, v40
	v_and_b32_e32 v45, 0xffff0000, v40
	v_pk_fma_f32 v[6:7], v[6:7], s[28:29], v[10:11] op_sel_hi:[1,0,1]
	v_cvt_pk_f32_fp8_e32 v[10:11], v8
	v_pk_add_f32 v[58:59], v[58:59], v[72:73]
	v_pk_mul_f32 v[60:61], v[60:61], s[26:27] op_sel_hi:[1,0]
	v_pk_add_f32 v[42:43], v[42:43], v[56:57]
	v_pk_mul_f32 v[44:45], v[44:45], s[26:27] op_sel_hi:[1,0]
	v_cvt_pk_f32_fp8_e32 v[18:19], v12
	v_pk_fma_f32 v[58:59], v[58:59], s[28:29], v[60:61] op_sel_hi:[1,0,1]
	v_pk_fma_f32 v[42:43], v[42:43], s[28:29], v[44:45] op_sel_hi:[1,0,1]
	v_cvt_pk_f32_fp8_e32 v[26:27], v16
	v_cvt_pk_bf16_f32 v38, v58, v59
	v_cvt_pk_bf16_f32 v40, v42, v43
	v_cvt_pk_bf16_f32 v41, v6, v7
	v_lshl_add_u64 v[6:7], v[86:87], 0, s[6:7]
	v_cvt_pk_f32_fp8_e32 v[34:35], v20
	global_store_dwordx4 v[6:7], v[38:41], off
	v_pk_add_f32 v[10:11], v[10:11], 0 op_sel_hi:[1,0]
	v_cvt_pk_f32_fp8_e32 v[44:45], v28
	v_cvt_pk_f32_fp8_e32 v[40:41], v24
	v_pk_add_f32 v[10:11], v[10:11], v[18:19]
	v_cvt_pk_f32_fp8_e32 v[48:49], v32
	v_pk_add_f32 v[10:11], v[10:11], v[26:27]
	v_cvt_pk_f32_fp8_e32 v[52:53], v36
	v_pk_add_f32 v[10:11], v[10:11], v[34:35]
	v_cvt_pk_f32_fp8_sdwa v[14:15], v8 src0_sel:WORD_1
	v_pk_add_f32 v[10:11], v[10:11], v[40:41]
	v_cvt_pk_f32_fp8_sdwa v[22:23], v12 src0_sel:WORD_1
	v_pk_add_f32 v[10:11], v[10:11], v[44:45]
	v_lshlrev_b32_e32 v18, 16, v2
	v_pk_add_f32 v[10:11], v[10:11], v[48:49]
	v_and_b32_e32 v19, 0xffff0000, v2
	v_cvt_pk_f32_fp8_sdwa v[30:31], v16 src0_sel:WORD_1
	v_pk_add_f32 v[10:11], v[10:11], v[52:53]
	v_pk_mul_f32 v[18:19], v[18:19], s[26:27] op_sel_hi:[1,0]
	v_cvt_pk_f32_fp8_sdwa v[38:39], v20 src0_sel:WORD_1
	v_pk_fma_f32 v[10:11], v[10:11], s[28:29], v[18:19] op_sel_hi:[1,0,1]
	v_cvt_pk_f32_fp8_sdwa v[42:43], v24 src0_sel:WORD_1
	v_cvt_pk_bf16_f32 v2, v10, v11
	v_pk_add_f32 v[10:11], v[14:15], 0 op_sel_hi:[1,0]
	v_cvt_pk_f32_fp8_sdwa v[46:47], v28 src0_sel:WORD_1
	v_pk_add_f32 v[10:11], v[10:11], v[22:23]
	v_cvt_pk_f32_fp8_sdwa v[50:51], v32 src0_sel:WORD_1
	v_pk_add_f32 v[10:11], v[10:11], v[30:31]
	v_cvt_pk_f32_fp8_sdwa v[54:55], v36 src0_sel:WORD_1
	v_pk_add_f32 v[10:11], v[10:11], v[38:39]
	v_lshlrev_b32_e32 v14, 16, v3
	v_pk_add_f32 v[10:11], v[10:11], v[42:43]
	v_and_b32_e32 v15, 0xffff0000, v3
	v_pk_add_f32 v[10:11], v[10:11], v[46:47]
	v_pk_mul_f32 v[14:15], v[14:15], s[26:27] op_sel_hi:[1,0]
	v_pk_add_f32 v[10:11], v[10:11], v[50:51]
	v_cvt_pk_f32_fp8_e32 v[26:27], v9
	v_pk_add_f32 v[10:11], v[10:11], v[54:55]
	v_cvt_pk_f32_fp8_sdwa v[8:9], v9 src0_sel:WORD_1
	v_pk_fma_f32 v[10:11], v[10:11], s[28:29], v[14:15] op_sel_hi:[1,0,1]
	v_cvt_pk_f32_fp8_e32 v[30:31], v13
	v_cvt_pk_bf16_f32 v3, v10, v11
	v_cvt_pk_f32_fp8_sdwa v[10:11], v13 src0_sel:WORD_1
	v_cvt_pk_f32_fp8_e32 v[34:35], v17
	v_cvt_pk_f32_fp8_sdwa v[12:13], v17 src0_sel:WORD_1
	v_cvt_pk_f32_fp8_e32 v[38:39], v21
	v_cvt_pk_f32_fp8_sdwa v[14:15], v21 src0_sel:WORD_1
	v_cvt_pk_f32_fp8_e32 v[40:41], v25
	v_cvt_pk_f32_fp8_sdwa v[16:17], v25 src0_sel:WORD_1
	v_pk_add_f32 v[26:27], v[26:27], 0 op_sel_hi:[1,0]
	v_pk_add_f32 v[8:9], v[8:9], 0 op_sel_hi:[1,0]
	v_cvt_pk_f32_fp8_e32 v[24:25], v29
	v_cvt_pk_f32_fp8_sdwa v[18:19], v29 src0_sel:WORD_1
	v_pk_add_f32 v[26:27], v[26:27], v[30:31]
	v_pk_add_f32 v[8:9], v[8:9], v[10:11]
	v_cvt_pk_f32_fp8_e32 v[28:29], v33
	v_cvt_pk_f32_fp8_sdwa v[20:21], v33 src0_sel:WORD_1
	v_pk_add_f32 v[26:27], v[26:27], v[34:35]
	v_pk_add_f32 v[8:9], v[8:9], v[12:13]
	v_cvt_pk_f32_fp8_e32 v[32:33], v37
	v_cvt_pk_f32_fp8_sdwa v[22:23], v37 src0_sel:WORD_1
	v_pk_add_f32 v[26:27], v[26:27], v[38:39]
	v_pk_add_f32 v[8:9], v[8:9], v[14:15]
	v_pk_add_f32 v[26:27], v[26:27], v[40:41]
	v_pk_add_f32 v[8:9], v[8:9], v[16:17]
	v_pk_add_f32 v[24:25], v[26:27], v[24:25]
	v_pk_add_f32 v[8:9], v[8:9], v[18:19]
	v_pk_add_f32 v[24:25], v[24:25], v[28:29]
	v_lshlrev_b32_e32 v26, 16, v4
	v_and_b32_e32 v27, 0xffff0000, v4
	v_pk_add_f32 v[8:9], v[8:9], v[20:21]
	v_lshlrev_b32_e32 v10, 16, v5
	v_and_b32_e32 v11, 0xffff0000, v5
	v_pk_add_f32 v[24:25], v[24:25], v[32:33]
	v_pk_mul_f32 v[26:27], v[26:27], s[26:27] op_sel_hi:[1,0]
	v_pk_add_f32 v[8:9], v[8:9], v[22:23]
	v_pk_mul_f32 v[10:11], v[10:11], s[26:27] op_sel_hi:[1,0]
	v_pk_fma_f32 v[24:25], v[24:25], s[28:29], v[26:27] op_sel_hi:[1,0,1]
	v_pk_fma_f32 v[8:9], v[8:9], s[28:29], v[10:11] op_sel_hi:[1,0,1]
	v_cvt_pk_bf16_f32 v4, v24, v25
	v_cvt_pk_bf16_f32 v5, v8, v9
	global_store_dwordx4 v[6:7], v[2:5], off offset:16
	s_waitcnt vmcnt(21)
	v_cvt_pk_f32_fp8_e32 v[88:89], v170
	v_cvt_pk_f32_fp8_sdwa v[90:91], v170 src0_sel:WORD_1
	v_pk_add_f32 v[88:89], v[88:89], 0 op_sel_hi:[1,0]
	s_waitcnt vmcnt(20)
	v_cvt_pk_f32_fp8_e32 v[92:93], v174
	v_cvt_pk_f32_fp8_sdwa v[94:95], v174 src0_sel:WORD_1
	v_pk_add_f32 v[88:89], v[88:89], v[92:93]
	s_waitcnt vmcnt(19)
	v_cvt_pk_f32_fp8_e32 v[96:97], v178
	v_lshlrev_b32_e32 v92, 16, v182
	v_and_b32_e32 v93, 0xffff0000, v182
	v_cvt_pk_f32_fp8_sdwa v[98:99], v178 src0_sel:WORD_1
	v_pk_add_f32 v[88:89], v[88:89], v[96:97]
	s_waitcnt vmcnt(18)
	v_cvt_pk_f32_fp8_e32 v[100:101], v186
	v_pk_mul_f32 v[92:93], v[92:93], s[26:27] op_sel_hi:[1,0]
	v_cvt_pk_f32_fp8_sdwa v[102:103], v186 src0_sel:WORD_1
	v_pk_add_f32 v[88:89], v[88:89], v[100:101]
	s_waitcnt vmcnt(17)
	v_cvt_pk_f32_fp8_e32 v[104:105], v190
	v_cvt_pk_f32_fp8_sdwa v[106:107], v190 src0_sel:WORD_1
	v_cvt_pk_f32_fp8_e32 v[96:97], v191
	v_cvt_pk_f32_fp8_sdwa v[190:191], v191 src0_sel:WORD_1
	v_pk_add_f32 v[88:89], v[88:89], v[104:105]
	s_waitcnt vmcnt(16)
	v_cvt_pk_f32_fp8_e32 v[108:109], v194
	v_cvt_pk_f32_fp8_sdwa v[110:111], v194 src0_sel:WORD_1
	v_pk_add_f32 v[88:89], v[88:89], v[108:109]
	s_waitcnt vmcnt(15)
	v_cvt_pk_f32_fp8_e32 v[112:113], v198
	v_cvt_pk_f32_fp8_sdwa v[114:115], v198 src0_sel:WORD_1
	s_waitcnt vmcnt(14)
	v_cvt_pk_f32_fp8_e32 v[116:117], v202
	v_cvt_pk_f32_fp8_sdwa v[118:119], v202 src0_sel:WORD_1
	v_pk_add_f32 v[88:89], v[88:89], v[112:113]
	v_cvt_pk_f32_fp8_e32 v[100:101], v199
	v_pk_add_f32 v[88:89], v[88:89], v[116:117]
	v_cvt_pk_f32_fp8_sdwa v[198:199], v199 src0_sel:WORD_1
	v_pk_fma_f32 v[88:89], v[88:89], s[28:29], v[92:93] op_sel_hi:[1,0,1]
	v_cvt_pk_f32_fp8_e32 v[92:93], v179
	v_cvt_pk_bf16_f32 v182, v88, v89
	v_pk_add_f32 v[88:89], v[90:91], 0 op_sel_hi:[1,0]
	v_lshlrev_b32_e32 v90, 16, v183
	v_pk_add_f32 v[88:89], v[88:89], v[94:95]
	v_and_b32_e32 v91, 0xffff0000, v183
	v_pk_add_f32 v[88:89], v[88:89], v[98:99]
	v_pk_mul_f32 v[90:91], v[90:91], s[26:27] op_sel_hi:[1,0]
	v_pk_add_f32 v[88:89], v[88:89], v[102:103]
	v_cvt_pk_f32_fp8_sdwa v[178:179], v179 src0_sel:WORD_1
	v_pk_add_f32 v[88:89], v[88:89], v[106:107]
	v_cvt_pk_f32_fp8_e32 v[94:95], v187
	v_pk_add_f32 v[88:89], v[88:89], v[110:111]
	v_cvt_pk_f32_fp8_sdwa v[186:187], v187 src0_sel:WORD_1
	v_pk_add_f32 v[88:89], v[88:89], v[114:115]
	v_cvt_pk_f32_fp8_e32 v[98:99], v195
	v_pk_add_f32 v[88:89], v[88:89], v[118:119]
	v_cvt_pk_f32_fp8_sdwa v[194:195], v195 src0_sel:WORD_1
	v_pk_fma_f32 v[88:89], v[88:89], s[28:29], v[90:91] op_sel_hi:[1,0,1]
	v_cvt_pk_f32_fp8_e32 v[90:91], v175
	v_cvt_pk_bf16_f32 v183, v88, v89
	v_cvt_pk_f32_fp8_e32 v[88:89], v171
	v_cvt_pk_f32_fp8_sdwa v[170:171], v171 src0_sel:WORD_1
	v_cvt_pk_f32_fp8_sdwa v[174:175], v175 src0_sel:WORD_1
	v_cvt_pk_f32_fp8_e32 v[102:103], v203
	v_pk_add_f32 v[88:89], v[88:89], 0 op_sel_hi:[1,0]
	v_pk_add_f32 v[170:171], v[170:171], 0 op_sel_hi:[1,0]
	v_pk_add_f32 v[88:89], v[88:89], v[90:91]
	v_pk_add_f32 v[170:171], v[170:171], v[174:175]
	v_pk_add_f32 v[88:89], v[88:89], v[92:93]
	v_pk_add_f32 v[170:171], v[170:171], v[178:179]
	v_cvt_pk_f32_fp8_sdwa v[202:203], v203 src0_sel:WORD_1
	v_pk_add_f32 v[88:89], v[88:89], v[94:95]
	v_pk_add_f32 v[170:171], v[170:171], v[186:187]
	v_pk_add_f32 v[88:89], v[88:89], v[96:97]
	v_pk_add_f32 v[170:171], v[170:171], v[190:191]
	v_pk_add_f32 v[88:89], v[88:89], v[98:99]
	v_pk_add_f32 v[170:171], v[170:171], v[194:195]
	v_pk_add_f32 v[88:89], v[88:89], v[100:101]
	v_lshlrev_b32_e32 v90, 16, v184
	v_and_b32_e32 v91, 0xffff0000, v184
	v_pk_add_f32 v[170:171], v[170:171], v[198:199]
	v_lshlrev_b32_e32 v174, 16, v185
	v_and_b32_e32 v175, 0xffff0000, v185
	v_pk_add_f32 v[88:89], v[88:89], v[102:103]
	v_pk_mul_f32 v[90:91], v[90:91], s[26:27] op_sel_hi:[1,0]
	v_pk_add_f32 v[170:171], v[170:171], v[202:203]
	v_pk_mul_f32 v[174:175], v[174:175], s[26:27] op_sel_hi:[1,0]
	v_pk_fma_f32 v[88:89], v[88:89], s[28:29], v[90:91] op_sel_hi:[1,0,1]
	v_pk_fma_f32 v[170:171], v[170:171], s[28:29], v[174:175] op_sel_hi:[1,0,1]
	v_cvt_pk_bf16_f32 v184, v88, v89
	v_cvt_pk_bf16_f32 v185, v170, v171
	v_lshl_add_u64 v[170:171], v[86:87], 0, s[100:101]
	v_cvt_pk_f32_fp8_e32 v[174:175], v172
	global_store_dwordx4 v[170:171], v[182:185], off
	v_cvt_pk_f32_fp8_e32 v[186:187], v180
	v_cvt_pk_f32_fp8_e32 v[194:195], v188
	v_cvt_pk_f32_fp8_e32 v[182:183], v176
	v_cvt_pk_f32_fp8_e32 v[202:203], v192
	v_pk_add_f32 v[174:175], v[174:175], 0 op_sel_hi:[1,0]
	v_cvt_pk_f32_fp8_e32 v[90:91], v196
	v_pk_add_f32 v[174:175], v[174:175], v[182:183]
	v_cvt_pk_f32_fp8_e32 v[94:95], v200
	v_pk_add_f32 v[174:175], v[174:175], v[186:187]
	v_cvt_pk_f32_fp8_e32 v[98:99], v204
	v_pk_add_f32 v[174:175], v[174:175], v[194:195]
	v_cvt_pk_f32_fp8_sdwa v[178:179], v172 src0_sel:WORD_1
	v_pk_add_f32 v[174:175], v[174:175], v[202:203]
	v_cvt_pk_f32_fp8_sdwa v[184:185], v176 src0_sel:WORD_1
	v_pk_add_f32 v[174:175], v[174:175], v[90:91]
	v_lshlrev_b32_e32 v182, 16, v166
	v_pk_add_f32 v[174:175], v[174:175], v[94:95]
	v_and_b32_e32 v183, 0xffff0000, v166
	v_cvt_pk_f32_fp8_sdwa v[190:191], v180 src0_sel:WORD_1
	v_pk_add_f32 v[174:175], v[174:175], v[98:99]
	v_pk_mul_f32 v[182:183], v[182:183], s[26:27] op_sel_hi:[1,0]
	v_cvt_pk_f32_fp8_sdwa v[198:199], v188 src0_sel:WORD_1
	v_pk_fma_f32 v[174:175], v[174:175], s[28:29], v[182:183] op_sel_hi:[1,0,1]
	v_cvt_pk_f32_fp8_sdwa v[88:89], v192 src0_sel:WORD_1
	v_cvt_pk_bf16_f32 v166, v174, v175
	v_pk_add_f32 v[174:175], v[178:179], 0 op_sel_hi:[1,0]
	v_cvt_pk_f32_fp8_sdwa v[92:93], v196 src0_sel:WORD_1
	v_pk_add_f32 v[174:175], v[174:175], v[184:185]
	v_cvt_pk_f32_fp8_sdwa v[96:97], v200 src0_sel:WORD_1
	v_pk_add_f32 v[174:175], v[174:175], v[190:191]
	v_cvt_pk_f32_fp8_sdwa v[100:101], v204 src0_sel:WORD_1
	v_pk_add_f32 v[174:175], v[174:175], v[198:199]
	v_lshlrev_b32_e32 v178, 16, v167
	v_pk_add_f32 v[174:175], v[174:175], v[88:89]
	v_and_b32_e32 v179, 0xffff0000, v167
	v_pk_add_f32 v[174:175], v[174:175], v[92:93]
	v_pk_mul_f32 v[178:179], v[178:179], s[26:27] op_sel_hi:[1,0]
	v_pk_add_f32 v[174:175], v[174:175], v[96:97]
	v_cvt_pk_f32_fp8_e32 v[182:183], v181
	v_pk_add_f32 v[174:175], v[174:175], v[100:101]
	v_cvt_pk_f32_fp8_e32 v[184:185], v189
	v_pk_fma_f32 v[174:175], v[174:175], s[28:29], v[178:179] op_sel_hi:[1,0,1]
	v_cvt_pk_f32_fp8_e32 v[178:179], v177
	v_cvt_pk_bf16_f32 v167, v174, v175
	v_cvt_pk_f32_fp8_e32 v[174:175], v173
	v_cvt_pk_f32_fp8_sdwa v[172:173], v173 src0_sel:WORD_1
	v_cvt_pk_f32_fp8_sdwa v[176:177], v177 src0_sel:WORD_1
	v_cvt_pk_f32_fp8_sdwa v[186:187], v189 src0_sel:WORD_1
	v_cvt_pk_f32_fp8_e32 v[188:189], v193
	v_pk_add_f32 v[174:175], v[174:175], 0 op_sel_hi:[1,0]
	v_cvt_pk_f32_fp8_sdwa v[180:181], v181 src0_sel:WORD_1
	v_cvt_pk_f32_fp8_sdwa v[190:191], v193 src0_sel:WORD_1
	v_cvt_pk_f32_fp8_e32 v[192:193], v197
	v_pk_add_f32 v[174:175], v[174:175], v[178:179]
	v_cvt_pk_f32_fp8_sdwa v[194:195], v197 src0_sel:WORD_1
	v_cvt_pk_f32_fp8_e32 v[196:197], v201
	v_pk_add_f32 v[174:175], v[174:175], v[182:183]
	v_cvt_pk_f32_fp8_sdwa v[198:199], v201 src0_sel:WORD_1
	v_cvt_pk_f32_fp8_e32 v[200:201], v205
	v_pk_add_f32 v[174:175], v[174:175], v[184:185]
	v_pk_add_f32 v[172:173], v[172:173], 0 op_sel_hi:[1,0]
	v_pk_add_f32 v[174:175], v[174:175], v[188:189]
	v_pk_add_f32 v[172:173], v[172:173], v[176:177]
	v_pk_add_f32 v[174:175], v[174:175], v[192:193]
	v_pk_add_f32 v[172:173], v[172:173], v[180:181]
	v_cvt_pk_f32_fp8_sdwa v[202:203], v205 src0_sel:WORD_1
	v_pk_add_f32 v[174:175], v[174:175], v[196:197]
	v_lshlrev_b32_e32 v178, 16, v168
	v_and_b32_e32 v179, 0xffff0000, v168
	v_pk_add_f32 v[172:173], v[172:173], v[186:187]
	v_pk_add_f32 v[174:175], v[174:175], v[200:201]
	v_pk_mul_f32 v[178:179], v[178:179], s[26:27] op_sel_hi:[1,0]
	v_pk_add_f32 v[172:173], v[172:173], v[190:191]
	v_pk_fma_f32 v[174:175], v[174:175], s[28:29], v[178:179] op_sel_hi:[1,0,1]
	v_pk_add_f32 v[172:173], v[172:173], v[194:195]
	v_cvt_pk_bf16_f32 v168, v174, v175
	v_pk_add_f32 v[172:173], v[172:173], v[198:199]
	v_lshlrev_b32_e32 v174, 16, v169
	v_and_b32_e32 v175, 0xffff0000, v169
	v_pk_add_f32 v[172:173], v[172:173], v[202:203]
	v_pk_mul_f32 v[174:175], v[174:175], s[26:27] op_sel_hi:[1,0]
	s_waitcnt vmcnt(7)
	v_cvt_pk_f32_fp8_sdwa v[176:177], v150 src0_sel:WORD_1
	v_pk_fma_f32 v[172:173], v[172:173], s[28:29], v[174:175] op_sel_hi:[1,0,1]
	v_cvt_pk_f32_fp8_sdwa v[174:175], v142 src0_sel:WORD_1
	v_cvt_pk_bf16_f32 v169, v172, v173
	global_store_dwordx4 v[170:171], v[166:169], off offset:16
	v_cvt_pk_f32_fp8_sdwa v[170:171], v134 src0_sel:WORD_1
	v_cvt_pk_f32_fp8_sdwa v[172:173], v138 src0_sel:WORD_1
	v_cvt_pk_f32_fp8_sdwa v[166:167], v126 src0_sel:WORD_1
	v_cvt_pk_f32_fp8_sdwa v[168:169], v130 src0_sel:WORD_1
	s_waitcnt vmcnt(7)
	v_cvt_pk_f32_fp8_sdwa v[178:179], v154 src0_sel:WORD_1
	s_waitcnt vmcnt(6)
	v_cvt_pk_f32_fp8_sdwa v[180:181], v158 src0_sel:WORD_1
	v_pk_add_f32 v[166:167], v[166:167], 0 op_sel_hi:[1,0]
	v_cvt_pk_f32_fp8_e32 v[182:183], v126
	v_pk_add_f32 v[166:167], v[166:167], v[168:169]
	v_lshlrev_b32_e32 v168, 16, v163
	v_pk_add_f32 v[166:167], v[166:167], v[170:171]
	v_and_b32_e32 v169, 0xffff0000, v163
	v_pk_add_f32 v[166:167], v[166:167], v[172:173]
	v_pk_mul_f32 v[168:169], v[168:169], s[26:27] op_sel_hi:[1,0]
	v_pk_add_f32 v[166:167], v[166:167], v[174:175]
	v_cvt_pk_f32_fp8_e32 v[184:185], v130
	v_pk_add_f32 v[166:167], v[166:167], v[176:177]
	v_cvt_pk_f32_fp8_e32 v[186:187], v134
	v_pk_add_f32 v[166:167], v[166:167], v[178:179]
	v_cvt_pk_f32_fp8_e32 v[170:171], v135
	v_pk_add_f32 v[166:167], v[166:167], v[180:181]
	v_cvt_pk_f32_fp8_sdwa v[134:135], v135 src0_sel:WORD_1
	v_pk_fma_f32 v[166:167], v[166:167], s[28:29], v[168:169] op_sel_hi:[1,0,1]
	v_cvt_pk_f32_fp8_e32 v[168:169], v131
	v_cvt_pk_bf16_f32 v163, v166, v167
	v_cvt_pk_f32_fp8_e32 v[166:167], v127
	v_cvt_pk_f32_fp8_sdwa v[126:127], v127 src0_sel:WORD_1
	v_cvt_pk_f32_fp8_sdwa v[130:131], v131 src0_sel:WORD_1
	v_cvt_pk_f32_fp8_e32 v[188:189], v138
	v_cvt_pk_f32_fp8_e32 v[172:173], v139
	v_cvt_pk_f32_fp8_sdwa v[138:139], v139 src0_sel:WORD_1
	v_cvt_pk_f32_fp8_e32 v[190:191], v142
	v_cvt_pk_f32_fp8_e32 v[174:175], v143
	v_cvt_pk_f32_fp8_sdwa v[142:143], v143 src0_sel:WORD_1
	v_pk_add_f32 v[126:127], v[126:127], 0 op_sel_hi:[1,0]
	v_cvt_pk_f32_fp8_e32 v[192:193], v150
	v_cvt_pk_f32_fp8_e32 v[176:177], v151
	v_cvt_pk_f32_fp8_sdwa v[150:151], v151 src0_sel:WORD_1
	v_pk_add_f32 v[126:127], v[126:127], v[130:131]
	v_cvt_pk_f32_fp8_e32 v[194:195], v154
	v_pk_add_f32 v[182:183], v[182:183], 0 op_sel_hi:[1,0]
	v_cvt_pk_f32_fp8_e32 v[178:179], v155
	v_cvt_pk_f32_fp8_sdwa v[154:155], v155 src0_sel:WORD_1
	v_pk_add_f32 v[166:167], v[166:167], 0 op_sel_hi:[1,0]
	v_pk_add_f32 v[126:127], v[126:127], v[134:135]
	v_cvt_pk_f32_fp8_e32 v[196:197], v158
	v_pk_add_f32 v[182:183], v[182:183], v[184:185]
	v_cvt_pk_f32_fp8_e32 v[180:181], v159
	v_cvt_pk_f32_fp8_sdwa v[158:159], v159 src0_sel:WORD_1
	v_pk_add_f32 v[166:167], v[166:167], v[168:169]
	v_pk_add_f32 v[126:127], v[126:127], v[138:139]
	v_pk_add_f32 v[182:183], v[182:183], v[186:187]
	v_pk_add_f32 v[166:167], v[166:167], v[170:171]
	v_pk_add_f32 v[126:127], v[126:127], v[142:143]
	v_pk_add_f32 v[182:183], v[182:183], v[188:189]
	v_pk_add_f32 v[166:167], v[166:167], v[172:173]
	v_pk_add_f32 v[126:127], v[126:127], v[150:151]
	v_pk_add_f32 v[182:183], v[182:183], v[190:191]
	v_pk_add_f32 v[166:167], v[166:167], v[174:175]
	v_pk_add_f32 v[126:127], v[126:127], v[154:155]
	v_lshlrev_b32_e32 v130, 16, v165
	v_and_b32_e32 v131, 0xffff0000, v165
	v_pk_add_f32 v[182:183], v[182:183], v[192:193]
	v_pk_add_f32 v[166:167], v[166:167], v[176:177]
	v_pk_add_f32 v[126:127], v[126:127], v[158:159]
	v_pk_mul_f32 v[130:131], v[130:131], s[26:27] op_sel_hi:[1,0]
	v_pk_add_f32 v[182:183], v[182:183], v[194:195]
	v_lshlrev_b32_e32 v184, 16, v162
	v_and_b32_e32 v185, 0xffff0000, v162
	v_pk_add_f32 v[166:167], v[166:167], v[178:179]
	v_lshlrev_b32_e32 v168, 16, v164
	v_and_b32_e32 v169, 0xffff0000, v164
	v_pk_fma_f32 v[126:127], v[126:127], s[28:29], v[130:131] op_sel_hi:[1,0,1]
	v_cvt_pk_f32_fp8_e32 v[130:131], v128
	v_pk_add_f32 v[182:183], v[182:183], v[196:197]
	v_pk_mul_f32 v[184:185], v[184:185], s[26:27] op_sel_hi:[1,0]
	v_pk_add_f32 v[166:167], v[166:167], v[180:181]
	v_pk_mul_f32 v[168:169], v[168:169], s[26:27] op_sel_hi:[1,0]
	v_cvt_pk_f32_fp8_e32 v[138:139], v132
	v_pk_fma_f32 v[182:183], v[182:183], s[28:29], v[184:185] op_sel_hi:[1,0,1]
	v_pk_fma_f32 v[166:167], v[166:167], s[28:29], v[168:169] op_sel_hi:[1,0,1]
	v_cvt_pk_f32_fp8_e32 v[150:151], v136
	v_cvt_pk_bf16_f32 v162, v182, v183
	v_cvt_pk_bf16_f32 v164, v166, v167
	v_cvt_pk_bf16_f32 v165, v126, v127
	v_lshl_add_u64 v[126:127], v[86:87], 0, s[98:99]
	v_cvt_pk_f32_fp8_e32 v[158:159], v140
	global_store_dwordx4 v[126:127], v[162:165], off
	v_pk_add_f32 v[130:131], v[130:131], 0 op_sel_hi:[1,0]
	v_cvt_pk_f32_fp8_e32 v[168:169], v152
	v_cvt_pk_f32_fp8_e32 v[164:165], v144
	v_pk_add_f32 v[130:131], v[130:131], v[138:139]
	v_cvt_pk_f32_fp8_e32 v[172:173], v156
	v_pk_add_f32 v[130:131], v[130:131], v[150:151]
	v_cvt_pk_f32_fp8_e32 v[176:177], v160
	v_pk_add_f32 v[130:131], v[130:131], v[158:159]
	v_cvt_pk_f32_fp8_sdwa v[134:135], v128 src0_sel:WORD_1
	v_pk_add_f32 v[130:131], v[130:131], v[164:165]
	v_cvt_pk_f32_fp8_sdwa v[142:143], v132 src0_sel:WORD_1
	v_pk_add_f32 v[130:131], v[130:131], v[168:169]
	v_lshlrev_b32_e32 v138, 16, v122
	v_pk_add_f32 v[130:131], v[130:131], v[172:173]
	v_and_b32_e32 v139, 0xffff0000, v122
	v_cvt_pk_f32_fp8_sdwa v[154:155], v136 src0_sel:WORD_1
	v_pk_add_f32 v[130:131], v[130:131], v[176:177]
	v_pk_mul_f32 v[138:139], v[138:139], s[26:27] op_sel_hi:[1,0]
	v_cvt_pk_f32_fp8_sdwa v[162:163], v140 src0_sel:WORD_1
	v_pk_fma_f32 v[130:131], v[130:131], s[28:29], v[138:139] op_sel_hi:[1,0,1]
	v_cvt_pk_f32_fp8_sdwa v[166:167], v144 src0_sel:WORD_1
	v_cvt_pk_bf16_f32 v122, v130, v131
	v_pk_add_f32 v[130:131], v[134:135], 0 op_sel_hi:[1,0]
	v_cvt_pk_f32_fp8_sdwa v[170:171], v152 src0_sel:WORD_1
	v_pk_add_f32 v[130:131], v[130:131], v[142:143]
	v_cvt_pk_f32_fp8_sdwa v[174:175], v156 src0_sel:WORD_1
	v_pk_add_f32 v[130:131], v[130:131], v[154:155]
	v_cvt_pk_f32_fp8_sdwa v[178:179], v160 src0_sel:WORD_1
	v_pk_add_f32 v[130:131], v[130:131], v[162:163]
	v_lshlrev_b32_e32 v134, 16, v123
	v_pk_add_f32 v[130:131], v[130:131], v[166:167]
	v_and_b32_e32 v135, 0xffff0000, v123
	v_pk_add_f32 v[130:131], v[130:131], v[170:171]
	v_pk_mul_f32 v[134:135], v[134:135], s[26:27] op_sel_hi:[1,0]
	v_pk_add_f32 v[130:131], v[130:131], v[174:175]
	v_cvt_pk_f32_fp8_e32 v[150:151], v129
	v_pk_add_f32 v[130:131], v[130:131], v[178:179]
	v_cvt_pk_f32_fp8_sdwa v[128:129], v129 src0_sel:WORD_1
	v_pk_fma_f32 v[130:131], v[130:131], s[28:29], v[134:135] op_sel_hi:[1,0,1]
	v_cvt_pk_f32_fp8_e32 v[154:155], v133
	v_cvt_pk_bf16_f32 v123, v130, v131
	v_cvt_pk_f32_fp8_sdwa v[130:131], v133 src0_sel:WORD_1
	v_cvt_pk_f32_fp8_e32 v[158:159], v137
	v_cvt_pk_f32_fp8_sdwa v[132:133], v137 src0_sel:WORD_1
	v_cvt_pk_f32_fp8_e32 v[162:163], v141
	v_cvt_pk_f32_fp8_sdwa v[134:135], v141 src0_sel:WORD_1
	v_cvt_pk_f32_fp8_e32 v[164:165], v145
	v_cvt_pk_f32_fp8_sdwa v[136:137], v145 src0_sel:WORD_1
	v_pk_add_f32 v[150:151], v[150:151], 0 op_sel_hi:[1,0]
	v_pk_add_f32 v[128:129], v[128:129], 0 op_sel_hi:[1,0]
	v_cvt_pk_f32_fp8_e32 v[144:145], v153
	v_cvt_pk_f32_fp8_sdwa v[138:139], v153 src0_sel:WORD_1
	v_pk_add_f32 v[150:151], v[150:151], v[154:155]
	v_pk_add_f32 v[128:129], v[128:129], v[130:131]
	v_cvt_pk_f32_fp8_e32 v[152:153], v157
	v_cvt_pk_f32_fp8_sdwa v[140:141], v157 src0_sel:WORD_1
	v_pk_add_f32 v[150:151], v[150:151], v[158:159]
	v_pk_add_f32 v[128:129], v[128:129], v[132:133]
	v_cvt_pk_f32_fp8_e32 v[156:157], v161
	v_cvt_pk_f32_fp8_sdwa v[142:143], v161 src0_sel:WORD_1
	v_pk_add_f32 v[150:151], v[150:151], v[162:163]
	v_pk_add_f32 v[128:129], v[128:129], v[134:135]
	v_pk_add_f32 v[150:151], v[150:151], v[164:165]
	v_pk_add_f32 v[128:129], v[128:129], v[136:137]
	v_pk_add_f32 v[144:145], v[150:151], v[144:145]
	v_pk_add_f32 v[128:129], v[128:129], v[138:139]
	v_pk_add_f32 v[144:145], v[144:145], v[152:153]
	v_lshlrev_b32_e32 v150, 16, v124
	v_and_b32_e32 v151, 0xffff0000, v124
	v_pk_add_f32 v[128:129], v[128:129], v[140:141]
	v_lshlrev_b32_e32 v130, 16, v125
	v_and_b32_e32 v131, 0xffff0000, v125
	v_pk_add_f32 v[144:145], v[144:145], v[156:157]
	v_pk_mul_f32 v[150:151], v[150:151], s[26:27] op_sel_hi:[1,0]
	v_pk_add_f32 v[128:129], v[128:129], v[142:143]
	v_pk_mul_f32 v[130:131], v[130:131], s[26:27] op_sel_hi:[1,0]
	v_pk_fma_f32 v[144:145], v[144:145], s[28:29], v[150:151] op_sel_hi:[1,0,1]
	v_pk_fma_f32 v[128:129], v[128:129], s[28:29], v[130:131] op_sel_hi:[1,0,1]
	v_cvt_pk_bf16_f32 v124, v144, v145
	v_cvt_pk_bf16_f32 v125, v128, v129
	global_store_dwordx4 v[126:127], v[122:125], off offset:16
	s_mov_b64 s[76:77], 0
	s_mov_b32 s82, s43
	s_mov_b32 s83, s45
